# baseline (speedup 1.0000x reference)
; #define GAS __attribute__((address_space(1)))
; #define LAS __attribute__((address_space(3)))
; #define LDS_WAIT() asm volatile("s_waitcnt lgkmcnt(0)" ::: "memory")
; __device__ __forceinline__ unsigned pk2(float lo, float hi) { return f2bf(lo) | (f2bf(hi) << 16); }
; __device__ __forceinline__ void p0_transpose_item(const float* W, int N, int k0, int n0, bf16* WT, int K, int dst_row0, LAS float* scr, int lane, const float* kscale = nullptr, int permhalf = -1) {
;     typedef float f32x4t __attribute__((ext_vector_type(4)));
;     const int c = lane & 7;
;     float ks[8];
; #pragma unroll
;     for (int i = 0; i < 8; ++i) ks[i] = kscale ? kscale[k0 + 8 * c + i] : 1.0f;
; #pragma unroll
;     for (int i = 0; i < 8; ++i) { const int kk = 8 * i + (lane >> 3), nn = (lane & 7) * 4;
;         *(LAS f32x4t*)(scr + kk * 36 + nn) = *(const GAS f32x4t*)(W + (size_t)(k0 + kk) * N + n0 + nn); }
;     LDS_WAIT(); asm volatile("" ::: "memory");
; #pragma unroll
;     for (int j = 0; j < 4; ++j) { const int n = (lane >> 3) + 8 * j; const LAS float* s = scr + (8 * c) * 36 + n;
;         v4u o; o.x = pk2(s[0 * 36] * ks[0], s[1 * 36] * ks[1]); o.y = pk2(s[2 * 36] * ks[2], s[3 * 36] * ks[3]); o.z = pk2(s[4 * 36] * ks[4], s[5 * 36] * ks[5]); o.w = pk2(s[6 * 36] * ks[6], s[7 * 36] * ks[7]);
;         const int drow = permhalf < 0 ? n : (32 * (n >> 4) + 8 * ((n >> 2) & 3) + 4 * permhalf + (n & 3));
;         *(GAS v4u*)(WT + (size_t)(dst_row0 + drow) * K + k0 + 8 * c) = o; }
;     LDS_WAIT(); asm volatile("" ::: "memory");
; }
; __device__ __forceinline__ void p0_prologue(const Frame& F, KArgs a) {
;     ...
;         { const int kb = r / 64, nb = r % 64; p0_transpose_item(a->in[14], 2048, 64 * kb, 32 * nb, (bf16*)(ws + WS_WO), 2048, 32 * nb, scr, F.lane); }
.LBB0_12:
	s_cmpk_gt_i32 s39, 0x11ff
	s_mov_b64 s[6:7], -1
	s_cbranch_scc0 .LBB0_26
	s_cmpk_gt_u32 s39, 0x21ff
	s_cbranch_scc0 .LBB0_23
	s_cmpk_gt_u32 s39, 0x25ff
	s_cbranch_scc0 .LBB0_20
	s_and_b32 s18, s3, 0x7e0
	s_cmpk_gt_u32 s39, 0x29ff
	v_or_b32_e32 v31, s18, v1
	v_or_b32_e32 v30, s18, v12
	v_or_b32_e32 v29, s18, v13
	v_or_b32_e32 v28, s18, v14
	s_cbranch_scc0 .LBB0_17
	s_load_dwordx2 s[6:7], s[12:13], 0x70
	s_and_b32 s4, s39, 0x7fffffc0
	s_lshl_b32 s19, s18, 2
	s_addk_i32 s4, 0xd600
	v_or_b32_e32 v32, s4, v1
	s_waitcnt lgkmcnt(0)
	s_add_u32 s6, s6, s19
	s_addc_u32 s7, s7, 0
	v_mov_b32_e32 v33, v3
	v_lshl_add_u64 v[56:57], s[6:7], 0, v[2:3]
	v_lshlrev_b64 v[32:33], 13, v[32:33]
	v_lshl_add_u64 v[40:41], v[56:57], 0, v[32:33]
	v_or_b32_e32 v32, s4, v12
	v_mov_b32_e32 v33, v3
	v_lshlrev_b64 v[32:33], 13, v[32:33]
	v_lshl_add_u64 v[42:43], v[56:57], 0, v[32:33]
	global_load_dwordx4 v[32:35], v[40:41], off
	global_load_dwordx4 v[36:39], v[42:43], off
	v_or_b32_e32 v40, s4, v13
	v_mov_b32_e32 v41, v3
	v_lshlrev_b64 v[40:41], 13, v[40:41]
	v_lshl_add_u64 v[48:49], v[56:57], 0, v[40:41]
	v_or_b32_e32 v40, s4, v14
	v_mov_b32_e32 v41, v3
	v_lshlrev_b64 v[40:41], 13, v[40:41]
	v_lshl_add_u64 v[50:51], v[56:57], 0, v[40:41]
	global_load_dwordx4 v[40:43], v[48:49], off
	global_load_dwordx4 v[44:47], v[50:51], off
	v_or_b32_e32 v48, s4, v15
	v_mov_b32_e32 v49, v3
	v_lshlrev_b64 v[48:49], 13, v[48:49]
	v_lshl_add_u64 v[58:59], v[56:57], 0, v[48:49]
	v_or_b32_e32 v48, s4, v16
	v_mov_b32_e32 v49, v3
	v_lshlrev_b64 v[48:49], 13, v[48:49]
	v_lshl_add_u64 v[60:61], v[56:57], 0, v[48:49]
	global_load_dwordx4 v[48:51], v[58:59], off
	global_load_dwordx4 v[52:55], v[60:61], off
	v_or_b32_e32 v58, s4, v17
	v_mov_b32_e32 v59, v3
	v_lshlrev_b64 v[58:59], 13, v[58:59]
	v_lshl_add_u64 v[64:65], v[56:57], 0, v[58:59]
	v_or_b32_e32 v58, s4, v18
	v_mov_b32_e32 v59, v3
	v_lshlrev_b64 v[58:59], 13, v[58:59]
	v_lshl_add_u64 v[66:67], v[56:57], 0, v[58:59]
	global_load_dwordx4 v[56:59], v[64:65], off
	global_load_dwordx4 v[60:63], v[66:67], off
	v_lshlrev_b32_e32 v64, 12, v31
	v_mov_b32_e32 v65, v3
	v_lshl_add_u64 v[66:67], s[4:5], 1, v[4:5]
	v_lshl_add_u64 v[64:65], v[66:67], 0, v[64:65]
	s_mov_b64 s[6:7], 0
	s_waitcnt vmcnt(7)
	ds_write_b128 v25, v[32:35]
	s_waitcnt vmcnt(6)
	ds_write_b128 v25, v[36:39] offset:1152
	s_waitcnt vmcnt(5)
	ds_write_b128 v25, v[40:43] offset:2304
	s_waitcnt vmcnt(4)
	ds_write_b128 v25, v[44:47] offset:3456
	s_waitcnt vmcnt(3)
	ds_write_b128 v25, v[48:51] offset:4608
	s_waitcnt vmcnt(2)
	ds_write_b128 v25, v[52:55] offset:5760
	s_waitcnt vmcnt(1)
	ds_write_b128 v25, v[56:59] offset:6912
	s_waitcnt vmcnt(0)
	ds_write_b128 v25, v[60:63] offset:8064
	s_waitcnt lgkmcnt(0)
	ds_read2_b32 v[32:33], v19 offset0:36 offset1:44
	ds_read2_b32 v[34:35], v19 offset1:8
	ds_read2_b32 v[36:37], v19 offset0:72 offset1:80
	ds_read2_b32 v[38:39], v19 offset0:108 offset1:116
	ds_read2_b32 v[40:41], v19 offset0:144 offset1:152
	ds_read2_b32 v[42:43], v19 offset0:180 offset1:188
	ds_read2_b32 v[44:45], v19 offset0:216 offset1:224
	ds_read2_b32 v[46:47], v26 offset0:124 offset1:132
	s_waitcnt lgkmcnt(6)
	v_bfe_u32 v48, v34, 16, 1
	s_waitcnt lgkmcnt(5)
	v_bfe_u32 v50, v36, 16, 1
	s_waitcnt lgkmcnt(3)
	v_bfe_u32 v52, v40, 16, 1
	s_waitcnt lgkmcnt(1)
	v_bfe_u32 v54, v44, 16, 1
	v_bfe_u32 v49, v32, 16, 1
	v_bfe_u32 v51, v38, 16, 1
	v_bfe_u32 v53, v42, 16, 1
	s_waitcnt lgkmcnt(0)
	v_bfe_u32 v55, v46, 16, 1
	v_bfe_u32 v56, v35, 16, 1
	v_bfe_u32 v57, v33, 16, 1
	v_add3_u32 v34, v34, v48, s29
	v_add3_u32 v36, v36, v50, s29
	v_add3_u32 v40, v40, v52, s29
	v_add3_u32 v44, v44, v54, s29
	v_add3_u32 v32, v32, v49, s29
	v_add3_u32 v38, v38, v51, s29
	v_add3_u32 v42, v42, v53, s29
	v_add3_u32 v46, v46, v55, s29
	v_add3_u32 v35, v35, v56, s29
	v_add3_u32 v48, v33, v57, s29
	v_lshrrev_b32_e32 v33, 16, v34
	v_lshrrev_b32_e32 v34, 16, v36
	v_lshrrev_b32_e32 v36, 16, v40
	v_lshrrev_b32_e32 v40, 16, v44
	v_bfe_u32 v58, v37, 16, 1
	v_lshrrev_b32_e32 v44, 16, v35
	v_and_or_b32 v32, v32, s31, v33
	v_and_or_b32 v33, v38, s31, v34
	v_and_or_b32 v34, v42, s31, v36
	v_and_or_b32 v35, v46, s31, v40
	v_add3_u32 v37, v37, v58, s29
	global_store_dwordx4 v[64:65], v[32:35], off sc1
	v_and_or_b32 v36, v48, s31, v44
	ds_read2_b32 v[48:49], v19 offset0:232 offset1:240
	v_bfe_u32 v33, v39, 16, 1
	v_lshrrev_b32_e32 v32, 16, v37
	v_add3_u32 v33, v39, v33, s29
	v_and_or_b32 v37, v33, s31, v32
	v_bfe_u32 v32, v41, 16, 1
	v_add3_u32 v32, v41, v32, s29
	v_bfe_u32 v33, v43, 16, 1
	v_lshrrev_b32_e32 v32, 16, v32
	v_add3_u32 v33, v43, v33, s29
	v_and_or_b32 v38, v33, s31, v32
	v_bfe_u32 v32, v45, 16, 1
	v_add3_u32 v32, v45, v32, s29
	v_bfe_u32 v33, v47, 16, 1
	v_lshrrev_b32_e32 v32, 16, v32
	v_add3_u32 v33, v47, v33, s29
	v_and_or_b32 v39, v33, s31, v32
	v_lshlrev_b32_e32 v32, 12, v30
	v_mov_b32_e32 v33, v3
	ds_read2_b32 v[40:41], v19 offset0:16 offset1:24
	v_lshl_add_u64 v[32:33], v[66:67], 0, v[32:33]
	global_store_dwordx4 v[32:33], v[36:39], off sc1
	ds_read2_b32 v[36:37], v19 offset0:52 offset1:60
	ds_read2_b32 v[38:39], v19 offset0:88 offset1:96
	ds_read2_b32 v[42:43], v19 offset0:124 offset1:132
	s_waitcnt lgkmcnt(3)
	v_bfe_u32 v32, v40, 16, 1
	v_add3_u32 v32, v40, v32, s29
	s_waitcnt lgkmcnt(2)
	v_bfe_u32 v33, v36, 16, 1
	ds_read2_b32 v[44:45], v19 offset0:160 offset1:168
	v_lshrrev_b32_e32 v32, 16, v32
	v_add3_u32 v33, v36, v33, s29
	ds_read2_b32 v[46:47], v19 offset0:196 offset1:204
	v_and_or_b32 v32, v33, s31, v32
	s_waitcnt lgkmcnt(3)
	v_bfe_u32 v33, v38, 16, 1
	v_add3_u32 v33, v38, v33, s29
	s_waitcnt lgkmcnt(2)
; #define GAS __attribute__((address_space(1)))
; #define LAS __attribute__((address_space(3)))
; __device__ __forceinline__ unsigned pk2(float lo, float hi) { return f2bf(lo) | (f2bf(hi) << 16); }
; __device__ __forceinline__ void p0_transpose_item(const float* W, int N, int k0, int n0, bf16* WT, int K, int dst_row0, LAS float* scr, int lane, const float* kscale = nullptr, int permhalf = -1) {
;     ...
;     for (int j = 0; j < 4; ++j) { const int n = (lane >> 3) + 8 * j; const LAS float* s = scr + (8 * c) * 36 + n;
;         v4u o; o.x = pk2(s[0 * 36] * ks[0], s[1 * 36] * ks[1]); o.y = pk2(s[2 * 36] * ks[2], s[3 * 36] * ks[3]); o.z = pk2(s[4 * 36] * ks[4], s[5 * 36] * ks[5]); o.w = pk2(s[6 * 36] * ks[6], s[7 * 36] * ks[7]);
;         const int drow = permhalf < 0 ? n : (32 * (n >> 4) + 8 * ((n >> 2) & 3) + 4 * permhalf + (n & 3));
;         *(GAS v4u*)(WT + (size_t)(dst_row0 + drow) * K + k0 + 8 * c) = o; }
	v_bfe_u32 v34, v42, 16, 1
	v_lshrrev_b32_e32 v33, 16, v33
	v_add3_u32 v34, v42, v34, s29
	ds_read2_b32 v[50:51], v27 offset0:12 offset1:20
	v_and_or_b32 v33, v34, s31, v33
	s_waitcnt lgkmcnt(2)
	v_bfe_u32 v34, v44, 16, 1
	v_add3_u32 v34, v44, v34, s29
	s_waitcnt lgkmcnt(1)
	v_bfe_u32 v35, v46, 16, 1
	v_lshrrev_b32_e32 v34, 16, v34
	v_add3_u32 v35, v46, v35, s29
	v_and_or_b32 v34, v35, s31, v34
	v_bfe_u32 v35, v48, 16, 1
	v_add3_u32 v35, v48, v35, s29
	s_waitcnt lgkmcnt(0)
	v_bfe_u32 v36, v50, 16, 1
	v_lshrrev_b32_e32 v35, 16, v35
	v_add3_u32 v36, v50, v36, s29
	v_lshlrev_b32_e32 v52, 12, v29
	v_mov_b32_e32 v53, v3
	v_and_or_b32 v35, v36, s31, v35
	v_lshl_add_u64 v[52:53], v[66:67], 0, v[52:53]
	global_store_dwordx4 v[52:53], v[32:35], off sc1
	v_bfe_u32 v36, v51, 16, 1
	v_add3_u32 v36, v51, v36, s29
	v_bfe_u32 v32, v41, 16, 1
	v_add3_u32 v32, v41, v32, s29
	v_bfe_u32 v33, v37, 16, 1
	v_lshrrev_b32_e32 v32, 16, v32
	v_add3_u32 v33, v37, v33, s29
	v_and_or_b32 v32, v33, s31, v32
	v_bfe_u32 v33, v39, 16, 1
	v_add3_u32 v33, v39, v33, s29
	v_bfe_u32 v34, v43, 16, 1
	v_lshrrev_b32_e32 v33, 16, v33
	v_add3_u32 v34, v43, v34, s29
	v_and_or_b32 v33, v34, s31, v33
	v_bfe_u32 v34, v45, 16, 1
	v_add3_u32 v34, v45, v34, s29
	v_bfe_u32 v35, v47, 16, 1
	v_lshrrev_b32_e32 v34, 16, v34
	v_add3_u32 v35, v47, v35, s29
	v_and_or_b32 v34, v35, s31, v34
	v_bfe_u32 v35, v49, 16, 1
	v_add3_u32 v35, v49, v35, s29
	v_lshrrev_b32_e32 v35, 16, v35
	v_and_or_b32 v35, v36, s31, v35
	v_lshlrev_b32_e32 v36, 12, v28
	v_mov_b32_e32 v37, v3
	v_lshl_add_u64 v[36:37], v[66:67], 0, v[36:37]
	global_store_dwordx4 v[36:37], v[32:35], off sc1
	s_waitcnt lgkmcnt(0)
; #define GAS __attribute__((address_space(1)))
; #define LAS __attribute__((address_space(3)))
; #define LDS_WAIT() asm volatile("s_waitcnt lgkmcnt(0)" ::: "memory")
; __device__ __forceinline__ unsigned pk2(float lo, float hi) { return f2bf(lo) | (f2bf(hi) << 16); }
; __device__ __forceinline__ void p0_transpose_item(const float* W, int N, int k0, int n0, bf16* WT, int K, int dst_row0, LAS float* scr, int lane, const float* kscale = nullptr, int permhalf = -1) {
;     typedef float f32x4t __attribute__((ext_vector_type(4)));
;     const int c = lane & 7;
;     float ks[8];
; #pragma unroll
;     for (int i = 0; i < 8; ++i) ks[i] = kscale ? kscale[k0 + 8 * c + i] : 1.0f;
; #pragma unroll
;     for (int i = 0; i < 8; ++i) { const int kk = 8 * i + (lane >> 3), nn = (lane & 7) * 4;
;         *(LAS f32x4t*)(scr + kk * 36 + nn) = *(const GAS f32x4t*)(W + (size_t)(k0 + kk) * N + n0 + nn); }
;     LDS_WAIT(); asm volatile("" ::: "memory");
; #pragma unroll
;     for (int j = 0; j < 4; ++j) { const int n = (lane >> 3) + 8 * j; const LAS float* s = scr + (8 * c) * 36 + n;
;         v4u o; o.x = pk2(s[0 * 36] * ks[0], s[1 * 36] * ks[1]); o.y = pk2(s[2 * 36] * ks[2], s[3 * 36] * ks[3]); o.z = pk2(s[4 * 36] * ks[4], s[5 * 36] * ks[5]); o.w = pk2(s[6 * 36] * ks[6], s[7 * 36] * ks[7]);
;         const int drow = permhalf < 0 ? n : (32 * (n >> 4) + 8 * ((n >> 2) & 3) + 4 * permhalf + (n & 3));
;         *(GAS v4u*)(WT + (size_t)(dst_row0 + drow) * K + k0 + 8 * c) = o; }
;     LDS_WAIT(); asm volatile("" ::: "memory");
; }
; __device__ __forceinline__ void p0_prologue(const Frame& F, KArgs a) {
;     ...
;         if (r < I_BA) { const int kb = r / 64, nb = r % 64; p0_transpose_item(a->in[11], 2048, 64 * kb, 32 * nb, (bf16*)(ws + WS_WA) + 1024, 2048, 32 * nb, scr, F.lane); continue; } r -= I_BA;
.LBB0_17:
	s_andn2_b64 vcc, exec, s[6:7]
	s_cbranch_vccnz .LBB0_19
	s_load_dwordx2 s[6:7], s[12:13], 0x58
	s_and_b32 s4, s39, 0x3fc0
	s_lshl_b32 s18, s18, 2
	s_addk_i32 s4, 0xda00
	v_or_b32_e32 v32, s4, v1
	s_waitcnt lgkmcnt(0)
	s_add_u32 s6, s6, s18
	s_addc_u32 s7, s7, 0
	v_mov_b32_e32 v33, v3
	v_lshl_add_u64 v[56:57], s[6:7], 0, v[2:3]
	v_lshlrev_b64 v[32:33], 13, v[32:33]
	v_lshl_add_u64 v[40:41], v[56:57], 0, v[32:33]
	v_or_b32_e32 v32, s4, v12
	v_mov_b32_e32 v33, v3
	v_lshlrev_b64 v[32:33], 13, v[32:33]
	v_lshl_add_u64 v[42:43], v[56:57], 0, v[32:33]
	global_load_dwordx4 v[32:35], v[40:41], off
	global_load_dwordx4 v[36:39], v[42:43], off
	v_or_b32_e32 v40, s4, v13
	v_mov_b32_e32 v41, v3
	v_lshlrev_b64 v[40:41], 13, v[40:41]
	v_lshl_add_u64 v[48:49], v[56:57], 0, v[40:41]
	v_or_b32_e32 v40, s4, v14
	v_mov_b32_e32 v41, v3
	v_lshlrev_b64 v[40:41], 13, v[40:41]
	v_lshl_add_u64 v[50:51], v[56:57], 0, v[40:41]
	global_load_dwordx4 v[40:43], v[48:49], off
	global_load_dwordx4 v[44:47], v[50:51], off
	v_or_b32_e32 v48, s4, v15
	v_mov_b32_e32 v49, v3
	v_lshlrev_b64 v[48:49], 13, v[48:49]
	v_lshl_add_u64 v[58:59], v[56:57], 0, v[48:49]
	v_or_b32_e32 v48, s4, v16
	v_mov_b32_e32 v49, v3
	v_lshlrev_b64 v[48:49], 13, v[48:49]
	v_lshl_add_u64 v[60:61], v[56:57], 0, v[48:49]
	global_load_dwordx4 v[48:51], v[58:59], off
	global_load_dwordx4 v[52:55], v[60:61], off
	v_or_b32_e32 v58, s4, v17
	v_mov_b32_e32 v59, v3
	v_lshlrev_b64 v[58:59], 13, v[58:59]
	v_lshl_add_u64 v[64:65], v[56:57], 0, v[58:59]
	v_or_b32_e32 v58, s4, v18
	v_mov_b32_e32 v59, v3
	v_lshlrev_b64 v[58:59], 13, v[58:59]
	v_lshl_add_u64 v[66:67], v[56:57], 0, v[58:59]
	global_load_dwordx4 v[56:59], v[64:65], off
	global_load_dwordx4 v[60:63], v[66:67], off
	v_lshlrev_b32_e32 v64, 12, v31
	v_mov_b32_e32 v65, v3
	v_lshl_add_u64 v[66:67], s[4:5], 1, v[6:7]
	v_lshl_add_u64 v[64:65], v[66:67], 0, v[64:65]
	v_lshlrev_b32_e32 v30, 12, v30
	v_lshlrev_b32_e32 v28, 12, v28
	s_waitcnt vmcnt(7)
	ds_write_b128 v25, v[32:35]
	s_waitcnt vmcnt(6)
	ds_write_b128 v25, v[36:39] offset:1152
	s_waitcnt vmcnt(5)
	ds_write_b128 v25, v[40:43] offset:2304
	s_waitcnt vmcnt(4)
	ds_write_b128 v25, v[44:47] offset:3456
	s_waitcnt vmcnt(3)
	ds_write_b128 v25, v[48:51] offset:4608
	s_waitcnt vmcnt(2)
	ds_write_b128 v25, v[52:55] offset:5760
	s_waitcnt vmcnt(1)
	ds_write_b128 v25, v[56:59] offset:6912
	s_waitcnt vmcnt(0)
	ds_write_b128 v25, v[60:63] offset:8064
	s_waitcnt lgkmcnt(0)
	ds_read2_b32 v[32:33], v19 offset0:36 offset1:44
	ds_read2_b32 v[34:35], v19 offset1:8
	ds_read2_b32 v[36:37], v19 offset0:72 offset1:80
	ds_read2_b32 v[38:39], v19 offset0:108 offset1:116
	ds_read2_b32 v[40:41], v19 offset0:144 offset1:152
	ds_read2_b32 v[42:43], v19 offset0:180 offset1:188
	ds_read2_b32 v[44:45], v19 offset0:216 offset1:224
	ds_read2_b32 v[46:47], v26 offset0:124 offset1:132
	s_waitcnt lgkmcnt(6)
	v_bfe_u32 v31, v34, 16, 1
	s_waitcnt lgkmcnt(5)
	v_bfe_u32 v49, v36, 16, 1
	s_waitcnt lgkmcnt(4)
	v_bfe_u32 v50, v38, 16, 1
	s_waitcnt lgkmcnt(3)
	v_bfe_u32 v51, v40, 16, 1
	s_waitcnt lgkmcnt(2)
	v_bfe_u32 v52, v42, 16, 1
	s_waitcnt lgkmcnt(1)
	v_bfe_u32 v53, v44, 16, 1
	v_bfe_u32 v48, v32, 16, 1
	s_waitcnt lgkmcnt(0)
	v_bfe_u32 v54, v46, 16, 1
	v_bfe_u32 v55, v35, 16, 1
	v_bfe_u32 v56, v33, 16, 1
	v_add3_u32 v31, v34, v31, s29
	v_add3_u32 v34, v36, v49, s29
	v_add3_u32 v36, v38, v50, s29
	v_add3_u32 v38, v40, v51, s29
	v_add3_u32 v40, v42, v52, s29
	v_add3_u32 v42, v44, v53, s29
	v_add3_u32 v32, v32, v48, s29
	v_add3_u32 v44, v46, v54, s29
	v_add3_u32 v35, v35, v55, s29
	v_add3_u32 v46, v33, v56, s29
	v_lshrrev_b32_e32 v31, 16, v31
	v_lshrrev_b32_e32 v33, 16, v34
	v_lshrrev_b32_e32 v34, 16, v38
	v_lshrrev_b32_e32 v38, 16, v42
	v_bfe_u32 v57, v37, 16, 1
	v_lshrrev_b32_e32 v42, 16, v35
	v_and_or_b32 v32, v32, s31, v31
	v_and_or_b32 v33, v36, s31, v33
	v_and_or_b32 v34, v40, s31, v34
	v_and_or_b32 v35, v44, s31, v38
	v_add3_u32 v37, v37, v57, s29
	global_store_dwordx4 v[64:65], v[32:35], off sc1
	v_lshrrev_b32_e32 v31, 16, v37
	v_and_or_b32 v36, v46, s31, v42
	v_bfe_u32 v32, v39, 16, 1
	v_add3_u32 v32, v39, v32, s29
	v_and_or_b32 v37, v32, s31, v31
	v_bfe_u32 v31, v41, 16, 1
	v_add3_u32 v31, v41, v31, s29
	v_bfe_u32 v32, v43, 16, 1
	v_lshrrev_b32_e32 v31, 16, v31
	v_add3_u32 v32, v43, v32, s29
	v_and_or_b32 v38, v32, s31, v31
	v_bfe_u32 v31, v45, 16, 1
	v_add3_u32 v31, v45, v31, s29
	v_bfe_u32 v32, v47, 16, 1
	v_lshrrev_b32_e32 v31, 16, v31
	v_add3_u32 v32, v47, v32, s29
	v_and_or_b32 v39, v32, s31, v31
	v_mov_b32_e32 v31, v3
	ds_read2_b32 v[34:35], v19 offset0:16 offset1:24
	v_lshl_add_u64 v[30:31], v[66:67], 0, v[30:31]
	global_store_dwordx4 v[30:31], v[36:39], off sc1
	ds_read2_b32 v[36:37], v19 offset0:52 offset1:60
	ds_read2_b32 v[38:39], v19 offset0:88 offset1:96
	ds_read2_b32 v[40:41], v19 offset0:124 offset1:132
	s_waitcnt lgkmcnt(3)
	v_bfe_u32 v30, v34, 16, 1
	v_add3_u32 v30, v34, v30, s29
	s_waitcnt lgkmcnt(2)
	v_bfe_u32 v31, v36, 16, 1
	ds_read2_b32 v[42:43], v19 offset0:160 offset1:168
	v_lshrrev_b32_e32 v30, 16, v30
	v_add3_u32 v31, v36, v31, s29
	ds_read2_b32 v[44:45], v19 offset0:196 offset1:204
	v_and_or_b32 v30, v31, s31, v30
	s_waitcnt lgkmcnt(3)
	v_bfe_u32 v31, v38, 16, 1
	v_add3_u32 v31, v38, v31, s29
	s_waitcnt lgkmcnt(2)
	v_bfe_u32 v32, v40, 16, 1
	ds_read2_b32 v[46:47], v19 offset0:232 offset1:240
	v_lshrrev_b32_e32 v31, 16, v31
	v_add3_u32 v32, v40, v32, s29
	ds_read2_b32 v[48:49], v27 offset0:12 offset1:20
	v_and_or_b32 v31, v32, s31, v31
	s_waitcnt lgkmcnt(3)
	v_bfe_u32 v32, v42, 16, 1
	v_add3_u32 v32, v42, v32, s29
	s_waitcnt lgkmcnt(2)
	v_bfe_u32 v33, v44, 16, 1
	v_lshrrev_b32_e32 v32, 16, v32
	v_add3_u32 v33, v44, v33, s29
	v_and_or_b32 v32, v33, s31, v32
	s_waitcnt lgkmcnt(1)
	v_bfe_u32 v33, v46, 16, 1
	v_add3_u32 v33, v46, v33, s29
	s_waitcnt lgkmcnt(0)
	v_bfe_u32 v34, v48, 16, 1
	v_lshrrev_b32_e32 v33, 16, v33
	v_add3_u32 v34, v48, v34, s29
	v_lshlrev_b32_e32 v50, 12, v29
	v_mov_b32_e32 v51, v3
	v_and_or_b32 v33, v34, s31, v33
	v_lshl_add_u64 v[50:51], v[66:67], 0, v[50:51]
	v_bfe_u32 v29, v35, 16, 1
	global_store_dwordx4 v[50:51], v[30:33], off sc1
	v_add3_u32 v29, v35, v29, s29
	v_lshrrev_b32_e32 v29, 16, v29
	v_bfe_u32 v30, v37, 16, 1
	v_add3_u32 v30, v37, v30, s29
	v_and_or_b32 v30, v30, s31, v29
	v_bfe_u32 v29, v39, 16, 1
	v_add3_u32 v29, v39, v29, s29
	v_bfe_u32 v31, v41, 16, 1
	v_lshrrev_b32_e32 v29, 16, v29
	v_add3_u32 v31, v41, v31, s29
	v_and_or_b32 v31, v31, s31, v29
	v_bfe_u32 v29, v43, 16, 1
	v_add3_u32 v29, v43, v29, s29
	v_bfe_u32 v32, v45, 16, 1
	v_lshrrev_b32_e32 v29, 16, v29
	v_add3_u32 v32, v45, v32, s29
	v_and_or_b32 v32, v32, s31, v29
	v_bfe_u32 v29, v47, 16, 1
	v_add3_u32 v29, v47, v29, s29
	v_bfe_u32 v33, v49, 16, 1
	v_lshrrev_b32_e32 v29, 16, v29
	v_add3_u32 v33, v49, v33, s29
	v_and_or_b32 v33, v33, s31, v29
	v_mov_b32_e32 v29, v3
	v_lshl_add_u64 v[28:29], v[66:67], 0, v[28:29]
	global_store_dwordx4 v[28:29], v[30:33], off sc1
	s_waitcnt lgkmcnt(0)

; #define GAS __attribute__((address_space(1)))
; #define LAS __attribute__((address_space(3)))
; #define LDS_WAIT() asm volatile("s_waitcnt lgkmcnt(0)" ::: "memory")
; __device__ __forceinline__ unsigned pk2(float lo, float hi) { return f2bf(lo) | (f2bf(hi) << 16); }
; __device__ __forceinline__ void p0_transpose_item(const float* W, int N, int k0, int n0, bf16* WT, int K, int dst_row0, LAS float* scr, int lane, const float* kscale = nullptr, int permhalf = -1) {
;     typedef float f32x4t __attribute__((ext_vector_type(4)));
;     const int c = lane & 7;
;     float ks[8];
; #pragma unroll
;     for (int i = 0; i < 8; ++i) ks[i] = kscale ? kscale[k0 + 8 * c + i] : 1.0f;
; #pragma unroll
;     for (int i = 0; i < 8; ++i) { const int kk = 8 * i + (lane >> 3), nn = (lane & 7) * 4;
;         *(LAS f32x4t*)(scr + kk * 36 + nn) = *(const GAS f32x4t*)(W + (size_t)(k0 + kk) * N + n0 + nn); }
;     LDS_WAIT(); asm volatile("" ::: "memory");
; #pragma unroll
;     for (int j = 0; j < 4; ++j) { const int n = (lane >> 3) + 8 * j; const LAS float* s = scr + (8 * c) * 36 + n;
;         v4u o; o.x = pk2(s[0 * 36] * ks[0], s[1 * 36] * ks[1]); o.y = pk2(s[2 * 36] * ks[2], s[3 * 36] * ks[3]); o.z = pk2(s[4 * 36] * ks[4], s[5 * 36] * ks[5]); o.w = pk2(s[6 * 36] * ks[6], s[7 * 36] * ks[7]);
;         const int drow = permhalf < 0 ? n : (32 * (n >> 4) + 8 * ((n >> 2) & 3) + 4 * permhalf + (n & 3));
;         *(GAS v4u*)(WT + (size_t)(dst_row0 + drow) * K + k0 + 8 * c) = o; }
;     LDS_WAIT(); asm volatile("" ::: "memory");
; }
; __device__ __forceinline__ void p0_prologue(const Frame& F, KArgs a) {
;     ...
;         if (r < I_BA) { const int kb = r / 64, nb = r % 64; p0_transpose_item(a->in[10], 2048, 64 * kb, 32 * nb, (bf16*)(ws + WS_WA), 2048, 32 * nb, scr, F.lane); continue; } r -= I_BA;
.LBB0_20:
	s_andn2_b64 vcc, exec, s[6:7]
	s_cbranch_vccnz .LBB0_22
	s_load_dwordx2 s[18:19], s[12:13], 0x50
	s_and_b32 s4, s39, 0x3fc0
	s_and_b32 s6, s3, 0x7e0
	s_addk_i32 s4, 0xde00
	s_lshl_b32 s7, s6, 2
	s_waitcnt lgkmcnt(0)
	s_add_u32 s18, s18, s7
	s_addc_u32 s19, s19, 0
	v_or_b32_e32 v28, s4, v1
	v_mov_b32_e32 v29, v3
	v_lshl_add_u64 v[52:53], s[18:19], 0, v[2:3]
	v_lshlrev_b64 v[28:29], 13, v[28:29]
	v_lshl_add_u64 v[36:37], v[52:53], 0, v[28:29]
	v_or_b32_e32 v28, s4, v12
	v_mov_b32_e32 v29, v3
	v_lshlrev_b64 v[28:29], 13, v[28:29]
	v_lshl_add_u64 v[38:39], v[52:53], 0, v[28:29]
	global_load_dwordx4 v[28:31], v[36:37], off
	global_load_dwordx4 v[32:35], v[38:39], off
	v_or_b32_e32 v36, s4, v13
	v_mov_b32_e32 v37, v3
	v_lshlrev_b64 v[36:37], 13, v[36:37]
	v_lshl_add_u64 v[44:45], v[52:53], 0, v[36:37]
	v_or_b32_e32 v36, s4, v14
	v_mov_b32_e32 v37, v3
	v_lshlrev_b64 v[36:37], 13, v[36:37]
	v_lshl_add_u64 v[46:47], v[52:53], 0, v[36:37]
	global_load_dwordx4 v[36:39], v[44:45], off
	global_load_dwordx4 v[40:43], v[46:47], off
	v_or_b32_e32 v44, s4, v15
	v_mov_b32_e32 v45, v3
	v_lshlrev_b64 v[44:45], 13, v[44:45]
	v_lshl_add_u64 v[54:55], v[52:53], 0, v[44:45]
	v_or_b32_e32 v44, s4, v16
	v_mov_b32_e32 v45, v3
	v_lshlrev_b64 v[44:45], 13, v[44:45]
	v_lshl_add_u64 v[56:57], v[52:53], 0, v[44:45]
	global_load_dwordx4 v[44:47], v[54:55], off
	global_load_dwordx4 v[48:51], v[56:57], off
	v_or_b32_e32 v54, s4, v17
	v_mov_b32_e32 v55, v3
	v_lshlrev_b64 v[54:55], 13, v[54:55]
	v_lshl_add_u64 v[60:61], v[52:53], 0, v[54:55]
	v_or_b32_e32 v54, s4, v18
	v_mov_b32_e32 v55, v3
	v_lshlrev_b64 v[54:55], 13, v[54:55]
	v_lshl_add_u64 v[62:63], v[52:53], 0, v[54:55]
	global_load_dwordx4 v[52:55], v[60:61], off
	global_load_dwordx4 v[56:59], v[62:63], off
	v_or_b32_e32 v60, s6, v1
	v_mov_b32_e32 v61, v3
	v_lshl_add_u64 v[62:63], s[4:5], 1, v[8:9]
	v_lshlrev_b32_e32 v60, 12, v60
	v_lshl_add_u64 v[60:61], v[62:63], 0, v[60:61]
	s_waitcnt vmcnt(7)
	ds_write_b128 v25, v[28:31]
	s_waitcnt vmcnt(6)
	ds_write_b128 v25, v[32:35] offset:1152
	s_waitcnt vmcnt(5)
	ds_write_b128 v25, v[36:39] offset:2304
	s_waitcnt vmcnt(4)
	ds_write_b128 v25, v[40:43] offset:3456
	s_waitcnt vmcnt(3)
	ds_write_b128 v25, v[44:47] offset:4608
	s_waitcnt vmcnt(2)
	ds_write_b128 v25, v[48:51] offset:5760
	s_waitcnt vmcnt(1)
	ds_write_b128 v25, v[52:55] offset:6912
	s_waitcnt vmcnt(0)
	ds_write_b128 v25, v[56:59] offset:8064
	s_waitcnt lgkmcnt(0)
	ds_read2_b32 v[28:29], v19 offset0:36 offset1:44
	ds_read2_b32 v[30:31], v19 offset1:8
	ds_read2_b32 v[32:33], v19 offset0:72 offset1:80
	ds_read2_b32 v[34:35], v19 offset0:108 offset1:116
	ds_read2_b32 v[36:37], v19 offset0:144 offset1:152
	ds_read2_b32 v[38:39], v19 offset0:180 offset1:188
	ds_read2_b32 v[40:41], v19 offset0:216 offset1:224
	ds_read2_b32 v[42:43], v26 offset0:124 offset1:132
	s_waitcnt lgkmcnt(6)
	v_bfe_u32 v44, v30, 16, 1
	s_waitcnt lgkmcnt(5)
	v_bfe_u32 v46, v32, 16, 1
	s_waitcnt lgkmcnt(3)
	v_bfe_u32 v48, v36, 16, 1
	s_waitcnt lgkmcnt(1)
	v_bfe_u32 v50, v40, 16, 1
	v_bfe_u32 v45, v28, 16, 1
	v_bfe_u32 v47, v34, 16, 1
	v_bfe_u32 v49, v38, 16, 1
	s_waitcnt lgkmcnt(0)
	v_bfe_u32 v51, v42, 16, 1
	v_bfe_u32 v52, v31, 16, 1
	v_bfe_u32 v53, v29, 16, 1
	v_add3_u32 v30, v30, v44, s29
	v_add3_u32 v32, v32, v46, s29
	v_add3_u32 v36, v36, v48, s29
	v_add3_u32 v40, v40, v50, s29
	v_add3_u32 v28, v28, v45, s29
	v_add3_u32 v34, v34, v47, s29
	v_add3_u32 v38, v38, v49, s29
	v_add3_u32 v42, v42, v51, s29
	v_add3_u32 v31, v31, v52, s29
	v_add3_u32 v44, v29, v53, s29
	v_lshrrev_b32_e32 v29, 16, v30
	v_lshrrev_b32_e32 v30, 16, v32
	v_lshrrev_b32_e32 v32, 16, v36
	v_lshrrev_b32_e32 v36, 16, v40
	v_lshrrev_b32_e32 v40, 16, v31
	v_and_or_b32 v28, v28, s31, v29
	v_and_or_b32 v29, v34, s31, v30
	v_and_or_b32 v30, v38, s31, v32
	v_and_or_b32 v31, v42, s31, v36
	global_store_dwordx4 v[60:61], v[28:31], off sc1
	v_and_or_b32 v32, v44, s31, v40
	ds_read2_b32 v[44:45], v19 offset0:232 offset1:240
	v_bfe_u32 v28, v33, 16, 1
	v_add3_u32 v28, v33, v28, s29
	v_bfe_u32 v29, v35, 16, 1
	v_lshrrev_b32_e32 v28, 16, v28
	v_add3_u32 v29, v35, v29, s29
	v_and_or_b32 v33, v29, s31, v28
	v_bfe_u32 v28, v37, 16, 1
	v_add3_u32 v28, v37, v28, s29
	v_bfe_u32 v29, v39, 16, 1
	v_lshrrev_b32_e32 v28, 16, v28
	v_add3_u32 v29, v39, v29, s29
	v_and_or_b32 v34, v29, s31, v28
	v_bfe_u32 v28, v41, 16, 1
	v_add3_u32 v28, v41, v28, s29
	v_bfe_u32 v29, v43, 16, 1
	v_lshrrev_b32_e32 v28, 16, v28
	v_add3_u32 v29, v43, v29, s29
	v_and_or_b32 v35, v29, s31, v28
	v_or_b32_e32 v28, s6, v12
	v_lshlrev_b32_e32 v28, 12, v28
	v_mov_b32_e32 v29, v3
	ds_read2_b32 v[36:37], v19 offset0:16 offset1:24
	v_lshl_add_u64 v[28:29], v[62:63], 0, v[28:29]
	global_store_dwordx4 v[28:29], v[32:35], off sc1
	ds_read2_b32 v[32:33], v19 offset0:52 offset1:60
	ds_read2_b32 v[34:35], v19 offset0:88 offset1:96
	ds_read2_b32 v[38:39], v19 offset0:124 offset1:132
	s_waitcnt lgkmcnt(3)
	v_bfe_u32 v28, v36, 16, 1
	v_add3_u32 v28, v36, v28, s29
	s_waitcnt lgkmcnt(2)
	v_bfe_u32 v29, v32, 16, 1
	ds_read2_b32 v[40:41], v19 offset0:160 offset1:168
	v_lshrrev_b32_e32 v28, 16, v28
	v_add3_u32 v29, v32, v29, s29
	ds_read2_b32 v[42:43], v19 offset0:196 offset1:204
	v_and_or_b32 v28, v29, s31, v28
	s_waitcnt lgkmcnt(3)
	v_bfe_u32 v29, v34, 16, 1
	v_add3_u32 v29, v34, v29, s29
	s_waitcnt lgkmcnt(2)
	v_bfe_u32 v30, v38, 16, 1
	v_lshrrev_b32_e32 v29, 16, v29
	v_add3_u32 v30, v38, v30, s29
	ds_read2_b32 v[46:47], v27 offset0:12 offset1:20
	v_and_or_b32 v29, v30, s31, v29
	s_waitcnt lgkmcnt(2)
	v_bfe_u32 v30, v40, 16, 1
	v_add3_u32 v30, v40, v30, s29
	s_waitcnt lgkmcnt(1)
	v_bfe_u32 v31, v42, 16, 1
	v_lshrrev_b32_e32 v30, 16, v30
	v_add3_u32 v31, v42, v31, s29
	v_and_or_b32 v30, v31, s31, v30
	v_bfe_u32 v31, v44, 16, 1
	v_add3_u32 v31, v44, v31, s29
	s_waitcnt lgkmcnt(0)
	v_bfe_u32 v32, v46, 16, 1
	v_lshrrev_b32_e32 v31, 16, v31
	v_add3_u32 v32, v46, v32, s29
	v_and_or_b32 v31, v32, s31, v31
	v_or_b32_e32 v32, s6, v13
	v_lshlrev_b32_e32 v48, 12, v32
	v_mov_b32_e32 v49, v3
	v_lshl_add_u64 v[48:49], v[62:63], 0, v[48:49]
	global_store_dwordx4 v[48:49], v[28:31], off sc1
	v_bfe_u32 v32, v47, 16, 1
	v_add3_u32 v32, v47, v32, s29
	v_bfe_u32 v28, v37, 16, 1
	v_add3_u32 v28, v37, v28, s29
	v_bfe_u32 v29, v33, 16, 1
	v_lshrrev_b32_e32 v28, 16, v28
	v_add3_u32 v29, v33, v29, s29
	v_and_or_b32 v28, v29, s31, v28
	v_bfe_u32 v29, v35, 16, 1
	v_add3_u32 v29, v35, v29, s29
	v_bfe_u32 v30, v39, 16, 1
	v_lshrrev_b32_e32 v29, 16, v29
	v_add3_u32 v30, v39, v30, s29
	v_and_or_b32 v29, v30, s31, v29
	v_bfe_u32 v30, v41, 16, 1
	v_add3_u32 v30, v41, v30, s29
	v_bfe_u32 v31, v43, 16, 1
	v_lshrrev_b32_e32 v30, 16, v30
	v_add3_u32 v31, v43, v31, s29
	v_and_or_b32 v30, v31, s31, v30
	v_bfe_u32 v31, v45, 16, 1
	v_add3_u32 v31, v45, v31, s29
	v_lshrrev_b32_e32 v31, 16, v31
	v_and_or_b32 v31, v32, s31, v31
	v_or_b32_e32 v32, s6, v14
	v_lshlrev_b32_e32 v32, 12, v32
	v_mov_b32_e32 v33, v3
	v_lshl_add_u64 v[32:33], v[62:63], 0, v[32:33]
	global_store_dwordx4 v[32:33], v[28:31], off sc1
	s_waitcnt lgkmcnt(0)

; #define GAS __attribute__((address_space(1)))
; #define LAS __attribute__((address_space(3)))
; #define LDS_WAIT() asm volatile("s_waitcnt lgkmcnt(0)" ::: "memory")
; __device__ __forceinline__ unsigned pk2(float lo, float hi) { return f2bf(lo) | (f2bf(hi) << 16); }
; __device__ __forceinline__ void p0_transpose_item(const float* W, int N, int k0, int n0, bf16* WT, int K, int dst_row0, LAS float* scr, int lane, const float* kscale = nullptr, int permhalf = -1) {
;     typedef float f32x4t __attribute__((ext_vector_type(4)));
;     const int c = lane & 7;
;     float ks[8];
; #pragma unroll
;     for (int i = 0; i < 8; ++i) ks[i] = kscale ? kscale[k0 + 8 * c + i] : 1.0f;
; #pragma unroll
;     for (int i = 0; i < 8; ++i) { const int kk = 8 * i + (lane >> 3), nn = (lane & 7) * 4;
;         *(LAS f32x4t*)(scr + kk * 36 + nn) = *(const GAS f32x4t*)(W + (size_t)(k0 + kk) * N + n0 + nn); }
;     LDS_WAIT(); asm volatile("" ::: "memory");
; #pragma unroll
;     for (int j = 0; j < 4; ++j) { const int n = (lane >> 3) + 8 * j; const LAS float* s = scr + (8 * c) * 36 + n;
;         v4u o; o.x = pk2(s[0 * 36] * ks[0], s[1 * 36] * ks[1]); o.y = pk2(s[2 * 36] * ks[2], s[3 * 36] * ks[3]); o.z = pk2(s[4 * 36] * ks[4], s[5 * 36] * ks[5]); o.w = pk2(s[6 * 36] * ks[6], s[7 * 36] * ks[7]);
;         const int drow = permhalf < 0 ? n : (32 * (n >> 4) + 8 * ((n >> 2) & 3) + 4 * permhalf + (n & 3));
;         *(GAS v4u*)(WT + (size_t)(dst_row0 + drow) * K + k0 + 8 * c) = o; }
; __device__ __forceinline__ void p0_prologue(const Frame& F, KArgs a) {
;     ...
;                         p0_transpose_item(a->in[12], 4096, 64 * kb, n0, (bf16*)(ws + WS_WIN), 2048, 4608 + 256 * ((n0 & 2047) >> 7) + 128 * (n0 >> 11) + (n0 & 127), scr, F.lane); continue; } r -= I_GT;
.LBB0_23:
	s_andn2_b64 vcc, exec, s[6:7]
	s_cbranch_vccnz .LBB0_25
	s_load_dwordx2 s[18:19], s[12:13], 0x60
	s_and_b32 s6, s24, 0xf00
	s_and_b32 s36, s26, 0x80
	s_add_i32 s4, s39, 0xffffee00
	s_or_b32 s6, s6, s36
	s_and_b32 s36, s3, 0x60
	s_and_b32 s7, s3, 0xfe0
	s_lshr_b32 s4, s4, 1
	s_or_b32 s6, s6, s36
	s_and_b32 s4, s4, 0x7fffffc0
	s_addk_i32 s6, 0x1200
	s_lshl_b32 s7, s7, 2
	s_waitcnt lgkmcnt(0)
	s_add_u32 s18, s18, s7
	s_addc_u32 s19, s19, 0
	v_or_b32_e32 v28, s4, v1
	v_mov_b32_e32 v29, v3
	v_lshl_add_u64 v[52:53], s[18:19], 0, v[2:3]
	v_lshlrev_b64 v[28:29], 14, v[28:29]
	v_lshl_add_u64 v[36:37], v[52:53], 0, v[28:29]
	v_or_b32_e32 v28, s4, v12
	v_mov_b32_e32 v29, v3
	v_lshlrev_b64 v[28:29], 14, v[28:29]
	v_lshl_add_u64 v[38:39], v[52:53], 0, v[28:29]
	global_load_dwordx4 v[28:31], v[36:37], off
	global_load_dwordx4 v[32:35], v[38:39], off
	v_or_b32_e32 v36, s4, v13
	v_mov_b32_e32 v37, v3
	v_lshlrev_b64 v[36:37], 14, v[36:37]
	v_lshl_add_u64 v[44:45], v[52:53], 0, v[36:37]
	v_or_b32_e32 v36, s4, v14
	v_mov_b32_e32 v37, v3
	v_lshlrev_b64 v[36:37], 14, v[36:37]
	v_lshl_add_u64 v[46:47], v[52:53], 0, v[36:37]
	global_load_dwordx4 v[36:39], v[44:45], off
	global_load_dwordx4 v[40:43], v[46:47], off
	v_or_b32_e32 v44, s4, v15
	v_mov_b32_e32 v45, v3
	v_lshlrev_b64 v[44:45], 14, v[44:45]
	v_lshl_add_u64 v[54:55], v[52:53], 0, v[44:45]
	v_or_b32_e32 v44, s4, v16
	v_mov_b32_e32 v45, v3
	v_lshlrev_b64 v[44:45], 14, v[44:45]
	v_lshl_add_u64 v[56:57], v[52:53], 0, v[44:45]
	global_load_dwordx4 v[44:47], v[54:55], off
	global_load_dwordx4 v[48:51], v[56:57], off
	v_or_b32_e32 v54, s4, v17
	v_mov_b32_e32 v55, v3
	v_lshlrev_b64 v[54:55], 14, v[54:55]
	v_lshl_add_u64 v[60:61], v[52:53], 0, v[54:55]
	v_or_b32_e32 v54, s4, v18
	v_mov_b32_e32 v55, v3
	v_lshlrev_b64 v[54:55], 14, v[54:55]
	v_lshl_add_u64 v[62:63], v[52:53], 0, v[54:55]
	global_load_dwordx4 v[52:55], v[60:61], off
	global_load_dwordx4 v[56:59], v[62:63], off
	v_or_b32_e32 v60, s6, v1
	s_lshl_b32 s4, s4, 1
	v_lshlrev_b32_e32 v60, 12, v60
	v_lshl_add_u64 v[62:63], v[10:11], 0, s[4:5]
	v_mov_b32_e32 v61, v3
	s_waitcnt vmcnt(7)
	ds_write_b128 v25, v[28:31]
	s_waitcnt vmcnt(6)
	ds_write_b128 v25, v[32:35] offset:1152
	s_waitcnt vmcnt(5)
	ds_write_b128 v25, v[36:39] offset:2304
	s_waitcnt vmcnt(4)
	ds_write_b128 v25, v[40:43] offset:3456
	s_waitcnt vmcnt(3)
	ds_write_b128 v25, v[44:47] offset:4608
	s_waitcnt vmcnt(2)
	ds_write_b128 v25, v[48:51] offset:5760
	s_waitcnt vmcnt(1)
	ds_write_b128 v25, v[52:55] offset:6912
	s_waitcnt vmcnt(0)
	ds_write_b128 v25, v[56:59] offset:8064
	s_waitcnt lgkmcnt(0)
	ds_read2_b32 v[32:33], v19 offset0:36 offset1:44
	ds_read2_b32 v[34:35], v19 offset1:8
	ds_read2_b32 v[36:37], v19 offset0:72 offset1:80
	ds_read2_b32 v[38:39], v19 offset0:108 offset1:116
	ds_read2_b32 v[40:41], v19 offset0:144 offset1:152
	ds_read2_b32 v[42:43], v19 offset0:180 offset1:188
	ds_read2_b32 v[44:45], v19 offset0:216 offset1:224
	ds_read2_b32 v[46:47], v26 offset0:124 offset1:132
	s_waitcnt lgkmcnt(6)
	v_bfe_u32 v28, v34, 16, 1
	v_bfe_u32 v29, v32, 16, 1
	s_waitcnt lgkmcnt(5)
	v_bfe_u32 v30, v36, 16, 1
	s_waitcnt lgkmcnt(3)
	v_bfe_u32 v48, v40, 16, 1
	s_waitcnt lgkmcnt(1)
	v_bfe_u32 v50, v44, 16, 1
	v_bfe_u32 v31, v38, 16, 1
	v_bfe_u32 v49, v42, 16, 1
	s_waitcnt lgkmcnt(0)
; #define GAS __attribute__((address_space(1)))
; #define LAS __attribute__((address_space(3)))
; __device__ __forceinline__ unsigned pk2(float lo, float hi) { return f2bf(lo) | (f2bf(hi) << 16); }
; __device__ __forceinline__ void p0_transpose_item(const float* W, int N, int k0, int n0, bf16* WT, int K, int dst_row0, LAS float* scr, int lane, const float* kscale = nullptr, int permhalf = -1) {
;     ...
;     for (int j = 0; j < 4; ++j) { const int n = (lane >> 3) + 8 * j; const LAS float* s = scr + (8 * c) * 36 + n;
;         v4u o; o.x = pk2(s[0 * 36] * ks[0], s[1 * 36] * ks[1]); o.y = pk2(s[2 * 36] * ks[2], s[3 * 36] * ks[3]); o.z = pk2(s[4 * 36] * ks[4], s[5 * 36] * ks[5]); o.w = pk2(s[6 * 36] * ks[6], s[7 * 36] * ks[7]);
;         const int drow = permhalf < 0 ? n : (32 * (n >> 4) + 8 * ((n >> 2) & 3) + 4 * permhalf + (n & 3));
;         *(GAS v4u*)(WT + (size_t)(dst_row0 + drow) * K + k0 + 8 * c) = o; }
	v_bfe_u32 v51, v46, 16, 1
	v_add3_u32 v28, v34, v28, s29
	v_add3_u32 v29, v32, v29, s29
	v_add3_u32 v30, v36, v30, s29
	v_add3_u32 v32, v40, v48, s29
	v_add3_u32 v36, v44, v50, s29
	v_add3_u32 v31, v38, v31, s29
	v_add3_u32 v34, v42, v49, s29
	v_add3_u32 v38, v46, v51, s29
	v_lshrrev_b32_e32 v28, 16, v28
	v_lshrrev_b32_e32 v30, 16, v30
	v_lshrrev_b32_e32 v32, 16, v32
	v_lshrrev_b32_e32 v36, 16, v36
	v_and_or_b32 v28, v29, s31, v28
	v_and_or_b32 v29, v31, s31, v30
	v_and_or_b32 v30, v34, s31, v32
	v_and_or_b32 v31, v38, s31, v36
	v_lshl_add_u64 v[48:49], v[62:63], 0, v[60:61]
	global_store_dwordx4 v[48:49], v[28:31], off sc1
	v_bfe_u32 v32, v47, 16, 1
	v_add3_u32 v32, v47, v32, s29
	v_bfe_u32 v28, v35, 16, 1
	v_add3_u32 v28, v35, v28, s29
	v_bfe_u32 v29, v33, 16, 1
	v_lshrrev_b32_e32 v28, 16, v28
	v_add3_u32 v29, v33, v29, s29
	v_and_or_b32 v28, v29, s31, v28
	v_bfe_u32 v29, v37, 16, 1
	v_add3_u32 v29, v37, v29, s29
	v_bfe_u32 v30, v39, 16, 1
	v_lshrrev_b32_e32 v29, 16, v29
	v_add3_u32 v30, v39, v30, s29
	v_and_or_b32 v29, v30, s31, v29
	v_bfe_u32 v30, v41, 16, 1
	v_add3_u32 v30, v41, v30, s29
	v_bfe_u32 v31, v43, 16, 1
	v_lshrrev_b32_e32 v30, 16, v30
	v_add3_u32 v31, v43, v31, s29
	v_and_or_b32 v30, v31, s31, v30
	v_bfe_u32 v31, v45, 16, 1
	v_add3_u32 v31, v45, v31, s29
	v_lshrrev_b32_e32 v31, 16, v31
	v_and_or_b32 v31, v32, s31, v31
	v_or_b32_e32 v32, s6, v12
	v_lshlrev_b32_e32 v32, 12, v32
	v_mov_b32_e32 v33, v3
	ds_read2_b32 v[34:35], v19 offset0:16 offset1:24
	v_lshl_add_u64 v[32:33], v[62:63], 0, v[32:33]
	global_store_dwordx4 v[32:33], v[28:31], off sc1
	ds_read2_b32 v[32:33], v19 offset0:52 offset1:60
	ds_read2_b32 v[36:37], v19 offset0:88 offset1:96
	ds_read2_b32 v[38:39], v19 offset0:124 offset1:132
	s_waitcnt lgkmcnt(3)
	v_bfe_u32 v28, v34, 16, 1
	v_add3_u32 v28, v34, v28, s29
	s_waitcnt lgkmcnt(2)
	v_bfe_u32 v29, v32, 16, 1
	ds_read2_b32 v[40:41], v19 offset0:160 offset1:168
	v_lshrrev_b32_e32 v28, 16, v28
	v_add3_u32 v29, v32, v29, s29
	ds_read2_b32 v[42:43], v19 offset0:196 offset1:204
	v_and_or_b32 v28, v29, s31, v28
	s_waitcnt lgkmcnt(3)
	v_bfe_u32 v29, v36, 16, 1
	v_add3_u32 v29, v36, v29, s29
	s_waitcnt lgkmcnt(2)
	v_bfe_u32 v30, v38, 16, 1
	ds_read2_b32 v[44:45], v19 offset0:232 offset1:240
	v_lshrrev_b32_e32 v29, 16, v29
	v_add3_u32 v30, v38, v30, s29
	ds_read2_b32 v[46:47], v27 offset0:12 offset1:20
	v_and_or_b32 v29, v30, s31, v29
	s_waitcnt lgkmcnt(3)
	v_bfe_u32 v30, v40, 16, 1
	v_add3_u32 v30, v40, v30, s29
	s_waitcnt lgkmcnt(2)
	v_bfe_u32 v31, v42, 16, 1
	v_lshrrev_b32_e32 v30, 16, v30
	v_add3_u32 v31, v42, v31, s29
	v_and_or_b32 v30, v31, s31, v30
	s_waitcnt lgkmcnt(1)
	v_bfe_u32 v31, v44, 16, 1
	v_add3_u32 v31, v44, v31, s29
	s_waitcnt lgkmcnt(0)
	v_bfe_u32 v32, v46, 16, 1
	v_lshrrev_b32_e32 v31, 16, v31
	v_add3_u32 v32, v46, v32, s29
	v_and_or_b32 v31, v32, s31, v31
	v_or_b32_e32 v32, s6, v13
	v_lshlrev_b32_e32 v48, 12, v32
	v_mov_b32_e32 v49, v3
	v_lshl_add_u64 v[48:49], v[62:63], 0, v[48:49]
	global_store_dwordx4 v[48:49], v[28:31], off sc1
	v_bfe_u32 v32, v47, 16, 1
	v_add3_u32 v32, v47, v32, s29
	v_bfe_u32 v28, v35, 16, 1
	v_add3_u32 v28, v35, v28, s29
	v_bfe_u32 v29, v33, 16, 1
	v_lshrrev_b32_e32 v28, 16, v28
	v_add3_u32 v29, v33, v29, s29
	v_and_or_b32 v28, v29, s31, v28
	v_bfe_u32 v29, v37, 16, 1
	v_add3_u32 v29, v37, v29, s29
	v_bfe_u32 v30, v39, 16, 1
	v_lshrrev_b32_e32 v29, 16, v29
	v_add3_u32 v30, v39, v30, s29
	v_and_or_b32 v29, v30, s31, v29
	v_bfe_u32 v30, v41, 16, 1
	v_add3_u32 v30, v41, v30, s29
	v_bfe_u32 v31, v43, 16, 1
	v_lshrrev_b32_e32 v30, 16, v30
	v_add3_u32 v31, v43, v31, s29
	v_and_or_b32 v30, v31, s31, v30
	v_bfe_u32 v31, v45, 16, 1
	v_add3_u32 v31, v45, v31, s29
	v_lshrrev_b32_e32 v31, 16, v31
	v_and_or_b32 v31, v32, s31, v31
	v_or_b32_e32 v32, s6, v14
	v_lshlrev_b32_e32 v32, 12, v32
	v_mov_b32_e32 v33, v3
	v_lshl_add_u64 v[32:33], v[62:63], 0, v[32:33]
	global_store_dwordx4 v[32:33], v[28:31], off sc1
	s_waitcnt lgkmcnt(0)

; #define GAS __attribute__((address_space(1)))
; #define LAS __attribute__((address_space(3)))
; #define LDS_WAIT() asm volatile("s_waitcnt lgkmcnt(0)" ::: "memory")
; __device__ __forceinline__ unsigned pk2(float lo, float hi) { return f2bf(lo) | (f2bf(hi) << 16); }
; __device__ __forceinline__ void p0_transpose_item(const float* W, int N, int k0, int n0, bf16* WT, int K, int dst_row0, LAS float* scr, int lane, const float* kscale = nullptr, int permhalf = -1) {
;     typedef float f32x4t __attribute__((ext_vector_type(4)));
;     const int c = lane & 7;
;     float ks[8];
; #pragma unroll
;     for (int i = 0; i < 8; ++i) ks[i] = kscale ? kscale[k0 + 8 * c + i] : 1.0f;
; #pragma unroll
;     for (int i = 0; i < 8; ++i) { const int kk = 8 * i + (lane >> 3), nn = (lane & 7) * 4;
;         *(LAS f32x4t*)(scr + kk * 36 + nn) = *(const GAS f32x4t*)(W + (size_t)(k0 + kk) * N + n0 + nn); }
;     LDS_WAIT(); asm volatile("" ::: "memory");
; #pragma unroll
;     for (int j = 0; j < 4; ++j) { const int n = (lane >> 3) + 8 * j; const LAS float* s = scr + (8 * c) * 36 + n;
;         v4u o; o.x = pk2(s[0 * 36] * ks[0], s[1 * 36] * ks[1]); o.y = pk2(s[2 * 36] * ks[2], s[3 * 36] * ks[3]); o.z = pk2(s[4 * 36] * ks[4], s[5 * 36] * ks[5]); o.w = pk2(s[6 * 36] * ks[6], s[7 * 36] * ks[7]);
;         const int drow = permhalf < 0 ? n : (32 * (n >> 4) + 8 * ((n >> 2) & 3) + 4 * permhalf + (n & 3));
;         *(GAS v4u*)(WT + (size_t)(dst_row0 + drow) * K + k0 + 8 * c) = o; }
; __device__ __forceinline__ void p0_prologue(const Frame& F, KArgs a) {
;     ...
;         if (r < I_IN) { const int kb = r / 144, nb = r % 144, n0 = 32 * nb; const bool pb = n0 >= 1536 && n0 < 3584;
;                         p0_transpose_item(a->in[2], 4608, 64 * kb, n0, (bf16*)(ws + WS_WIN), 2048, pb ? (n0 & ~63) : n0, scr, F.lane, nullptr, pb ? ((n0 >> 5) & 1) : -1); continue; } r -= I_IN;
.LBB0_26:
	s_andn2_b64 vcc, exec, s[6:7]
	s_cbranch_vccnz .LBB0_11
	s_mul_hi_i32 s4, s39, 0x38e38e39
	s_lshr_b32 s6, s4, 31
	s_ashr_i32 s4, s4, 5
	s_add_i32 s4, s4, s6
	s_load_dwordx2 s[18:19], s[12:13], 0x10
	s_mul_i32 s6, s4, 0xffffee00
	s_mul_i32 s7, s4, 0xffffff70
	s_add_i32 s6, s3, s6
	s_add_i32 s7, s39, s7
	s_add_i32 s42, s7, 0xffffff90
	s_ashr_i32 s7, s6, 31
	s_lshl_b32 s36, s4, 6
	s_and_b32 s4, s6, 0xffffffc0
	s_lshl_b64 s[40:41], s[6:7], 2
	s_waitcnt lgkmcnt(0)
	s_add_u32 s18, s18, s40
	s_addc_u32 s19, s19, s41
	v_lshl_add_u64 v[52:53], s[18:19], 0, v[2:3]
	v_or_b32_e32 v28, s36, v1
	v_mad_i64_i32 v[36:37], s[18:19], v28, s38, v[52:53]
	v_or_b32_e32 v28, s36, v12
	v_mad_i64_i32 v[38:39], s[18:19], v28, s38, v[52:53]
	global_load_dwordx4 v[28:31], v[36:37], off
	global_load_dwordx4 v[32:35], v[38:39], off
	v_or_b32_e32 v36, s36, v13
	v_mad_i64_i32 v[44:45], s[18:19], v36, s38, v[52:53]
	v_or_b32_e32 v36, s36, v14
	v_mad_i64_i32 v[46:47], s[18:19], v36, s38, v[52:53]
	global_load_dwordx4 v[36:39], v[44:45], off
	global_load_dwordx4 v[40:43], v[46:47], off
	v_or_b32_e32 v44, s36, v15
	v_mad_i64_i32 v[54:55], s[18:19], v44, s38, v[52:53]
	v_or_b32_e32 v44, s36, v16
	v_mad_i64_i32 v[56:57], s[18:19], v44, s38, v[52:53]
	global_load_dwordx4 v[44:47], v[54:55], off
	global_load_dwordx4 v[48:51], v[56:57], off
	v_or_b32_e32 v54, s36, v17
	v_mad_i64_i32 v[60:61], s[18:19], v54, s38, v[52:53]
	v_or_b32_e32 v54, s36, v18
	v_mad_i64_i32 v[62:63], s[18:19], v54, s38, v[52:53]
	global_load_dwordx4 v[52:55], v[60:61], off
	global_load_dwordx4 v[56:59], v[62:63], off
	s_ashr_i32 s37, s36, 31
	s_and_b32 s7, s15, 4
	s_cmp_lt_u32 s42, 0xffffffc0
	s_cselect_b64 vcc, -1, 0
	s_and_b64 s[18:19], vcc, exec
	s_cselect_b32 s4, s6, s4
	s_cselect_b32 s6, -4, s7
	v_or_b32_e32 v64, s6, v20
	v_add_u32_e32 v62, v64, v21
	v_cndmask_b32_e32 v62, v62, v1, vcc
	v_add_u32_e32 v62, s4, v62
	v_ashrrev_i32_e32 v63, 31, v62
	v_lshl_add_u64 v[60:61], s[36:37], 1, v[10:11]
	s_waitcnt vmcnt(7)
	ds_write_b128 v25, v[28:31]
	s_waitcnt vmcnt(6)
	ds_write_b128 v25, v[32:35] offset:1152
	s_waitcnt vmcnt(5)
	ds_write_b128 v25, v[36:39] offset:2304
	s_waitcnt vmcnt(4)
	ds_write_b128 v25, v[40:43] offset:3456
	s_waitcnt vmcnt(3)
	ds_write_b128 v25, v[44:47] offset:4608
	s_waitcnt vmcnt(2)
	ds_write_b128 v25, v[48:51] offset:5760
	s_waitcnt vmcnt(1)
	ds_write_b128 v25, v[52:55] offset:6912
	s_waitcnt vmcnt(0)
	ds_write_b128 v25, v[56:59] offset:8064
	s_waitcnt lgkmcnt(0)
	ds_read2_b32 v[32:33], v19 offset0:36 offset1:44
	ds_read2_b32 v[34:35], v19 offset1:8
	ds_read2_b32 v[36:37], v19 offset0:72 offset1:80
	ds_read2_b32 v[38:39], v19 offset0:108 offset1:116
	ds_read2_b32 v[40:41], v19 offset0:144 offset1:152
	ds_read2_b32 v[42:43], v19 offset0:180 offset1:188
	ds_read2_b32 v[44:45], v19 offset0:216 offset1:224
	ds_read2_b32 v[46:47], v26 offset0:124 offset1:132
	s_waitcnt lgkmcnt(6)
	v_bfe_u32 v28, v34, 16, 1
	v_bfe_u32 v29, v32, 16, 1
	s_waitcnt lgkmcnt(5)
	v_bfe_u32 v30, v36, 16, 1
	s_waitcnt lgkmcnt(3)
	v_bfe_u32 v48, v40, 16, 1
	s_waitcnt lgkmcnt(1)
	v_bfe_u32 v50, v44, 16, 1
	v_bfe_u32 v31, v38, 16, 1
	v_bfe_u32 v49, v42, 16, 1
	s_waitcnt lgkmcnt(0)
; #define GAS __attribute__((address_space(1)))
; #define LAS __attribute__((address_space(3)))
; __device__ __forceinline__ unsigned pk2(float lo, float hi) { return f2bf(lo) | (f2bf(hi) << 16); }
; __device__ __forceinline__ void p0_transpose_item(const float* W, int N, int k0, int n0, bf16* WT, int K, int dst_row0, LAS float* scr, int lane, const float* kscale = nullptr, int permhalf = -1) {
;     ...
;     for (int j = 0; j < 4; ++j) { const int n = (lane >> 3) + 8 * j; const LAS float* s = scr + (8 * c) * 36 + n;
;         v4u o; o.x = pk2(s[0 * 36] * ks[0], s[1 * 36] * ks[1]); o.y = pk2(s[2 * 36] * ks[2], s[3 * 36] * ks[3]); o.z = pk2(s[4 * 36] * ks[4], s[5 * 36] * ks[5]); o.w = pk2(s[6 * 36] * ks[6], s[7 * 36] * ks[7]);
;         const int drow = permhalf < 0 ? n : (32 * (n >> 4) + 8 * ((n >> 2) & 3) + 4 * permhalf + (n & 3));
;         *(GAS v4u*)(WT + (size_t)(dst_row0 + drow) * K + k0 + 8 * c) = o; }
	v_bfe_u32 v51, v46, 16, 1
	v_add3_u32 v28, v34, v28, s29
	v_add3_u32 v29, v32, v29, s29
	v_add3_u32 v30, v36, v30, s29
	v_add3_u32 v32, v40, v48, s29
	v_add3_u32 v36, v44, v50, s29
	v_add3_u32 v31, v38, v31, s29
	v_add3_u32 v34, v42, v49, s29
	v_add3_u32 v38, v46, v51, s29
	v_lshrrev_b32_e32 v28, 16, v28
	v_lshrrev_b32_e32 v30, 16, v30
	v_lshrrev_b32_e32 v32, 16, v32
	v_lshrrev_b32_e32 v36, 16, v36
	v_lshlrev_b64 v[48:49], 12, v[62:63]
	v_and_or_b32 v28, v29, s31, v28
	v_and_or_b32 v29, v31, s31, v30
	v_and_or_b32 v30, v34, s31, v32
	v_and_or_b32 v31, v38, s31, v36
	v_lshl_add_u64 v[48:49], v[60:61], 0, v[48:49]
	global_store_dwordx4 v[48:49], v[28:31], off sc1
	v_bfe_u32 v32, v47, 16, 1
	v_add3_u32 v32, v47, v32, s29
	v_bfe_u32 v28, v35, 16, 1
	v_add3_u32 v28, v35, v28, s29
	v_bfe_u32 v29, v33, 16, 1
	v_lshrrev_b32_e32 v28, 16, v28
	v_add3_u32 v29, v33, v29, s29
	v_and_or_b32 v28, v29, s31, v28
	v_bfe_u32 v29, v37, 16, 1
	v_add3_u32 v29, v37, v29, s29
	v_bfe_u32 v30, v39, 16, 1
	v_lshrrev_b32_e32 v29, 16, v29
	v_add3_u32 v30, v39, v30, s29
	v_and_or_b32 v29, v30, s31, v29
	v_bfe_u32 v30, v41, 16, 1
	v_add3_u32 v30, v41, v30, s29
	v_bfe_u32 v31, v43, 16, 1
	v_lshrrev_b32_e32 v30, 16, v30
	v_add3_u32 v31, v43, v31, s29
	v_and_or_b32 v30, v31, s31, v30
	v_bfe_u32 v31, v45, 16, 1
	v_add3_u32 v31, v45, v31, s29
	v_lshrrev_b32_e32 v31, 16, v31
	v_and_or_b32 v31, v32, s31, v31
	v_add_u32_e32 v32, v64, v22
	v_cndmask_b32_e32 v32, v32, v12, vcc
	v_add_u32_e32 v32, s4, v32
	v_ashrrev_i32_e32 v33, 31, v32
	v_lshlrev_b64 v[32:33], 12, v[32:33]
	ds_read2_b32 v[34:35], v19 offset0:16 offset1:24
	v_lshl_add_u64 v[32:33], v[60:61], 0, v[32:33]
	global_store_dwordx4 v[32:33], v[28:31], off sc1
	ds_read2_b32 v[32:33], v19 offset0:52 offset1:60
	ds_read2_b32 v[36:37], v19 offset0:88 offset1:96
	ds_read2_b32 v[38:39], v19 offset0:124 offset1:132
	s_waitcnt lgkmcnt(3)
	v_bfe_u32 v28, v34, 16, 1
	v_add3_u32 v28, v34, v28, s29
	s_waitcnt lgkmcnt(2)
	v_bfe_u32 v29, v32, 16, 1
	ds_read2_b32 v[40:41], v19 offset0:160 offset1:168
	v_lshrrev_b32_e32 v28, 16, v28
	v_add3_u32 v29, v32, v29, s29
	ds_read2_b32 v[42:43], v19 offset0:196 offset1:204
	v_and_or_b32 v28, v29, s31, v28
	s_waitcnt lgkmcnt(3)
	v_bfe_u32 v29, v36, 16, 1
	v_add3_u32 v29, v36, v29, s29
	s_waitcnt lgkmcnt(2)
	v_bfe_u32 v30, v38, 16, 1
	ds_read2_b32 v[44:45], v19 offset0:232 offset1:240
	v_lshrrev_b32_e32 v29, 16, v29
	v_add3_u32 v30, v38, v30, s29
	ds_read2_b32 v[46:47], v27 offset0:12 offset1:20
	v_and_or_b32 v29, v30, s31, v29
	s_waitcnt lgkmcnt(3)
	v_bfe_u32 v30, v40, 16, 1
	v_add3_u32 v30, v40, v30, s29
	s_waitcnt lgkmcnt(2)
	v_bfe_u32 v31, v42, 16, 1
	v_lshrrev_b32_e32 v30, 16, v30
	v_add3_u32 v31, v42, v31, s29
	v_and_or_b32 v30, v31, s31, v30
	s_waitcnt lgkmcnt(1)
	v_bfe_u32 v31, v44, 16, 1
	v_add3_u32 v31, v44, v31, s29
	s_waitcnt lgkmcnt(0)
	v_bfe_u32 v32, v46, 16, 1
	v_lshrrev_b32_e32 v31, 16, v31
	v_add3_u32 v32, v46, v32, s29
	v_and_or_b32 v31, v32, s31, v31
	v_add_u32_e32 v32, v64, v23
	v_cndmask_b32_e32 v32, v32, v13, vcc
	v_add_u32_e32 v48, s4, v32
	v_ashrrev_i32_e32 v49, 31, v48
	v_lshlrev_b64 v[48:49], 12, v[48:49]
	v_lshl_add_u64 v[48:49], v[60:61], 0, v[48:49]
	global_store_dwordx4 v[48:49], v[28:31], off sc1
	v_bfe_u32 v32, v47, 16, 1
	v_add3_u32 v32, v47, v32, s29
	v_bfe_u32 v28, v35, 16, 1
	v_add3_u32 v28, v35, v28, s29
	v_bfe_u32 v29, v33, 16, 1
	v_lshrrev_b32_e32 v28, 16, v28
	v_add3_u32 v29, v33, v29, s29
	v_and_or_b32 v28, v29, s31, v28
	v_bfe_u32 v29, v37, 16, 1
	v_add3_u32 v29, v37, v29, s29
	v_bfe_u32 v30, v39, 16, 1
	v_lshrrev_b32_e32 v29, 16, v29
	v_add3_u32 v30, v39, v30, s29
	v_and_or_b32 v29, v30, s31, v29
	v_bfe_u32 v30, v41, 16, 1
	v_add3_u32 v30, v41, v30, s29
	v_bfe_u32 v31, v43, 16, 1
	v_lshrrev_b32_e32 v30, 16, v30
	v_add3_u32 v31, v43, v31, s29
	v_and_or_b32 v30, v31, s31, v30
	v_bfe_u32 v31, v45, 16, 1
	v_add3_u32 v31, v45, v31, s29
	v_lshrrev_b32_e32 v31, 16, v31
	v_and_or_b32 v31, v32, s31, v31
	v_add_u32_e32 v32, v64, v24
	v_cndmask_b32_e32 v32, v32, v14, vcc
	v_add_u32_e32 v32, s4, v32
	v_ashrrev_i32_e32 v33, 31, v32
	v_lshlrev_b64 v[32:33], 12, v[32:33]
	v_lshl_add_u64 v[32:33], v[60:61], 0, v[32:33]
	global_store_dwordx4 v[32:33], v[28:31], off sc1
	s_waitcnt lgkmcnt(0)
	s_branch .LBB0_11

; __device__ __forceinline__ unsigned cvt_pk_bf16(float lo, float hi) { f32x2v_ v = {lo, hi}; bf16x2v_ b = __builtin_convertvector(v, bf16x2v_); return __builtin_bit_cast(unsigned, b); }
;     __device__ __forceinline__ void operator()(const f32x4 (&acc)[2][2][4][2], const Unit& u, int wr, int wc, int fr, int fq) const {
;     ...
; #pragma unroll
;         for (int ai = 0; ai < 2; ++ai)
; #pragma unroll
;             for (int m = 0; m < 4; ++m) { bf16_t* rowp = base + (size_t)(row0 + ai * HALF + m * 16) * ld + col0;
; #pragma unroll
;                 for (int bj = 0; bj < 2; ++bj) { const f32x4 v0 = acc[ai][bj][m][0], v1 = acc[ai][bj][m][1];
;                     u32x4 w; w.x = cvt_pk_bf16(v0[0], v0[1]); w.y = cvt_pk_bf16(v0[2], v0[3]); w.z = cvt_pk_bf16(v1[0], v1[1]); w.w = cvt_pk_bf16(v1[2], v1[3]);
;                     *(u32x4*)(rowp + bj * HALF) = w; } }
.LBB0_133:
	s_add_u32 s54, s12, s62
	s_addc_u32 s55, s13, s63
	s_add_i32 s18, s56, -10
	s_mov_b64 s[64:65], -1
	v_lshl_add_u32 v162, s58, 8, v1
	s_cmp_gt_u32 s18, 3
	v_add_u32_e32 v164, s9, v171
	s_cbranch_scc0 .LBB0_139
	s_xor_b64 s[18:19], s[60:61], -1
	s_andn2_b64 vcc, exec, s[18:19]
	s_mov_b64 s[58:59], -1
	s_cbranch_vccnz .LBB0_136
	v_ashrrev_i32_e32 v130, 31, v162
	v_ashrrev_i32_e32 v165, 31, v164
	v_mul_lo_u32 v132, s11, v162
	v_mul_lo_u32 v138, s10, v130
	v_mad_u64_u32 v[130:131], s[18:19], s10, v162, 0
	v_lshl_add_u64 v[134:135], v[164:165], 1, s[54:55]
	v_add3_u32 v131, v131, v138, v132
	v_lshl_add_u64 v[136:137], v[130:131], 1, v[134:135]
	v_cvt_pk_bf16_f32 v130, v114, v115
	v_cvt_pk_bf16_f32 v131, v116, v117
	v_cvt_pk_bf16_f32 v132, v118, v119
	v_cvt_pk_bf16_f32 v133, v120, v121
	global_store_dwordx4 v[136:137], v[130:133], off sc1
	s_mov_b64 s[58:59], 0
	s_nop 0
	v_cvt_pk_bf16_f32 v130, v122, v123
	v_cvt_pk_bf16_f32 v131, v124, v125
	v_cvt_pk_bf16_f32 v132, v126, v127
	v_cvt_pk_bf16_f32 v133, v128, v129
	global_store_dwordx4 v[136:137], v[130:133], off offset:256 sc1
	s_nop 1
	v_or_b32_e32 v130, 16, v162
	v_mul_lo_u32 v132, s11, v130
	v_mad_u64_u32 v[130:131], s[18:19], s10, v130, 0
	v_add3_u32 v131, v131, v138, v132
	v_lshl_add_u64 v[136:137], v[130:131], 1, v[134:135]
	v_cvt_pk_bf16_f32 v130, v98, v99
	v_cvt_pk_bf16_f32 v131, v100, v101
	v_cvt_pk_bf16_f32 v132, v102, v103
	v_cvt_pk_bf16_f32 v133, v104, v105
	global_store_dwordx4 v[136:137], v[130:133], off sc1
	s_nop 1
	v_cvt_pk_bf16_f32 v130, v106, v107
	v_cvt_pk_bf16_f32 v131, v108, v109
	v_cvt_pk_bf16_f32 v132, v110, v111
	v_cvt_pk_bf16_f32 v133, v112, v113
	global_store_dwordx4 v[136:137], v[130:133], off offset:256 sc1
	s_nop 1
	v_or_b32_e32 v130, 32, v162
	v_mul_lo_u32 v132, s11, v130
	v_mad_u64_u32 v[130:131], s[18:19], s10, v130, 0
	v_add3_u32 v131, v131, v138, v132
	v_lshl_add_u64 v[136:137], v[130:131], 1, v[134:135]
	v_cvt_pk_bf16_f32 v130, v82, v83
	v_cvt_pk_bf16_f32 v131, v84, v85
	v_cvt_pk_bf16_f32 v132, v86, v87
	v_cvt_pk_bf16_f32 v133, v88, v89
	global_store_dwordx4 v[136:137], v[130:133], off sc1
	s_nop 1
	v_cvt_pk_bf16_f32 v130, v90, v91
	v_cvt_pk_bf16_f32 v131, v92, v93
	v_cvt_pk_bf16_f32 v132, v94, v95
	v_cvt_pk_bf16_f32 v133, v96, v97
	global_store_dwordx4 v[136:137], v[130:133], off offset:256 sc1
	s_nop 1
	v_or_b32_e32 v130, 48, v162
	v_mul_lo_u32 v132, s11, v130
	v_mad_u64_u32 v[130:131], s[18:19], s10, v130, 0
	v_add3_u32 v131, v131, v138, v132
	v_lshl_add_u64 v[136:137], v[130:131], 1, v[134:135]
	v_cvt_pk_bf16_f32 v130, v66, v67
	v_cvt_pk_bf16_f32 v131, v68, v69
	v_cvt_pk_bf16_f32 v132, v70, v71
	v_cvt_pk_bf16_f32 v133, v72, v73
	global_store_dwordx4 v[136:137], v[130:133], off sc1
	s_nop 1
	v_cvt_pk_bf16_f32 v130, v74, v75
	v_cvt_pk_bf16_f32 v131, v76, v77
	v_cvt_pk_bf16_f32 v132, v78, v79
	v_cvt_pk_bf16_f32 v133, v80, v81
	global_store_dwordx4 v[136:137], v[130:133], off offset:256 sc1
	s_nop 1
	v_add_u32_e32 v130, 0x80, v162
	v_ashrrev_i32_e32 v131, 31, v130
	v_mul_lo_u32 v132, s10, v131
	v_mul_lo_u32 v133, s11, v130
	v_mad_u64_u32 v[130:131], s[18:19], s10, v130, 0
	v_add3_u32 v131, v131, v132, v133
	v_lshl_add_u64 v[136:137], v[130:131], 1, v[134:135]
	v_cvt_pk_bf16_f32 v130, v58, v59
	v_cvt_pk_bf16_f32 v131, v60, v61
	v_cvt_pk_bf16_f32 v132, v62, v63
	v_cvt_pk_bf16_f32 v133, v64, v65
	global_store_dwordx4 v[136:137], v[130:133], off sc1
	s_nop 1
	v_cvt_pk_bf16_f32 v130, v50, v51
	v_cvt_pk_bf16_f32 v131, v52, v53
	v_cvt_pk_bf16_f32 v132, v54, v55
	v_cvt_pk_bf16_f32 v133, v56, v57
	global_store_dwordx4 v[136:137], v[130:133], off offset:256 sc1
	s_nop 1
	v_add_u32_e32 v130, 0x90, v162
	v_ashrrev_i32_e32 v131, 31, v130
	v_mul_lo_u32 v132, s10, v131
	v_mul_lo_u32 v133, s11, v130
	v_mad_u64_u32 v[130:131], s[18:19], s10, v130, 0
	v_add3_u32 v131, v131, v132, v133
	v_lshl_add_u64 v[136:137], v[130:131], 1, v[134:135]
	v_cvt_pk_bf16_f32 v130, v42, v43
	v_cvt_pk_bf16_f32 v131, v44, v45
	v_cvt_pk_bf16_f32 v132, v46, v47
	v_cvt_pk_bf16_f32 v133, v48, v49
	global_store_dwordx4 v[136:137], v[130:133], off sc1
	s_nop 1
	v_cvt_pk_bf16_f32 v130, v34, v35
	v_cvt_pk_bf16_f32 v131, v36, v37
	v_cvt_pk_bf16_f32 v132, v38, v39
	v_cvt_pk_bf16_f32 v133, v40, v41
	global_store_dwordx4 v[136:137], v[130:133], off offset:256 sc1
	s_nop 1
	v_add_u32_e32 v130, 0xa0, v162
	v_ashrrev_i32_e32 v131, 31, v130
	v_mul_lo_u32 v132, s10, v131
	v_mul_lo_u32 v133, s11, v130
	v_mad_u64_u32 v[130:131], s[18:19], s10, v130, 0
	v_add3_u32 v131, v131, v132, v133
	v_lshl_add_u64 v[136:137], v[130:131], 1, v[134:135]
	v_cvt_pk_bf16_f32 v130, v18, v19
	v_cvt_pk_bf16_f32 v131, v20, v21
	v_cvt_pk_bf16_f32 v132, v22, v23
	v_cvt_pk_bf16_f32 v133, v24, v25
	global_store_dwordx4 v[136:137], v[130:133], off sc1
	s_nop 1
	v_cvt_pk_bf16_f32 v130, v26, v27
	v_cvt_pk_bf16_f32 v131, v28, v29
	v_cvt_pk_bf16_f32 v132, v30, v31
	v_cvt_pk_bf16_f32 v133, v32, v33
	global_store_dwordx4 v[136:137], v[130:133], off offset:256 sc1
	s_nop 1
	v_add_u32_e32 v130, 0xb0, v162
	v_ashrrev_i32_e32 v131, 31, v130
	v_mul_lo_u32 v132, s10, v131
	v_mul_lo_u32 v133, s11, v130
	v_mad_u64_u32 v[130:131], s[18:19], s10, v130, 0
	v_add3_u32 v131, v131, v132, v133
	v_lshl_add_u64 v[134:135], v[130:131], 1, v[134:135]
	v_cvt_pk_bf16_f32 v130, v6, v7
	v_cvt_pk_bf16_f32 v131, v8, v9
	v_cvt_pk_bf16_f32 v132, v14, v15
	v_cvt_pk_bf16_f32 v133, v16, v17
	global_store_dwordx4 v[134:135], v[130:133], off sc1
	s_nop 1
	v_cvt_pk_bf16_f32 v130, v10, v11
	v_cvt_pk_bf16_f32 v131, v12, v13
	v_cvt_pk_bf16_f32 v132, v2, v3
	v_cvt_pk_bf16_f32 v133, v4, v5
	global_store_dwordx4 v[134:135], v[130:133], off offset:256 sc1
; __device__ __forceinline__ unsigned cvt_pk_bf16(float lo, float hi) { f32x2v_ v = {lo, hi}; bf16x2v_ b = __builtin_convertvector(v, bf16x2v_); return __builtin_bit_cast(unsigned, b); }
; __device__ __forceinline__ float bf_lo(unsigned w) { return __uint_as_float(w << 16); }
; __device__ __forceinline__ float bf_hi(unsigned w) { return __uint_as_float(w & 0xffff0000u); }
;     __device__ __forceinline__ void operator()(const f32x4 (&acc)[2][2][4][2], const Unit& u, int wr, int wc, int fr, int fq) const {
;     ...
;         if (gate) {
;             const int ch0 = (pn - 18) * HALF + wc * 32 + 8 * fq;
;             f32x4 ba[2], bb[2];
; #pragma unroll
;             for (int n = 0; n < 2; ++n) { ba[n] = *(const f32x4*)(bgate + ch0 + 4 * n); bb[n] = *(const f32x4*)(bgate + 2048 + ch0 + 4 * n); }
; #pragma unroll
;             for (int ai = 0; ai < 2; ++ai)
; #pragma unroll
;                 for (int m = 0; m < 4; ++m) { bf16_t* rowp = GT + (size_t)(row0 + ai * HALF + m * 16) * 4096 + ch0;
;                     f32x4 a0 = acc[ai][0][m][0] + ba[0], a1 = acc[ai][0][m][1] + ba[1], b0 = acc[ai][1][m][0] + bb[0], b1 = acc[ai][1][m][1] + bb[1];
; #pragma unroll
;                     for (int e = 0; e < 4; ++e) { a0[e] = sigmoid_f(a0[e]); a1[e] = sigmoid_f(a1[e]); b0[e] = sigmoid_f(b0[e]); b1[e] = sigmoid_f(b1[e]); }
;                     u32x4 wb; wb.x = cvt_pk_bf16(b0[0], b0[1]); wb.y = cvt_pk_bf16(b0[2], b0[3]); wb.z = cvt_pk_bf16(b1[0], b1[1]); wb.w = cvt_pk_bf16(b1[2], b1[3]);
;                     const float q0 = __builtin_amdgcn_rcpf(fmaxf(bf_lo(wb.x), 1e-30f)), q1 = __builtin_amdgcn_rcpf(fmaxf(bf_hi(wb.x), 1e-30f)), q2 = __builtin_amdgcn_rcpf(fmaxf(bf_lo(wb.y), 1e-30f)), q3 = __builtin_amdgcn_rcpf(fmaxf(bf_hi(wb.y), 1e-30f));
;                     const float q4 = __builtin_amdgcn_rcpf(fmaxf(bf_lo(wb.z), 1e-30f)), q5 = __builtin_amdgcn_rcpf(fmaxf(bf_hi(wb.z), 1e-30f)), q6 = __builtin_amdgcn_rcpf(fmaxf(bf_lo(wb.w), 1e-30f)), q7 = __builtin_amdgcn_rcpf(fmaxf(bf_hi(wb.w), 1e-30f));
;                     u32x4 wr_; wr_.x = cvt_pk_bf16(a0[0] * q0, a0[1] * q1); wr_.y = cvt_pk_bf16(a0[2] * q2, a0[3] * q3); wr_.z = cvt_pk_bf16(a1[0] * q4, a1[1] * q5); wr_.w = cvt_pk_bf16(a1[2] * q6, a1[3] * q7);
;                     *(u32x4*)rowp = wr_; *(u32x4*)(rowp + 2048) = wb; }
.LBB0_136:
	s_andn2_b64 vcc, exec, s[58:59]
	s_cbranch_vccnz .LBB0_138
	v_lshl_add_u32 v166, s56, 7, v172
	v_ashrrev_i32_e32 v167, 31, v166
	v_lshlrev_b64 v[130:131], 2, v[166:167]
	v_lshl_add_u64 v[132:133], s[14:15], 0, v[130:131]
	global_load_dwordx4 v[142:145], v[132:133], off
	global_load_dwordx4 v[138:141], v[132:133], off offset:16
	v_lshl_add_u64 v[130:131], s[42:43], 0, v[130:131]
	global_load_dwordx4 v[134:137], v[130:131], off
	s_nop 0
	global_load_dwordx4 v[130:133], v[130:131], off offset:16
	v_ashrrev_i32_e32 v163, 31, v162
	v_lshlrev_b64 v[176:177], 13, v[162:163]
	v_lshl_add_u64 v[168:169], v[166:167], 1, s[40:41]
	v_lshl_add_u64 v[166:167], v[168:169], 0, v[176:177]
	s_waitcnt vmcnt(0)
	v_pk_add_f32 v[178:179], v[114:115], v[142:143]
	v_pk_add_f32 v[182:183], v[118:119], v[138:139]
	v_pk_add_f32 v[186:187], v[122:123], v[134:135]
	v_pk_add_f32 v[180:181], v[120:121], v[140:141]
	v_mul_f32_e32 v163, 0xbfb8aa3b, v178
	v_mul_f32_e32 v165, 0xbfb8aa3b, v182
	v_mul_f32_e32 v175, 0xbfb8aa3b, v186
	v_mul_f32_e32 v182, 0xbfb8aa3b, v183
	v_mul_f32_e32 v183, 0xbfb8aa3b, v187
	v_mul_f32_e32 v180, 0xbfb8aa3b, v180
	v_exp_f32_e32 v163, v163
	v_exp_f32_e32 v175, v175
	v_exp_f32_e32 v183, v183
	v_pk_add_f32 v[176:177], v[116:117], v[144:145]
	v_pk_add_f32 v[184:185], v[124:125], v[136:137]
	v_exp_f32_e32 v180, v180
	v_pk_add_f32 v[188:189], v[128:129], v[132:133]
	v_mul_f32_e32 v179, 0xbfb8aa3b, v179
	v_mul_f32_e32 v184, 0xbfb8aa3b, v184
	v_mul_f32_e32 v177, 0xbfb8aa3b, v177
	v_mul_f32_e32 v185, 0xbfb8aa3b, v185
	v_pk_add_f32 v[190:191], v[126:127], v[130:131]
	v_mul_f32_e32 v176, 0xbfb8aa3b, v176
	v_mul_f32_e32 v187, 0xbfb8aa3b, v188
	v_mul_f32_e32 v181, 0xbfb8aa3b, v181
	v_mul_f32_e32 v188, 0xbfb8aa3b, v189
	v_exp_f32_e32 v179, v179
	v_exp_f32_e32 v184, v184
	v_exp_f32_e32 v177, v177
	v_exp_f32_e32 v185, v185
	v_mul_f32_e32 v178, 0xbfb8aa3b, v190
	v_mul_f32_e32 v186, 0xbfb8aa3b, v191
	v_exp_f32_e32 v182, v182
	v_exp_f32_e32 v176, v176
	v_exp_f32_e32 v187, v187
	v_exp_f32_e32 v181, v181
	v_exp_f32_e32 v188, v188
	v_add_f32_e32 v163, 1.0, v163
	v_add_f32_e32 v175, 1.0, v175
	v_add_f32_e32 v190, 1.0, v183
	v_exp_f32_e32 v165, v165
	v_exp_f32_e32 v178, v178
	v_exp_f32_e32 v186, v186
	v_add_f32_e32 v191, 1.0, v180
	v_rcp_f32_e32 v180, v163
	v_rcp_f32_e32 v163, v175
	v_rcp_f32_e32 v175, v190
	v_add_f32_e32 v179, 1.0, v179
	v_add_f32_e32 v192, 1.0, v184
	v_add_f32_e32 v177, 1.0, v177
	v_add_f32_e32 v194, 1.0, v185
	v_add_f32_e32 v189, 1.0, v182
	v_add_f32_e32 v176, 1.0, v176
	v_add_f32_e32 v187, 1.0, v187
	v_add_f32_e32 v193, 1.0, v181
	v_add_f32_e32 v188, 1.0, v188
	v_rcp_f32_e32 v181, v179
	v_rcp_f32_e32 v179, v192
	v_rcp_f32_e32 v185, v177
	v_rcp_f32_e32 v177, v194
	v_add_f32_e32 v165, 1.0, v165
	v_add_f32_e32 v178, 1.0, v178
	v_add_f32_e32 v186, 1.0, v186
	v_rcp_f32_e32 v183, v189
	v_rcp_f32_e32 v184, v176
	v_rcp_f32_e32 v189, v187
	v_rcp_f32_e32 v188, v188
	v_cvt_pk_bf16_f32 v176, v163, v175
	v_rcp_f32_e32 v182, v165
	v_rcp_f32_e32 v165, v178
	v_rcp_f32_e32 v178, v186
	v_lshlrev_b32_e32 v163, 16, v176
	v_max_f32_e32 v163, v163, v163
	v_cvt_pk_bf16_f32 v177, v179, v177
	v_max_f32_e32 v163, 0xda24260, v163
	v_cvt_pk_bf16_f32 v179, v189, v188
	v_rcp_f32_e32 v188, v163
	v_and_b32_e32 v163, 0xffff0000, v177
	v_cvt_pk_bf16_f32 v178, v165, v178
	v_max_f32_e32 v163, 0xda24260, v163
	v_rcp_f32_e32 v186, v191
	v_rcp_f32_e32 v191, v163
	v_lshlrev_b32_e32 v163, 16, v178
	v_max_f32_e32 v163, v163, v163
	v_max_f32_e32 v163, 0xda24260, v163
	v_rcp_f32_e32 v192, v163
	v_and_b32_e32 v163, 0xffff0000, v178
	v_max_f32_e32 v163, 0xda24260, v163
	v_rcp_f32_e32 v187, v193
	v_rcp_f32_e32 v193, v163
	v_lshlrev_b32_e32 v163, 16, v179
	v_and_b32_e32 v165, 0xffff0000, v176
	v_lshlrev_b32_e32 v175, 16, v177
	v_max_f32_e32 v163, v163, v163
	v_max_f32_e32 v165, 0xda24260, v165
	v_max_f32_e32 v175, v175, v175
	v_max_f32_e32 v163, 0xda24260, v163
	v_rcp_f32_e32 v189, v165
	v_max_f32_e32 v165, 0xda24260, v175
	v_rcp_f32_e32 v194, v163
	v_and_b32_e32 v163, 0xffff0000, v179
	v_rcp_f32_e32 v190, v165
	v_max_f32_e32 v163, 0xda24260, v163
	v_rcp_f32_e32 v195, v163
	v_pk_mul_f32 v[180:181], v[180:181], v[188:189]
	v_pk_mul_f32 v[184:185], v[184:185], v[190:191]
	v_cvt_pk_bf16_f32 v180, v180, v181
	v_cvt_pk_bf16_f32 v181, v184, v185
	v_pk_mul_f32 v[182:183], v[182:183], v[192:193]
	v_pk_mul_f32 v[184:185], v[186:187], v[194:195]
	v_cvt_pk_bf16_f32 v182, v182, v183
	v_cvt_pk_bf16_f32 v183, v184, v185
	global_store_dwordx4 v[166:167], v[180:183], off sc1
	v_pk_add_f32 v[184:185], v[102:103], v[138:139]
	v_pk_add_f32 v[188:189], v[106:107], v[134:135]
	v_add_co_u32_e32 v180, vcc, s81, v166
	v_mul_f32_e32 v165, 0xbfb8aa3b, v184
	s_nop 0
	v_addc_co_u32_e32 v181, vcc, 0, v167, vcc
	global_store_dwordx4 v[180:181], v[176:179], off sc1
	v_pk_add_f32 v[180:181], v[98:99], v[142:143]
	v_exp_f32_e32 v165, v165
	v_mul_f32_e32 v163, 0xbfb8aa3b, v180
	v_exp_f32_e32 v163, v163
	v_pk_add_f32 v[192:193], v[110:111], v[130:131]
	v_pk_add_f32 v[178:179], v[100:101], v[144:145]
	v_mul_f32_e32 v175, 0xbfb8aa3b, v192
	v_add_f32_e32 v163, 1.0, v163
	v_rcp_f32_e32 v180, v163
	v_add_f32_e32 v163, 1.0, v165
	v_mul_f32_e32 v165, 0xbfb8aa3b, v188
	v_exp_f32_e32 v165, v165
	v_exp_f32_e32 v175, v175
	v_rcp_f32_e32 v184, v163
	v_pk_add_f32 v[182:183], v[104:105], v[140:141]
	v_add_f32_e32 v163, 1.0, v165
	v_add_f32_e32 v165, 1.0, v175
	v_mul_f32_e32 v175, 0xbfb8aa3b, v181
	v_exp_f32_e32 v175, v175
	v_mul_f32_e32 v181, 0xbfb8aa3b, v185
	v_exp_f32_e32 v185, v181
	v_mul_f32_e32 v178, 0xbfb8aa3b, v178
	v_add_f32_e32 v175, 1.0, v175
	v_rcp_f32_e32 v181, v175
	v_add_f32_e32 v175, 1.0, v185
; __device__ __forceinline__ unsigned cvt_pk_bf16(float lo, float hi) { f32x2v_ v = {lo, hi}; bf16x2v_ b = __builtin_convertvector(v, bf16x2v_); return __builtin_bit_cast(unsigned, b); }
; __device__ __forceinline__ float bf_lo(unsigned w) { return __uint_as_float(w << 16); }
; __device__ __forceinline__ float bf_hi(unsigned w) { return __uint_as_float(w & 0xffff0000u); }
; __device__ __forceinline__ float sigmoid_f(float x) { return __builtin_amdgcn_rcpf(1.0f + __builtin_amdgcn_exp2f(-1.4426950408889634f * x)); }
;     __device__ __forceinline__ void operator()(const f32x4 (&acc)[2][2][4][2], const Unit& u, int wr, int wc, int fr, int fq) const {
;     ...
;             for (int ai = 0; ai < 2; ++ai)
; #pragma unroll
;                 for (int m = 0; m < 4; ++m) { bf16_t* rowp = GT + (size_t)(row0 + ai * HALF + m * 16) * 4096 + ch0;
;                     f32x4 a0 = acc[ai][0][m][0] + ba[0], a1 = acc[ai][0][m][1] + ba[1], b0 = acc[ai][1][m][0] + bb[0], b1 = acc[ai][1][m][1] + bb[1];
; #pragma unroll
;                     for (int e = 0; e < 4; ++e) { a0[e] = sigmoid_f(a0[e]); a1[e] = sigmoid_f(a1[e]); b0[e] = sigmoid_f(b0[e]); b1[e] = sigmoid_f(b1[e]); }
;                     u32x4 wb; wb.x = cvt_pk_bf16(b0[0], b0[1]); wb.y = cvt_pk_bf16(b0[2], b0[3]); wb.z = cvt_pk_bf16(b1[0], b1[1]); wb.w = cvt_pk_bf16(b1[2], b1[3]);
;                     const float q0 = __builtin_amdgcn_rcpf(fmaxf(bf_lo(wb.x), 1e-30f)), q1 = __builtin_amdgcn_rcpf(fmaxf(bf_hi(wb.x), 1e-30f)), q2 = __builtin_amdgcn_rcpf(fmaxf(bf_lo(wb.y), 1e-30f)), q3 = __builtin_amdgcn_rcpf(fmaxf(bf_hi(wb.y), 1e-30f));
;                     const float q4 = __builtin_amdgcn_rcpf(fmaxf(bf_lo(wb.z), 1e-30f)), q5 = __builtin_amdgcn_rcpf(fmaxf(bf_hi(wb.z), 1e-30f)), q6 = __builtin_amdgcn_rcpf(fmaxf(bf_lo(wb.w), 1e-30f)), q7 = __builtin_amdgcn_rcpf(fmaxf(bf_hi(wb.w), 1e-30f));
;                     u32x4 wr_; wr_.x = cvt_pk_bf16(a0[0] * q0, a0[1] * q1); wr_.y = cvt_pk_bf16(a0[2] * q2, a0[3] * q3); wr_.z = cvt_pk_bf16(a1[0] * q4, a1[1] * q5); wr_.w = cvt_pk_bf16(a1[2] * q6, a1[3] * q7);
;                     *(u32x4*)rowp = wr_; *(u32x4*)(rowp + 2048) = wb; }
	v_mul_f32_e32 v185, 0xbfb8aa3b, v189
	v_exp_f32_e32 v188, v185
	v_mul_f32_e32 v185, 0xbfb8aa3b, v193
	v_exp_f32_e32 v189, v185
	v_exp_f32_e32 v178, v178
	v_mul_f32_e32 v182, 0xbfb8aa3b, v182
	v_rcp_f32_e32 v185, v175
	v_add_f32_e32 v175, 1.0, v188
	v_add_f32_e32 v188, 1.0, v189
	v_exp_f32_e32 v189, v182
	v_pk_add_f32 v[186:187], v[108:109], v[136:137]
	v_pk_add_f32 v[190:191], v[112:113], v[132:133]
	v_mul_f32_e32 v186, 0xbfb8aa3b, v186
	v_rcp_f32_e32 v192, v188
	v_add_f32_e32 v178, 1.0, v178
	v_exp_f32_e32 v188, v186
	v_mul_f32_e32 v186, 0xbfb8aa3b, v190
	v_rcp_f32_e32 v182, v178
	v_add_f32_e32 v178, 1.0, v189
	v_exp_f32_e32 v189, v186
	v_mul_f32_e32 v179, 0xbfb8aa3b, v179
	v_exp_f32_e32 v179, v179
	v_mul_f32_e32 v183, 0xbfb8aa3b, v183
	v_rcp_f32_e32 v186, v178
	v_add_f32_e32 v178, 1.0, v188
	v_add_f32_e32 v188, 1.0, v189
	v_exp_f32_e32 v189, v183
	v_mul_f32_e32 v187, 0xbfb8aa3b, v187
	v_rcp_f32_e32 v190, v188
	v_add_f32_e32 v179, 1.0, v179
	v_exp_f32_e32 v188, v187
	v_mul_f32_e32 v187, 0xbfb8aa3b, v191
	v_rcp_f32_e32 v183, v179
	v_add_f32_e32 v179, 1.0, v189
	v_exp_f32_e32 v189, v187
	v_rcp_f32_e32 v163, v163
	v_rcp_f32_e32 v175, v175
	v_or_b32_e32 v176, 16, v162
	v_ashrrev_i32_e32 v177, 31, v176
	v_lshlrev_b64 v[176:177], 13, v[176:177]
	v_rcp_f32_e32 v187, v179
	v_add_f32_e32 v179, 1.0, v188
	v_add_f32_e32 v188, 1.0, v189
	v_rcp_f32_e32 v178, v178
	v_rcp_f32_e32 v179, v179
	v_rcp_f32_e32 v191, v188
	v_lshl_add_u64 v[188:189], v[168:169], 0, v[176:177]
	v_cvt_pk_bf16_f32 v176, v163, v175
	v_lshlrev_b32_e32 v163, 16, v176
	v_max_f32_e32 v163, v163, v163
	v_max_f32_e32 v163, 0xda24260, v163
	v_cvt_pk_bf16_f32 v177, v178, v179
	v_cvt_pk_bf16_f32 v179, v190, v191
	v_rcp_f32_e32 v190, v163
	v_and_b32_e32 v163, 0xffff0000, v176
	v_rcp_f32_e32 v165, v165
	v_max_f32_e32 v163, 0xda24260, v163
	v_rcp_f32_e32 v191, v163
	v_lshlrev_b32_e32 v163, 16, v177
	v_max_f32_e32 v163, v163, v163
	v_max_f32_e32 v163, 0xda24260, v163
	v_cvt_pk_bf16_f32 v178, v165, v192
	v_rcp_f32_e32 v192, v163
	v_and_b32_e32 v163, 0xffff0000, v177
	v_max_f32_e32 v163, 0xda24260, v163
	v_rcp_f32_e32 v193, v163
	v_lshlrev_b32_e32 v163, 16, v178
	v_max_f32_e32 v163, v163, v163
	v_max_f32_e32 v163, 0xda24260, v163
	v_rcp_f32_e32 v194, v163
	v_and_b32_e32 v163, 0xffff0000, v178
	v_max_f32_e32 v163, 0xda24260, v163
	v_rcp_f32_e32 v195, v163
	v_lshlrev_b32_e32 v163, 16, v179
	v_max_f32_e32 v163, v163, v163
	v_max_f32_e32 v163, 0xda24260, v163
	v_rcp_f32_e32 v196, v163
	v_and_b32_e32 v163, 0xffff0000, v179
	v_max_f32_e32 v163, 0xda24260, v163
	v_rcp_f32_e32 v197, v163
	v_pk_mul_f32 v[180:181], v[180:181], v[190:191]
	v_pk_mul_f32 v[182:183], v[182:183], v[192:193]
	v_cvt_pk_bf16_f32 v180, v180, v181
	v_cvt_pk_bf16_f32 v181, v182, v183
	v_pk_mul_f32 v[182:183], v[184:185], v[194:195]
	v_pk_mul_f32 v[184:185], v[186:187], v[196:197]
	v_cvt_pk_bf16_f32 v182, v182, v183
	v_cvt_pk_bf16_f32 v183, v184, v185
	global_store_dwordx4 v[188:189], v[180:183], off sc1
	v_pk_add_f32 v[184:185], v[86:87], v[138:139]
	v_pk_add_f32 v[192:193], v[94:95], v[130:131]
	v_add_co_u32_e32 v180, vcc, s81, v188
	v_mul_f32_e32 v165, 0xbfb8aa3b, v184
	s_nop 0
	v_addc_co_u32_e32 v181, vcc, 0, v189, vcc
	global_store_dwordx4 v[180:181], v[176:179], off sc1
	v_pk_add_f32 v[180:181], v[82:83], v[142:143]
	v_exp_f32_e32 v165, v165
	v_mul_f32_e32 v163, 0xbfb8aa3b, v180
	v_exp_f32_e32 v163, v163
	v_pk_add_f32 v[188:189], v[90:91], v[134:135]
	v_mul_f32_e32 v175, 0xbfb8aa3b, v192
	v_exp_f32_e32 v175, v175
	v_add_f32_e32 v163, 1.0, v163
	v_rcp_f32_e32 v180, v163
	v_add_f32_e32 v163, 1.0, v165
	v_mul_f32_e32 v165, 0xbfb8aa3b, v188
	v_exp_f32_e32 v165, v165
	v_rcp_f32_e32 v184, v163
	v_pk_add_f32 v[178:179], v[84:85], v[144:145]
	v_pk_add_f32 v[182:183], v[88:89], v[140:141]
	v_add_f32_e32 v163, 1.0, v165
	v_add_f32_e32 v165, 1.0, v175
	v_mul_f32_e32 v175, 0xbfb8aa3b, v181
	v_exp_f32_e32 v175, v175
	v_mul_f32_e32 v181, 0xbfb8aa3b, v185
	v_exp_f32_e32 v185, v181
	v_mul_f32_e32 v178, 0xbfb8aa3b, v178
	v_add_f32_e32 v175, 1.0, v175
	v_rcp_f32_e32 v181, v175
	v_add_f32_e32 v175, 1.0, v185
	v_mul_f32_e32 v185, 0xbfb8aa3b, v189
	v_exp_f32_e32 v188, v185
	v_mul_f32_e32 v185, 0xbfb8aa3b, v193
	v_exp_f32_e32 v189, v185
	v_exp_f32_e32 v178, v178
	v_mul_f32_e32 v182, 0xbfb8aa3b, v182
	v_rcp_f32_e32 v185, v175
	v_add_f32_e32 v175, 1.0, v188
	v_add_f32_e32 v188, 1.0, v189
	v_exp_f32_e32 v189, v182
	v_pk_add_f32 v[186:187], v[92:93], v[136:137]
	v_pk_add_f32 v[190:191], v[96:97], v[132:133]
	v_mul_f32_e32 v186, 0xbfb8aa3b, v186
	v_rcp_f32_e32 v192, v188
	v_add_f32_e32 v178, 1.0, v178
	v_exp_f32_e32 v188, v186
	v_mul_f32_e32 v186, 0xbfb8aa3b, v190
	v_rcp_f32_e32 v182, v178
	v_add_f32_e32 v178, 1.0, v189
	v_exp_f32_e32 v189, v186
	v_mul_f32_e32 v179, 0xbfb8aa3b, v179
	v_exp_f32_e32 v179, v179
	v_mul_f32_e32 v183, 0xbfb8aa3b, v183
	v_rcp_f32_e32 v186, v178
	v_add_f32_e32 v178, 1.0, v188
	v_add_f32_e32 v188, 1.0, v189
	v_exp_f32_e32 v189, v183
	v_mul_f32_e32 v187, 0xbfb8aa3b, v187
	v_rcp_f32_e32 v190, v188
	v_add_f32_e32 v179, 1.0, v179
	v_exp_f32_e32 v188, v187
	v_mul_f32_e32 v187, 0xbfb8aa3b, v191
	v_rcp_f32_e32 v183, v179
	v_add_f32_e32 v179, 1.0, v189
	v_exp_f32_e32 v189, v187
	v_rcp_f32_e32 v163, v163
	v_rcp_f32_e32 v175, v175
	v_or_b32_e32 v176, 32, v162
	v_ashrrev_i32_e32 v177, 31, v176
	v_lshlrev_b64 v[176:177], 13, v[176:177]
	v_rcp_f32_e32 v187, v179
	v_add_f32_e32 v179, 1.0, v188
	v_add_f32_e32 v188, 1.0, v189
	v_rcp_f32_e32 v178, v178
	v_rcp_f32_e32 v179, v179
	v_rcp_f32_e32 v191, v188
	v_lshl_add_u64 v[188:189], v[168:169], 0, v[176:177]
	v_cvt_pk_bf16_f32 v176, v163, v175
	v_lshlrev_b32_e32 v163, 16, v176
; __device__ __forceinline__ unsigned cvt_pk_bf16(float lo, float hi) { f32x2v_ v = {lo, hi}; bf16x2v_ b = __builtin_convertvector(v, bf16x2v_); return __builtin_bit_cast(unsigned, b); }
; __device__ __forceinline__ float bf_lo(unsigned w) { return __uint_as_float(w << 16); }
; __device__ __forceinline__ float bf_hi(unsigned w) { return __uint_as_float(w & 0xffff0000u); }
; __device__ __forceinline__ float sigmoid_f(float x) { return __builtin_amdgcn_rcpf(1.0f + __builtin_amdgcn_exp2f(-1.4426950408889634f * x)); }
;     __device__ __forceinline__ void operator()(const f32x4 (&acc)[2][2][4][2], const Unit& u, int wr, int wc, int fr, int fq) const {
;     ...
;             for (int ai = 0; ai < 2; ++ai)
; #pragma unroll
;                 for (int m = 0; m < 4; ++m) { bf16_t* rowp = GT + (size_t)(row0 + ai * HALF + m * 16) * 4096 + ch0;
;                     f32x4 a0 = acc[ai][0][m][0] + ba[0], a1 = acc[ai][0][m][1] + ba[1], b0 = acc[ai][1][m][0] + bb[0], b1 = acc[ai][1][m][1] + bb[1];
; #pragma unroll
;                     for (int e = 0; e < 4; ++e) { a0[e] = sigmoid_f(a0[e]); a1[e] = sigmoid_f(a1[e]); b0[e] = sigmoid_f(b0[e]); b1[e] = sigmoid_f(b1[e]); }
;                     u32x4 wb; wb.x = cvt_pk_bf16(b0[0], b0[1]); wb.y = cvt_pk_bf16(b0[2], b0[3]); wb.z = cvt_pk_bf16(b1[0], b1[1]); wb.w = cvt_pk_bf16(b1[2], b1[3]);
;                     const float q0 = __builtin_amdgcn_rcpf(fmaxf(bf_lo(wb.x), 1e-30f)), q1 = __builtin_amdgcn_rcpf(fmaxf(bf_hi(wb.x), 1e-30f)), q2 = __builtin_amdgcn_rcpf(fmaxf(bf_lo(wb.y), 1e-30f)), q3 = __builtin_amdgcn_rcpf(fmaxf(bf_hi(wb.y), 1e-30f));
;                     const float q4 = __builtin_amdgcn_rcpf(fmaxf(bf_lo(wb.z), 1e-30f)), q5 = __builtin_amdgcn_rcpf(fmaxf(bf_hi(wb.z), 1e-30f)), q6 = __builtin_amdgcn_rcpf(fmaxf(bf_lo(wb.w), 1e-30f)), q7 = __builtin_amdgcn_rcpf(fmaxf(bf_hi(wb.w), 1e-30f));
;                     u32x4 wr_; wr_.x = cvt_pk_bf16(a0[0] * q0, a0[1] * q1); wr_.y = cvt_pk_bf16(a0[2] * q2, a0[3] * q3); wr_.z = cvt_pk_bf16(a1[0] * q4, a1[1] * q5); wr_.w = cvt_pk_bf16(a1[2] * q6, a1[3] * q7);
;                     *(u32x4*)rowp = wr_; *(u32x4*)(rowp + 2048) = wb; }
	v_max_f32_e32 v163, v163, v163
	v_max_f32_e32 v163, 0xda24260, v163
	v_cvt_pk_bf16_f32 v177, v178, v179
	v_cvt_pk_bf16_f32 v179, v190, v191
	v_rcp_f32_e32 v190, v163
	v_and_b32_e32 v163, 0xffff0000, v176
	v_rcp_f32_e32 v165, v165
	v_max_f32_e32 v163, 0xda24260, v163
	v_rcp_f32_e32 v191, v163
	v_lshlrev_b32_e32 v163, 16, v177
	v_max_f32_e32 v163, v163, v163
	v_max_f32_e32 v163, 0xda24260, v163
	v_cvt_pk_bf16_f32 v178, v165, v192
	v_rcp_f32_e32 v192, v163
	v_and_b32_e32 v163, 0xffff0000, v177
	v_max_f32_e32 v163, 0xda24260, v163
	v_rcp_f32_e32 v193, v163
	v_lshlrev_b32_e32 v163, 16, v178
	v_max_f32_e32 v163, v163, v163
	v_max_f32_e32 v163, 0xda24260, v163
	v_rcp_f32_e32 v194, v163
	v_and_b32_e32 v163, 0xffff0000, v178
	v_max_f32_e32 v163, 0xda24260, v163
	v_rcp_f32_e32 v195, v163
	v_lshlrev_b32_e32 v163, 16, v179
	v_max_f32_e32 v163, v163, v163
	v_max_f32_e32 v163, 0xda24260, v163
	v_rcp_f32_e32 v196, v163
	v_and_b32_e32 v163, 0xffff0000, v179
	v_max_f32_e32 v163, 0xda24260, v163
	v_rcp_f32_e32 v197, v163
	v_pk_mul_f32 v[180:181], v[180:181], v[190:191]
	v_pk_mul_f32 v[182:183], v[182:183], v[192:193]
	v_cvt_pk_bf16_f32 v180, v180, v181
	v_cvt_pk_bf16_f32 v181, v182, v183
	v_pk_mul_f32 v[182:183], v[184:185], v[194:195]
	v_pk_mul_f32 v[184:185], v[186:187], v[196:197]
	v_cvt_pk_bf16_f32 v182, v182, v183
	v_cvt_pk_bf16_f32 v183, v184, v185
	global_store_dwordx4 v[188:189], v[180:183], off sc1
	v_pk_add_f32 v[184:185], v[70:71], v[138:139]
	v_pk_add_f32 v[192:193], v[78:79], v[130:131]
	v_add_co_u32_e32 v180, vcc, s81, v188
	v_mul_f32_e32 v165, 0xbfb8aa3b, v184
	s_nop 0
	v_addc_co_u32_e32 v181, vcc, 0, v189, vcc
	global_store_dwordx4 v[180:181], v[176:179], off sc1
	v_pk_add_f32 v[180:181], v[66:67], v[142:143]
	v_exp_f32_e32 v165, v165
	v_mul_f32_e32 v163, 0xbfb8aa3b, v180
	v_exp_f32_e32 v163, v163
	v_pk_add_f32 v[188:189], v[74:75], v[134:135]
	v_mul_f32_e32 v175, 0xbfb8aa3b, v192
	v_exp_f32_e32 v175, v175
	v_add_f32_e32 v163, 1.0, v163
	v_rcp_f32_e32 v180, v163
	v_add_f32_e32 v163, 1.0, v165
	v_mul_f32_e32 v165, 0xbfb8aa3b, v188
	v_exp_f32_e32 v165, v165
	v_rcp_f32_e32 v184, v163
	v_pk_add_f32 v[178:179], v[68:69], v[144:145]
	v_pk_add_f32 v[182:183], v[72:73], v[140:141]
	v_add_f32_e32 v163, 1.0, v165
	v_add_f32_e32 v165, 1.0, v175
	v_mul_f32_e32 v175, 0xbfb8aa3b, v181
	v_exp_f32_e32 v175, v175
	v_mul_f32_e32 v181, 0xbfb8aa3b, v185
	v_exp_f32_e32 v185, v181
	v_mul_f32_e32 v178, 0xbfb8aa3b, v178
	v_add_f32_e32 v175, 1.0, v175
	v_rcp_f32_e32 v181, v175
	v_add_f32_e32 v175, 1.0, v185
	v_mul_f32_e32 v185, 0xbfb8aa3b, v189
	v_exp_f32_e32 v188, v185
	v_mul_f32_e32 v185, 0xbfb8aa3b, v193
	v_exp_f32_e32 v189, v185
	v_exp_f32_e32 v178, v178
	v_mul_f32_e32 v182, 0xbfb8aa3b, v182
	v_rcp_f32_e32 v185, v175
	v_add_f32_e32 v175, 1.0, v188
	v_add_f32_e32 v188, 1.0, v189
	v_exp_f32_e32 v189, v182
	v_pk_add_f32 v[186:187], v[76:77], v[136:137]
	v_pk_add_f32 v[190:191], v[80:81], v[132:133]
	v_add_f32_e32 v178, 1.0, v178
	v_mul_f32_e32 v186, 0xbfb8aa3b, v186
	v_rcp_f32_e32 v182, v178
	v_add_f32_e32 v178, 1.0, v189
	v_exp_f32_e32 v189, v186
	v_mul_f32_e32 v186, 0xbfb8aa3b, v190
	v_exp_f32_e32 v190, v186
	v_mul_f32_e32 v179, 0xbfb8aa3b, v179
	v_exp_f32_e32 v179, v179
	v_mul_f32_e32 v183, 0xbfb8aa3b, v183
	v_rcp_f32_e32 v186, v178
	v_add_f32_e32 v178, 1.0, v189
	v_add_f32_e32 v189, 1.0, v190
	v_exp_f32_e32 v190, v183
	v_add_f32_e32 v179, 1.0, v179
	v_mul_f32_e32 v187, 0xbfb8aa3b, v187
	v_rcp_f32_e32 v183, v179
	v_add_f32_e32 v179, 1.0, v190
	v_exp_f32_e32 v190, v187
	v_rcp_f32_e32 v163, v163
	v_rcp_f32_e32 v175, v175
	v_mul_f32_e32 v187, 0xbfb8aa3b, v191
	v_or_b32_e32 v176, 48, v162
	v_exp_f32_e32 v191, v187
	v_ashrrev_i32_e32 v177, 31, v176
	v_lshlrev_b64 v[176:177], 13, v[176:177]
	v_rcp_f32_e32 v187, v179
	v_add_f32_e32 v179, 1.0, v190
	v_rcp_f32_e32 v165, v165
	v_rcp_f32_e32 v188, v188
	v_rcp_f32_e32 v178, v178
	v_rcp_f32_e32 v179, v179
	v_lshl_add_u64 v[168:169], v[168:169], 0, v[176:177]
	v_cvt_pk_bf16_f32 v176, v163, v175
	v_add_f32_e32 v190, 1.0, v191
	v_lshlrev_b32_e32 v163, 16, v176
	v_rcp_f32_e32 v189, v189
	v_rcp_f32_e32 v190, v190
	v_max_f32_e32 v163, v163, v163
	v_max_f32_e32 v163, 0xda24260, v163
	v_cvt_pk_bf16_f32 v177, v178, v179
	v_cvt_pk_bf16_f32 v178, v165, v188
	v_rcp_f32_e32 v188, v163
	v_and_b32_e32 v163, 0xffff0000, v176
	v_max_f32_e32 v163, 0xda24260, v163
	v_cvt_pk_bf16_f32 v179, v189, v190
	v_rcp_f32_e32 v189, v163
	v_lshlrev_b32_e32 v163, 16, v177
	v_max_f32_e32 v163, v163, v163
	v_max_f32_e32 v163, 0xda24260, v163
	v_rcp_f32_e32 v190, v163
	v_and_b32_e32 v163, 0xffff0000, v177
	v_max_f32_e32 v163, 0xda24260, v163
	v_rcp_f32_e32 v191, v163
	v_lshlrev_b32_e32 v163, 16, v178
	v_max_f32_e32 v163, v163, v163
	v_max_f32_e32 v163, 0xda24260, v163
	v_rcp_f32_e32 v192, v163
	v_and_b32_e32 v163, 0xffff0000, v178
	v_max_f32_e32 v163, 0xda24260, v163
	v_rcp_f32_e32 v193, v163
	v_lshlrev_b32_e32 v163, 16, v179
	v_max_f32_e32 v163, v163, v163
	v_max_f32_e32 v163, 0xda24260, v163
	v_rcp_f32_e32 v194, v163
	v_and_b32_e32 v163, 0xffff0000, v179
	v_max_f32_e32 v163, 0xda24260, v163
	v_rcp_f32_e32 v195, v163
	v_pk_mul_f32 v[180:181], v[180:181], v[188:189]
	v_pk_mul_f32 v[182:183], v[182:183], v[190:191]
	v_cvt_pk_bf16_f32 v180, v180, v181
	v_cvt_pk_bf16_f32 v181, v182, v183
	v_pk_mul_f32 v[182:183], v[184:185], v[192:193]
	v_pk_mul_f32 v[184:185], v[186:187], v[194:195]
	v_cvt_pk_bf16_f32 v182, v182, v183
	v_cvt_pk_bf16_f32 v183, v184, v185
	global_store_dwordx4 v[168:169], v[180:183], off sc1
	v_add_co_u32_e32 v168, vcc, s81, v168
	s_nop 0
	v_pk_add_f32 v[180:181], v[62:63], v[138:139]
	v_addc_co_u32_e32 v169, vcc, 0, v169, vcc
; __device__ __forceinline__ unsigned cvt_pk_bf16(float lo, float hi) { f32x2v_ v = {lo, hi}; bf16x2v_ b = __builtin_convertvector(v, bf16x2v_); return __builtin_bit_cast(unsigned, b); }
; __device__ __forceinline__ float bf_lo(unsigned w) { return __uint_as_float(w << 16); }
; __device__ __forceinline__ float bf_hi(unsigned w) { return __uint_as_float(w & 0xffff0000u); }
; __device__ __forceinline__ float sigmoid_f(float x) { return __builtin_amdgcn_rcpf(1.0f + __builtin_amdgcn_exp2f(-1.4426950408889634f * x)); }
;     __device__ __forceinline__ void operator()(const f32x4 (&acc)[2][2][4][2], const Unit& u, int wr, int wc, int fr, int fq) const {
;     ...
;             for (int ai = 0; ai < 2; ++ai)
; #pragma unroll
;                 for (int m = 0; m < 4; ++m) { bf16_t* rowp = GT + (size_t)(row0 + ai * HALF + m * 16) * 4096 + ch0;
;                     f32x4 a0 = acc[ai][0][m][0] + ba[0], a1 = acc[ai][0][m][1] + ba[1], b0 = acc[ai][1][m][0] + bb[0], b1 = acc[ai][1][m][1] + bb[1];
; #pragma unroll
;                     for (int e = 0; e < 4; ++e) { a0[e] = sigmoid_f(a0[e]); a1[e] = sigmoid_f(a1[e]); b0[e] = sigmoid_f(b0[e]); b1[e] = sigmoid_f(b1[e]); }
;                     u32x4 wb; wb.x = cvt_pk_bf16(b0[0], b0[1]); wb.y = cvt_pk_bf16(b0[2], b0[3]); wb.z = cvt_pk_bf16(b1[0], b1[1]); wb.w = cvt_pk_bf16(b1[2], b1[3]);
;                     const float q0 = __builtin_amdgcn_rcpf(fmaxf(bf_lo(wb.x), 1e-30f)), q1 = __builtin_amdgcn_rcpf(fmaxf(bf_hi(wb.x), 1e-30f)), q2 = __builtin_amdgcn_rcpf(fmaxf(bf_lo(wb.y), 1e-30f)), q3 = __builtin_amdgcn_rcpf(fmaxf(bf_hi(wb.y), 1e-30f));
;                     const float q4 = __builtin_amdgcn_rcpf(fmaxf(bf_lo(wb.z), 1e-30f)), q5 = __builtin_amdgcn_rcpf(fmaxf(bf_hi(wb.z), 1e-30f)), q6 = __builtin_amdgcn_rcpf(fmaxf(bf_lo(wb.w), 1e-30f)), q7 = __builtin_amdgcn_rcpf(fmaxf(bf_hi(wb.w), 1e-30f));
;                     u32x4 wr_; wr_.x = cvt_pk_bf16(a0[0] * q0, a0[1] * q1); wr_.y = cvt_pk_bf16(a0[2] * q2, a0[3] * q3); wr_.z = cvt_pk_bf16(a1[0] * q4, a1[1] * q5); wr_.w = cvt_pk_bf16(a1[2] * q6, a1[3] * q7);
;                     *(u32x4*)rowp = wr_; *(u32x4*)(rowp + 2048) = wb; }
	global_store_dwordx4 v[168:169], v[176:179], off sc1
	v_mul_f32_e32 v165, 0xbfb8aa3b, v180
	v_exp_f32_e32 v165, v165
	v_pk_add_f32 v[176:177], v[58:59], v[142:143]
	v_pk_add_f32 v[184:185], v[50:51], v[134:135]
	v_mul_f32_e32 v163, 0xbfb8aa3b, v176
	v_exp_f32_e32 v163, v163
	v_pk_add_f32 v[188:189], v[54:55], v[130:131]
	v_mul_f32_e32 v176, 0xbfb8aa3b, v181
	v_mul_f32_e32 v175, 0xbfb8aa3b, v188
	v_add_f32_e32 v163, 1.0, v163
	v_rcp_f32_e32 v180, v163
	v_add_f32_e32 v163, 1.0, v165
	v_mul_f32_e32 v165, 0xbfb8aa3b, v184
	v_exp_f32_e32 v165, v165
	v_exp_f32_e32 v175, v175
	v_rcp_f32_e32 v184, v163
	v_exp_f32_e32 v176, v176
	v_add_f32_e32 v163, 1.0, v165
	v_add_f32_e32 v165, 1.0, v175
	v_mul_f32_e32 v175, 0xbfb8aa3b, v177
	v_exp_f32_e32 v175, v175
	v_mul_f32_e32 v177, 0xbfb8aa3b, v189
	v_exp_f32_e32 v177, v177
	v_pk_add_f32 v[178:179], v[64:65], v[140:141]
	v_add_f32_e32 v175, 1.0, v175
	v_rcp_f32_e32 v181, v175
	v_add_f32_e32 v175, 1.0, v176
	v_mul_f32_e32 v176, 0xbfb8aa3b, v185
	v_exp_f32_e32 v176, v176
	v_rcp_f32_e32 v185, v175
	v_pk_add_f32 v[182:183], v[52:53], v[136:137]
	v_pk_add_f32 v[186:187], v[56:57], v[132:133]
	v_add_f32_e32 v175, 1.0, v176
	v_add_f32_e32 v176, 1.0, v177
	v_mul_f32_e32 v177, 0xbfb8aa3b, v178
	v_exp_f32_e32 v177, v177
	v_rcp_f32_e32 v178, v176
	v_mul_f32_e32 v179, 0xbfb8aa3b, v179
	v_exp_f32_e32 v179, v179
	v_add_f32_e32 v176, 1.0, v177
	v_mul_f32_e32 v177, 0xbfb8aa3b, v182
	v_exp_f32_e32 v177, v177
	v_mul_f32_e32 v182, 0xbfb8aa3b, v186
	v_exp_f32_e32 v182, v182
	v_rcp_f32_e32 v186, v176
	v_add_f32_e32 v176, 1.0, v177
	v_rcp_f32_e32 v177, v176
	v_add_f32_e32 v176, 1.0, v182
	v_rcp_f32_e32 v182, v176
	v_add_f32_e32 v176, 1.0, v179
	v_mul_f32_e32 v179, 0xbfb8aa3b, v183
	v_exp_f32_e32 v179, v179
	v_mul_f32_e32 v183, 0xbfb8aa3b, v187
	v_exp_f32_e32 v183, v183
	v_rcp_f32_e32 v163, v163
	v_rcp_f32_e32 v175, v175
	v_rcp_f32_e32 v187, v176
	v_add_f32_e32 v176, 1.0, v179
	v_rcp_f32_e32 v179, v176
	v_add_f32_e32 v176, 1.0, v183
	v_rcp_f32_e32 v183, v176
	v_cvt_pk_bf16_f32 v176, v163, v175
	v_lshlrev_b32_e32 v163, 16, v176
	v_max_f32_e32 v163, v163, v163
	v_max_f32_e32 v163, 0xda24260, v163
	v_cvt_pk_bf16_f32 v177, v177, v179
	v_cvt_pk_bf16_f32 v179, v182, v183
	v_rcp_f32_e32 v182, v163
	v_and_b32_e32 v163, 0xffff0000, v176
	v_max_f32_e32 v163, 0xda24260, v163
	v_rcp_f32_e32 v165, v165
	v_rcp_f32_e32 v183, v163
	v_lshlrev_b32_e32 v163, 16, v177
	v_max_f32_e32 v163, v163, v163
	v_max_f32_e32 v163, 0xda24260, v163
	v_rcp_f32_e32 v188, v163
	v_and_b32_e32 v163, 0xffff0000, v177
	v_cvt_pk_bf16_f32 v178, v165, v178
	v_max_f32_e32 v163, 0xda24260, v163
	v_rcp_f32_e32 v189, v163
	v_lshlrev_b32_e32 v163, 16, v178
	v_pk_add_f32 v[168:169], v[60:61], v[144:145]
	v_max_f32_e32 v163, v163, v163
	v_mul_f32_e32 v168, 0xbfb8aa3b, v168
	v_mul_f32_e32 v169, 0xbfb8aa3b, v169
	v_max_f32_e32 v163, 0xda24260, v163
	v_exp_f32_e32 v168, v168
	v_exp_f32_e32 v169, v169
	v_rcp_f32_e32 v190, v163
	v_and_b32_e32 v163, 0xffff0000, v178
	v_max_f32_e32 v163, 0xda24260, v163
	v_rcp_f32_e32 v191, v163
	v_lshlrev_b32_e32 v163, 16, v179
	v_max_f32_e32 v163, v163, v163
	v_add_f32_e32 v168, 1.0, v168
	v_add_f32_e32 v169, 1.0, v169
	v_max_f32_e32 v163, 0xda24260, v163
	v_rcp_f32_e32 v168, v168
	v_rcp_f32_e32 v169, v169
	v_rcp_f32_e32 v192, v163
	v_and_b32_e32 v163, 0xffff0000, v179
	v_max_f32_e32 v163, 0xda24260, v163
	v_rcp_f32_e32 v193, v163
	v_pk_mul_f32 v[180:181], v[180:181], v[182:183]
	v_pk_mul_f32 v[168:169], v[168:169], v[188:189]
	v_cvt_pk_bf16_f32 v180, v180, v181
	v_cvt_pk_bf16_f32 v181, v168, v169
	v_pk_mul_f32 v[168:169], v[184:185], v[190:191]
	v_pk_add_f32 v[184:185], v[34:35], v[134:135]
	v_cvt_pk_bf16_f32 v182, v168, v169
	v_pk_mul_f32 v[168:169], v[186:187], v[192:193]
	v_pk_add_f32 v[188:189], v[38:39], v[130:131]
	v_cvt_pk_bf16_f32 v183, v168, v169
	v_add_co_u32_e32 v168, vcc, s82, v166
	v_mul_f32_e32 v175, 0xbfb8aa3b, v188
	s_nop 0
	v_addc_co_u32_e32 v169, vcc, 0, v167, vcc
	global_store_dwordx4 v[168:169], v[180:183], off offset:-4096 sc1
	global_store_dwordx4 v[168:169], v[176:179], off sc1
	v_exp_f32_e32 v175, v175
	v_pk_add_f32 v[180:181], v[46:47], v[138:139]
	v_pk_add_f32 v[176:177], v[42:43], v[142:143]
	v_mul_f32_e32 v165, 0xbfb8aa3b, v180
	v_mul_f32_e32 v163, 0xbfb8aa3b, v176
	v_exp_f32_e32 v163, v163
	v_exp_f32_e32 v165, v165
	v_mul_f32_e32 v176, 0xbfb8aa3b, v181
	v_exp_f32_e32 v176, v176
	v_add_f32_e32 v163, 1.0, v163
	v_rcp_f32_e32 v180, v163
	v_add_f32_e32 v163, 1.0, v165
	v_mul_f32_e32 v165, 0xbfb8aa3b, v184
	v_exp_f32_e32 v165, v165
	v_rcp_f32_e32 v184, v163
	v_pk_add_f32 v[178:179], v[48:49], v[140:141]
	v_pk_add_f32 v[182:183], v[36:37], v[136:137]
	v_add_f32_e32 v163, 1.0, v165
	v_add_f32_e32 v165, 1.0, v175
	v_mul_f32_e32 v175, 0xbfb8aa3b, v177
	v_exp_f32_e32 v175, v175
	v_mul_f32_e32 v177, 0xbfb8aa3b, v189
	v_exp_f32_e32 v177, v177
	v_pk_add_f32 v[186:187], v[40:41], v[132:133]
	v_add_f32_e32 v175, 1.0, v175
	v_rcp_f32_e32 v181, v175
	v_add_f32_e32 v175, 1.0, v176
	v_mul_f32_e32 v176, 0xbfb8aa3b, v185
	v_exp_f32_e32 v176, v176
	v_rcp_f32_e32 v185, v175
	v_mul_f32_e32 v179, 0xbfb8aa3b, v179
	v_exp_f32_e32 v179, v179
	v_add_f32_e32 v175, 1.0, v176
	v_add_f32_e32 v176, 1.0, v177
	v_mul_f32_e32 v177, 0xbfb8aa3b, v178
	v_exp_f32_e32 v177, v177
	v_rcp_f32_e32 v178, v176
	v_rcp_f32_e32 v163, v163
	v_rcp_f32_e32 v175, v175
	v_add_f32_e32 v176, 1.0, v177
	v_mul_f32_e32 v177, 0xbfb8aa3b, v182
	v_exp_f32_e32 v177, v177
	v_mul_f32_e32 v182, 0xbfb8aa3b, v186
	v_exp_f32_e32 v182, v182
	v_rcp_f32_e32 v186, v176
	v_add_f32_e32 v176, 1.0, v177
	v_rcp_f32_e32 v177, v176
	v_add_f32_e32 v176, 1.0, v182
	v_rcp_f32_e32 v182, v176
; __device__ __forceinline__ unsigned cvt_pk_bf16(float lo, float hi) { f32x2v_ v = {lo, hi}; bf16x2v_ b = __builtin_convertvector(v, bf16x2v_); return __builtin_bit_cast(unsigned, b); }
; __device__ __forceinline__ float bf_lo(unsigned w) { return __uint_as_float(w << 16); }
; __device__ __forceinline__ float bf_hi(unsigned w) { return __uint_as_float(w & 0xffff0000u); }
; __device__ __forceinline__ float sigmoid_f(float x) { return __builtin_amdgcn_rcpf(1.0f + __builtin_amdgcn_exp2f(-1.4426950408889634f * x)); }
;     __device__ __forceinline__ void operator()(const f32x4 (&acc)[2][2][4][2], const Unit& u, int wr, int wc, int fr, int fq) const {
;     ...
;             for (int ai = 0; ai < 2; ++ai)
; #pragma unroll
;                 for (int m = 0; m < 4; ++m) { bf16_t* rowp = GT + (size_t)(row0 + ai * HALF + m * 16) * 4096 + ch0;
;                     f32x4 a0 = acc[ai][0][m][0] + ba[0], a1 = acc[ai][0][m][1] + ba[1], b0 = acc[ai][1][m][0] + bb[0], b1 = acc[ai][1][m][1] + bb[1];
; #pragma unroll
;                     for (int e = 0; e < 4; ++e) { a0[e] = sigmoid_f(a0[e]); a1[e] = sigmoid_f(a1[e]); b0[e] = sigmoid_f(b0[e]); b1[e] = sigmoid_f(b1[e]); }
;                     u32x4 wb; wb.x = cvt_pk_bf16(b0[0], b0[1]); wb.y = cvt_pk_bf16(b0[2], b0[3]); wb.z = cvt_pk_bf16(b1[0], b1[1]); wb.w = cvt_pk_bf16(b1[2], b1[3]);
;                     const float q0 = __builtin_amdgcn_rcpf(fmaxf(bf_lo(wb.x), 1e-30f)), q1 = __builtin_amdgcn_rcpf(fmaxf(bf_hi(wb.x), 1e-30f)), q2 = __builtin_amdgcn_rcpf(fmaxf(bf_lo(wb.y), 1e-30f)), q3 = __builtin_amdgcn_rcpf(fmaxf(bf_hi(wb.y), 1e-30f));
;                     const float q4 = __builtin_amdgcn_rcpf(fmaxf(bf_lo(wb.z), 1e-30f)), q5 = __builtin_amdgcn_rcpf(fmaxf(bf_hi(wb.z), 1e-30f)), q6 = __builtin_amdgcn_rcpf(fmaxf(bf_lo(wb.w), 1e-30f)), q7 = __builtin_amdgcn_rcpf(fmaxf(bf_hi(wb.w), 1e-30f));
;                     u32x4 wr_; wr_.x = cvt_pk_bf16(a0[0] * q0, a0[1] * q1); wr_.y = cvt_pk_bf16(a0[2] * q2, a0[3] * q3); wr_.z = cvt_pk_bf16(a1[0] * q4, a1[1] * q5); wr_.w = cvt_pk_bf16(a1[2] * q6, a1[3] * q7);
;                     *(u32x4*)rowp = wr_; *(u32x4*)(rowp + 2048) = wb; }
	v_add_f32_e32 v176, 1.0, v179
	v_mul_f32_e32 v179, 0xbfb8aa3b, v183
	v_exp_f32_e32 v179, v179
	v_mul_f32_e32 v183, 0xbfb8aa3b, v187
	v_exp_f32_e32 v183, v183
	v_rcp_f32_e32 v187, v176
	v_add_f32_e32 v176, 1.0, v179
	v_rcp_f32_e32 v179, v176
	v_add_f32_e32 v176, 1.0, v183
	v_rcp_f32_e32 v183, v176
	v_cvt_pk_bf16_f32 v176, v163, v175
	v_lshlrev_b32_e32 v163, 16, v176
	v_max_f32_e32 v163, v163, v163
	v_max_f32_e32 v163, 0xda24260, v163
	v_cvt_pk_bf16_f32 v177, v177, v179
	v_cvt_pk_bf16_f32 v179, v182, v183
	v_rcp_f32_e32 v182, v163
	v_and_b32_e32 v163, 0xffff0000, v176
	v_max_f32_e32 v163, 0xda24260, v163
	v_rcp_f32_e32 v165, v165
	v_rcp_f32_e32 v183, v163
	v_lshlrev_b32_e32 v163, 16, v177
	v_max_f32_e32 v163, v163, v163
	v_max_f32_e32 v163, 0xda24260, v163
	v_rcp_f32_e32 v188, v163
	v_and_b32_e32 v163, 0xffff0000, v177
	v_cvt_pk_bf16_f32 v178, v165, v178
	v_max_f32_e32 v163, 0xda24260, v163
	v_rcp_f32_e32 v189, v163
	v_lshlrev_b32_e32 v163, 16, v178
	v_pk_add_f32 v[168:169], v[44:45], v[144:145]
	v_max_f32_e32 v163, v163, v163
	v_mul_f32_e32 v168, 0xbfb8aa3b, v168
	v_mul_f32_e32 v169, 0xbfb8aa3b, v169
	v_max_f32_e32 v163, 0xda24260, v163
	v_exp_f32_e32 v168, v168
	v_exp_f32_e32 v169, v169
	v_rcp_f32_e32 v190, v163
	v_and_b32_e32 v163, 0xffff0000, v178
	v_max_f32_e32 v163, 0xda24260, v163
	v_rcp_f32_e32 v191, v163
	v_lshlrev_b32_e32 v163, 16, v179
	v_max_f32_e32 v163, v163, v163
	v_add_f32_e32 v168, 1.0, v168
	v_add_f32_e32 v169, 1.0, v169
	v_max_f32_e32 v163, 0xda24260, v163
	v_rcp_f32_e32 v168, v168
	v_rcp_f32_e32 v169, v169
	v_rcp_f32_e32 v192, v163
	v_and_b32_e32 v163, 0xffff0000, v179
	v_max_f32_e32 v163, 0xda24260, v163
	v_rcp_f32_e32 v193, v163
	v_pk_mul_f32 v[180:181], v[180:181], v[182:183]
	v_pk_mul_f32 v[168:169], v[168:169], v[188:189]
	v_cvt_pk_bf16_f32 v180, v180, v181
	v_cvt_pk_bf16_f32 v181, v168, v169
	v_pk_mul_f32 v[168:169], v[184:185], v[190:191]
	v_pk_add_f32 v[184:185], v[26:27], v[134:135]
	v_cvt_pk_bf16_f32 v182, v168, v169
	v_pk_mul_f32 v[168:169], v[186:187], v[192:193]
	v_pk_add_f32 v[188:189], v[30:31], v[130:131]
	v_cvt_pk_bf16_f32 v183, v168, v169
	v_add_co_u32_e32 v168, vcc, s83, v166
	v_mul_f32_e32 v175, 0xbfb8aa3b, v188
	s_nop 0
	v_addc_co_u32_e32 v169, vcc, 0, v167, vcc
	global_store_dwordx4 v[168:169], v[180:183], off offset:-4096 sc1
	global_store_dwordx4 v[168:169], v[176:179], off sc1
	v_exp_f32_e32 v175, v175
	v_pk_add_f32 v[180:181], v[22:23], v[138:139]
	v_pk_add_f32 v[176:177], v[18:19], v[142:143]
	v_mul_f32_e32 v165, 0xbfb8aa3b, v180
	v_mul_f32_e32 v163, 0xbfb8aa3b, v176
	v_exp_f32_e32 v163, v163
	v_exp_f32_e32 v165, v165
	v_mul_f32_e32 v176, 0xbfb8aa3b, v181
	v_exp_f32_e32 v176, v176
	v_add_f32_e32 v163, 1.0, v163
	v_rcp_f32_e32 v180, v163
	v_add_f32_e32 v163, 1.0, v165
	v_mul_f32_e32 v165, 0xbfb8aa3b, v184
	v_exp_f32_e32 v165, v165
	v_rcp_f32_e32 v184, v163
	v_pk_add_f32 v[178:179], v[24:25], v[140:141]
	v_pk_add_f32 v[182:183], v[28:29], v[136:137]
	v_add_f32_e32 v163, 1.0, v165
	v_add_f32_e32 v165, 1.0, v175
	v_mul_f32_e32 v175, 0xbfb8aa3b, v177
	v_exp_f32_e32 v175, v175
	v_mul_f32_e32 v177, 0xbfb8aa3b, v189
	v_exp_f32_e32 v177, v177
	v_pk_add_f32 v[186:187], v[32:33], v[132:133]
	v_add_f32_e32 v175, 1.0, v175
	v_rcp_f32_e32 v181, v175
	v_add_f32_e32 v175, 1.0, v176
	v_mul_f32_e32 v176, 0xbfb8aa3b, v185
	v_exp_f32_e32 v176, v176
	v_rcp_f32_e32 v185, v175
	v_mul_f32_e32 v179, 0xbfb8aa3b, v179
	v_exp_f32_e32 v179, v179
	v_add_f32_e32 v175, 1.0, v176
	v_add_f32_e32 v176, 1.0, v177
	v_mul_f32_e32 v177, 0xbfb8aa3b, v178
	v_exp_f32_e32 v177, v177
	v_rcp_f32_e32 v178, v176
	v_rcp_f32_e32 v163, v163
	v_rcp_f32_e32 v175, v175
	v_add_f32_e32 v176, 1.0, v177
	v_mul_f32_e32 v177, 0xbfb8aa3b, v182
	v_exp_f32_e32 v177, v177
	v_mul_f32_e32 v182, 0xbfb8aa3b, v186
	v_exp_f32_e32 v182, v182
	v_rcp_f32_e32 v186, v176
	v_add_f32_e32 v176, 1.0, v177
	v_rcp_f32_e32 v177, v176
	v_add_f32_e32 v176, 1.0, v182
	v_rcp_f32_e32 v182, v176
	v_add_f32_e32 v176, 1.0, v179
	v_mul_f32_e32 v179, 0xbfb8aa3b, v183
	v_exp_f32_e32 v179, v179
	v_mul_f32_e32 v183, 0xbfb8aa3b, v187
	v_exp_f32_e32 v183, v183
	v_rcp_f32_e32 v187, v176
	v_add_f32_e32 v176, 1.0, v179
	v_rcp_f32_e32 v179, v176
	v_add_f32_e32 v176, 1.0, v183
	v_rcp_f32_e32 v183, v176
	v_cvt_pk_bf16_f32 v176, v163, v175
	v_lshlrev_b32_e32 v163, 16, v176
	v_max_f32_e32 v163, v163, v163
	v_max_f32_e32 v163, 0xda24260, v163
	v_cvt_pk_bf16_f32 v177, v177, v179
	v_cvt_pk_bf16_f32 v179, v182, v183
	v_rcp_f32_e32 v182, v163
	v_and_b32_e32 v163, 0xffff0000, v176
	v_max_f32_e32 v163, 0xda24260, v163
	v_rcp_f32_e32 v165, v165
	v_rcp_f32_e32 v183, v163
	v_lshlrev_b32_e32 v163, 16, v177
	v_max_f32_e32 v163, v163, v163
	v_max_f32_e32 v163, 0xda24260, v163
	v_rcp_f32_e32 v188, v163
	v_and_b32_e32 v163, 0xffff0000, v177
	v_cvt_pk_bf16_f32 v178, v165, v178
	v_max_f32_e32 v163, 0xda24260, v163
	v_rcp_f32_e32 v189, v163
	v_lshlrev_b32_e32 v163, 16, v178
	v_max_f32_e32 v163, v163, v163
	v_max_f32_e32 v163, 0xda24260, v163
	v_rcp_f32_e32 v190, v163
	v_and_b32_e32 v163, 0xffff0000, v178
	v_max_f32_e32 v163, 0xda24260, v163
	v_rcp_f32_e32 v191, v163
; __device__ __forceinline__ unsigned cvt_pk_bf16(float lo, float hi) { f32x2v_ v = {lo, hi}; bf16x2v_ b = __builtin_convertvector(v, bf16x2v_); return __builtin_bit_cast(unsigned, b); }
; __device__ __forceinline__ float bf_lo(unsigned w) { return __uint_as_float(w << 16); }
; __device__ __forceinline__ float bf_hi(unsigned w) { return __uint_as_float(w & 0xffff0000u); }
; __device__ __forceinline__ float sigmoid_f(float x) { return __builtin_amdgcn_rcpf(1.0f + __builtin_amdgcn_exp2f(-1.4426950408889634f * x)); }
;     __device__ __forceinline__ void operator()(const f32x4 (&acc)[2][2][4][2], const Unit& u, int wr, int wc, int fr, int fq) const {
;     ...
;             for (int ai = 0; ai < 2; ++ai)
; #pragma unroll
;                 for (int m = 0; m < 4; ++m) { bf16_t* rowp = GT + (size_t)(row0 + ai * HALF + m * 16) * 4096 + ch0;
;                     f32x4 a0 = acc[ai][0][m][0] + ba[0], a1 = acc[ai][0][m][1] + ba[1], b0 = acc[ai][1][m][0] + bb[0], b1 = acc[ai][1][m][1] + bb[1];
; #pragma unroll
;                     for (int e = 0; e < 4; ++e) { a0[e] = sigmoid_f(a0[e]); a1[e] = sigmoid_f(a1[e]); b0[e] = sigmoid_f(b0[e]); b1[e] = sigmoid_f(b1[e]); }
;                     u32x4 wb; wb.x = cvt_pk_bf16(b0[0], b0[1]); wb.y = cvt_pk_bf16(b0[2], b0[3]); wb.z = cvt_pk_bf16(b1[0], b1[1]); wb.w = cvt_pk_bf16(b1[2], b1[3]);
;                     const float q0 = __builtin_amdgcn_rcpf(fmaxf(bf_lo(wb.x), 1e-30f)), q1 = __builtin_amdgcn_rcpf(fmaxf(bf_hi(wb.x), 1e-30f)), q2 = __builtin_amdgcn_rcpf(fmaxf(bf_lo(wb.y), 1e-30f)), q3 = __builtin_amdgcn_rcpf(fmaxf(bf_hi(wb.y), 1e-30f));
;                     const float q4 = __builtin_amdgcn_rcpf(fmaxf(bf_lo(wb.z), 1e-30f)), q5 = __builtin_amdgcn_rcpf(fmaxf(bf_hi(wb.z), 1e-30f)), q6 = __builtin_amdgcn_rcpf(fmaxf(bf_lo(wb.w), 1e-30f)), q7 = __builtin_amdgcn_rcpf(fmaxf(bf_hi(wb.w), 1e-30f));
;                     u32x4 wr_; wr_.x = cvt_pk_bf16(a0[0] * q0, a0[1] * q1); wr_.y = cvt_pk_bf16(a0[2] * q2, a0[3] * q3); wr_.z = cvt_pk_bf16(a1[0] * q4, a1[1] * q5); wr_.w = cvt_pk_bf16(a1[2] * q6, a1[3] * q7);
;                     *(u32x4*)rowp = wr_; *(u32x4*)(rowp + 2048) = wb; }
	v_lshlrev_b32_e32 v163, 16, v179
	v_max_f32_e32 v163, v163, v163
	v_max_f32_e32 v163, 0xda24260, v163
	v_rcp_f32_e32 v192, v163
	v_and_b32_e32 v163, 0xffff0000, v179
	v_pk_add_f32 v[142:143], v[6:7], v[142:143]
	v_pk_add_f32 v[138:139], v[14:15], v[138:139]
	v_max_f32_e32 v163, 0xda24260, v163
	v_mul_f32_e32 v142, 0xbfb8aa3b, v142
	v_mul_f32_e32 v138, 0xbfb8aa3b, v138
	v_rcp_f32_e32 v193, v163
	v_exp_f32_e32 v142, v142
	v_exp_f32_e32 v163, v138
	v_pk_add_f32 v[130:131], v[2:3], v[130:131]
	v_mul_f32_e32 v143, 0xbfb8aa3b, v143
	v_mul_f32_e32 v130, 0xbfb8aa3b, v130
	v_exp_f32_e32 v130, v130
	v_pk_add_f32 v[134:135], v[10:11], v[134:135]
	v_exp_f32_e32 v143, v143
	v_mul_f32_e32 v139, 0xbfb8aa3b, v139
	v_add_f32_e32 v138, 1.0, v142
	v_add_f32_e32 v142, 1.0, v163
	v_exp_f32_e32 v163, v139
	v_mul_f32_e32 v135, 0xbfb8aa3b, v135
	v_exp_f32_e32 v135, v135
	v_add_f32_e32 v130, 1.0, v130
	v_rcp_f32_e32 v165, v130
	v_add_f32_e32 v130, 1.0, v143
	v_pk_add_f32 v[168:169], v[20:21], v[144:145]
	v_pk_add_f32 v[144:145], v[8:9], v[144:145]
	v_rcp_f32_e32 v139, v130
	v_add_f32_e32 v130, 1.0, v163
	v_mul_f32_e32 v131, 0xbfb8aa3b, v131
	v_mul_f32_e32 v168, 0xbfb8aa3b, v168
	v_mul_f32_e32 v169, 0xbfb8aa3b, v169
	v_exp_f32_e32 v131, v131
	v_rcp_f32_e32 v143, v130
	v_add_f32_e32 v130, 1.0, v135
	v_mul_f32_e32 v135, 0xbfb8aa3b, v144
	v_exp_f32_e32 v168, v168
	v_exp_f32_e32 v169, v169
	v_exp_f32_e32 v135, v135
	v_pk_add_f32 v[140:141], v[16:17], v[140:141]
	v_pk_add_f32 v[136:137], v[12:13], v[136:137]
	v_add_f32_e32 v131, 1.0, v131
	v_mul_f32_e32 v140, 0xbfb8aa3b, v140
	v_add_f32_e32 v168, 1.0, v168
	v_add_f32_e32 v169, 1.0, v169
	v_exp_f32_e32 v144, v140
	v_rcp_f32_e32 v163, v131
	v_add_f32_e32 v131, 1.0, v135
	v_mul_f32_e32 v135, 0xbfb8aa3b, v136
	v_rcp_f32_e32 v168, v168
	v_rcp_f32_e32 v169, v169
	v_exp_f32_e32 v135, v135
	v_pk_add_f32 v[132:133], v[4:5], v[132:133]
	v_rcp_f32_e32 v140, v131
	v_add_f32_e32 v131, 1.0, v144
	v_mul_f32_e32 v132, 0xbfb8aa3b, v132
	v_pk_mul_f32 v[180:181], v[180:181], v[182:183]
	v_pk_mul_f32 v[168:169], v[168:169], v[188:189]
	v_exp_f32_e32 v132, v132
	v_rcp_f32_e32 v144, v131
	v_add_f32_e32 v131, 1.0, v135
	v_mul_f32_e32 v135, 0xbfb8aa3b, v145
	v_cvt_pk_bf16_f32 v180, v180, v181
	v_cvt_pk_bf16_f32 v181, v168, v169
	v_pk_mul_f32 v[168:169], v[184:185], v[190:191]
	v_exp_f32_e32 v135, v135
	v_cvt_pk_bf16_f32 v182, v168, v169
	v_pk_mul_f32 v[168:169], v[186:187], v[192:193]
	v_add_f32_e32 v132, 1.0, v132
	v_cvt_pk_bf16_f32 v183, v168, v169
	v_add_co_u32_e32 v168, vcc, s84, v166
	v_mul_f32_e32 v136, 0xbfb8aa3b, v141
	s_nop 0
	v_addc_co_u32_e32 v169, vcc, 0, v167, vcc
	global_store_dwordx4 v[168:169], v[180:183], off offset:-4096 sc1
	global_store_dwordx4 v[168:169], v[176:179], off sc1
	v_exp_f32_e32 v136, v136
	v_rcp_f32_e32 v168, v132
	v_add_f32_e32 v132, 1.0, v135
	v_mul_f32_e32 v135, 0xbfb8aa3b, v137
	v_exp_f32_e32 v135, v135
	v_rcp_f32_e32 v141, v132
	v_add_f32_e32 v132, 1.0, v136
	v_mul_f32_e32 v133, 0xbfb8aa3b, v133
	v_exp_f32_e32 v133, v133
	v_rcp_f32_e32 v145, v132
	v_add_f32_e32 v132, 1.0, v135
	v_mul_f32_e32 v134, 0xbfb8aa3b, v134
	v_rcp_f32_e32 v131, v131
	v_rcp_f32_e32 v132, v132
	v_exp_f32_e32 v134, v134
	v_add_f32_e32 v133, 1.0, v133
	v_rcp_f32_e32 v133, v133
	v_cvt_pk_bf16_f32 v131, v131, v132
	v_cvt_pk_bf16_f32 v132, v165, v163
	v_add_f32_e32 v134, 1.0, v134
	v_lshlrev_b32_e32 v163, 16, v132
	v_rcp_f32_e32 v134, v134
	v_rcp_f32_e32 v130, v130
	v_max_f32_e32 v163, v163, v163
	v_max_f32_e32 v163, 0xda24260, v163
	v_cvt_pk_bf16_f32 v133, v168, v133
	v_rcp_f32_e32 v168, v163
	v_and_b32_e32 v163, 0xffff0000, v132
	v_max_f32_e32 v163, 0xda24260, v163
	v_cvt_pk_bf16_f32 v130, v134, v130
	v_rcp_f32_e32 v169, v163
	v_lshlrev_b32_e32 v163, 16, v133
	v_lshlrev_b32_e32 v134, 16, v130
	v_lshlrev_b32_e32 v136, 16, v131
	v_max_f32_e32 v163, v163, v163
	v_max_f32_e32 v134, v134, v134
	v_and_b32_e32 v135, 0xffff0000, v130
	v_max_f32_e32 v136, v136, v136
	v_and_b32_e32 v137, 0xffff0000, v131
	v_max_f32_e32 v163, 0xda24260, v163
	v_max_f32_e32 v134, 0xda24260, v134
	v_max_f32_e32 v135, 0xda24260, v135
	v_max_f32_e32 v136, 0xda24260, v136
	v_max_f32_e32 v137, 0xda24260, v137
	v_rcp_f32_e32 v176, v163
	v_and_b32_e32 v163, 0xffff0000, v133
	v_rcp_f32_e32 v138, v138
	v_rcp_f32_e32 v134, v134
	v_rcp_f32_e32 v135, v135
	v_rcp_f32_e32 v136, v136
	v_rcp_f32_e32 v137, v137
	v_max_f32_e32 v163, 0xda24260, v163
	v_rcp_f32_e32 v142, v142
	v_rcp_f32_e32 v177, v163
	v_pk_mul_f32 v[134:135], v[138:139], v[134:135]
	v_pk_mul_f32 v[136:137], v[140:141], v[136:137]
	v_cvt_pk_bf16_f32 v134, v134, v135
	v_cvt_pk_bf16_f32 v135, v136, v137
	v_pk_mul_f32 v[136:137], v[142:143], v[168:169]
	v_pk_mul_f32 v[138:139], v[144:145], v[176:177]
	v_cvt_pk_bf16_f32 v136, v136, v137
	v_cvt_pk_bf16_f32 v137, v138, v139
	v_add_co_u32_e32 v138, vcc, 0x160000, v166
	s_nop 1
	v_addc_co_u32_e32 v139, vcc, 0, v167, vcc
	global_store_dwordx4 v[138:139], v[134:137], off sc1
	s_nop 1
	v_add_co_u32_e32 v134, vcc, 0x161000, v166
	s_nop 1
	v_addc_co_u32_e32 v135, vcc, 0, v167, vcc
	global_store_dwordx4 v[134:135], v[130:133], off sc1

; __device__ __forceinline__ unsigned cvt_pk_bf16(float lo, float hi) { f32x2v_ v = {lo, hi}; bf16x2v_ b = __builtin_convertvector(v, bf16x2v_); return __builtin_bit_cast(unsigned, b); }
;     __device__ __forceinline__ void operator()(const f32x4 (&acc)[2][2][4][2], const Unit& u, int wr, int wc, int fr, int fq) const {
;     ...
;         if (pn >= 10 && pn < 14) {
;             const float* tab = (const float*)(ws + ((size_t)2 << 20));
;             const int f0 = 16 * (wc & 1) + 4 * fq;
; #pragma unroll
;             for (int ai = 0; ai < 2; ++ai)
; #pragma unroll
;                 for (int m = 0; m < 4; ++m) { const int r = row0 + ai * HALF + m * 16; const int pos = r & 8191;
;                     const f32x4 t0 = *(const f32x4*)(tab + ((size_t)pos * 32 + f0) * 2), t1 = *(const f32x4*)(tab + ((size_t)pos * 32 + f0) * 2 + 4);
;                     const float cs[4] = {t0[0], t0[2], t1[0], t1[2]}, sn[4] = {t0[1], t0[3], t1[1], t1[3]};
;                     bf16_t* rowp = base + (size_t)r * ld + col0;
; #pragma unroll
;                     for (int bj = 0; bj < 2; ++bj) { f32x4 v0, v1;
; #pragma unroll
;                         for (int e = 0; e < 4; ++e) { const float x1 = acc[ai][bj][m][0][e], x2 = acc[ai][bj][m][1][e]; v0[e] = x1 * cs[e] - x2 * sn[e]; v1[e] = x2 * cs[e] + x1 * sn[e]; }
;                         u32x4 w; w.x = cvt_pk_bf16(v0[0], v0[1]); w.y = cvt_pk_bf16(v0[2], v0[3]); w.z = cvt_pk_bf16(v1[0], v1[1]); w.w = cvt_pk_bf16(v1[2], v1[3]);
;                         *(u32x4*)(rowp + bj * HALF) = w; } }
.LBB0_140:
	v_lshlrev_b32_e32 v130, 6, v162
	v_and_or_b32 v130, v130, s85, v173
	v_lshlrev_b32_e32 v130, 2, v130
	global_load_dwordx4 v[132:135], v130, s[44:45]
	global_load_dwordx4 v[136:139], v130, s[44:45] offset:16
	v_ashrrev_i32_e32 v142, 31, v162
	v_or_b32_e32 v163, 16, v162
	v_mul_lo_u32 v168, s10, v142
	v_lshlrev_b32_e32 v142, 6, v163
	v_mul_lo_u32 v143, s11, v162
	v_mad_u64_u32 v[140:141], s[18:19], s10, v162, 0
	v_and_or_b32 v142, v142, s86, v173
	v_add3_u32 v141, v141, v168, v143
	v_lshlrev_b32_e32 v169, 2, v142
	v_ashrrev_i32_e32 v165, 31, v164
	v_lshl_add_u64 v[130:131], v[164:165], 1, s[54:55]
	v_lshl_add_u64 v[140:141], v[140:141], 1, v[130:131]
	s_waitcnt vmcnt(0)
	v_mov_b32_e32 v142, v132
	v_mov_b32_e32 v143, v134
	v_mov_b32_e32 v134, v133
	v_mov_b32_e32 v132, v136
	v_mov_b32_e32 v133, v138
	v_mov_b32_e32 v138, v137
	v_pk_mul_f32 v[136:137], v[118:119], v[134:135]
	v_pk_mul_f32 v[118:119], v[118:119], v[142:143]
	v_pk_mul_f32 v[144:145], v[120:121], v[138:139]
	v_pk_mul_f32 v[120:121], v[120:121], v[132:133]
	v_pk_mul_f32 v[164:165], v[126:127], v[134:135]
	v_pk_mul_f32 v[126:127], v[126:127], v[142:143]
	v_pk_mul_f32 v[166:167], v[128:129], v[138:139]
	v_pk_mul_f32 v[128:129], v[128:129], v[132:133]
	v_pk_fma_f32 v[136:137], v[114:115], v[142:143], v[136:137] neg_lo:[0,0,1] neg_hi:[0,0,1]
	v_pk_fma_f32 v[118:119], v[114:115], v[134:135], v[118:119]
	v_pk_fma_f32 v[144:145], v[116:117], v[132:133], v[144:145] neg_lo:[0,0,1] neg_hi:[0,0,1]
	v_pk_fma_f32 v[120:121], v[116:117], v[138:139], v[120:121]
	v_pk_fma_f32 v[142:143], v[122:123], v[142:143], v[164:165] neg_lo:[0,0,1] neg_hi:[0,0,1]
	v_pk_fma_f32 v[122:123], v[122:123], v[134:135], v[126:127]
	v_pk_fma_f32 v[126:127], v[124:125], v[132:133], v[166:167] neg_lo:[0,0,1] neg_hi:[0,0,1]
	v_pk_fma_f32 v[124:125], v[124:125], v[138:139], v[128:129]
	v_cvt_pk_bf16_f32 v114, v136, v137
	v_cvt_pk_bf16_f32 v115, v144, v145
	v_cvt_pk_bf16_f32 v116, v118, v119
	v_cvt_pk_bf16_f32 v117, v120, v121
	v_cvt_pk_bf16_f32 v118, v142, v143
	v_cvt_pk_bf16_f32 v119, v126, v127
	v_cvt_pk_bf16_f32 v120, v122, v123
	v_cvt_pk_bf16_f32 v121, v124, v125
	global_store_dwordx4 v[140:141], v[114:117], off sc1
	global_store_dwordx4 v[140:141], v[118:121], off offset:256 sc1
	global_load_dwordx4 v[114:117], v169, s[44:45]
	s_nop 0
	global_load_dwordx4 v[118:121], v169, s[44:45] offset:16
	v_or_b32_e32 v134, 32, v162
	v_mul_lo_u32 v124, s11, v163
	v_mad_u64_u32 v[122:123], s[18:19], s10, v163, 0
	v_lshlrev_b32_e32 v125, 6, v134
	v_add3_u32 v123, v123, v168, v124
	v_and_or_b32 v124, v125, s87, v173
	v_lshlrev_b32_e32 v135, 2, v124
	v_lshl_add_u64 v[122:123], v[122:123], 1, v[130:131]
	s_waitcnt vmcnt(1)
	v_mov_b32_e32 v124, v114
	v_mov_b32_e32 v125, v116
	v_mov_b32_e32 v116, v115
	s_waitcnt vmcnt(0)
	v_mov_b32_e32 v114, v118
	v_mov_b32_e32 v115, v120
	v_mov_b32_e32 v120, v119
	v_pk_mul_f32 v[118:119], v[102:103], v[116:117]
	v_pk_mul_f32 v[102:103], v[102:103], v[124:125]
	v_pk_mul_f32 v[126:127], v[104:105], v[120:121]
	v_pk_mul_f32 v[104:105], v[104:105], v[114:115]
	v_pk_mul_f32 v[128:129], v[110:111], v[116:117]
	v_pk_mul_f32 v[110:111], v[110:111], v[124:125]
	v_pk_mul_f32 v[132:133], v[112:113], v[120:121]
	v_pk_mul_f32 v[112:113], v[112:113], v[114:115]
	v_pk_fma_f32 v[118:119], v[98:99], v[124:125], v[118:119] neg_lo:[0,0,1] neg_hi:[0,0,1]
	v_pk_fma_f32 v[102:103], v[98:99], v[116:117], v[102:103]
	v_pk_fma_f32 v[126:127], v[100:101], v[114:115], v[126:127] neg_lo:[0,0,1] neg_hi:[0,0,1]
	v_pk_fma_f32 v[104:105], v[100:101], v[120:121], v[104:105]
	v_pk_fma_f32 v[124:125], v[106:107], v[124:125], v[128:129] neg_lo:[0,0,1] neg_hi:[0,0,1]
	v_pk_fma_f32 v[106:107], v[106:107], v[116:117], v[110:111]
	v_pk_fma_f32 v[110:111], v[108:109], v[114:115], v[132:133] neg_lo:[0,0,1] neg_hi:[0,0,1]
	v_pk_fma_f32 v[108:109], v[108:109], v[120:121], v[112:113]
	v_cvt_pk_bf16_f32 v98, v118, v119
	v_cvt_pk_bf16_f32 v99, v126, v127
	v_cvt_pk_bf16_f32 v100, v102, v103
	v_cvt_pk_bf16_f32 v101, v104, v105
	v_cvt_pk_bf16_f32 v102, v124, v125
	v_cvt_pk_bf16_f32 v103, v110, v111
	v_cvt_pk_bf16_f32 v104, v106, v107
	v_cvt_pk_bf16_f32 v105, v108, v109
	global_store_dwordx4 v[122:123], v[98:101], off sc1
	global_store_dwordx4 v[122:123], v[102:105], off offset:256 sc1
	global_load_dwordx4 v[98:101], v135, s[44:45]
	s_nop 0
	global_load_dwordx4 v[102:105], v135, s[44:45] offset:16
	v_or_b32_e32 v116, 48, v162
	v_mul_lo_u32 v108, s11, v134
	v_mad_u64_u32 v[106:107], s[18:19], s10, v134, 0
	v_lshlrev_b32_e32 v109, 6, v116
	v_add3_u32 v107, v107, v168, v108
	v_and_or_b32 v108, v109, s88, v173
	v_lshlrev_b32_e32 v117, 2, v108
	v_lshl_add_u64 v[106:107], v[106:107], 1, v[130:131]
	s_waitcnt vmcnt(1)
	v_mov_b32_e32 v108, v98
	v_mov_b32_e32 v109, v100
	v_mov_b32_e32 v100, v99
	s_waitcnt vmcnt(0)
; __device__ __forceinline__ unsigned cvt_pk_bf16(float lo, float hi) { f32x2v_ v = {lo, hi}; bf16x2v_ b = __builtin_convertvector(v, bf16x2v_); return __builtin_bit_cast(unsigned, b); }
;     __device__ __forceinline__ void operator()(const f32x4 (&acc)[2][2][4][2], const Unit& u, int wr, int wc, int fr, int fq) const {
;     ...
;         if (pn >= 10 && pn < 14) {
;             const float* tab = (const float*)(ws + ((size_t)2 << 20));
;             const int f0 = 16 * (wc & 1) + 4 * fq;
; #pragma unroll
;             for (int ai = 0; ai < 2; ++ai)
; #pragma unroll
;                 for (int m = 0; m < 4; ++m) { const int r = row0 + ai * HALF + m * 16; const int pos = r & 8191;
;                     const f32x4 t0 = *(const f32x4*)(tab + ((size_t)pos * 32 + f0) * 2), t1 = *(const f32x4*)(tab + ((size_t)pos * 32 + f0) * 2 + 4);
;                     const float cs[4] = {t0[0], t0[2], t1[0], t1[2]}, sn[4] = {t0[1], t0[3], t1[1], t1[3]};
;                     bf16_t* rowp = base + (size_t)r * ld + col0;
; #pragma unroll
;                     for (int bj = 0; bj < 2; ++bj) { f32x4 v0, v1;
; #pragma unroll
;                         for (int e = 0; e < 4; ++e) { const float x1 = acc[ai][bj][m][0][e], x2 = acc[ai][bj][m][1][e]; v0[e] = x1 * cs[e] - x2 * sn[e]; v1[e] = x2 * cs[e] + x1 * sn[e]; }
;                         u32x4 w; w.x = cvt_pk_bf16(v0[0], v0[1]); w.y = cvt_pk_bf16(v0[2], v0[3]); w.z = cvt_pk_bf16(v1[0], v1[1]); w.w = cvt_pk_bf16(v1[2], v1[3]);
;                         *(u32x4*)(rowp + bj * HALF) = w; } }
	v_mov_b32_e32 v98, v102
	v_mov_b32_e32 v99, v104
	v_mov_b32_e32 v104, v103
	v_pk_mul_f32 v[102:103], v[86:87], v[100:101]
	v_pk_mul_f32 v[86:87], v[86:87], v[108:109]
	v_pk_mul_f32 v[110:111], v[88:89], v[104:105]
	v_pk_mul_f32 v[88:89], v[88:89], v[98:99]
	v_pk_mul_f32 v[112:113], v[94:95], v[100:101]
	v_pk_mul_f32 v[94:95], v[94:95], v[108:109]
	v_pk_mul_f32 v[114:115], v[96:97], v[104:105]
	v_pk_mul_f32 v[96:97], v[96:97], v[98:99]
	v_pk_fma_f32 v[102:103], v[82:83], v[108:109], v[102:103] neg_lo:[0,0,1] neg_hi:[0,0,1]
	v_pk_fma_f32 v[86:87], v[82:83], v[100:101], v[86:87]
	v_pk_fma_f32 v[110:111], v[84:85], v[98:99], v[110:111] neg_lo:[0,0,1] neg_hi:[0,0,1]
	v_pk_fma_f32 v[88:89], v[84:85], v[104:105], v[88:89]
	v_pk_fma_f32 v[108:109], v[90:91], v[108:109], v[112:113] neg_lo:[0,0,1] neg_hi:[0,0,1]
	v_pk_fma_f32 v[90:91], v[90:91], v[100:101], v[94:95]
	v_pk_fma_f32 v[94:95], v[92:93], v[98:99], v[114:115] neg_lo:[0,0,1] neg_hi:[0,0,1]
	v_pk_fma_f32 v[92:93], v[92:93], v[104:105], v[96:97]
	v_cvt_pk_bf16_f32 v82, v102, v103
	v_cvt_pk_bf16_f32 v83, v110, v111
	v_cvt_pk_bf16_f32 v84, v86, v87
	v_cvt_pk_bf16_f32 v85, v88, v89
	v_cvt_pk_bf16_f32 v86, v108, v109
	v_cvt_pk_bf16_f32 v87, v94, v95
	v_cvt_pk_bf16_f32 v88, v90, v91
	v_cvt_pk_bf16_f32 v89, v92, v93
	global_store_dwordx4 v[106:107], v[82:85], off sc1
	global_store_dwordx4 v[106:107], v[86:89], off offset:256 sc1
	global_load_dwordx4 v[82:85], v117, s[44:45]
	s_nop 0
	global_load_dwordx4 v[86:89], v117, s[44:45] offset:16
	v_add_u32_e32 v100, 0x80, v162
	v_mul_lo_u32 v92, s11, v116
	v_mad_u64_u32 v[90:91], s[18:19], s10, v116, 0
	v_lshlrev_b32_e32 v93, 6, v100
	v_add3_u32 v91, v91, v168, v92
	v_and_or_b32 v92, v93, s85, v173
	v_lshlrev_b32_e32 v101, 2, v92
	v_lshl_add_u64 v[90:91], v[90:91], 1, v[130:131]
	s_waitcnt vmcnt(1)
	v_mov_b32_e32 v92, v82
	v_mov_b32_e32 v93, v84
	v_mov_b32_e32 v84, v83
	s_waitcnt vmcnt(0)
	v_mov_b32_e32 v82, v86
	v_mov_b32_e32 v83, v88
	v_mov_b32_e32 v88, v87
	v_pk_mul_f32 v[86:87], v[70:71], v[84:85]
	v_pk_mul_f32 v[70:71], v[70:71], v[92:93]
	v_pk_mul_f32 v[94:95], v[72:73], v[88:89]
	v_pk_mul_f32 v[72:73], v[72:73], v[82:83]
	v_pk_mul_f32 v[96:97], v[78:79], v[84:85]
	v_pk_mul_f32 v[78:79], v[78:79], v[92:93]
	v_pk_mul_f32 v[98:99], v[80:81], v[88:89]
	v_pk_mul_f32 v[80:81], v[80:81], v[82:83]
	v_pk_fma_f32 v[86:87], v[66:67], v[92:93], v[86:87] neg_lo:[0,0,1] neg_hi:[0,0,1]
	v_pk_fma_f32 v[70:71], v[66:67], v[84:85], v[70:71]
	v_pk_fma_f32 v[94:95], v[68:69], v[82:83], v[94:95] neg_lo:[0,0,1] neg_hi:[0,0,1]
	v_pk_fma_f32 v[72:73], v[68:69], v[88:89], v[72:73]
	v_pk_fma_f32 v[92:93], v[74:75], v[92:93], v[96:97] neg_lo:[0,0,1] neg_hi:[0,0,1]
	v_pk_fma_f32 v[74:75], v[74:75], v[84:85], v[78:79]
	v_pk_fma_f32 v[78:79], v[76:77], v[82:83], v[98:99] neg_lo:[0,0,1] neg_hi:[0,0,1]
	v_pk_fma_f32 v[76:77], v[76:77], v[88:89], v[80:81]
	v_cvt_pk_bf16_f32 v66, v86, v87
	v_cvt_pk_bf16_f32 v67, v94, v95
	v_cvt_pk_bf16_f32 v68, v70, v71
	v_cvt_pk_bf16_f32 v69, v72, v73
	v_cvt_pk_bf16_f32 v70, v92, v93
	v_cvt_pk_bf16_f32 v71, v78, v79
	v_cvt_pk_bf16_f32 v72, v74, v75
	v_cvt_pk_bf16_f32 v73, v76, v77
	global_store_dwordx4 v[90:91], v[66:69], off sc1
	global_store_dwordx4 v[90:91], v[70:73], off offset:256 sc1
	global_load_dwordx4 v[66:69], v101, s[44:45]
	s_nop 0
	global_load_dwordx4 v[70:73], v101, s[44:45] offset:16
	v_add_u32_e32 v84, 0x90, v162
	v_ashrrev_i32_e32 v76, 31, v100
	v_mul_lo_u32 v77, s11, v100
	v_mad_u64_u32 v[74:75], s[18:19], s10, v100, 0
	v_lshlrev_b32_e32 v78, 6, v84
	v_mul_lo_u32 v76, s10, v76
	v_and_or_b32 v78, v78, s86, v173
	v_add3_u32 v75, v75, v76, v77
	v_lshlrev_b32_e32 v85, 2, v78
	v_lshl_add_u64 v[74:75], v[74:75], 1, v[130:131]
	s_waitcnt vmcnt(1)
	v_mov_b32_e32 v76, v66
	v_mov_b32_e32 v77, v68
	v_mov_b32_e32 v68, v67
	s_waitcnt vmcnt(0)
	v_mov_b32_e32 v66, v70
	v_mov_b32_e32 v67, v72
	v_mov_b32_e32 v72, v71
	v_pk_mul_f32 v[70:71], v[62:63], v[68:69]
	v_pk_mul_f32 v[62:63], v[62:63], v[76:77]
	v_pk_mul_f32 v[78:79], v[64:65], v[72:73]
	v_pk_mul_f32 v[64:65], v[64:65], v[66:67]
	v_pk_mul_f32 v[80:81], v[54:55], v[68:69]
	v_pk_mul_f32 v[54:55], v[54:55], v[76:77]
	v_pk_mul_f32 v[82:83], v[56:57], v[72:73]
	v_pk_mul_f32 v[56:57], v[56:57], v[66:67]
	v_pk_fma_f32 v[70:71], v[58:59], v[76:77], v[70:71] neg_lo:[0,0,1] neg_hi:[0,0,1]
	v_pk_fma_f32 v[58:59], v[58:59], v[68:69], v[62:63]
	v_pk_fma_f32 v[62:63], v[60:61], v[66:67], v[78:79] neg_lo:[0,0,1] neg_hi:[0,0,1]
	v_pk_fma_f32 v[60:61], v[60:61], v[72:73], v[64:65]
	v_pk_fma_f32 v[64:65], v[50:51], v[76:77], v[80:81] neg_lo:[0,0,1] neg_hi:[0,0,1]
	v_pk_fma_f32 v[68:69], v[50:51], v[68:69], v[54:55]
	v_pk_fma_f32 v[66:67], v[52:53], v[66:67], v[82:83] neg_lo:[0,0,1] neg_hi:[0,0,1]
	v_pk_fma_f32 v[72:73], v[52:53], v[72:73], v[56:57]
	v_cvt_pk_bf16_f32 v50, v70, v71
	v_cvt_pk_bf16_f32 v51, v62, v63
	v_cvt_pk_bf16_f32 v52, v58, v59
	v_cvt_pk_bf16_f32 v53, v60, v61
	v_cvt_pk_bf16_f32 v54, v64, v65
	v_cvt_pk_bf16_f32 v55, v66, v67
	v_cvt_pk_bf16_f32 v56, v68, v69
	v_cvt_pk_bf16_f32 v57, v72, v73
	global_store_dwordx4 v[74:75], v[50:53], off sc1
	global_store_dwordx4 v[74:75], v[54:57], off offset:256 sc1
	global_load_dwordx4 v[50:53], v85, s[44:45]
	s_nop 0
	global_load_dwordx4 v[54:57], v85, s[44:45] offset:16
	v_add_u32_e32 v68, 0xa0, v162
	v_ashrrev_i32_e32 v60, 31, v84
	v_mul_lo_u32 v61, s11, v84
	v_mad_u64_u32 v[58:59], s[18:19], s10, v84, 0
	v_lshlrev_b32_e32 v62, 6, v68
	v_mul_lo_u32 v60, s10, v60
	v_and_or_b32 v62, v62, s87, v173
	v_add3_u32 v59, v59, v60, v61
	v_lshlrev_b32_e32 v69, 2, v62
	v_lshl_add_u64 v[58:59], v[58:59], 1, v[130:131]
	s_waitcnt vmcnt(1)
; __device__ __forceinline__ unsigned cvt_pk_bf16(float lo, float hi) { f32x2v_ v = {lo, hi}; bf16x2v_ b = __builtin_convertvector(v, bf16x2v_); return __builtin_bit_cast(unsigned, b); }
;     __device__ __forceinline__ void operator()(const f32x4 (&acc)[2][2][4][2], const Unit& u, int wr, int wc, int fr, int fq) const {
;     ...
;         if (pn >= 10 && pn < 14) {
;             const float* tab = (const float*)(ws + ((size_t)2 << 20));
;             const int f0 = 16 * (wc & 1) + 4 * fq;
; #pragma unroll
;             for (int ai = 0; ai < 2; ++ai)
; #pragma unroll
;                 for (int m = 0; m < 4; ++m) { const int r = row0 + ai * HALF + m * 16; const int pos = r & 8191;
;                     const f32x4 t0 = *(const f32x4*)(tab + ((size_t)pos * 32 + f0) * 2), t1 = *(const f32x4*)(tab + ((size_t)pos * 32 + f0) * 2 + 4);
;                     const float cs[4] = {t0[0], t0[2], t1[0], t1[2]}, sn[4] = {t0[1], t0[3], t1[1], t1[3]};
;                     bf16_t* rowp = base + (size_t)r * ld + col0;
; #pragma unroll
;                     for (int bj = 0; bj < 2; ++bj) { f32x4 v0, v1;
; #pragma unroll
;                         for (int e = 0; e < 4; ++e) { const float x1 = acc[ai][bj][m][0][e], x2 = acc[ai][bj][m][1][e]; v0[e] = x1 * cs[e] - x2 * sn[e]; v1[e] = x2 * cs[e] + x1 * sn[e]; }
;                         u32x4 w; w.x = cvt_pk_bf16(v0[0], v0[1]); w.y = cvt_pk_bf16(v0[2], v0[3]); w.z = cvt_pk_bf16(v1[0], v1[1]); w.w = cvt_pk_bf16(v1[2], v1[3]);
;                         *(u32x4*)(rowp + bj * HALF) = w; } }
	v_mov_b32_e32 v60, v50
	v_mov_b32_e32 v61, v52
	v_mov_b32_e32 v52, v51
	s_waitcnt vmcnt(0)
	v_mov_b32_e32 v50, v54
	v_mov_b32_e32 v51, v56
	v_mov_b32_e32 v56, v55
	v_pk_mul_f32 v[54:55], v[46:47], v[52:53]
	v_pk_mul_f32 v[46:47], v[46:47], v[60:61]
	v_pk_mul_f32 v[62:63], v[48:49], v[56:57]
	v_pk_mul_f32 v[48:49], v[48:49], v[50:51]
	v_pk_mul_f32 v[64:65], v[38:39], v[52:53]
	v_pk_mul_f32 v[38:39], v[38:39], v[60:61]
	v_pk_mul_f32 v[66:67], v[40:41], v[56:57]
	v_pk_mul_f32 v[40:41], v[40:41], v[50:51]
	v_pk_fma_f32 v[54:55], v[42:43], v[60:61], v[54:55] neg_lo:[0,0,1] neg_hi:[0,0,1]
	v_pk_fma_f32 v[42:43], v[42:43], v[52:53], v[46:47]
	v_pk_fma_f32 v[46:47], v[44:45], v[50:51], v[62:63] neg_lo:[0,0,1] neg_hi:[0,0,1]
	v_pk_fma_f32 v[44:45], v[44:45], v[56:57], v[48:49]
	v_pk_fma_f32 v[48:49], v[34:35], v[60:61], v[64:65] neg_lo:[0,0,1] neg_hi:[0,0,1]
	v_pk_fma_f32 v[52:53], v[34:35], v[52:53], v[38:39]
	v_pk_fma_f32 v[50:51], v[36:37], v[50:51], v[66:67] neg_lo:[0,0,1] neg_hi:[0,0,1]
	v_pk_fma_f32 v[56:57], v[36:37], v[56:57], v[40:41]
	v_cvt_pk_bf16_f32 v34, v54, v55
	v_cvt_pk_bf16_f32 v35, v46, v47
	v_cvt_pk_bf16_f32 v36, v42, v43
	v_cvt_pk_bf16_f32 v37, v44, v45
	v_cvt_pk_bf16_f32 v38, v48, v49
	v_cvt_pk_bf16_f32 v39, v50, v51
	v_cvt_pk_bf16_f32 v40, v52, v53
	v_cvt_pk_bf16_f32 v41, v56, v57
	global_store_dwordx4 v[58:59], v[34:37], off sc1
	global_store_dwordx4 v[58:59], v[38:41], off offset:256 sc1
	global_load_dwordx4 v[34:37], v69, s[44:45]
	s_nop 0
	global_load_dwordx4 v[38:41], v69, s[44:45] offset:16
	v_add_u32_e32 v52, 0xb0, v162
	v_ashrrev_i32_e32 v44, 31, v68
	v_mul_lo_u32 v45, s11, v68
	v_mad_u64_u32 v[42:43], s[18:19], s10, v68, 0
	v_lshlrev_b32_e32 v46, 6, v52
	v_mul_lo_u32 v44, s10, v44
	v_and_or_b32 v46, v46, s88, v173
	v_add3_u32 v43, v43, v44, v45
	v_lshlrev_b32_e32 v53, 2, v46
	v_lshl_add_u64 v[42:43], v[42:43], 1, v[130:131]
	s_waitcnt vmcnt(1)
	v_mov_b32_e32 v44, v34
	v_mov_b32_e32 v45, v36
	v_mov_b32_e32 v36, v35
	s_waitcnt vmcnt(0)
	v_mov_b32_e32 v34, v38
	v_mov_b32_e32 v35, v40
	v_mov_b32_e32 v40, v39
	v_pk_mul_f32 v[38:39], v[22:23], v[36:37]
	v_pk_mul_f32 v[22:23], v[22:23], v[44:45]
	v_pk_mul_f32 v[46:47], v[24:25], v[40:41]
	v_pk_mul_f32 v[24:25], v[24:25], v[34:35]
	v_pk_mul_f32 v[48:49], v[30:31], v[36:37]
	v_pk_mul_f32 v[30:31], v[30:31], v[44:45]
	v_pk_mul_f32 v[50:51], v[32:33], v[40:41]
	v_pk_mul_f32 v[32:33], v[32:33], v[34:35]
	v_pk_fma_f32 v[38:39], v[18:19], v[44:45], v[38:39] neg_lo:[0,0,1] neg_hi:[0,0,1]
	v_pk_fma_f32 v[22:23], v[18:19], v[36:37], v[22:23]
	v_pk_fma_f32 v[46:47], v[20:21], v[34:35], v[46:47] neg_lo:[0,0,1] neg_hi:[0,0,1]
	v_pk_fma_f32 v[24:25], v[20:21], v[40:41], v[24:25]
	v_pk_fma_f32 v[44:45], v[26:27], v[44:45], v[48:49] neg_lo:[0,0,1] neg_hi:[0,0,1]
	v_pk_fma_f32 v[26:27], v[26:27], v[36:37], v[30:31]
	v_pk_fma_f32 v[30:31], v[28:29], v[34:35], v[50:51] neg_lo:[0,0,1] neg_hi:[0,0,1]
	v_pk_fma_f32 v[28:29], v[28:29], v[40:41], v[32:33]
	v_cvt_pk_bf16_f32 v18, v38, v39
	v_cvt_pk_bf16_f32 v19, v46, v47
	v_cvt_pk_bf16_f32 v20, v22, v23
	v_cvt_pk_bf16_f32 v21, v24, v25
	v_cvt_pk_bf16_f32 v22, v44, v45
	v_cvt_pk_bf16_f32 v23, v30, v31
	v_cvt_pk_bf16_f32 v24, v26, v27
	v_cvt_pk_bf16_f32 v25, v28, v29
	global_store_dwordx4 v[42:43], v[18:21], off sc1
	global_store_dwordx4 v[42:43], v[22:25], off offset:256 sc1
	global_load_dwordx4 v[18:21], v53, s[44:45]
	s_nop 0
	global_load_dwordx4 v[22:25], v53, s[44:45] offset:16
	v_ashrrev_i32_e32 v28, 31, v52
	v_mul_lo_u32 v29, s11, v52
	v_mad_u64_u32 v[26:27], s[18:19], s10, v52, 0
	v_mul_lo_u32 v28, s10, v28
	v_add3_u32 v27, v27, v28, v29
	v_lshl_add_u64 v[26:27], v[26:27], 1, v[130:131]
	s_waitcnt vmcnt(1)
	v_mov_b32_e32 v28, v18
	v_mov_b32_e32 v29, v20
	v_mov_b32_e32 v20, v19
	s_waitcnt vmcnt(0)
	v_mov_b32_e32 v18, v22
	v_mov_b32_e32 v19, v24
	v_mov_b32_e32 v24, v23
	v_pk_mul_f32 v[22:23], v[14:15], v[20:21]
	v_pk_mul_f32 v[14:15], v[14:15], v[28:29]
	v_pk_mul_f32 v[30:31], v[16:17], v[24:25]
	v_pk_mul_f32 v[16:17], v[16:17], v[18:19]
	v_pk_mul_f32 v[32:33], v[2:3], v[20:21]
	v_pk_mul_f32 v[2:3], v[2:3], v[28:29]
	v_pk_mul_f32 v[34:35], v[4:5], v[24:25]
	v_pk_mul_f32 v[4:5], v[4:5], v[18:19]
	v_pk_fma_f32 v[22:23], v[6:7], v[28:29], v[22:23] neg_lo:[0,0,1] neg_hi:[0,0,1]
	v_pk_fma_f32 v[6:7], v[6:7], v[20:21], v[14:15]
	v_pk_fma_f32 v[14:15], v[8:9], v[18:19], v[30:31] neg_lo:[0,0,1] neg_hi:[0,0,1]
	v_pk_fma_f32 v[8:9], v[8:9], v[24:25], v[16:17]
	v_pk_fma_f32 v[16:17], v[10:11], v[28:29], v[32:33] neg_lo:[0,0,1] neg_hi:[0,0,1]
	v_pk_fma_f32 v[10:11], v[10:11], v[20:21], v[2:3]
	v_pk_fma_f32 v[18:19], v[12:13], v[18:19], v[34:35] neg_lo:[0,0,1] neg_hi:[0,0,1]
	v_pk_fma_f32 v[12:13], v[12:13], v[24:25], v[4:5]
	v_cvt_pk_bf16_f32 v2, v22, v23
	v_cvt_pk_bf16_f32 v3, v14, v15
	v_cvt_pk_bf16_f32 v4, v6, v7
	v_cvt_pk_bf16_f32 v5, v8, v9
	v_cvt_pk_bf16_f32 v6, v16, v17
	v_cvt_pk_bf16_f32 v7, v18, v19
	v_cvt_pk_bf16_f32 v8, v10, v11
	v_cvt_pk_bf16_f32 v9, v12, v13
	global_store_dwordx4 v[26:27], v[2:5], off sc1
	global_store_dwordx4 v[26:27], v[6:9], off offset:256 sc1

; #define GAS __attribute__((address_space(1)))
; __device__ __forceinline__ void unpack8(const v4u w, float (&v)[8]) { v[0] = bflo(w.x); v[1] = bfhi(w.x); v[2] = bflo(w.y); v[3] = bfhi(w.y); v[4] = bflo(w.z); v[5] = bfhi(w.z); v[6] = bflo(w.w); v[7] = bfhi(w.w); }
; __device__ __forceinline__ v4u pack8(const float (&v)[8]) { v4u w; w.x = pk2(v[0], v[1]); w.y = pk2(v[2], v[3]); w.z = pk2(v[4], v[5]); w.w = pk2(v[6], v[7]); return w; }
; __device__ __forceinline__ void rope8(float (&v)[8], const float2* tab, int pos, int cc) {
;     const GAS f32x4* tp = (const GAS f32x4*)(tab + (size_t)pos * 32 + 8 * (cc & 3));
;     const f32x4 t0 = tp[0], t1 = tp[1], t2 = tp[2], t3 = tp[3];
;     const float cs[8] = {t0.x, t0.z, t1.x, t1.z, t2.x, t2.z, t3.x, t3.z}, sn[8] = {t0.y, t0.w, t1.y, t1.w, t2.y, t2.w, t3.y, t3.w};
;     const float sg = (cc & 4) ? 1.f : -1.f;
; #pragma unroll
;     for (int e = 0; e < 8; ++e) { const float p = __shfl_xor(v[e], 4); v[e] = v[e] * cs[e] + sg * p * sn[e]; }
; }
; __device__ __forceinline__ void p1b_normrope(const Frame& F, KArgs a) {
;     ...
;     for (int tA = F.gw; tA < T; tA += 2 * F.NGW) {
;         const int tB = (tA + F.NGW < T) ? tA + F.NGW : tA;
;         v4u raw[2][3];
; #pragma unroll
;         for (int u = 0; u < 2; ++u) { const int t = u ? tB : tA;
;             raw[u][0] = *(const GAS v4u*)(KA + (size_t)t * 256 + (F.lane & 31) * 8);
;             }
; #pragma unroll
;         for (int u = 0; u < 2; ++u) { const int t = u ? tB : tA;
;             if (u == 1 && tB == tA) break;
;             const int s = t & (SEQ - 1), prow = s >> 6, pcol = s & 63;
;             const int posA = (cc16 < 8) ? prow : pcol;
;             {
;                 bf16* p = KA + (size_t)t * 256 + (F.lane & 31) * 8;
;                 float v[8]; unpack8(raw[u][0], v);
;                 float ss = 0.f;
; #pragma unroll
;                 for (int e = 0; e < 8; ++e) ss += v[e] * v[e];
;                 ss += __shfl_xor(ss, 1); ss += __shfl_xor(ss, 2); ss += __shfl_xor(ss, 4); ss += __shfl_xor(ss, 8);
;                 const float rstd = 1.0f / sqrtf(ss * (1.0f / 128.0f) + EPS);
; #pragma unroll
;                 for (int e = 0; e < 8; ++e) v[e] = v[e] * rstd * gk[e];
;                 rope8(v, tab, posA, cc16 & 7);
;                 if (F.lane < 32) *(GAS v4u*)p = pack8(v);
;             }
.LBB0_201:
	s_add_i32 s23, s24, s28
	s_cmp_lt_i32 s23, 0x8000
	s_cselect_b32 s14, s23, s24
	s_ashr_i32 s25, s24, 31
	s_lshl_b64 s[10:11], s[24:25], 9
	v_lshl_add_u64 v[22:23], v[18:19], 0, s[10:11]
	s_waitcnt lgkmcnt(1)
	global_load_dwordx4 v[24:27], v[22:23], off
	s_ashr_i32 s15, s14, 31
	s_lshl_b64 s[10:11], s[14:15], 9
	v_lshl_add_u64 v[6:7], v[18:19], 0, s[10:11]
	global_load_dwordx4 v[10:13], v[6:7], off
	s_waitcnt vmcnt(1) lgkmcnt(0)
	v_lshlrev_b32_e32 v29, 16, v25
	v_lshlrev_b32_e32 v28, 16, v24
	v_and_b32_e32 v25, 0xffff0000, v25
	v_and_b32_e32 v24, 0xffff0000, v24
	v_pk_mul_f32 v[38:39], v[28:29], v[28:29]
	v_pk_mul_f32 v[40:41], v[24:25], v[24:25]
	v_lshlrev_b32_e32 v30, 16, v26
	v_and_b32_e32 v26, 0xffff0000, v26
	v_add_f32_e32 v14, v38, v40
	v_mov_b32_e32 v42, v26
	v_mov_b32_e32 v43, v30
	v_add_f32_e32 v14, v39, v14
	v_lshlrev_b32_e32 v31, 16, v27
	v_and_b32_e32 v27, 0xffff0000, v27
	v_pk_mul_f32 v[42:43], v[42:43], v[42:43]
	v_add_f32_e32 v14, v41, v14
	v_mov_b32_e32 v44, v27
	v_mov_b32_e32 v45, v31
	v_add_f32_e32 v14, v43, v14
	v_pk_mul_f32 v[44:45], v[44:45], v[44:45]
	v_add_f32_e32 v14, v42, v14
	v_add_f32_e32 v14, v45, v14
	v_add_f32_e32 v14, v44, v14
	ds_bpermute_b32 v37, v33, v14
	s_waitcnt lgkmcnt(0)
	v_add_f32_e32 v14, v14, v37
	ds_bpermute_b32 v37, v34, v14
	s_waitcnt lgkmcnt(0)
	v_add_f32_e32 v14, v14, v37
	ds_bpermute_b32 v37, v35, v14
	s_waitcnt lgkmcnt(0)
	v_add_f32_e32 v14, v14, v37
	ds_bpermute_b32 v37, v36, v14
	s_waitcnt lgkmcnt(0)
	v_add_f32_e32 v14, v14, v37
	v_fmamk_f32 v14, v14, 0x3c000000, v1
	v_mul_f32_e32 v37, 0x4f800000, v14
	v_cmp_gt_f32_e32 vcc, s19, v14
	s_nop 1
	v_cndmask_b32_e32 v14, v14, v37, vcc
	v_sqrt_f32_e32 v37, v14
	s_nop 0
	v_add_u32_e32 v38, -1, v37
	v_add_u32_e32 v39, 1, v37
	v_fma_f32 v40, -v38, v37, v14
	v_fma_f32 v41, -v39, v37, v14
	v_cmp_ge_f32_e64 s[10:11], 0, v40
	s_nop 1
	v_cndmask_b32_e64 v37, v37, v38, s[10:11]
	v_cmp_lt_f32_e64 s[10:11], 0, v41
	s_nop 1
	v_cndmask_b32_e64 v37, v37, v39, s[10:11]
	v_mul_f32_e32 v38, 0x37800000, v37
	v_cndmask_b32_e32 v37, v37, v38, vcc
	v_cmp_class_f32_e32 vcc, v14, v32
	s_nop 1
	v_cndmask_b32_e32 v14, v37, v14, vcc
	v_div_scale_f32 v37, s[10:11], v14, v14, 1.0
	v_rcp_f32_e32 v38, v37
	v_div_scale_f32 v39, vcc, 1.0, v14, 1.0
	v_fma_f32 v40, -v37, v38, 1.0
	v_fmac_f32_e32 v38, v40, v38
	v_mul_f32_e32 v40, v39, v38
	v_fma_f32 v41, -v37, v40, v39
	v_fmac_f32_e32 v40, v41, v38
	v_fma_f32 v37, -v37, v40, v39
	v_div_fmas_f32 v37, v37, v38, v40
	v_div_fixup_f32 v14, v37, v14, 1.0
	v_pk_mul_f32 v[28:29], v[14:15], v[28:29] op_sel_hi:[0,1]
	v_pk_mul_f32 v[24:25], v[14:15], v[24:25] op_sel_hi:[0,1]
	v_pk_mul_f32 v[30:31], v[14:15], v[30:31] op_sel_hi:[0,1]
	v_pk_mul_f32 v[38:39], v[14:15], v[26:27] op_sel_hi:[0,1]
	v_pk_mul_f32 v[26:27], v[20:21], v[28:29]
	v_pk_mul_f32 v[28:29], v[4:5], v[24:25]
	v_pk_mul_f32 v[24:25], v[2:3], v[30:31]
	v_pk_mul_f32 v[30:31], v[8:9], v[38:39]
	ds_bpermute_b32 v43, v35, v26
	ds_bpermute_b32 v41, v35, v28
	ds_bpermute_b32 v44, v35, v27
	ds_bpermute_b32 v42, v35, v29
	ds_bpermute_b32 v37, v35, v24
	ds_bpermute_b32 v39, v35, v30
	ds_bpermute_b32 v38, v35, v25
	ds_bpermute_b32 v40, v35, v31
	s_and_saveexec_b64 s[10:11], s[8:9]
	s_cbranch_execz .LBB0_203
	s_bfe_u32 s15, s24, 0x70006
	s_and_b32 s25, s24, 63
	v_mov_b32_e32 v14, s25
	v_mov_b32_e32 v45, s15
	v_cndmask_b32_e64 v14, v14, v45, s[4:5]
	v_lshlrev_b32_e32 v14, 8, v14
	v_lshl_add_u64 v[62:63], v[16:17], 0, v[14:15]
	global_load_dwordx4 v[46:49], v[62:63], off
	global_load_dwordx4 v[50:53], v[62:63], off offset:16
	global_load_dwordx4 v[54:57], v[62:63], off offset:32
	global_load_dwordx4 v[58:61], v[62:63], off offset:48
	s_waitcnt lgkmcnt(7)
	v_cndmask_b32_e64 v62, v43, -v43, s[6:7]
	s_waitcnt lgkmcnt(5)
	v_cndmask_b32_e64 v63, v44, -v44, s[6:7]
	v_cndmask_b32_e64 v44, v41, -v41, s[6:7]
	s_waitcnt lgkmcnt(4)
	v_cndmask_b32_e64 v45, v42, -v42, s[6:7]
	s_waitcnt lgkmcnt(2)
	v_cndmask_b32_e64 v42, v39, -v39, s[6:7]
	s_waitcnt lgkmcnt(0)
	v_cndmask_b32_e64 v43, v40, -v40, s[6:7]
	v_cndmask_b32_e64 v40, v37, -v37, s[6:7]
	v_cndmask_b32_e64 v41, v38, -v38, s[6:7]
	s_waitcnt vmcnt(3)
	v_mov_b32_e32 v38, v46
	s_waitcnt vmcnt(2)
	v_mov_b32_e32 v39, v50
	v_mov_b32_e32 v50, v47
	v_mov_b32_e32 v47, v52
	v_mov_b32_e32 v52, v49
	s_waitcnt vmcnt(0)
	v_mov_b32_e32 v49, v60
	v_mov_b32_e32 v60, v57
	v_mov_b32_e32 v57, v58
	v_mov_b32_e32 v58, v55
	v_mov_b32_e32 v46, v48
	v_mov_b32_e32 v48, v56
	v_mov_b32_e32 v56, v54
	v_pk_mul_f32 v[50:51], v[62:63], v[50:51]
	v_pk_mul_f32 v[40:41], v[40:41], v[58:59]
	v_pk_mul_f32 v[44:45], v[44:45], v[52:53]
	v_pk_mul_f32 v[42:43], v[42:43], v[60:61]
	v_pk_fma_f32 v[26:27], v[26:27], v[38:39], v[50:51]
	v_pk_fma_f32 v[24:25], v[24:25], v[56:57], v[40:41]
	v_pk_fma_f32 v[28:29], v[28:29], v[46:47], v[44:45]
	v_pk_fma_f32 v[30:31], v[30:31], v[48:49], v[42:43]
	v_bfe_u32 v40, v26, 16, 1
	v_bfe_u32 v41, v27, 16, 1
	v_bfe_u32 v42, v24, 16, 1
	v_bfe_u32 v43, v25, 16, 1
	v_bfe_u32 v14, v31, 16, 1
	v_bfe_u32 v37, v30, 16, 1
	v_bfe_u32 v38, v29, 16, 1
	v_bfe_u32 v39, v28, 16, 1
	v_add3_u32 v25, v25, v43, s3
	v_add3_u32 v24, v24, v42, s3
	v_add3_u32 v27, v27, v41, s3
	v_add3_u32 v26, v26, v40, s3
	v_add3_u32 v28, v28, v39, s3
	v_add3_u32 v29, v29, v38, s3
	v_add3_u32 v30, v30, v37, s3
	v_add3_u32 v14, v31, v14, s3
	v_lshrrev_b32_e32 v31, 16, v26
	v_lshrrev_b32_e32 v37, 16, v27
	v_lshrrev_b32_e32 v24, 16, v24
	v_lshrrev_b32_e32 v25, 16, v25
	v_and_or_b32 v27, v14, s18, v25
	v_and_or_b32 v26, v30, s18, v24
	v_and_or_b32 v25, v29, s18, v37
	v_and_or_b32 v24, v28, s18, v31
	global_store_dwordx4 v[22:23], v[24:27], off sc1
	s_or_b64 exec, exec, s[10:11]
	s_cmp_eq_u32 s24, s14
	s_cbranch_scc1 .LBB0_200
	s_branch .LBB0_204

; #define GAS __attribute__((address_space(1)))
; __device__ __forceinline__ void unpack8(const v4u w, float (&v)[8]) { v[0] = bflo(w.x); v[1] = bfhi(w.x); v[2] = bflo(w.y); v[3] = bfhi(w.y); v[4] = bflo(w.z); v[5] = bfhi(w.z); v[6] = bflo(w.w); v[7] = bfhi(w.w); }
; __device__ __forceinline__ v4u pack8(const float (&v)[8]) { v4u w; w.x = pk2(v[0], v[1]); w.y = pk2(v[2], v[3]); w.z = pk2(v[4], v[5]); w.w = pk2(v[6], v[7]); return w; }
; __device__ __forceinline__ void rope8(float (&v)[8], const float2* tab, int pos, int cc) {
;     const GAS f32x4* tp = (const GAS f32x4*)(tab + (size_t)pos * 32 + 8 * (cc & 3));
;     const f32x4 t0 = tp[0], t1 = tp[1], t2 = tp[2], t3 = tp[3];
;     const float cs[8] = {t0.x, t0.z, t1.x, t1.z, t2.x, t2.z, t3.x, t3.z}, sn[8] = {t0.y, t0.w, t1.y, t1.w, t2.y, t2.w, t3.y, t3.w};
;     const float sg = (cc & 4) ? 1.f : -1.f;
; #pragma unroll
;     for (int e = 0; e < 8; ++e) { const float p = __shfl_xor(v[e], 4); v[e] = v[e] * cs[e] + sg * p * sn[e]; }
; }
; __device__ __forceinline__ void p1b_normrope(const Frame& F, KArgs a) {
;     ...
;     for (int tA = F.gw; tA < T; tA += 2 * F.NGW) {
;         const int tB = (tA + F.NGW < T) ? tA + F.NGW : tA;
;         v4u raw[2][3];
; #pragma unroll
;         for (int u = 0; u < 2; ++u) { const int t = u ? tB : tA;
;             raw[u][0] = *(const GAS v4u*)(KA + (size_t)t * 256 + (F.lane & 31) * 8);
;             }
; #pragma unroll
;         for (int u = 0; u < 2; ++u) { const int t = u ? tB : tA;
;             if (u == 1 && tB == tA) break;
;             const int s = t & (SEQ - 1), prow = s >> 6, pcol = s & 63;
;             const int posA = (cc16 < 8) ? prow : pcol;
;             {
;                 bf16* p = KA + (size_t)t * 256 + (F.lane & 31) * 8;
;                 float v[8]; unpack8(raw[u][0], v);
;                 float ss = 0.f;
; #pragma unroll
;                 for (int e = 0; e < 8; ++e) ss += v[e] * v[e];
;                 ss += __shfl_xor(ss, 1); ss += __shfl_xor(ss, 2); ss += __shfl_xor(ss, 4); ss += __shfl_xor(ss, 8);
;                 const float rstd = 1.0f / sqrtf(ss * (1.0f / 128.0f) + EPS);
; #pragma unroll
;                 for (int e = 0; e < 8; ++e) v[e] = v[e] * rstd * gk[e];
;                 rope8(v, tab, posA, cc16 & 7);
;                 if (F.lane < 32) *(GAS v4u*)p = pack8(v);
;             }
.LBB0_204:
	s_waitcnt vmcnt(0)
	v_lshlrev_b32_e32 v23, 16, v11
	v_lshlrev_b32_e32 v22, 16, v10
	v_and_b32_e32 v25, 0xffff0000, v11
	v_and_b32_e32 v24, 0xffff0000, v10
	v_lshlrev_b32_e32 v27, 16, v13
	v_lshlrev_b32_e32 v26, 16, v12
	v_and_b32_e32 v29, 0xffff0000, v13
	v_and_b32_e32 v28, 0xffff0000, v12
	v_pk_mul_f32 v[10:11], v[22:23], v[22:23]
	v_pk_mul_f32 v[12:13], v[24:25], v[24:25]
	v_mov_b32_e32 v30, v28
	v_add_f32_e32 v10, v10, v12
	v_mov_b32_e32 v31, v26
	v_add_f32_e32 v10, v11, v10
	v_pk_mul_f32 v[30:31], v[30:31], v[30:31]
	v_add_f32_e32 v10, v13, v10
	s_waitcnt lgkmcnt(1)
	v_mov_b32_e32 v38, v29
	v_mov_b32_e32 v39, v27
	v_add_f32_e32 v10, v31, v10
	v_pk_mul_f32 v[38:39], v[38:39], v[38:39]
	v_add_f32_e32 v10, v30, v10
	v_add_f32_e32 v10, v39, v10
	v_add_f32_e32 v10, v38, v10
	ds_bpermute_b32 v11, v33, v10
	s_waitcnt lgkmcnt(0)
	v_add_f32_e32 v10, v10, v11
	ds_bpermute_b32 v11, v34, v10
	s_waitcnt lgkmcnt(0)
	v_add_f32_e32 v10, v10, v11
	ds_bpermute_b32 v11, v35, v10
	s_waitcnt lgkmcnt(0)
	v_add_f32_e32 v10, v10, v11
	ds_bpermute_b32 v11, v36, v10
	s_waitcnt lgkmcnt(0)
	v_add_f32_e32 v10, v10, v11
	v_fmamk_f32 v10, v10, 0x3c000000, v1
	v_mul_f32_e32 v11, 0x4f800000, v10
	v_cmp_gt_f32_e32 vcc, s19, v10
	s_nop 1
	v_cndmask_b32_e32 v10, v10, v11, vcc
	v_sqrt_f32_e32 v11, v10
	s_nop 0
	v_add_u32_e32 v12, -1, v11
	v_add_u32_e32 v13, 1, v11
	v_fma_f32 v14, -v12, v11, v10
	v_fma_f32 v30, -v13, v11, v10
	v_cmp_ge_f32_e64 s[10:11], 0, v14
	s_nop 1
	v_cndmask_b32_e64 v11, v11, v12, s[10:11]
	v_cmp_lt_f32_e64 s[10:11], 0, v30
	s_nop 1
	v_cndmask_b32_e64 v11, v11, v13, s[10:11]
	v_mul_f32_e32 v12, 0x37800000, v11
	v_cndmask_b32_e32 v11, v11, v12, vcc
	v_cmp_class_f32_e32 vcc, v10, v32
	s_nop 1
	v_cndmask_b32_e32 v10, v11, v10, vcc
	v_div_scale_f32 v11, s[10:11], v10, v10, 1.0
	v_rcp_f32_e32 v12, v11
	s_nop 0
	v_fma_f32 v13, -v11, v12, 1.0
	v_fmac_f32_e32 v12, v13, v12
	v_div_scale_f32 v13, vcc, 1.0, v10, 1.0
	v_mul_f32_e32 v14, v13, v12
	v_fma_f32 v30, -v11, v14, v13
	v_fmac_f32_e32 v14, v30, v12
	v_fma_f32 v11, -v11, v14, v13
	v_div_fmas_f32 v11, v11, v12, v14
	v_div_fixup_f32 v14, v11, v10, 1.0
	v_pk_mul_f32 v[10:11], v[14:15], v[22:23] op_sel_hi:[0,1]
	v_pk_mul_f32 v[12:13], v[14:15], v[24:25] op_sel_hi:[0,1]
	v_pk_mul_f32 v[22:23], v[14:15], v[26:27] op_sel_hi:[0,1]
	v_pk_mul_f32 v[24:25], v[14:15], v[28:29] op_sel_hi:[0,1]
	v_pk_mul_f32 v[10:11], v[20:21], v[10:11]
	v_pk_mul_f32 v[12:13], v[4:5], v[12:13]
	v_pk_mul_f32 v[22:23], v[2:3], v[22:23]
	v_pk_mul_f32 v[24:25], v[8:9], v[24:25]
	ds_bpermute_b32 v37, v35, v10
	ds_bpermute_b32 v30, v35, v12
	ds_bpermute_b32 v38, v35, v11
	ds_bpermute_b32 v31, v35, v13
	ds_bpermute_b32 v26, v35, v22
	ds_bpermute_b32 v28, v35, v24
	ds_bpermute_b32 v27, v35, v23
	ds_bpermute_b32 v29, v35, v25
	s_and_saveexec_b64 s[10:11], s[8:9]
	s_cbranch_execz .LBB0_199
	s_bfe_u32 s15, s14, 0x70006
	s_and_b32 s14, s14, 63
	v_mov_b32_e32 v14, s14
	v_mov_b32_e32 v39, s15
	v_cndmask_b32_e64 v14, v14, v39, s[4:5]
	v_lshlrev_b32_e32 v14, 8, v14
	v_lshl_add_u64 v[56:57], v[16:17], 0, v[14:15]
	global_load_dwordx4 v[40:43], v[56:57], off
	global_load_dwordx4 v[44:47], v[56:57], off offset:16
	global_load_dwordx4 v[48:51], v[56:57], off offset:32
	global_load_dwordx4 v[52:55], v[56:57], off offset:48
	s_waitcnt lgkmcnt(7)
	v_cndmask_b32_e64 v56, v37, -v37, s[6:7]
	s_waitcnt lgkmcnt(5)
	v_cndmask_b32_e64 v57, v38, -v38, s[6:7]
	v_cndmask_b32_e64 v30, v30, -v30, s[6:7]
	s_waitcnt lgkmcnt(4)
	v_cndmask_b32_e64 v31, v31, -v31, s[6:7]
	s_waitcnt lgkmcnt(2)
	v_cndmask_b32_e64 v28, v28, -v28, s[6:7]
	s_waitcnt lgkmcnt(0)
	v_cndmask_b32_e64 v29, v29, -v29, s[6:7]
	v_cndmask_b32_e64 v26, v26, -v26, s[6:7]
	v_cndmask_b32_e64 v27, v27, -v27, s[6:7]
	s_waitcnt vmcnt(3)
	v_mov_b32_e32 v38, v40
	s_waitcnt vmcnt(2)
	v_mov_b32_e32 v39, v44
	v_mov_b32_e32 v44, v41
	v_mov_b32_e32 v41, v46
	v_mov_b32_e32 v46, v43
	s_waitcnt vmcnt(0)
	v_mov_b32_e32 v43, v54
	v_mov_b32_e32 v54, v51
	v_mov_b32_e32 v51, v52
	v_mov_b32_e32 v52, v49
	v_mov_b32_e32 v40, v42
	v_mov_b32_e32 v42, v50
	v_mov_b32_e32 v50, v48
	v_pk_mul_f32 v[44:45], v[56:57], v[44:45]
	v_pk_mul_f32 v[30:31], v[30:31], v[46:47]
	v_pk_mul_f32 v[28:29], v[28:29], v[54:55]
	v_pk_mul_f32 v[26:27], v[26:27], v[52:53]
	v_pk_fma_f32 v[10:11], v[10:11], v[38:39], v[44:45]
	v_pk_fma_f32 v[12:13], v[12:13], v[40:41], v[30:31]
	v_pk_fma_f32 v[24:25], v[24:25], v[42:43], v[28:29]
	v_pk_fma_f32 v[22:23], v[22:23], v[50:51], v[26:27]
	v_bfe_u32 v14, v25, 16, 1
	v_bfe_u32 v27, v13, 16, 1
	v_bfe_u32 v29, v10, 16, 1
	v_bfe_u32 v30, v11, 16, 1
	v_bfe_u32 v31, v22, 16, 1
	v_bfe_u32 v37, v23, 16, 1
	v_bfe_u32 v26, v24, 16, 1
	v_bfe_u32 v28, v12, 16, 1
	v_add3_u32 v27, v13, v27, s3
	v_add3_u32 v13, v25, v14, s3
	v_add3_u32 v14, v23, v37, s3
	v_add3_u32 v22, v22, v31, s3
	v_add3_u32 v11, v11, v30, s3
	v_add3_u32 v10, v10, v29, s3
	v_add3_u32 v28, v12, v28, s3
	v_add3_u32 v12, v24, v26, s3
	v_lshrrev_b32_e32 v10, 16, v10
	v_lshrrev_b32_e32 v11, 16, v11
	v_lshrrev_b32_e32 v22, 16, v22
	v_lshrrev_b32_e32 v14, 16, v14
	v_and_or_b32 v13, v13, s18, v14
	v_and_or_b32 v12, v12, s18, v22
	v_and_or_b32 v11, v27, s18, v11
	v_and_or_b32 v10, v28, s18, v10
	global_store_dwordx4 v[6:7], v[10:13], off sc1
	s_branch .LBB0_199

; __device__ __forceinline__ unsigned cvt_pk_bf16(float lo, float hi) { f32x2v_ v = {lo, hi}; bf16x2v_ b = __builtin_convertvector(v, bf16x2v_); return __builtin_bit_cast(unsigned, b); }
; __device__ __forceinline__ float bf_lo(unsigned w) { return __uint_as_float(w << 16); }
; __device__ __forceinline__ float bf_hi(unsigned w) { return __uint_as_float(w & 0xffff0000u); }
;     __device__ __forceinline__ void operator()(const f32x4 (&acc)[2][2][4][2], const Unit& u, int wr, int wc, int fr, int fq) const {
;         asm volatile("" : "+v"(fr), "+v"(fq));
;         const int row0 = u.pm * BM + wr * 64 + fr, col0 = u.pn * BM + wc * 32 + 8 * fq;
; #pragma unroll
;         for (int ai = 0; ai < 2; ++ai)
; #pragma unroll
;             for (int m = 0; m < 4; ++m) { const size_t r = (size_t)(row0 + ai * HALF + m * 16);
; #pragma unroll
;                 for (int bj = 0; bj < 2; ++bj) { const u32x4 g = *(const u32x4*)(GT + r * 4096 + 2048 + col0 + bj * HALF);
;                     f32x4 v0 = acc[ai][bj][m][0], v1 = acc[ai][bj][m][1];
;                     v0[0] *= fmaxf(bf_lo(g.x), 1e-30f); v0[1] *= fmaxf(bf_hi(g.x), 1e-30f); v0[2] *= fmaxf(bf_lo(g.y), 1e-30f); v0[3] *= fmaxf(bf_hi(g.y), 1e-30f);
;                     v1[0] *= fmaxf(bf_lo(g.z), 1e-30f); v1[1] *= fmaxf(bf_hi(g.z), 1e-30f); v1[2] *= fmaxf(bf_lo(g.w), 1e-30f); v1[3] *= fmaxf(bf_hi(g.w), 1e-30f);
;                     u32x4 w; w.x = cvt_pk_bf16(v0[0], v0[1]); w.y = cvt_pk_bf16(v0[2], v0[3]); w.z = cvt_pk_bf16(v1[0], v1[1]); w.w = cvt_pk_bf16(v1[2], v1[3]);
;                     *(u32x4*)(MG + r * 2048 + col0 + bj * HALF) = w; }
;                 if (m & 1) asm volatile("" ::: "memory"); }
.LBB0_388:
	v_mov_b32_e32 v130, v1
	v_mov_b32_e32 v131, v172
	s_nop 0
	v_add_u32_e32 v132, s88, v130
	v_lshl_add_u32 v130, v131, 3, s51
	v_ashrrev_i32_e32 v133, 31, v132
	v_ashrrev_i32_e32 v131, 31, v130
	v_lshlrev_b64 v[134:135], 13, v[132:133]
	v_lshl_add_u64 v[134:135], s[14:15], 0, v[134:135]
	v_lshlrev_b64 v[130:131], 1, v[130:131]
	v_lshl_add_u64 v[134:135], v[134:135], 0, v[130:131]
	v_add_co_u32_e32 v138, vcc, 0x1000, v134
	v_add_u32_e32 v142, 16, v132
	s_nop 0
	v_addc_co_u32_e32 v139, vcc, 0, v135, vcc
	global_load_dwordx4 v[134:137], v[138:139], off
	s_nop 0
	global_load_dwordx4 v[138:141], v[138:139], off offset:256
	v_lshlrev_b64 v[144:145], 12, v[132:133]
	v_ashrrev_i32_e32 v143, 31, v142
	v_lshlrev_b64 v[146:147], 13, v[142:143]
	v_lshl_add_u64 v[146:147], s[14:15], 0, v[146:147]
	v_lshl_add_u64 v[144:145], s[24:25], 0, v[144:145]
	v_lshl_add_u64 v[146:147], v[146:147], 0, v[130:131]
	v_lshl_add_u64 v[144:145], v[144:145], 0, v[130:131]
	v_add_co_u32_e32 v146, vcc, s86, v146
	s_waitcnt vmcnt(0)
	v_lshlrev_b32_e32 v133, 16, v134
	v_and_b32_e32 v134, 0xffff0000, v134
	v_lshlrev_b32_e32 v148, 16, v135
	v_and_b32_e32 v135, 0xffff0000, v135
	v_lshlrev_b32_e32 v149, 16, v136
	v_and_b32_e32 v136, 0xffff0000, v136
	v_lshlrev_b32_e32 v150, 16, v137
	v_and_b32_e32 v137, 0xffff0000, v137
	v_lshlrev_b32_e32 v151, 16, v138
	v_and_b32_e32 v138, 0xffff0000, v138
	v_lshlrev_b32_e32 v152, 16, v139
	v_and_b32_e32 v139, 0xffff0000, v139
	v_lshlrev_b32_e32 v153, 16, v140
	v_and_b32_e32 v140, 0xffff0000, v140
	v_lshlrev_b32_e32 v154, 16, v141
	v_and_b32_e32 v141, 0xffff0000, v141
	v_max_f32_e32 v133, v133, v133
	v_max_f32_e32 v155, v134, v134
	v_max_f32_e32 v148, v148, v148
	v_max_f32_e32 v156, v135, v135
	v_max_f32_e32 v149, v149, v149
	v_max_f32_e32 v157, v136, v136
	v_max_f32_e32 v150, v150, v150
	v_max_f32_e32 v170, v137, v137
	v_max_f32_e32 v151, v151, v151
	v_max_f32_e32 v171, v138, v138
	v_max_f32_e32 v152, v152, v152
	v_max_f32_e32 v175, v139, v139
	v_max_f32_e32 v153, v153, v153
	v_max_f32_e32 v176, v140, v140
	v_max_f32_e32 v154, v154, v154
	v_max_f32_e32 v177, v141, v141
	v_max_f32_e32 v134, 0xda24260, v133
	v_max_f32_e32 v135, 0xda24260, v155
	v_max_f32_e32 v136, 0xda24260, v148
	v_max_f32_e32 v137, 0xda24260, v156
	v_max_f32_e32 v138, 0xda24260, v149
	v_max_f32_e32 v139, 0xda24260, v157
	v_max_f32_e32 v140, 0xda24260, v150
	v_max_f32_e32 v141, 0xda24260, v170
	v_max_f32_e32 v148, 0xda24260, v151
	v_max_f32_e32 v149, 0xda24260, v171
	v_max_f32_e32 v150, 0xda24260, v152
	v_max_f32_e32 v151, 0xda24260, v175
	v_max_f32_e32 v152, 0xda24260, v153
	v_max_f32_e32 v153, 0xda24260, v176
	v_max_f32_e32 v154, 0xda24260, v154
	v_max_f32_e32 v155, 0xda24260, v177
	v_pk_mul_f32 v[118:119], v[118:119], v[134:135]
	v_pk_mul_f32 v[120:121], v[120:121], v[136:137]
	v_pk_mul_f32 v[134:135], v[114:115], v[138:139]
	v_pk_mul_f32 v[136:137], v[116:117], v[140:141]
	v_pk_mul_f32 v[126:127], v[126:127], v[148:149]
	v_pk_mul_f32 v[128:129], v[128:129], v[150:151]
	v_cvt_pk_bf16_f32 v114, v118, v119
	v_cvt_pk_bf16_f32 v115, v120, v121
	v_cvt_pk_bf16_f32 v116, v134, v135
	v_cvt_pk_bf16_f32 v117, v136, v137
	v_pk_mul_f32 v[120:121], v[122:123], v[152:153]
	v_pk_mul_f32 v[122:123], v[124:125], v[154:155]
	v_addc_co_u32_e32 v147, vcc, 0, v147, vcc
	global_store_dwordx4 v[144:145], v[114:117], off sc1
	v_cvt_pk_bf16_f32 v118, v126, v127
	v_cvt_pk_bf16_f32 v119, v128, v129
	v_cvt_pk_bf16_f32 v120, v120, v121
	v_cvt_pk_bf16_f32 v121, v122, v123
	global_load_dwordx4 v[114:117], v[146:147], off
	v_add_u32_e32 v122, 32, v132
	global_store_dwordx4 v[144:145], v[118:121], off offset:256 sc1
	global_load_dwordx4 v[118:121], v[146:147], off offset:256
	v_ashrrev_i32_e32 v123, 31, v122
	v_lshlrev_b64 v[124:125], 12, v[142:143]
	v_lshlrev_b64 v[126:127], 13, v[122:123]
	v_lshl_add_u64 v[124:125], s[24:25], 0, v[124:125]
	v_lshl_add_u64 v[126:127], s[14:15], 0, v[126:127]
	v_lshl_add_u64 v[124:125], v[124:125], 0, v[130:131]
	v_lshl_add_u64 v[126:127], v[126:127], 0, v[130:131]
	v_add_co_u32_e32 v126, vcc, s86, v126
	s_waitcnt vmcnt(0)
	v_lshlrev_b32_e32 v128, 16, v114
	v_and_b32_e32 v114, 0xffff0000, v114
	v_lshlrev_b32_e32 v129, 16, v115
	v_and_b32_e32 v115, 0xffff0000, v115
	v_lshlrev_b32_e32 v133, 16, v116
	v_and_b32_e32 v116, 0xffff0000, v116
	v_lshlrev_b32_e32 v134, 16, v117
	v_and_b32_e32 v117, 0xffff0000, v117
	v_lshlrev_b32_e32 v135, 16, v118
	v_and_b32_e32 v118, 0xffff0000, v118
	v_lshlrev_b32_e32 v136, 16, v119
	v_and_b32_e32 v119, 0xffff0000, v119
	v_lshlrev_b32_e32 v137, 16, v120
	v_and_b32_e32 v120, 0xffff0000, v120
	v_lshlrev_b32_e32 v138, 16, v121
	v_and_b32_e32 v121, 0xffff0000, v121
	v_max_f32_e32 v128, v128, v128
	v_max_f32_e32 v139, v114, v114
	v_max_f32_e32 v129, v129, v129
	v_max_f32_e32 v140, v115, v115
	v_max_f32_e32 v133, v133, v133
	v_max_f32_e32 v141, v116, v116
	v_max_f32_e32 v134, v134, v134
	v_max_f32_e32 v142, v117, v117
	v_max_f32_e32 v135, v135, v135
	v_max_f32_e32 v143, v118, v118
	v_max_f32_e32 v136, v136, v136
	v_max_f32_e32 v144, v119, v119
	v_max_f32_e32 v137, v137, v137
	v_max_f32_e32 v145, v120, v120
	v_max_f32_e32 v138, v138, v138
	v_max_f32_e32 v146, v121, v121
	v_max_f32_e32 v114, 0xda24260, v128
	v_max_f32_e32 v115, 0xda24260, v139
	v_max_f32_e32 v116, 0xda24260, v129
	v_max_f32_e32 v117, 0xda24260, v140
	v_max_f32_e32 v118, 0xda24260, v133
	v_max_f32_e32 v119, 0xda24260, v141
	v_max_f32_e32 v120, 0xda24260, v134
	v_max_f32_e32 v121, 0xda24260, v142
	v_max_f32_e32 v128, 0xda24260, v135
	v_max_f32_e32 v129, 0xda24260, v143
	v_max_f32_e32 v134, 0xda24260, v136
	v_max_f32_e32 v135, 0xda24260, v144
	v_max_f32_e32 v136, 0xda24260, v137
; __device__ __forceinline__ unsigned cvt_pk_bf16(float lo, float hi) { f32x2v_ v = {lo, hi}; bf16x2v_ b = __builtin_convertvector(v, bf16x2v_); return __builtin_bit_cast(unsigned, b); }
; __device__ __forceinline__ float bf_lo(unsigned w) { return __uint_as_float(w << 16); }
; __device__ __forceinline__ float bf_hi(unsigned w) { return __uint_as_float(w & 0xffff0000u); }
;     __device__ __forceinline__ void operator()(const f32x4 (&acc)[2][2][4][2], const Unit& u, int wr, int wc, int fr, int fq) const {
;         asm volatile("" : "+v"(fr), "+v"(fq));
;         const int row0 = u.pm * BM + wr * 64 + fr, col0 = u.pn * BM + wc * 32 + 8 * fq;
; #pragma unroll
;         for (int ai = 0; ai < 2; ++ai)
; #pragma unroll
;             for (int m = 0; m < 4; ++m) { const size_t r = (size_t)(row0 + ai * HALF + m * 16);
; #pragma unroll
;                 for (int bj = 0; bj < 2; ++bj) { const u32x4 g = *(const u32x4*)(GT + r * 4096 + 2048 + col0 + bj * HALF);
;                     f32x4 v0 = acc[ai][bj][m][0], v1 = acc[ai][bj][m][1];
;                     v0[0] *= fmaxf(bf_lo(g.x), 1e-30f); v0[1] *= fmaxf(bf_hi(g.x), 1e-30f); v0[2] *= fmaxf(bf_lo(g.y), 1e-30f); v0[3] *= fmaxf(bf_hi(g.y), 1e-30f);
;                     v1[0] *= fmaxf(bf_lo(g.z), 1e-30f); v1[1] *= fmaxf(bf_hi(g.z), 1e-30f); v1[2] *= fmaxf(bf_lo(g.w), 1e-30f); v1[3] *= fmaxf(bf_hi(g.w), 1e-30f);
;                     u32x4 w; w.x = cvt_pk_bf16(v0[0], v0[1]); w.y = cvt_pk_bf16(v0[2], v0[3]); w.z = cvt_pk_bf16(v1[0], v1[1]); w.w = cvt_pk_bf16(v1[2], v1[3]);
;                     *(u32x4*)(MG + r * 2048 + col0 + bj * HALF) = w; }
;                 if (m & 1) asm volatile("" ::: "memory"); }
	v_max_f32_e32 v137, 0xda24260, v145
	v_max_f32_e32 v138, 0xda24260, v138
	v_max_f32_e32 v139, 0xda24260, v146
	v_pk_mul_f32 v[102:103], v[102:103], v[114:115]
	v_pk_mul_f32 v[104:105], v[104:105], v[116:117]
	v_pk_mul_f32 v[114:115], v[98:99], v[118:119]
	v_pk_mul_f32 v[116:117], v[100:101], v[120:121]
	v_pk_mul_f32 v[110:111], v[110:111], v[128:129]
	v_pk_mul_f32 v[112:113], v[112:113], v[134:135]
	v_pk_mul_f32 v[106:107], v[106:107], v[136:137]
	v_pk_mul_f32 v[108:109], v[108:109], v[138:139]
	v_cvt_pk_bf16_f32 v98, v102, v103
	v_cvt_pk_bf16_f32 v99, v104, v105
	v_cvt_pk_bf16_f32 v100, v114, v115
	v_cvt_pk_bf16_f32 v101, v116, v117
	v_cvt_pk_bf16_f32 v102, v110, v111
	v_cvt_pk_bf16_f32 v103, v112, v113
	v_cvt_pk_bf16_f32 v104, v106, v107
	v_cvt_pk_bf16_f32 v105, v108, v109
	global_store_dwordx4 v[124:125], v[98:101], off sc1
	global_store_dwordx4 v[124:125], v[102:105], off offset:256 sc1
	v_addc_co_u32_e32 v127, vcc, 0, v127, vcc
	global_load_dwordx4 v[98:101], v[126:127], off
	global_load_dwordx4 v[102:105], v[126:127], off offset:256
	v_add_u32_e32 v106, 48, v132
	v_ashrrev_i32_e32 v107, 31, v106
	v_lshlrev_b64 v[108:109], 12, v[122:123]
	v_lshlrev_b64 v[110:111], 13, v[106:107]
	v_lshl_add_u64 v[110:111], s[14:15], 0, v[110:111]
	v_lshl_add_u64 v[108:109], s[24:25], 0, v[108:109]
	v_lshl_add_u64 v[110:111], v[110:111], 0, v[130:131]
	v_lshl_add_u64 v[108:109], v[108:109], 0, v[130:131]
	v_add_co_u32_e32 v110, vcc, s86, v110
	s_waitcnt vmcnt(0)
	v_lshlrev_b32_e32 v112, 16, v98
	v_and_b32_e32 v98, 0xffff0000, v98
	v_lshlrev_b32_e32 v113, 16, v99
	v_and_b32_e32 v99, 0xffff0000, v99
	v_lshlrev_b32_e32 v114, 16, v100
	v_and_b32_e32 v100, 0xffff0000, v100
	v_lshlrev_b32_e32 v115, 16, v101
	v_and_b32_e32 v101, 0xffff0000, v101
	v_lshlrev_b32_e32 v116, 16, v102
	v_and_b32_e32 v102, 0xffff0000, v102
	v_lshlrev_b32_e32 v117, 16, v103
	v_and_b32_e32 v103, 0xffff0000, v103
	v_lshlrev_b32_e32 v118, 16, v104
	v_and_b32_e32 v104, 0xffff0000, v104
	v_lshlrev_b32_e32 v119, 16, v105
	v_and_b32_e32 v105, 0xffff0000, v105
	v_max_f32_e32 v112, v112, v112
	v_max_f32_e32 v120, v98, v98
	v_max_f32_e32 v113, v113, v113
	v_max_f32_e32 v121, v99, v99
	v_max_f32_e32 v114, v114, v114
	v_max_f32_e32 v122, v100, v100
	v_max_f32_e32 v115, v115, v115
	v_max_f32_e32 v123, v101, v101
	v_max_f32_e32 v116, v116, v116
	v_max_f32_e32 v124, v102, v102
	v_max_f32_e32 v117, v117, v117
	v_max_f32_e32 v125, v103, v103
	v_max_f32_e32 v118, v118, v118
	v_max_f32_e32 v126, v104, v104
	v_max_f32_e32 v119, v119, v119
	v_max_f32_e32 v127, v105, v105
	v_max_f32_e32 v98, 0xda24260, v112
	v_max_f32_e32 v99, 0xda24260, v120
	v_max_f32_e32 v100, 0xda24260, v113
	v_max_f32_e32 v101, 0xda24260, v121
	v_max_f32_e32 v102, 0xda24260, v114
	v_max_f32_e32 v103, 0xda24260, v122
	v_max_f32_e32 v104, 0xda24260, v115
	v_max_f32_e32 v105, 0xda24260, v123
	v_max_f32_e32 v112, 0xda24260, v116
	v_max_f32_e32 v113, 0xda24260, v124
	v_max_f32_e32 v114, 0xda24260, v117
	v_max_f32_e32 v115, 0xda24260, v125
	v_max_f32_e32 v116, 0xda24260, v118
	v_max_f32_e32 v117, 0xda24260, v126
	v_max_f32_e32 v118, 0xda24260, v119
	v_max_f32_e32 v119, 0xda24260, v127
	v_pk_mul_f32 v[86:87], v[86:87], v[98:99]
	v_pk_mul_f32 v[88:89], v[88:89], v[100:101]
	v_pk_mul_f32 v[98:99], v[82:83], v[102:103]
	v_pk_mul_f32 v[100:101], v[84:85], v[104:105]
	v_pk_mul_f32 v[94:95], v[94:95], v[112:113]
	v_pk_mul_f32 v[96:97], v[96:97], v[114:115]
	v_cvt_pk_bf16_f32 v82, v86, v87
	v_cvt_pk_bf16_f32 v83, v88, v89
	v_cvt_pk_bf16_f32 v84, v98, v99
	v_cvt_pk_bf16_f32 v85, v100, v101
	v_pk_mul_f32 v[88:89], v[90:91], v[116:117]
	v_pk_mul_f32 v[90:91], v[92:93], v[118:119]
	v_addc_co_u32_e32 v111, vcc, 0, v111, vcc
	global_store_dwordx4 v[108:109], v[82:85], off sc1
	v_cvt_pk_bf16_f32 v86, v94, v95
	v_cvt_pk_bf16_f32 v87, v96, v97
	v_cvt_pk_bf16_f32 v88, v88, v89
	v_cvt_pk_bf16_f32 v89, v90, v91
	global_load_dwordx4 v[82:85], v[110:111], off
	v_add_u32_e32 v90, 0x80, v132
	global_store_dwordx4 v[108:109], v[86:89], off offset:256 sc1
	global_load_dwordx4 v[86:89], v[110:111], off offset:256
	v_ashrrev_i32_e32 v91, 31, v90
	v_lshlrev_b64 v[92:93], 12, v[106:107]
	v_lshlrev_b64 v[94:95], 13, v[90:91]
	v_lshl_add_u64 v[92:93], s[24:25], 0, v[92:93]
	v_lshl_add_u64 v[94:95], s[14:15], 0, v[94:95]
	v_lshl_add_u64 v[92:93], v[92:93], 0, v[130:131]
	v_lshl_add_u64 v[94:95], v[94:95], 0, v[130:131]
	v_add_co_u32_e32 v94, vcc, s86, v94
	s_waitcnt vmcnt(0)
; __device__ __forceinline__ unsigned cvt_pk_bf16(float lo, float hi) { f32x2v_ v = {lo, hi}; bf16x2v_ b = __builtin_convertvector(v, bf16x2v_); return __builtin_bit_cast(unsigned, b); }
; __device__ __forceinline__ float bf_lo(unsigned w) { return __uint_as_float(w << 16); }
; __device__ __forceinline__ float bf_hi(unsigned w) { return __uint_as_float(w & 0xffff0000u); }
;     __device__ __forceinline__ void operator()(const f32x4 (&acc)[2][2][4][2], const Unit& u, int wr, int wc, int fr, int fq) const {
;         asm volatile("" : "+v"(fr), "+v"(fq));
;         const int row0 = u.pm * BM + wr * 64 + fr, col0 = u.pn * BM + wc * 32 + 8 * fq;
; #pragma unroll
;         for (int ai = 0; ai < 2; ++ai)
; #pragma unroll
;             for (int m = 0; m < 4; ++m) { const size_t r = (size_t)(row0 + ai * HALF + m * 16);
; #pragma unroll
;                 for (int bj = 0; bj < 2; ++bj) { const u32x4 g = *(const u32x4*)(GT + r * 4096 + 2048 + col0 + bj * HALF);
;                     f32x4 v0 = acc[ai][bj][m][0], v1 = acc[ai][bj][m][1];
;                     v0[0] *= fmaxf(bf_lo(g.x), 1e-30f); v0[1] *= fmaxf(bf_hi(g.x), 1e-30f); v0[2] *= fmaxf(bf_lo(g.y), 1e-30f); v0[3] *= fmaxf(bf_hi(g.y), 1e-30f);
;                     v1[0] *= fmaxf(bf_lo(g.z), 1e-30f); v1[1] *= fmaxf(bf_hi(g.z), 1e-30f); v1[2] *= fmaxf(bf_lo(g.w), 1e-30f); v1[3] *= fmaxf(bf_hi(g.w), 1e-30f);
;                     u32x4 w; w.x = cvt_pk_bf16(v0[0], v0[1]); w.y = cvt_pk_bf16(v0[2], v0[3]); w.z = cvt_pk_bf16(v1[0], v1[1]); w.w = cvt_pk_bf16(v1[2], v1[3]);
;                     *(u32x4*)(MG + r * 2048 + col0 + bj * HALF) = w; }
;                 if (m & 1) asm volatile("" ::: "memory"); }
	v_lshlrev_b32_e32 v96, 16, v82
	v_and_b32_e32 v82, 0xffff0000, v82
	v_lshlrev_b32_e32 v97, 16, v83
	v_and_b32_e32 v83, 0xffff0000, v83
	v_lshlrev_b32_e32 v98, 16, v84
	v_and_b32_e32 v84, 0xffff0000, v84
	v_lshlrev_b32_e32 v99, 16, v85
	v_and_b32_e32 v85, 0xffff0000, v85
	v_lshlrev_b32_e32 v100, 16, v86
	v_and_b32_e32 v86, 0xffff0000, v86
	v_lshlrev_b32_e32 v101, 16, v87
	v_and_b32_e32 v87, 0xffff0000, v87
	v_lshlrev_b32_e32 v102, 16, v88
	v_and_b32_e32 v88, 0xffff0000, v88
	v_lshlrev_b32_e32 v103, 16, v89
	v_and_b32_e32 v89, 0xffff0000, v89
	v_max_f32_e32 v96, v96, v96
	v_max_f32_e32 v104, v82, v82
	v_max_f32_e32 v97, v97, v97
	v_max_f32_e32 v105, v83, v83
	v_max_f32_e32 v98, v98, v98
	v_max_f32_e32 v106, v84, v84
	v_max_f32_e32 v99, v99, v99
	v_max_f32_e32 v107, v85, v85
	v_max_f32_e32 v100, v100, v100
	v_max_f32_e32 v108, v86, v86
	v_max_f32_e32 v101, v101, v101
	v_max_f32_e32 v109, v87, v87
	v_max_f32_e32 v102, v102, v102
	v_max_f32_e32 v110, v88, v88
	v_max_f32_e32 v103, v103, v103
	v_max_f32_e32 v111, v89, v89
	v_max_f32_e32 v82, 0xda24260, v96
	v_max_f32_e32 v83, 0xda24260, v104
	v_max_f32_e32 v84, 0xda24260, v97
	v_max_f32_e32 v85, 0xda24260, v105
	v_max_f32_e32 v86, 0xda24260, v98
	v_max_f32_e32 v87, 0xda24260, v106
	v_max_f32_e32 v88, 0xda24260, v99
	v_max_f32_e32 v89, 0xda24260, v107
	v_max_f32_e32 v96, 0xda24260, v100
	v_max_f32_e32 v97, 0xda24260, v108
	v_max_f32_e32 v98, 0xda24260, v101
	v_max_f32_e32 v99, 0xda24260, v109
	v_max_f32_e32 v100, 0xda24260, v102
	v_max_f32_e32 v101, 0xda24260, v110
	v_max_f32_e32 v102, 0xda24260, v103
	v_max_f32_e32 v103, 0xda24260, v111
	v_pk_mul_f32 v[70:71], v[70:71], v[82:83]
	v_pk_mul_f32 v[72:73], v[72:73], v[84:85]
	v_pk_mul_f32 v[82:83], v[66:67], v[86:87]
	v_pk_mul_f32 v[84:85], v[68:69], v[88:89]
	v_pk_mul_f32 v[78:79], v[78:79], v[96:97]
	v_pk_mul_f32 v[80:81], v[80:81], v[98:99]
	v_pk_mul_f32 v[74:75], v[74:75], v[100:101]
	v_pk_mul_f32 v[76:77], v[76:77], v[102:103]
	v_cvt_pk_bf16_f32 v66, v70, v71
	v_cvt_pk_bf16_f32 v67, v72, v73
	v_cvt_pk_bf16_f32 v68, v82, v83
	v_cvt_pk_bf16_f32 v69, v84, v85
	v_cvt_pk_bf16_f32 v70, v78, v79
	v_cvt_pk_bf16_f32 v71, v80, v81
	v_cvt_pk_bf16_f32 v72, v74, v75
	v_cvt_pk_bf16_f32 v73, v76, v77
	global_store_dwordx4 v[92:93], v[66:69], off sc1
	global_store_dwordx4 v[92:93], v[70:73], off offset:256 sc1
	v_addc_co_u32_e32 v95, vcc, 0, v95, vcc
	global_load_dwordx4 v[66:69], v[94:95], off
	global_load_dwordx4 v[70:73], v[94:95], off offset:256
	v_add_u32_e32 v74, 0x90, v132
	v_ashrrev_i32_e32 v75, 31, v74
	v_lshlrev_b64 v[76:77], 12, v[90:91]
	v_lshlrev_b64 v[78:79], 13, v[74:75]
	v_lshl_add_u64 v[78:79], s[14:15], 0, v[78:79]
	v_lshl_add_u64 v[76:77], s[24:25], 0, v[76:77]
	v_lshl_add_u64 v[78:79], v[78:79], 0, v[130:131]
	v_lshl_add_u64 v[76:77], v[76:77], 0, v[130:131]
	v_add_co_u32_e32 v78, vcc, s86, v78
	s_waitcnt vmcnt(0)
	v_lshlrev_b32_e32 v80, 16, v66
	v_and_b32_e32 v66, 0xffff0000, v66
	v_lshlrev_b32_e32 v81, 16, v67
	v_and_b32_e32 v67, 0xffff0000, v67
	v_lshlrev_b32_e32 v82, 16, v68
	v_and_b32_e32 v68, 0xffff0000, v68
	v_lshlrev_b32_e32 v83, 16, v69
	v_and_b32_e32 v69, 0xffff0000, v69
	v_lshlrev_b32_e32 v84, 16, v70
	v_and_b32_e32 v70, 0xffff0000, v70
	v_lshlrev_b32_e32 v85, 16, v71
	v_and_b32_e32 v71, 0xffff0000, v71
	v_lshlrev_b32_e32 v86, 16, v72
	v_and_b32_e32 v72, 0xffff0000, v72
	v_lshlrev_b32_e32 v87, 16, v73
	v_and_b32_e32 v73, 0xffff0000, v73
	v_max_f32_e32 v80, v80, v80
	v_max_f32_e32 v88, v66, v66
	v_max_f32_e32 v81, v81, v81
	v_max_f32_e32 v89, v67, v67
	v_max_f32_e32 v82, v82, v82
	v_max_f32_e32 v90, v68, v68
	v_max_f32_e32 v83, v83, v83
	v_max_f32_e32 v91, v69, v69
	v_max_f32_e32 v84, v84, v84
	v_max_f32_e32 v92, v70, v70
	v_max_f32_e32 v85, v85, v85
	v_max_f32_e32 v93, v71, v71
	v_max_f32_e32 v86, v86, v86
	v_max_f32_e32 v94, v72, v72
	v_max_f32_e32 v87, v87, v87
	v_max_f32_e32 v95, v73, v73
	v_max_f32_e32 v66, 0xda24260, v80
	v_max_f32_e32 v67, 0xda24260, v88
	v_max_f32_e32 v68, 0xda24260, v81
	v_max_f32_e32 v69, 0xda24260, v89
	v_max_f32_e32 v70, 0xda24260, v82
	v_max_f32_e32 v71, 0xda24260, v90
	v_max_f32_e32 v72, 0xda24260, v83
	v_max_f32_e32 v73, 0xda24260, v91
	v_max_f32_e32 v80, 0xda24260, v84
	v_max_f32_e32 v81, 0xda24260, v92
	v_max_f32_e32 v82, 0xda24260, v85
	v_max_f32_e32 v83, 0xda24260, v93
	v_max_f32_e32 v84, 0xda24260, v86
	v_max_f32_e32 v85, 0xda24260, v94
	v_max_f32_e32 v86, 0xda24260, v87
	v_max_f32_e32 v87, 0xda24260, v95
	v_pk_mul_f32 v[54:55], v[54:55], v[66:67]
	v_pk_mul_f32 v[56:57], v[56:57], v[68:69]
	v_pk_mul_f32 v[66:67], v[50:51], v[70:71]
	v_pk_mul_f32 v[68:69], v[52:53], v[72:73]
	v_pk_mul_f32 v[62:63], v[62:63], v[80:81]
	v_pk_mul_f32 v[64:65], v[64:65], v[82:83]
	v_cvt_pk_bf16_f32 v50, v54, v55
	v_cvt_pk_bf16_f32 v51, v56, v57
	v_cvt_pk_bf16_f32 v52, v66, v67
	v_cvt_pk_bf16_f32 v53, v68, v69
	v_pk_mul_f32 v[56:57], v[58:59], v[84:85]
	v_pk_mul_f32 v[58:59], v[60:61], v[86:87]
	v_addc_co_u32_e32 v79, vcc, 0, v79, vcc
	global_store_dwordx4 v[76:77], v[50:53], off sc1
	v_cvt_pk_bf16_f32 v54, v62, v63
	v_cvt_pk_bf16_f32 v55, v64, v65
	v_cvt_pk_bf16_f32 v56, v56, v57
	v_cvt_pk_bf16_f32 v57, v58, v59
	global_load_dwordx4 v[50:53], v[78:79], off
	v_add_u32_e32 v58, 0xa0, v132
	global_store_dwordx4 v[76:77], v[54:57], off offset:256 sc1
	global_load_dwordx4 v[54:57], v[78:79], off offset:256
	v_ashrrev_i32_e32 v59, 31, v58
	v_lshlrev_b64 v[60:61], 12, v[74:75]
	v_lshlrev_b64 v[62:63], 13, v[58:59]
	v_lshl_add_u64 v[60:61], s[24:25], 0, v[60:61]
	v_lshl_add_u64 v[62:63], s[14:15], 0, v[62:63]
	v_lshl_add_u64 v[60:61], v[60:61], 0, v[130:131]
	v_lshl_add_u64 v[62:63], v[62:63], 0, v[130:131]
	v_add_co_u32_e32 v62, vcc, s86, v62
	s_waitcnt vmcnt(0)
; __device__ __forceinline__ unsigned cvt_pk_bf16(float lo, float hi) { f32x2v_ v = {lo, hi}; bf16x2v_ b = __builtin_convertvector(v, bf16x2v_); return __builtin_bit_cast(unsigned, b); }
; __device__ __forceinline__ float bf_lo(unsigned w) { return __uint_as_float(w << 16); }
; __device__ __forceinline__ float bf_hi(unsigned w) { return __uint_as_float(w & 0xffff0000u); }
;     __device__ __forceinline__ void operator()(const f32x4 (&acc)[2][2][4][2], const Unit& u, int wr, int wc, int fr, int fq) const {
;         asm volatile("" : "+v"(fr), "+v"(fq));
;         const int row0 = u.pm * BM + wr * 64 + fr, col0 = u.pn * BM + wc * 32 + 8 * fq;
; #pragma unroll
;         for (int ai = 0; ai < 2; ++ai)
; #pragma unroll
;             for (int m = 0; m < 4; ++m) { const size_t r = (size_t)(row0 + ai * HALF + m * 16);
; #pragma unroll
;                 for (int bj = 0; bj < 2; ++bj) { const u32x4 g = *(const u32x4*)(GT + r * 4096 + 2048 + col0 + bj * HALF);
;                     f32x4 v0 = acc[ai][bj][m][0], v1 = acc[ai][bj][m][1];
;                     v0[0] *= fmaxf(bf_lo(g.x), 1e-30f); v0[1] *= fmaxf(bf_hi(g.x), 1e-30f); v0[2] *= fmaxf(bf_lo(g.y), 1e-30f); v0[3] *= fmaxf(bf_hi(g.y), 1e-30f);
;                     v1[0] *= fmaxf(bf_lo(g.z), 1e-30f); v1[1] *= fmaxf(bf_hi(g.z), 1e-30f); v1[2] *= fmaxf(bf_lo(g.w), 1e-30f); v1[3] *= fmaxf(bf_hi(g.w), 1e-30f);
;                     u32x4 w; w.x = cvt_pk_bf16(v0[0], v0[1]); w.y = cvt_pk_bf16(v0[2], v0[3]); w.z = cvt_pk_bf16(v1[0], v1[1]); w.w = cvt_pk_bf16(v1[2], v1[3]);
;                     *(u32x4*)(MG + r * 2048 + col0 + bj * HALF) = w; }
;                 if (m & 1) asm volatile("" ::: "memory"); }
	v_lshlrev_b32_e32 v64, 16, v50
	v_and_b32_e32 v50, 0xffff0000, v50
	v_lshlrev_b32_e32 v65, 16, v51
	v_and_b32_e32 v51, 0xffff0000, v51
	v_lshlrev_b32_e32 v66, 16, v52
	v_and_b32_e32 v52, 0xffff0000, v52
	v_lshlrev_b32_e32 v67, 16, v53
	v_and_b32_e32 v53, 0xffff0000, v53
	v_lshlrev_b32_e32 v68, 16, v54
	v_and_b32_e32 v54, 0xffff0000, v54
	v_lshlrev_b32_e32 v69, 16, v55
	v_and_b32_e32 v55, 0xffff0000, v55
	v_lshlrev_b32_e32 v70, 16, v56
	v_and_b32_e32 v56, 0xffff0000, v56
	v_lshlrev_b32_e32 v71, 16, v57
	v_and_b32_e32 v57, 0xffff0000, v57
	v_max_f32_e32 v64, v64, v64
	v_max_f32_e32 v72, v50, v50
	v_max_f32_e32 v65, v65, v65
	v_max_f32_e32 v73, v51, v51
	v_max_f32_e32 v66, v66, v66
	v_max_f32_e32 v74, v52, v52
	v_max_f32_e32 v67, v67, v67
	v_max_f32_e32 v75, v53, v53
	v_max_f32_e32 v68, v68, v68
	v_max_f32_e32 v76, v54, v54
	v_max_f32_e32 v69, v69, v69
	v_max_f32_e32 v77, v55, v55
	v_max_f32_e32 v70, v70, v70
	v_max_f32_e32 v78, v56, v56
	v_max_f32_e32 v71, v71, v71
	v_max_f32_e32 v79, v57, v57
	v_max_f32_e32 v50, 0xda24260, v64
	v_max_f32_e32 v51, 0xda24260, v72
	v_max_f32_e32 v52, 0xda24260, v65
	v_max_f32_e32 v53, 0xda24260, v73
	v_max_f32_e32 v54, 0xda24260, v66
	v_max_f32_e32 v55, 0xda24260, v74
	v_max_f32_e32 v56, 0xda24260, v67
	v_max_f32_e32 v57, 0xda24260, v75
	v_max_f32_e32 v64, 0xda24260, v68
	v_max_f32_e32 v65, 0xda24260, v76
	v_max_f32_e32 v66, 0xda24260, v69
	v_max_f32_e32 v67, 0xda24260, v77
	v_max_f32_e32 v68, 0xda24260, v70
	v_max_f32_e32 v69, 0xda24260, v78
	v_max_f32_e32 v70, 0xda24260, v71
	v_max_f32_e32 v71, 0xda24260, v79
	v_pk_mul_f32 v[38:39], v[38:39], v[50:51]
	v_pk_mul_f32 v[40:41], v[40:41], v[52:53]
	v_pk_mul_f32 v[50:51], v[34:35], v[54:55]
	v_pk_mul_f32 v[52:53], v[36:37], v[56:57]
	v_pk_mul_f32 v[46:47], v[46:47], v[64:65]
	v_pk_mul_f32 v[48:49], v[48:49], v[66:67]
	v_pk_mul_f32 v[42:43], v[42:43], v[68:69]
	v_pk_mul_f32 v[44:45], v[44:45], v[70:71]
	v_cvt_pk_bf16_f32 v34, v38, v39
	v_cvt_pk_bf16_f32 v35, v40, v41
	v_cvt_pk_bf16_f32 v36, v50, v51
	v_cvt_pk_bf16_f32 v37, v52, v53
	v_cvt_pk_bf16_f32 v38, v46, v47
	v_cvt_pk_bf16_f32 v39, v48, v49
	v_cvt_pk_bf16_f32 v40, v42, v43
	v_cvt_pk_bf16_f32 v41, v44, v45
	global_store_dwordx4 v[60:61], v[34:37], off sc1
	global_store_dwordx4 v[60:61], v[38:41], off offset:256 sc1
	v_addc_co_u32_e32 v63, vcc, 0, v63, vcc
	global_load_dwordx4 v[34:37], v[62:63], off
	global_load_dwordx4 v[38:41], v[62:63], off offset:256
	v_add_u32_e32 v42, 0xb0, v132
	v_ashrrev_i32_e32 v43, 31, v42
	v_lshlrev_b64 v[44:45], 12, v[58:59]
	v_lshlrev_b64 v[46:47], 13, v[42:43]
	v_lshl_add_u64 v[46:47], s[14:15], 0, v[46:47]
	v_lshl_add_u64 v[44:45], s[24:25], 0, v[44:45]
	v_lshl_add_u64 v[46:47], v[46:47], 0, v[130:131]
	v_lshl_add_u64 v[44:45], v[44:45], 0, v[130:131]
	v_add_co_u32_e32 v46, vcc, s86, v46
	s_waitcnt vmcnt(0)
	v_lshlrev_b32_e32 v48, 16, v34
	v_and_b32_e32 v34, 0xffff0000, v34
	v_lshlrev_b32_e32 v49, 16, v35
	v_and_b32_e32 v35, 0xffff0000, v35
	v_lshlrev_b32_e32 v50, 16, v36
	v_and_b32_e32 v36, 0xffff0000, v36
	v_lshlrev_b32_e32 v51, 16, v37
	v_and_b32_e32 v37, 0xffff0000, v37
	v_lshlrev_b32_e32 v52, 16, v38
	v_and_b32_e32 v38, 0xffff0000, v38
	v_lshlrev_b32_e32 v53, 16, v39
	v_and_b32_e32 v39, 0xffff0000, v39
	v_lshlrev_b32_e32 v54, 16, v40
	v_and_b32_e32 v40, 0xffff0000, v40
	v_lshlrev_b32_e32 v55, 16, v41
	v_and_b32_e32 v41, 0xffff0000, v41
	v_max_f32_e32 v48, v48, v48
	v_max_f32_e32 v56, v34, v34
	v_max_f32_e32 v49, v49, v49
	v_max_f32_e32 v57, v35, v35
	v_max_f32_e32 v50, v50, v50
	v_max_f32_e32 v58, v36, v36
	v_max_f32_e32 v51, v51, v51
	v_max_f32_e32 v59, v37, v37
	v_max_f32_e32 v52, v52, v52
	v_max_f32_e32 v60, v38, v38
	v_max_f32_e32 v53, v53, v53
	v_max_f32_e32 v61, v39, v39
	v_max_f32_e32 v54, v54, v54
	v_max_f32_e32 v62, v40, v40
	v_max_f32_e32 v55, v55, v55
	v_max_f32_e32 v63, v41, v41
	v_max_f32_e32 v34, 0xda24260, v48
	v_max_f32_e32 v35, 0xda24260, v56
	v_max_f32_e32 v36, 0xda24260, v49
	v_max_f32_e32 v37, 0xda24260, v57
	v_max_f32_e32 v38, 0xda24260, v50
	v_max_f32_e32 v39, 0xda24260, v58
	v_max_f32_e32 v40, 0xda24260, v51
	v_max_f32_e32 v41, 0xda24260, v59
	v_max_f32_e32 v48, 0xda24260, v52
	v_max_f32_e32 v49, 0xda24260, v60
	v_max_f32_e32 v50, 0xda24260, v53
	v_max_f32_e32 v51, 0xda24260, v61
	v_max_f32_e32 v52, 0xda24260, v54
	v_max_f32_e32 v53, 0xda24260, v62
	v_max_f32_e32 v54, 0xda24260, v55
	v_max_f32_e32 v55, 0xda24260, v63
	v_pk_mul_f32 v[22:23], v[22:23], v[34:35]
	v_pk_mul_f32 v[24:25], v[24:25], v[36:37]
	v_pk_mul_f32 v[34:35], v[18:19], v[38:39]
	v_pk_mul_f32 v[36:37], v[20:21], v[40:41]
	v_pk_mul_f32 v[30:31], v[30:31], v[48:49]
	v_pk_mul_f32 v[32:33], v[32:33], v[50:51]
	v_cvt_pk_bf16_f32 v18, v22, v23
	v_cvt_pk_bf16_f32 v19, v24, v25
	v_cvt_pk_bf16_f32 v20, v34, v35
	v_cvt_pk_bf16_f32 v21, v36, v37
	v_pk_mul_f32 v[24:25], v[26:27], v[52:53]
	v_pk_mul_f32 v[26:27], v[28:29], v[54:55]
	v_addc_co_u32_e32 v47, vcc, 0, v47, vcc
	global_store_dwordx4 v[44:45], v[18:21], off sc1
	v_cvt_pk_bf16_f32 v22, v30, v31
	v_cvt_pk_bf16_f32 v23, v32, v33
	v_cvt_pk_bf16_f32 v24, v24, v25
	v_cvt_pk_bf16_f32 v25, v26, v27
	global_load_dwordx4 v[18:21], v[46:47], off
	v_lshlrev_b64 v[26:27], 12, v[42:43]
	global_store_dwordx4 v[44:45], v[22:25], off offset:256 sc1
	global_load_dwordx4 v[22:25], v[46:47], off offset:256
	v_lshl_add_u64 v[26:27], s[24:25], 0, v[26:27]
	v_lshl_add_u64 v[26:27], v[26:27], 0, v[130:131]
	s_andn2_b64 vcc, exec, s[4:5]
	s_mov_b64 s[4:5], -1
	s_waitcnt vmcnt(0)
; __device__ __forceinline__ unsigned cvt_pk_bf16(float lo, float hi) { f32x2v_ v = {lo, hi}; bf16x2v_ b = __builtin_convertvector(v, bf16x2v_); return __builtin_bit_cast(unsigned, b); }
; #define PG8_BAR __builtin_amdgcn_s_barrier()
;     __device__ __forceinline__ void operator()(const f32x4 (&acc)[2][2][4][2], const Unit& u, int wr, int wc, int fr, int fq) const {
;         asm volatile("" : "+v"(fr), "+v"(fq));
;         const int row0 = u.pm * BM + wr * 64 + fr, col0 = u.pn * BM + wc * 32 + 8 * fq;
; #pragma unroll
;         for (int ai = 0; ai < 2; ++ai)
; #pragma unroll
;             for (int m = 0; m < 4; ++m) { const size_t r = (size_t)(row0 + ai * HALF + m * 16);
; #pragma unroll
;                 for (int bj = 0; bj < 2; ++bj) { const u32x4 g = *(const u32x4*)(GT + r * 4096 + 2048 + col0 + bj * HALF);
;                     f32x4 v0 = acc[ai][bj][m][0], v1 = acc[ai][bj][m][1];
;                     v0[0] *= fmaxf(bf_lo(g.x), 1e-30f); v0[1] *= fmaxf(bf_hi(g.x), 1e-30f); v0[2] *= fmaxf(bf_lo(g.y), 1e-30f); v0[3] *= fmaxf(bf_hi(g.y), 1e-30f);
;                     v1[0] *= fmaxf(bf_lo(g.z), 1e-30f); v1[1] *= fmaxf(bf_hi(g.z), 1e-30f); v1[2] *= fmaxf(bf_lo(g.w), 1e-30f); v1[3] *= fmaxf(bf_hi(g.w), 1e-30f);
;                     u32x4 w; w.x = cvt_pk_bf16(v0[0], v0[1]); w.y = cvt_pk_bf16(v0[2], v0[3]); w.z = cvt_pk_bf16(v1[0], v1[1]); w.w = cvt_pk_bf16(v1[2], v1[3]);
;                     *(u32x4*)(MG + r * 2048 + col0 + bj * HALF) = w; }
;                 if (m & 1) asm volatile("" ::: "memory"); }
; template <class Epi, class Sched, bool ALIGN_EPI = false, bool SP2 = false>
; __device__ __forceinline__ void gemm_phase(PG8_LAS unsigned char* lds, const Gemm g, const Sched& S, const Epi& E) {
;     ...
;         if (!has_next) break;
; #pragma unroll
;         for (int a = 0; a < 2; ++a)
; #pragma unroll
;             for (int b = 0; b < 2; ++b)
; #pragma unroll
;                 for (int m = 0; m < 4; ++m)
; #pragma unroll
;                     for (int n = 0; n < 2; ++n) { acc[a][b][m][n] = (f32x4){0.f, 0.f, 0.f, 0.f}; asm volatile("" : "+v"(acc[a][b][m][n])); }
;         cur = nxt; cA = nA; cB = nB; ++ui;
;         if constexpr (Sched::GATHER) {
; #pragma unroll
;             for (int h = 0; h < 2; ++h)
; #pragma unroll
;                 for (int i = 0; i < 2; ++i) voffAc[h][i] = voffAn[h][i]; }
;         if constexpr (ALIGN_EPI) { if (wr == 1) PG8_BAR; }
	v_lshlrev_b32_e32 v28, 16, v18
	v_and_b32_e32 v18, 0xffff0000, v18
	v_lshlrev_b32_e32 v29, 16, v19
	v_and_b32_e32 v19, 0xffff0000, v19
	v_lshlrev_b32_e32 v30, 16, v20
	v_and_b32_e32 v20, 0xffff0000, v20
	v_lshlrev_b32_e32 v31, 16, v21
	v_and_b32_e32 v21, 0xffff0000, v21
	v_lshlrev_b32_e32 v32, 16, v22
	v_and_b32_e32 v22, 0xffff0000, v22
	v_lshlrev_b32_e32 v33, 16, v23
	v_and_b32_e32 v23, 0xffff0000, v23
	v_lshlrev_b32_e32 v34, 16, v24
	v_and_b32_e32 v24, 0xffff0000, v24
	v_lshlrev_b32_e32 v35, 16, v25
	v_and_b32_e32 v25, 0xffff0000, v25
	v_max_f32_e32 v28, v28, v28
	v_max_f32_e32 v36, v18, v18
	v_max_f32_e32 v29, v29, v29
	v_max_f32_e32 v37, v19, v19
	v_max_f32_e32 v30, v30, v30
	v_max_f32_e32 v38, v20, v20
	v_max_f32_e32 v31, v31, v31
	v_max_f32_e32 v39, v21, v21
	v_max_f32_e32 v32, v32, v32
	v_max_f32_e32 v40, v22, v22
	v_max_f32_e32 v33, v33, v33
	v_max_f32_e32 v41, v23, v23
	v_max_f32_e32 v34, v34, v34
	v_max_f32_e32 v42, v24, v24
	v_max_f32_e32 v35, v35, v35
	v_max_f32_e32 v43, v25, v25
	v_max_f32_e32 v18, 0xda24260, v28
	v_max_f32_e32 v19, 0xda24260, v36
	v_max_f32_e32 v20, 0xda24260, v29
	v_max_f32_e32 v21, 0xda24260, v37
	v_max_f32_e32 v22, 0xda24260, v30
	v_max_f32_e32 v23, 0xda24260, v38
	v_max_f32_e32 v24, 0xda24260, v31
	v_max_f32_e32 v25, 0xda24260, v39
	v_max_f32_e32 v28, 0xda24260, v32
	v_max_f32_e32 v29, 0xda24260, v40
	v_max_f32_e32 v30, 0xda24260, v33
	v_max_f32_e32 v31, 0xda24260, v41
	v_max_f32_e32 v32, 0xda24260, v34
	v_max_f32_e32 v33, 0xda24260, v42
	v_max_f32_e32 v34, 0xda24260, v35
	v_max_f32_e32 v35, 0xda24260, v43
	v_pk_mul_f32 v[10:11], v[10:11], v[18:19]
	v_pk_mul_f32 v[12:13], v[12:13], v[20:21]
	v_pk_mul_f32 v[6:7], v[6:7], v[22:23]
	v_pk_mul_f32 v[8:9], v[8:9], v[24:25]
	v_pk_mul_f32 v[14:15], v[14:15], v[28:29]
	v_pk_mul_f32 v[16:17], v[16:17], v[30:31]
	v_pk_mul_f32 v[18:19], v[2:3], v[32:33]
	v_pk_mul_f32 v[20:21], v[4:5], v[34:35]
	v_cvt_pk_bf16_f32 v2, v10, v11
	v_cvt_pk_bf16_f32 v3, v12, v13
	v_cvt_pk_bf16_f32 v4, v6, v7
	v_cvt_pk_bf16_f32 v5, v8, v9
	v_cvt_pk_bf16_f32 v6, v14, v15
	v_cvt_pk_bf16_f32 v7, v16, v17
	v_cvt_pk_bf16_f32 v8, v18, v19
	v_cvt_pk_bf16_f32 v9, v20, v21
	global_store_dwordx4 v[26:27], v[2:5], off sc1
	global_store_dwordx4 v[26:27], v[6:9], off offset:256 sc1
	s_cbranch_vccnz .LBB0_372
	s_mov_b32 s9, s8
	s_mov_b32 s10, s8
	s_mov_b32 s11, s8
	v_mov_b64_e32 v[2:3], s[8:9]
	v_mov_b64_e32 v[120:121], s[10:11]
	v_mov_b64_e32 v[116:117], s[10:11]
	v_mov_b64_e32 v[104:105], s[10:11]
	v_mov_b64_e32 v[100:101], s[10:11]
	v_mov_b64_e32 v[88:89], s[10:11]
	v_mov_b64_e32 v[84:85], s[10:11]
	v_mov_b64_e32 v[72:73], s[10:11]
	v_mov_b64_e32 v[68:69], s[10:11]
	v_mov_b64_e32 v[128:129], s[10:11]
	v_mov_b64_e32 v[124:125], s[10:11]
	v_mov_b64_e32 v[112:113], s[10:11]
	v_mov_b64_e32 v[108:109], s[10:11]
	v_mov_b64_e32 v[96:97], s[10:11]
	v_mov_b64_e32 v[92:93], s[10:11]
	v_mov_b64_e32 v[80:81], s[10:11]
	v_mov_b64_e32 v[76:77], s[10:11]
	v_mov_b64_e32 v[56:57], s[10:11]
	v_mov_b64_e32 v[52:53], s[10:11]
	v_mov_b64_e32 v[40:41], s[10:11]
	v_mov_b64_e32 v[36:37], s[10:11]
	v_mov_b64_e32 v[24:25], s[10:11]
	v_mov_b64_e32 v[20:21], s[10:11]
	v_mov_b64_e32 v[12:13], s[10:11]
	v_mov_b64_e32 v[6:7], s[8:9]
	v_mov_b64_e32 v[64:65], s[10:11]
	v_mov_b64_e32 v[60:61], s[10:11]
	v_mov_b64_e32 v[48:49], s[10:11]
	v_mov_b64_e32 v[44:45], s[10:11]
	v_mov_b64_e32 v[32:33], s[10:11]
	v_mov_b64_e32 v[28:29], s[10:11]
	v_mov_b64_e32 v[16:17], s[10:11]
	v_mov_b64_e32 v[4:5], s[10:11]
	v_mov_b64_e32 v[118:119], s[8:9]
	v_mov_b64_e32 v[114:115], s[8:9]
	v_mov_b64_e32 v[102:103], s[8:9]
	v_mov_b64_e32 v[98:99], s[8:9]
	v_mov_b64_e32 v[86:87], s[8:9]
	v_mov_b64_e32 v[82:83], s[8:9]
	v_mov_b64_e32 v[70:71], s[8:9]
	v_mov_b64_e32 v[66:67], s[8:9]
	v_mov_b64_e32 v[126:127], s[8:9]
	v_mov_b64_e32 v[122:123], s[8:9]
	v_mov_b64_e32 v[110:111], s[8:9]
	v_mov_b64_e32 v[106:107], s[8:9]
	v_mov_b64_e32 v[94:95], s[8:9]
	v_mov_b64_e32 v[90:91], s[8:9]
	v_mov_b64_e32 v[78:79], s[8:9]
	v_mov_b64_e32 v[74:75], s[8:9]
	v_mov_b64_e32 v[54:55], s[8:9]
	v_mov_b64_e32 v[50:51], s[8:9]
	v_mov_b64_e32 v[38:39], s[8:9]
	v_mov_b64_e32 v[34:35], s[8:9]
	v_mov_b64_e32 v[22:23], s[8:9]
	v_mov_b64_e32 v[18:19], s[8:9]
	v_mov_b64_e32 v[10:11], s[8:9]
	v_mov_b64_e32 v[8:9], s[10:11]
	v_mov_b64_e32 v[62:63], s[8:9]
	v_mov_b64_e32 v[58:59], s[8:9]
	v_mov_b64_e32 v[46:47], s[8:9]
	v_mov_b64_e32 v[42:43], s[8:9]
	v_mov_b64_e32 v[30:31], s[8:9]
	v_mov_b64_e32 v[26:27], s[8:9]
	v_mov_b64_e32 v[14:15], s[8:9]
	s_andn2_b64 vcc, exec, s[12:13]
	s_cbranch_vccnz .LBB0_371
	s_barrier
	s_branch .LBB0_371

; #define GAS __attribute__((address_space(1)))
; #define LAS __attribute__((address_space(3)))
; #define LDS_WAIT() asm volatile("s_waitcnt lgkmcnt(0)" ::: "memory")
; __device__ __forceinline__ unsigned pk2(float lo, float hi) { return f2bf(lo) | (f2bf(hi) << 16); }
; __device__ __forceinline__ void p0_transpose_item(const float* W, int N, int k0, int n0, bf16* WT, int K, int dst_row0, LAS float* scr, int lane, const float* kscale = nullptr, int permhalf = -1) {
;     typedef float f32x4t __attribute__((ext_vector_type(4)));
;     const int c = lane & 7;
;     float ks[8];
; #pragma unroll
;     for (int i = 0; i < 8; ++i) ks[i] = kscale ? kscale[k0 + 8 * c + i] : 1.0f;
; #pragma unroll
;     for (int i = 0; i < 8; ++i) { const int kk = 8 * i + (lane >> 3), nn = (lane & 7) * 4;
;         *(LAS f32x4t*)(scr + kk * 36 + nn) = *(const GAS f32x4t*)(W + (size_t)(k0 + kk) * N + n0 + nn); }
;     LDS_WAIT(); asm volatile("" ::: "memory");
; #pragma unroll
;     for (int j = 0; j < 4; ++j) { const int n = (lane >> 3) + 8 * j; const LAS float* s = scr + (8 * c) * 36 + n;
;         v4u o; o.x = pk2(s[0 * 36] * ks[0], s[1 * 36] * ks[1]); o.y = pk2(s[2 * 36] * ks[2], s[3 * 36] * ks[3]); o.z = pk2(s[4 * 36] * ks[4], s[5 * 36] * ks[5]); o.w = pk2(s[6 * 36] * ks[6], s[7 * 36] * ks[7]);
;         const int drow = permhalf < 0 ? n : (32 * (n >> 4) + 8 * ((n >> 2) & 3) + 4 * permhalf + (n & 3));
;         *(GAS v4u*)(WT + (size_t)(dst_row0 + drow) * K + k0 + 8 * c) = o; }
;     LDS_WAIT(); asm volatile("" ::: "memory");
; }
; __device__ __forceinline__ void conv_item(KArgs a, int r, LAS float* scr, int lane) {
;     ...
;     if (r < CONV_IE) { const int e = r / 512, q = r % 512, kb = q / 16, nb = q % 16, n0 = 32 * nb;
;         p0_transpose_item(a->in[18] + (size_t)e * 2048 * 512, 512, 64 * kb, n0, (bf16*)(ws + WS_W13), 2048, e * 1024 + (n0 >> 7) * 256 + (n0 & 127), scr, lane, a->in[15]); return; } r -= CONV_IE;
.LBB0_406:
	s_load_dwordx2 s[36:37], s[14:15], 0x90
	s_lshl_b32 s7, s24, 4
	s_ashr_i32 s6, s19, 9
	s_sub_i32 s7, s18, s7
	s_sext_i32_i16 s19, s7
	s_ashr_i32 s7, s6, 31
	s_lshl_b32 s18, s19, 5
	s_lshl_b64 s[46:47], s[6:7], 22
	s_waitcnt lgkmcnt(0)
	s_add_u32 s7, s36, s46
	s_addc_u32 s24, s37, s47
	s_lshl_b32 s19, s19, 6
	s_lshl_b32 s6, s6, 10
	s_and_b32 s19, s19, 0xffffff00
	s_add_i32 s19, s19, s6
	s_and_b32 s6, s18, 0x60
	s_or_b32 s6, s19, s6
	s_ashr_i32 s19, s18, 31
	s_lshl_b64 s[18:19], s[18:19], 2
	s_add_u32 s18, s7, s18
	v_or_b32_e32 v36, s44, v18
	s_addc_u32 s19, s24, s19
	v_ashrrev_i32_e32 v37, 31, v36
	v_lshl_add_u64 v[16:17], s[18:19], 0, v[4:5]
	v_or_b32_e32 v28, s44, v1
	v_or_b32_e32 v30, s44, v3
	v_lshlrev_b64 v[36:37], 11, v[36:37]
	v_ashrrev_i32_e32 v29, 31, v28
	v_ashrrev_i32_e32 v31, 31, v30
	v_lshl_add_u64 v[44:45], v[16:17], 0, v[36:37]
	v_or_b32_e32 v36, s44, v19
	v_lshlrev_b64 v[28:29], 11, v[28:29]
	v_lshlrev_b64 v[30:31], 11, v[30:31]
	v_ashrrev_i32_e32 v37, 31, v36
	v_lshl_add_u64 v[28:29], v[16:17], 0, v[28:29]
	v_lshl_add_u64 v[32:33], v[16:17], 0, v[30:31]
	v_lshlrev_b64 v[36:37], 11, v[36:37]
	global_load_dwordx4 v[28:31], v[28:29], off
	s_nop 0
	global_load_dwordx4 v[32:35], v[32:33], off
	v_lshl_add_u64 v[46:47], v[16:17], 0, v[36:37]
	global_load_dwordx4 v[36:39], v[44:45], off
	global_load_dwordx4 v[40:43], v[46:47], off
	v_or_b32_e32 v44, s44, v20
	v_ashrrev_i32_e32 v45, 31, v44
	v_lshlrev_b64 v[44:45], 11, v[44:45]
	v_lshl_add_u64 v[52:53], v[16:17], 0, v[44:45]
	v_or_b32_e32 v44, s44, v21
	v_ashrrev_i32_e32 v45, 31, v44
	v_lshlrev_b64 v[44:45], 11, v[44:45]
	v_lshl_add_u64 v[54:55], v[16:17], 0, v[44:45]
	global_load_dwordx4 v[44:47], v[52:53], off
	global_load_dwordx4 v[48:51], v[54:55], off
	v_or_b32_e32 v52, s44, v22
	v_ashrrev_i32_e32 v53, 31, v52
	v_lshlrev_b64 v[52:53], 11, v[52:53]
	v_lshl_add_u64 v[60:61], v[16:17], 0, v[52:53]
	v_or_b32_e32 v52, s44, v23
	v_ashrrev_i32_e32 v53, 31, v52
	v_lshlrev_b64 v[52:53], 11, v[52:53]
	v_lshl_add_u64 v[16:17], v[16:17], 0, v[52:53]
	global_load_dwordx4 v[52:55], v[60:61], off
	global_load_dwordx4 v[56:59], v[16:17], off
	s_ashr_i32 s45, s44, 31
	s_lshl_b64 s[18:19], s[44:45], 1
	s_add_u32 s18, s42, s18
	v_mov_b32_e32 v7, v5
	s_addc_u32 s19, s43, s19
	v_lshl_add_u64 v[16:17], s[18:19], 0, v[6:7]
	v_lshl_add_u64 v[16:17], v[16:17], 0, s[38:39]
	s_waitcnt vmcnt(7)
	ds_write_b128 v25, v[28:31]
	s_waitcnt vmcnt(6)
	ds_write_b128 v25, v[32:35] offset:1152
	s_waitcnt vmcnt(5)
	ds_write_b128 v25, v[36:39] offset:2304
	s_waitcnt vmcnt(4)
	ds_write_b128 v25, v[40:43] offset:3456
	s_waitcnt vmcnt(3)
	ds_write_b128 v25, v[44:47] offset:4608
	s_waitcnt vmcnt(2)
	ds_write_b128 v25, v[48:51] offset:5760
	s_waitcnt vmcnt(1)
	ds_write_b128 v25, v[52:55] offset:6912
	s_waitcnt vmcnt(0)
	ds_write_b128 v25, v[56:59] offset:8064
	s_waitcnt lgkmcnt(0)
	ds_read2_b32 v[32:33], v24 offset0:36 offset1:44
	ds_read2_b32 v[34:35], v24 offset0:72 offset1:80
	ds_read2_b32 v[36:37], v24 offset0:108 offset1:116
	ds_read2_b32 v[38:39], v24 offset1:8
	ds_read2_b32 v[40:41], v24 offset0:144 offset1:152
	ds_read2_b32 v[42:43], v24 offset0:180 offset1:188
	ds_read2_b32 v[44:45], v24 offset0:216 offset1:224
	ds_read2_b32 v[46:47], v26 offset0:124 offset1:132
	s_waitcnt lgkmcnt(7)
	v_mov_b32_e32 v30, v32
	s_waitcnt lgkmcnt(5)
	v_mov_b32_e32 v31, v36
	s_waitcnt lgkmcnt(3)
	v_mov_b32_e32 v48, v40
	s_waitcnt lgkmcnt(1)
	v_mov_b32_e32 v49, v44
	v_mov_b32_e32 v50, v42
	s_waitcnt lgkmcnt(0)
; #define GAS __attribute__((address_space(1)))
; #define LAS __attribute__((address_space(3)))
; #define LDS_WAIT() asm volatile("s_waitcnt lgkmcnt(0)" ::: "memory")
; __device__ __forceinline__ unsigned pk2(float lo, float hi) { return f2bf(lo) | (f2bf(hi) << 16); }
; __device__ __forceinline__ void p0_transpose_item(const float* W, int N, int k0, int n0, bf16* WT, int K, int dst_row0, LAS float* scr, int lane, const float* kscale = nullptr, int permhalf = -1) {
;     typedef float f32x4t __attribute__((ext_vector_type(4)));
;     const int c = lane & 7;
;     float ks[8];
; #pragma unroll
;     for (int i = 0; i < 8; ++i) ks[i] = kscale ? kscale[k0 + 8 * c + i] : 1.0f;
; #pragma unroll
;     for (int i = 0; i < 8; ++i) { const int kk = 8 * i + (lane >> 3), nn = (lane & 7) * 4;
;         *(LAS f32x4t*)(scr + kk * 36 + nn) = *(const GAS f32x4t*)(W + (size_t)(k0 + kk) * N + n0 + nn); }
;     LDS_WAIT(); asm volatile("" ::: "memory");
; #pragma unroll
;     for (int j = 0; j < 4; ++j) { const int n = (lane >> 3) + 8 * j; const LAS float* s = scr + (8 * c) * 36 + n;
;         v4u o; o.x = pk2(s[0 * 36] * ks[0], s[1 * 36] * ks[1]); o.y = pk2(s[2 * 36] * ks[2], s[3 * 36] * ks[3]); o.z = pk2(s[4 * 36] * ks[4], s[5 * 36] * ks[5]); o.w = pk2(s[6 * 36] * ks[6], s[7 * 36] * ks[7]);
;         const int drow = permhalf < 0 ? n : (32 * (n >> 4) + 8 * ((n >> 2) & 3) + 4 * permhalf + (n & 3));
;         *(GAS v4u*)(WT + (size_t)(dst_row0 + drow) * K + k0 + 8 * c) = o; }
;     LDS_WAIT(); asm volatile("" ::: "memory");
; }
	v_mov_b32_e32 v51, v46
	v_mov_b32_e32 v28, v38
	v_mov_b32_e32 v29, v34
	v_pk_mul_f32 v[30:31], v[8:9], v[30:31]
	v_pk_mul_f32 v[48:49], v[14:15], v[48:49]
	v_pk_mul_f32 v[50:51], v[12:13], v[50:51]
	v_pk_mul_f32 v[28:29], v[10:11], v[28:29]
	v_bfe_u32 v32, v50, 16, 1
	v_bfe_u32 v34, v31, 16, 1
	v_bfe_u32 v36, v30, 16, 1
	v_bfe_u32 v38, v48, 16, 1
	v_add3_u32 v36, v30, v36, s23
	v_add3_u32 v34, v31, v34, s23
	v_add3_u32 v30, v50, v32, s23
	v_bfe_u32 v31, v28, 16, 1
	v_bfe_u32 v32, v29, 16, 1
	v_bfe_u32 v40, v49, 16, 1
	v_add3_u32 v38, v48, v38, s23
	v_or_b32_e32 v48, s6, v1
	v_bfe_u32 v7, v51, 16, 1
	v_add3_u32 v40, v49, v40, s23
	v_add3_u32 v29, v29, v32, s23
	v_add3_u32 v28, v28, v31, s23
	v_ashrrev_i32_e32 v49, 31, v48
	v_add3_u32 v7, v51, v7, s23
	v_lshrrev_b32_e32 v28, 16, v28
	v_lshrrev_b32_e32 v29, 16, v29
	v_lshrrev_b32_e32 v32, 16, v38
	v_lshrrev_b32_e32 v31, 16, v40
	v_lshlrev_b64 v[48:49], 12, v[48:49]
	v_and_or_b32 v31, v7, s29, v31
	v_and_or_b32 v30, v30, s29, v32
	v_and_or_b32 v29, v34, s29, v29
	v_and_or_b32 v28, v36, s29, v28
	v_lshl_add_u64 v[48:49], v[16:17], 0, v[48:49]
	v_mov_b32_e32 v34, v39
	v_mov_b32_e32 v46, v43
	global_store_dwordx4 v[48:49], v[28:31], off sc1
	v_mov_b32_e32 v44, v41
	v_mov_b32_e32 v36, v33
	v_pk_mul_f32 v[28:29], v[10:11], v[34:35]
	v_pk_mul_f32 v[34:35], v[12:13], v[46:47]
	v_pk_mul_f32 v[32:33], v[14:15], v[44:45]
	v_bfe_u32 v7, v35, 16, 1
	v_pk_mul_f32 v[30:31], v[8:9], v[36:37]
	v_add3_u32 v7, v35, v7, s23
	v_bfe_u32 v35, v32, 16, 1
	v_bfe_u32 v36, v34, 16, 1
	v_bfe_u32 v38, v30, 16, 1
	v_add3_u32 v32, v32, v35, s23
	v_bfe_u32 v37, v31, 16, 1
	v_add3_u32 v38, v30, v38, s23
	v_add3_u32 v30, v34, v36, s23
	v_bfe_u32 v36, v33, 16, 1
	v_lshrrev_b32_e32 v32, 16, v32
	v_add3_u32 v37, v31, v37, s23
	v_bfe_u32 v31, v28, 16, 1
	v_bfe_u32 v34, v29, 16, 1
	v_add3_u32 v33, v33, v36, s23
	v_and_or_b32 v30, v30, s29, v32
	v_or_b32_e32 v32, s6, v3
	v_add3_u32 v29, v29, v34, s23
	v_add3_u32 v28, v28, v31, s23
	v_lshrrev_b32_e32 v31, 16, v33
	v_ashrrev_i32_e32 v33, 31, v32
	v_lshrrev_b32_e32 v28, 16, v28
	v_lshrrev_b32_e32 v29, 16, v29
	v_lshlrev_b64 v[32:33], 12, v[32:33]
	v_and_or_b32 v31, v7, s29, v31
	v_and_or_b32 v29, v37, s29, v29
	v_and_or_b32 v28, v38, s29, v28
	v_lshl_add_u64 v[32:33], v[16:17], 0, v[32:33]
	ds_read2_b32 v[34:35], v24 offset0:16 offset1:24
	ds_read2_b32 v[36:37], v24 offset0:88 offset1:96
	global_store_dwordx4 v[32:33], v[28:31], off sc1
	ds_read2_b32 v[32:33], v24 offset0:52 offset1:60
	ds_read2_b32 v[38:39], v24 offset0:124 offset1:132
	ds_read2_b32 v[40:41], v24 offset0:160 offset1:168
	ds_read2_b32 v[42:43], v24 offset0:232 offset1:240
	ds_read2_b32 v[44:45], v24 offset0:196 offset1:204
	ds_read2_b32 v[46:47], v27 offset0:12 offset1:20
	s_waitcnt lgkmcnt(7)
	v_mov_b32_e32 v28, v34
	s_waitcnt lgkmcnt(5)
	v_mov_b32_e32 v30, v32
	s_waitcnt lgkmcnt(4)
	v_mov_b32_e32 v31, v38
	s_waitcnt lgkmcnt(3)
	v_mov_b32_e32 v48, v40
	s_waitcnt lgkmcnt(2)
	v_mov_b32_e32 v49, v42
	s_waitcnt lgkmcnt(1)
	v_mov_b32_e32 v50, v44
	s_waitcnt lgkmcnt(0)
	v_mov_b32_e32 v51, v46
	v_mov_b32_e32 v29, v36
	v_pk_mul_f32 v[30:31], v[8:9], v[30:31]
	v_pk_mul_f32 v[48:49], v[14:15], v[48:49]
	v_pk_mul_f32 v[50:51], v[12:13], v[50:51]
	v_pk_mul_f32 v[28:29], v[10:11], v[28:29]
	v_bfe_u32 v32, v50, 16, 1
	v_bfe_u32 v34, v31, 16, 1
	v_bfe_u32 v36, v30, 16, 1
	v_bfe_u32 v38, v48, 16, 1
	v_add3_u32 v36, v30, v36, s23
	v_add3_u32 v34, v31, v34, s23
	v_add3_u32 v30, v50, v32, s23
	v_bfe_u32 v31, v28, 16, 1
	v_bfe_u32 v32, v29, 16, 1
	v_bfe_u32 v40, v49, 16, 1
	v_add3_u32 v38, v48, v38, s23
	v_or_b32_e32 v48, s6, v18
	v_bfe_u32 v7, v51, 16, 1
	v_add3_u32 v40, v49, v40, s23
	v_add3_u32 v29, v29, v32, s23
	v_add3_u32 v28, v28, v31, s23
	v_ashrrev_i32_e32 v49, 31, v48
	v_add3_u32 v7, v51, v7, s23
	v_lshrrev_b32_e32 v28, 16, v28
	v_lshrrev_b32_e32 v29, 16, v29
	v_lshrrev_b32_e32 v32, 16, v38
	v_lshrrev_b32_e32 v31, 16, v40
	v_lshlrev_b64 v[48:49], 12, v[48:49]
	v_mov_b32_e32 v38, v33
	v_mov_b32_e32 v46, v45
	v_and_or_b32 v31, v7, s29, v31
	v_and_or_b32 v30, v30, s29, v32
	v_and_or_b32 v29, v34, s29, v29
	v_and_or_b32 v28, v36, s29, v28
	v_lshl_add_u64 v[48:49], v[16:17], 0, v[48:49]
	v_mov_b32_e32 v36, v35
	v_pk_mul_f32 v[8:9], v[8:9], v[38:39]
	v_mov_b32_e32 v42, v41
	v_pk_mul_f32 v[12:13], v[12:13], v[46:47]
	global_store_dwordx4 v[48:49], v[28:31], off sc1
	v_pk_mul_f32 v[10:11], v[10:11], v[36:37]
	v_pk_mul_f32 v[14:15], v[14:15], v[42:43]
	v_bfe_u32 v7, v13, 16, 1
	v_bfe_u32 v29, v9, 16, 1
	v_add3_u32 v9, v9, v29, s23
	v_add3_u32 v7, v13, v7, s23
	v_bfe_u32 v13, v10, 16, 1
	v_bfe_u32 v29, v14, 16, 1
	v_bfe_u32 v28, v12, 16, 1
	v_add3_u32 v14, v14, v29, s23
	v_add3_u32 v10, v10, v13, s23
	v_bfe_u32 v30, v8, 16, 1
	v_add3_u32 v12, v12, v28, s23
	v_lshrrev_b32_e32 v13, 16, v10
	v_lshrrev_b32_e32 v10, 16, v14
	v_add3_u32 v8, v8, v30, s23
	v_bfe_u32 v28, v11, 16, 1
	v_bfe_u32 v30, v15, 16, 1
	v_and_or_b32 v10, v12, s29, v10
	v_or_b32_e32 v12, s6, v19
	v_add3_u32 v15, v15, v30, s23
	v_add3_u32 v11, v11, v28, s23
	v_and_or_b32 v8, v8, s29, v13
	v_ashrrev_i32_e32 v13, 31, v12
	v_lshrrev_b32_e32 v28, 16, v11
	v_lshrrev_b32_e32 v11, 16, v15
	v_lshlrev_b64 v[12:13], 12, v[12:13]
	v_and_or_b32 v11, v7, s29, v11
	v_and_or_b32 v9, v9, s29, v28
	v_lshl_add_u64 v[12:13], v[16:17], 0, v[12:13]
	global_store_dwordx4 v[12:13], v[8:11], off sc1
	s_waitcnt lgkmcnt(0)

; #define GAS __attribute__((address_space(1)))
; #define LAS __attribute__((address_space(3)))
; #define LDS_WAIT() asm volatile("s_waitcnt lgkmcnt(0)" ::: "memory")
; __device__ __forceinline__ unsigned pk2(float lo, float hi) { return f2bf(lo) | (f2bf(hi) << 16); }
; __device__ __forceinline__ void p0_transpose_item(const float* W, int N, int k0, int n0, bf16* WT, int K, int dst_row0, LAS float* scr, int lane, const float* kscale = nullptr, int permhalf = -1) {
;     typedef float f32x4t __attribute__((ext_vector_type(4)));
;     const int c = lane & 7;
;     float ks[8];
; #pragma unroll
;     for (int i = 0; i < 8; ++i) ks[i] = kscale ? kscale[k0 + 8 * c + i] : 1.0f;
; #pragma unroll
;     for (int i = 0; i < 8; ++i) { const int kk = 8 * i + (lane >> 3), nn = (lane & 7) * 4;
;         *(LAS f32x4t*)(scr + kk * 36 + nn) = *(const GAS f32x4t*)(W + (size_t)(k0 + kk) * N + n0 + nn); }
;     LDS_WAIT(); asm volatile("" ::: "memory");
; #pragma unroll
;     for (int j = 0; j < 4; ++j) { const int n = (lane >> 3) + 8 * j; const LAS float* s = scr + (8 * c) * 36 + n;
;         v4u o; o.x = pk2(s[0 * 36] * ks[0], s[1 * 36] * ks[1]); o.y = pk2(s[2 * 36] * ks[2], s[3 * 36] * ks[3]); o.z = pk2(s[4 * 36] * ks[4], s[5 * 36] * ks[5]); o.w = pk2(s[6 * 36] * ks[6], s[7 * 36] * ks[7]);
;         const int drow = permhalf < 0 ? n : (32 * (n >> 4) + 8 * ((n >> 2) & 3) + 4 * permhalf + (n & 3));
;         *(GAS v4u*)(WT + (size_t)(dst_row0 + drow) * K + k0 + 8 * c) = o; }
;     LDS_WAIT(); asm volatile("" ::: "memory");
; }
; __device__ __forceinline__ void conv_item(KArgs a, int r, LAS float* scr, int lane) {
;     ...
;     { const int e = r / 512, q = r % 512, kb = q / 64, nb = q % 64;
;       p0_transpose_item(a->in[20] + (size_t)e * 512 * 2048, 2048, 64 * kb, 32 * nb, (bf16*)(ws + WS_W2), 512, e * 2048 + 32 * nb, scr, lane); }
.LBB0_420:
	s_load_dwordx2 s[42:43], s[14:15], 0xb8
	s_cmpk_gt_i32 s51, 0x3fff
	s_mov_b64 s[6:7], -1
	s_cbranch_scc0 .LBB0_442
	s_cmpk_gt_u32 s51, 0x7fff
	s_cbranch_scc0 .LBB0_423
	s_load_dwordx2 s[6:7], s[14:15], 0xa0
	s_add_i32 s36, s51, 0xffff8000
	s_and_b32 s24, s36, 0xfffffe00
	s_and_b32 s37, s51, 0x1c0
	s_lshl_b64 s[18:19], s[24:25], 13
	s_waitcnt lgkmcnt(0)
	s_add_u32 s18, s6, s18
	s_addc_u32 s7, s7, s19
	s_lshl_b32 s6, s51, 5
	s_and_b32 s19, s6, 0x7e0
	s_lshl_b32 s6, s36, 2
	s_and_b32 s6, s6, 0x7ffff800
	s_or_b32 s6, s6, s19
	s_lshl_b32 s19, s19, 2
	v_or_b32_e32 v7, s37, v1
	s_add_u32 s18, s18, s19
	v_lshlrev_b32_e32 v8, 13, v7
	v_or_b32_e32 v7, s37, v3
	s_addc_u32 s19, s7, 0
	v_lshlrev_b32_e32 v10, 13, v7
	v_or_b32_e32 v7, s37, v18
	v_lshl_add_u64 v[16:17], s[18:19], 0, v[4:5]
	v_mov_b32_e32 v9, v5
	v_mov_b32_e32 v11, v5
	v_lshlrev_b32_e32 v28, 13, v7
	v_mov_b32_e32 v29, v5
	v_or_b32_e32 v7, s37, v19
	v_lshl_add_u64 v[8:9], v[16:17], 0, v[8:9]
	v_lshl_add_u64 v[12:13], v[16:17], 0, v[10:11]
	v_lshl_add_u64 v[36:37], v[16:17], 0, v[28:29]
	v_lshlrev_b32_e32 v28, 13, v7
	v_or_b32_e32 v7, s37, v20
	global_load_dwordx4 v[8:11], v[8:9], off
	s_nop 0
	global_load_dwordx4 v[12:15], v[12:13], off
	v_lshl_add_u64 v[38:39], v[16:17], 0, v[28:29]
	global_load_dwordx4 v[28:31], v[36:37], off
	global_load_dwordx4 v[32:35], v[38:39], off
	v_lshlrev_b32_e32 v36, 13, v7
	v_mov_b32_e32 v37, v5
	v_or_b32_e32 v7, s37, v21
	v_lshl_add_u64 v[44:45], v[16:17], 0, v[36:37]
	v_lshlrev_b32_e32 v36, 13, v7
	v_or_b32_e32 v7, s37, v22
	v_lshl_add_u64 v[46:47], v[16:17], 0, v[36:37]
	global_load_dwordx4 v[36:39], v[44:45], off
	global_load_dwordx4 v[40:43], v[46:47], off
	v_lshlrev_b32_e32 v44, 13, v7
	v_mov_b32_e32 v45, v5
	v_or_b32_e32 v7, s37, v23
	v_lshl_add_u64 v[52:53], v[16:17], 0, v[44:45]
	v_lshlrev_b32_e32 v44, 13, v7
	v_lshl_add_u64 v[16:17], v[16:17], 0, v[44:45]
	global_load_dwordx4 v[44:47], v[52:53], off
	global_load_dwordx4 v[48:51], v[16:17], off
	s_lshl_b32 s7, s37, 1
	s_add_u32 s18, s42, s7
	v_mov_b32_e32 v7, v5
	s_addc_u32 s19, s43, 0
	v_lshl_add_u64 v[52:53], s[18:19], 0, v[6:7]
	v_or_b32_e32 v16, s6, v1
	v_lshl_add_u64 v[52:53], v[52:53], 0, s[26:27]
	s_waitcnt vmcnt(7)
	ds_write_b128 v25, v[8:11]
	s_waitcnt vmcnt(6)
	ds_write_b128 v25, v[12:15] offset:1152
	s_waitcnt vmcnt(5)
	ds_write_b128 v25, v[28:31] offset:2304
	s_waitcnt vmcnt(4)
	ds_write_b128 v25, v[32:35] offset:3456
	s_waitcnt vmcnt(3)
	ds_write_b128 v25, v[36:39] offset:4608
	s_waitcnt vmcnt(2)
	ds_write_b128 v25, v[40:43] offset:5760
	s_waitcnt vmcnt(1)
	ds_write_b128 v25, v[44:47] offset:6912
	s_waitcnt vmcnt(0)
	ds_write_b128 v25, v[48:51] offset:8064
	s_waitcnt lgkmcnt(0)
	ds_read2_b32 v[12:13], v24 offset0:36 offset1:44
	ds_read2_b32 v[14:15], v24 offset1:8
	ds_read2_b32 v[28:29], v24 offset0:72 offset1:80
	ds_read2_b32 v[30:31], v24 offset0:108 offset1:116
	ds_read2_b32 v[32:33], v24 offset0:144 offset1:152
	ds_read2_b32 v[34:35], v24 offset0:180 offset1:188
	ds_read2_b32 v[36:37], v24 offset0:216 offset1:224
	ds_read2_b32 v[38:39], v26 offset0:124 offset1:132
	s_waitcnt lgkmcnt(6)
	v_bfe_u32 v7, v14, 16, 1
	s_waitcnt lgkmcnt(5)
	v_bfe_u32 v9, v28, 16, 1
	s_waitcnt lgkmcnt(3)
	v_bfe_u32 v11, v32, 16, 1
	s_waitcnt lgkmcnt(1)
	v_bfe_u32 v40, v36, 16, 1
	v_bfe_u32 v8, v12, 16, 1
	v_bfe_u32 v10, v30, 16, 1
	v_bfe_u32 v17, v34, 16, 1
	s_waitcnt lgkmcnt(0)
; #define GAS __attribute__((address_space(1)))
; #define LAS __attribute__((address_space(3)))
; #define LDS_WAIT() asm volatile("s_waitcnt lgkmcnt(0)" ::: "memory")
; __device__ __forceinline__ unsigned pk2(float lo, float hi) { return f2bf(lo) | (f2bf(hi) << 16); }
; __device__ __forceinline__ void p0_transpose_item(const float* W, int N, int k0, int n0, bf16* WT, int K, int dst_row0, LAS float* scr, int lane, const float* kscale = nullptr, int permhalf = -1) {
;     typedef float f32x4t __attribute__((ext_vector_type(4)));
;     const int c = lane & 7;
;     float ks[8];
; #pragma unroll
;     for (int i = 0; i < 8; ++i) ks[i] = kscale ? kscale[k0 + 8 * c + i] : 1.0f;
; #pragma unroll
;     for (int i = 0; i < 8; ++i) { const int kk = 8 * i + (lane >> 3), nn = (lane & 7) * 4;
;         *(LAS f32x4t*)(scr + kk * 36 + nn) = *(const GAS f32x4t*)(W + (size_t)(k0 + kk) * N + n0 + nn); }
;     LDS_WAIT(); asm volatile("" ::: "memory");
; #pragma unroll
;     for (int j = 0; j < 4; ++j) { const int n = (lane >> 3) + 8 * j; const LAS float* s = scr + (8 * c) * 36 + n;
;         v4u o; o.x = pk2(s[0 * 36] * ks[0], s[1 * 36] * ks[1]); o.y = pk2(s[2 * 36] * ks[2], s[3 * 36] * ks[3]); o.z = pk2(s[4 * 36] * ks[4], s[5 * 36] * ks[5]); o.w = pk2(s[6 * 36] * ks[6], s[7 * 36] * ks[7]);
;         const int drow = permhalf < 0 ? n : (32 * (n >> 4) + 8 * ((n >> 2) & 3) + 4 * permhalf + (n & 3));
;         *(GAS v4u*)(WT + (size_t)(dst_row0 + drow) * K + k0 + 8 * c) = o; }
;     LDS_WAIT(); asm volatile("" ::: "memory");
; }
	v_bfe_u32 v41, v38, 16, 1
	v_add3_u32 v7, v14, v7, s23
	v_add3_u32 v9, v28, v9, s23
	v_add3_u32 v11, v32, v11, s23
	v_add3_u32 v14, v36, v40, s23
	v_add3_u32 v8, v12, v8, s23
	v_add3_u32 v10, v30, v10, s23
	v_add3_u32 v12, v34, v17, s23
	v_add3_u32 v17, v38, v41, s23
	v_lshrrev_b32_e32 v9, 16, v9
	v_lshrrev_b32_e32 v11, 16, v11
	v_lshrrev_b32_e32 v14, 16, v14
	v_and_or_b32 v9, v10, s29, v9
	v_and_or_b32 v10, v12, s29, v11
	v_and_or_b32 v11, v17, s29, v14
	v_mov_b32_e32 v17, v5
	v_lshrrev_b32_e32 v7, 16, v7
	v_lshlrev_b64 v[16:17], 10, v[16:17]
	v_and_or_b32 v8, v8, s29, v7
	v_lshl_add_u64 v[16:17], v[52:53], 0, v[16:17]
	v_bfe_u32 v7, v15, 16, 1
	global_store_dwordx4 v[16:17], v[8:11], off sc1
	v_add3_u32 v7, v15, v7, s23
	v_lshrrev_b32_e32 v7, 16, v7
	v_bfe_u32 v8, v13, 16, 1
	v_add3_u32 v8, v13, v8, s23
	v_and_or_b32 v8, v8, s29, v7
	v_bfe_u32 v7, v29, 16, 1
	v_add3_u32 v7, v29, v7, s23
	v_bfe_u32 v9, v31, 16, 1
	v_lshrrev_b32_e32 v7, 16, v7
	v_add3_u32 v9, v31, v9, s23
	v_and_or_b32 v9, v9, s29, v7
	v_bfe_u32 v7, v33, 16, 1
	v_add3_u32 v7, v33, v7, s23
	v_bfe_u32 v10, v35, 16, 1
	v_lshrrev_b32_e32 v7, 16, v7
	v_add3_u32 v10, v35, v10, s23
	v_and_or_b32 v10, v10, s29, v7
	v_bfe_u32 v7, v37, 16, 1
	v_add3_u32 v7, v37, v7, s23
	v_bfe_u32 v11, v39, 16, 1
	v_or_b32_e32 v12, s6, v3
	v_mov_b32_e32 v13, v5
	v_lshrrev_b32_e32 v7, 16, v7
	v_add3_u32 v11, v39, v11, s23
	v_lshlrev_b64 v[12:13], 10, v[12:13]
	v_and_or_b32 v11, v11, s29, v7
	ds_read2_b32 v[14:15], v24 offset0:16 offset1:24
	v_lshl_add_u64 v[12:13], v[52:53], 0, v[12:13]
	global_store_dwordx4 v[12:13], v[8:11], off sc1
	ds_read2_b32 v[12:13], v24 offset0:52 offset1:60
	ds_read2_b32 v[16:17], v24 offset0:88 offset1:96
	ds_read2_b32 v[28:29], v24 offset0:124 offset1:132
	s_waitcnt lgkmcnt(3)
	v_bfe_u32 v7, v14, 16, 1
	v_add3_u32 v7, v14, v7, s23
	s_waitcnt lgkmcnt(2)
	v_bfe_u32 v8, v12, 16, 1
	ds_read2_b32 v[30:31], v24 offset0:160 offset1:168
	v_lshrrev_b32_e32 v7, 16, v7
	v_add3_u32 v8, v12, v8, s23
	ds_read2_b32 v[32:33], v24 offset0:196 offset1:204
	v_and_or_b32 v8, v8, s29, v7
	s_waitcnt lgkmcnt(3)
	v_bfe_u32 v7, v16, 16, 1
	v_add3_u32 v7, v16, v7, s23
	s_waitcnt lgkmcnt(2)
	v_bfe_u32 v9, v28, 16, 1
	ds_read2_b32 v[34:35], v24 offset0:232 offset1:240
	v_lshrrev_b32_e32 v7, 16, v7
	v_add3_u32 v9, v28, v9, s23
	ds_read2_b32 v[36:37], v27 offset0:12 offset1:20
	v_and_or_b32 v9, v9, s29, v7
	s_waitcnt lgkmcnt(3)
	v_bfe_u32 v7, v30, 16, 1
	v_add3_u32 v7, v30, v7, s23
	s_waitcnt lgkmcnt(2)
	v_bfe_u32 v10, v32, 16, 1
	v_lshrrev_b32_e32 v7, 16, v7
	v_add3_u32 v10, v32, v10, s23
	v_and_or_b32 v10, v10, s29, v7
	s_waitcnt lgkmcnt(1)
	v_bfe_u32 v7, v34, 16, 1
	v_add3_u32 v7, v34, v7, s23
	s_waitcnt lgkmcnt(0)
	v_bfe_u32 v11, v36, 16, 1
	v_or_b32_e32 v38, s6, v18
	v_mov_b32_e32 v39, v5
	v_lshrrev_b32_e32 v7, 16, v7
	v_add3_u32 v11, v36, v11, s23
	v_lshlrev_b64 v[38:39], 10, v[38:39]
	v_and_or_b32 v11, v11, s29, v7
	v_lshl_add_u64 v[38:39], v[52:53], 0, v[38:39]
	v_bfe_u32 v7, v15, 16, 1
	global_store_dwordx4 v[38:39], v[8:11], off sc1
	v_add3_u32 v7, v15, v7, s23
	v_lshrrev_b32_e32 v7, 16, v7
	v_bfe_u32 v8, v13, 16, 1
	v_add3_u32 v8, v13, v8, s23
	v_and_or_b32 v8, v8, s29, v7
	v_bfe_u32 v7, v17, 16, 1
	v_add3_u32 v7, v17, v7, s23
	v_bfe_u32 v9, v29, 16, 1
	v_lshrrev_b32_e32 v7, 16, v7
	v_add3_u32 v9, v29, v9, s23
	v_and_or_b32 v9, v9, s29, v7
	v_bfe_u32 v7, v31, 16, 1
	v_add3_u32 v7, v31, v7, s23
	v_bfe_u32 v10, v33, 16, 1
	v_lshrrev_b32_e32 v7, 16, v7
	v_add3_u32 v10, v33, v10, s23
	v_and_or_b32 v10, v10, s29, v7
	v_bfe_u32 v7, v35, 16, 1
	v_add3_u32 v7, v35, v7, s23
	v_bfe_u32 v11, v37, 16, 1
	v_or_b32_e32 v12, s6, v19
	v_mov_b32_e32 v13, v5
	v_lshrrev_b32_e32 v7, 16, v7
	v_add3_u32 v11, v37, v11, s23
	v_lshlrev_b64 v[12:13], 10, v[12:13]
	v_and_or_b32 v11, v11, s29, v7
	v_lshl_add_u64 v[12:13], v[52:53], 0, v[12:13]
	global_store_dwordx4 v[12:13], v[8:11], off sc1
	s_waitcnt lgkmcnt(0)
	s_mov_b64 s[6:7], 0

; #define GAS __attribute__((address_space(1)))
; #define LAS __attribute__((address_space(3)))
; #define LDS_WAIT() asm volatile("s_waitcnt lgkmcnt(0)" ::: "memory")
; __device__ __forceinline__ unsigned pk2(float lo, float hi) { return f2bf(lo) | (f2bf(hi) << 16); }
; __device__ __forceinline__ void p0_transpose_item(const float* W, int N, int k0, int n0, bf16* WT, int K, int dst_row0, LAS float* scr, int lane, const float* kscale = nullptr, int permhalf = -1) {
;     typedef float f32x4t __attribute__((ext_vector_type(4)));
;     const int c = lane & 7;
;     float ks[8];
; #pragma unroll
;     for (int i = 0; i < 8; ++i) ks[i] = kscale ? kscale[k0 + 8 * c + i] : 1.0f;
; #pragma unroll
;     for (int i = 0; i < 8; ++i) { const int kk = 8 * i + (lane >> 3), nn = (lane & 7) * 4;
;         *(LAS f32x4t*)(scr + kk * 36 + nn) = *(const GAS f32x4t*)(W + (size_t)(k0 + kk) * N + n0 + nn); }
;     LDS_WAIT(); asm volatile("" ::: "memory");
; #pragma unroll
;     for (int j = 0; j < 4; ++j) { const int n = (lane >> 3) + 8 * j; const LAS float* s = scr + (8 * c) * 36 + n;
;         v4u o; o.x = pk2(s[0 * 36] * ks[0], s[1 * 36] * ks[1]); o.y = pk2(s[2 * 36] * ks[2], s[3 * 36] * ks[3]); o.z = pk2(s[4 * 36] * ks[4], s[5 * 36] * ks[5]); o.w = pk2(s[6 * 36] * ks[6], s[7 * 36] * ks[7]);
;         const int drow = permhalf < 0 ? n : (32 * (n >> 4) + 8 * ((n >> 2) & 3) + 4 * permhalf + (n & 3));
;         *(GAS v4u*)(WT + (size_t)(dst_row0 + drow) * K + k0 + 8 * c) = o; }
;     LDS_WAIT(); asm volatile("" ::: "memory");
; }
; __device__ __forceinline__ void conv_item(KArgs a, int r, LAS float* scr, int lane) {
;     ...
;     if (r < CONV_IE) { const int e = r / 512, q = r % 512, kb = q / 16, nb = q % 16, n0 = 32 * nb;
;         p0_transpose_item(a->in[19] + (size_t)e * 2048 * 512, 512, 64 * kb, n0, (bf16*)(ws + WS_W13), 2048, e * 1024 + (n0 >> 7) * 256 + 128 + (n0 & 127), scr, lane, a->in[15]); return; } r -= CONV_IE;
.LBB0_440:
	s_load_dwordx2 s[6:7], s[14:15], 0x98
	s_add_i32 s19, s51, 0xffffc000
	s_lshr_b32 s24, s19, 9
	s_lshl_b32 s44, s51, 5
	s_lshl_b64 s[36:37], s[24:25], 22
	s_waitcnt lgkmcnt(0)
	s_add_u32 s19, s6, s36
	s_addc_u32 s7, s7, s37
	s_lshl_b32 s6, s24, 10
	s_lshl_b32 s24, s51, 6
	s_and_b32 s24, s24, 0x300
	s_or_b32 s6, s6, s24
	s_and_b32 s24, s44, 0x60
	s_or_b32 s6, s6, s24
	s_lshl_b32 s24, s51, 7
	s_bitset1_b32 s6, 7
	s_and_b32 s24, s24, 0x780
	v_or_b32_e32 v7, s18, v1
	s_add_u32 s36, s19, s24
	v_lshlrev_b32_e32 v28, 11, v7
	v_or_b32_e32 v7, s18, v3
	s_addc_u32 s37, s7, 0
	v_lshlrev_b32_e32 v30, 11, v7
	v_or_b32_e32 v7, s18, v18
	v_lshl_add_u64 v[16:17], s[36:37], 0, v[4:5]
	v_mov_b32_e32 v29, v5
	v_mov_b32_e32 v31, v5
	v_lshlrev_b32_e32 v36, 11, v7
	v_mov_b32_e32 v37, v5
	v_or_b32_e32 v7, s18, v19
	v_lshl_add_u64 v[28:29], v[16:17], 0, v[28:29]
	v_lshl_add_u64 v[32:33], v[16:17], 0, v[30:31]
	v_lshl_add_u64 v[44:45], v[16:17], 0, v[36:37]
	v_lshlrev_b32_e32 v36, 11, v7
	v_or_b32_e32 v7, s18, v20
	global_load_dwordx4 v[28:31], v[28:29], off
	s_nop 0
	global_load_dwordx4 v[32:35], v[32:33], off
	v_lshl_add_u64 v[46:47], v[16:17], 0, v[36:37]
	global_load_dwordx4 v[36:39], v[44:45], off
	global_load_dwordx4 v[40:43], v[46:47], off
	v_lshlrev_b32_e32 v44, 11, v7
	v_mov_b32_e32 v45, v5
	v_or_b32_e32 v7, s18, v21
	v_lshl_add_u64 v[52:53], v[16:17], 0, v[44:45]
	v_lshlrev_b32_e32 v44, 11, v7
	v_or_b32_e32 v7, s18, v22
	v_lshl_add_u64 v[54:55], v[16:17], 0, v[44:45]
	global_load_dwordx4 v[44:47], v[52:53], off
	global_load_dwordx4 v[48:51], v[54:55], off
	v_lshlrev_b32_e32 v52, 11, v7
	v_mov_b32_e32 v53, v5
	v_or_b32_e32 v7, s18, v23
	v_lshl_add_u64 v[60:61], v[16:17], 0, v[52:53]
	v_lshlrev_b32_e32 v52, 11, v7
	v_lshl_add_u64 v[16:17], v[16:17], 0, v[52:53]
	global_load_dwordx4 v[52:55], v[60:61], off
	global_load_dwordx4 v[56:59], v[16:17], off
	s_lshl_b32 s7, s18, 1
	s_add_u32 s18, s42, s7
	v_mov_b32_e32 v7, v5
	s_addc_u32 s19, s43, 0
	v_lshl_add_u64 v[16:17], s[18:19], 0, v[6:7]
	v_lshl_add_u64 v[16:17], v[16:17], 0, s[38:39]
	s_waitcnt vmcnt(7)
	ds_write_b128 v25, v[28:31]
	s_waitcnt vmcnt(6)
	ds_write_b128 v25, v[32:35] offset:1152
	s_waitcnt vmcnt(5)
	ds_write_b128 v25, v[36:39] offset:2304
	s_waitcnt vmcnt(4)
	ds_write_b128 v25, v[40:43] offset:3456
	s_waitcnt vmcnt(3)
	ds_write_b128 v25, v[44:47] offset:4608
	s_waitcnt vmcnt(2)
	ds_write_b128 v25, v[48:51] offset:5760
	s_waitcnt vmcnt(1)
	ds_write_b128 v25, v[52:55] offset:6912
	s_waitcnt vmcnt(0)
	ds_write_b128 v25, v[56:59] offset:8064
	s_waitcnt lgkmcnt(0)
	ds_read2_b32 v[32:33], v24 offset0:36 offset1:44
	ds_read2_b32 v[34:35], v24 offset0:72 offset1:80
	ds_read2_b32 v[36:37], v24 offset0:108 offset1:116
	ds_read2_b32 v[38:39], v24 offset1:8
	ds_read2_b32 v[40:41], v24 offset0:144 offset1:152
	ds_read2_b32 v[42:43], v24 offset0:180 offset1:188
	ds_read2_b32 v[44:45], v24 offset0:216 offset1:224
	ds_read2_b32 v[46:47], v26 offset0:124 offset1:132
	s_waitcnt lgkmcnt(4)
	v_mov_b32_e32 v28, v38
	v_mov_b32_e32 v29, v34
	v_mov_b32_e32 v30, v32
	v_mov_b32_e32 v31, v36
	s_waitcnt lgkmcnt(3)
	v_mov_b32_e32 v48, v40
	s_waitcnt lgkmcnt(1)
	v_mov_b32_e32 v49, v44
	v_mov_b32_e32 v50, v42
	s_waitcnt lgkmcnt(0)
; #define GAS __attribute__((address_space(1)))
; #define LAS __attribute__((address_space(3)))
; #define LDS_WAIT() asm volatile("s_waitcnt lgkmcnt(0)" ::: "memory")
; __device__ __forceinline__ unsigned pk2(float lo, float hi) { return f2bf(lo) | (f2bf(hi) << 16); }
; __device__ __forceinline__ void p0_transpose_item(const float* W, int N, int k0, int n0, bf16* WT, int K, int dst_row0, LAS float* scr, int lane, const float* kscale = nullptr, int permhalf = -1) {
;     typedef float f32x4t __attribute__((ext_vector_type(4)));
;     const int c = lane & 7;
;     float ks[8];
; #pragma unroll
;     for (int i = 0; i < 8; ++i) ks[i] = kscale ? kscale[k0 + 8 * c + i] : 1.0f;
; #pragma unroll
;     for (int i = 0; i < 8; ++i) { const int kk = 8 * i + (lane >> 3), nn = (lane & 7) * 4;
;         *(LAS f32x4t*)(scr + kk * 36 + nn) = *(const GAS f32x4t*)(W + (size_t)(k0 + kk) * N + n0 + nn); }
;     LDS_WAIT(); asm volatile("" ::: "memory");
; #pragma unroll
;     for (int j = 0; j < 4; ++j) { const int n = (lane >> 3) + 8 * j; const LAS float* s = scr + (8 * c) * 36 + n;
;         v4u o; o.x = pk2(s[0 * 36] * ks[0], s[1 * 36] * ks[1]); o.y = pk2(s[2 * 36] * ks[2], s[3 * 36] * ks[3]); o.z = pk2(s[4 * 36] * ks[4], s[5 * 36] * ks[5]); o.w = pk2(s[6 * 36] * ks[6], s[7 * 36] * ks[7]);
;         const int drow = permhalf < 0 ? n : (32 * (n >> 4) + 8 * ((n >> 2) & 3) + 4 * permhalf + (n & 3));
;         *(GAS v4u*)(WT + (size_t)(dst_row0 + drow) * K + k0 + 8 * c) = o; }
;     LDS_WAIT(); asm volatile("" ::: "memory");
; }
	v_mov_b32_e32 v51, v46
	v_pk_mul_f32 v[28:29], v[10:11], v[28:29]
	v_pk_mul_f32 v[30:31], v[8:9], v[30:31]
	v_pk_mul_f32 v[48:49], v[14:15], v[48:49]
	v_pk_mul_f32 v[50:51], v[12:13], v[50:51]
	v_bfe_u32 v34, v31, 16, 1
	v_bfe_u32 v32, v50, 16, 1
	v_bfe_u32 v36, v30, 16, 1
	v_bfe_u32 v38, v28, 16, 1
	v_bfe_u32 v40, v29, 16, 1
	v_bfe_u32 v42, v48, 16, 1
	v_bfe_u32 v44, v49, 16, 1
	v_bfe_u32 v7, v51, 16, 1
	v_add3_u32 v36, v30, v36, s23
	v_add3_u32 v34, v31, v34, s23
	v_add3_u32 v30, v50, v32, s23
	v_add3_u32 v31, v49, v44, s23
	v_add3_u32 v32, v48, v42, s23
	v_add3_u32 v29, v29, v40, s23
	v_add3_u32 v28, v28, v38, s23
	v_or_b32_e32 v48, s6, v1
	v_mov_b32_e32 v49, v5
	v_add3_u32 v7, v51, v7, s23
	v_lshrrev_b32_e32 v28, 16, v28
	v_lshrrev_b32_e32 v29, 16, v29
	v_lshrrev_b32_e32 v32, 16, v32
	v_lshrrev_b32_e32 v31, 16, v31
	v_lshlrev_b64 v[48:49], 12, v[48:49]
	v_and_or_b32 v31, v7, s29, v31
	v_and_or_b32 v30, v30, s29, v32
	v_and_or_b32 v29, v34, s29, v29
	v_and_or_b32 v28, v36, s29, v28
	v_lshl_add_u64 v[48:49], v[16:17], 0, v[48:49]
	v_mov_b32_e32 v34, v39
	v_mov_b32_e32 v46, v43
	global_store_dwordx4 v[48:49], v[28:31], off sc1
	v_mov_b32_e32 v36, v33
	v_mov_b32_e32 v44, v41
	v_pk_mul_f32 v[28:29], v[10:11], v[34:35]
	v_pk_mul_f32 v[34:35], v[12:13], v[46:47]
	v_pk_mul_f32 v[30:31], v[8:9], v[36:37]
	v_pk_mul_f32 v[32:33], v[14:15], v[44:45]
	v_bfe_u32 v7, v35, 16, 1
	v_bfe_u32 v36, v34, 16, 1
	v_bfe_u32 v38, v30, 16, 1
	v_add3_u32 v7, v35, v7, s23
	v_bfe_u32 v35, v32, 16, 1
	v_bfe_u32 v37, v31, 16, 1
	v_add3_u32 v38, v30, v38, s23
	v_add3_u32 v30, v34, v36, s23
	v_bfe_u32 v36, v33, 16, 1
	v_add3_u32 v32, v32, v35, s23
	v_add3_u32 v37, v31, v37, s23
	v_bfe_u32 v31, v28, 16, 1
	v_bfe_u32 v34, v29, 16, 1
	v_add3_u32 v33, v33, v36, s23
	v_lshrrev_b32_e32 v32, 16, v32
	v_add3_u32 v29, v29, v34, s23
	v_add3_u32 v28, v28, v31, s23
	v_lshrrev_b32_e32 v31, 16, v33
	v_and_or_b32 v30, v30, s29, v32
	v_or_b32_e32 v32, s6, v3
	v_mov_b32_e32 v33, v5
	v_lshrrev_b32_e32 v28, 16, v28
	v_lshrrev_b32_e32 v29, 16, v29
	v_lshlrev_b64 v[32:33], 12, v[32:33]
	v_and_or_b32 v31, v7, s29, v31
	v_and_or_b32 v29, v37, s29, v29
	v_and_or_b32 v28, v38, s29, v28
	v_lshl_add_u64 v[32:33], v[16:17], 0, v[32:33]
	ds_read2_b32 v[34:35], v24 offset0:16 offset1:24
	ds_read2_b32 v[36:37], v24 offset0:88 offset1:96
	global_store_dwordx4 v[32:33], v[28:31], off sc1
	ds_read2_b32 v[32:33], v24 offset0:52 offset1:60
	ds_read2_b32 v[38:39], v24 offset0:124 offset1:132
	ds_read2_b32 v[40:41], v24 offset0:160 offset1:168
	ds_read2_b32 v[42:43], v24 offset0:232 offset1:240
	ds_read2_b32 v[44:45], v24 offset0:196 offset1:204
	ds_read2_b32 v[46:47], v27 offset0:12 offset1:20
	s_waitcnt lgkmcnt(7)
	v_mov_b32_e32 v28, v34
	s_waitcnt lgkmcnt(5)
	v_mov_b32_e32 v30, v32
	s_waitcnt lgkmcnt(4)
	v_mov_b32_e32 v31, v38
	s_waitcnt lgkmcnt(1)
	v_mov_b32_e32 v50, v44
	s_waitcnt lgkmcnt(0)
	v_mov_b32_e32 v51, v46
	v_mov_b32_e32 v29, v36
	v_pk_mul_f32 v[30:31], v[8:9], v[30:31]
	v_mov_b32_e32 v48, v40
	v_mov_b32_e32 v49, v42
	v_pk_mul_f32 v[50:51], v[12:13], v[50:51]
	v_pk_mul_f32 v[28:29], v[10:11], v[28:29]
	v_pk_mul_f32 v[48:49], v[14:15], v[48:49]
	v_bfe_u32 v32, v50, 16, 1
	v_bfe_u32 v34, v31, 16, 1
	v_bfe_u32 v36, v30, 16, 1
	v_add3_u32 v36, v30, v36, s23
	v_add3_u32 v34, v31, v34, s23
	v_add3_u32 v30, v50, v32, s23
	v_bfe_u32 v31, v28, 16, 1
	v_bfe_u32 v32, v29, 16, 1
	v_bfe_u32 v38, v48, 16, 1
	v_bfe_u32 v40, v49, 16, 1
	v_bfe_u32 v7, v51, 16, 1
	v_add3_u32 v40, v49, v40, s23
	v_add3_u32 v38, v48, v38, s23
	v_add3_u32 v29, v29, v32, s23
	v_add3_u32 v28, v28, v31, s23
	v_or_b32_e32 v48, s6, v18
	v_mov_b32_e32 v49, v5
	v_add3_u32 v7, v51, v7, s23
	v_lshrrev_b32_e32 v28, 16, v28
	v_lshrrev_b32_e32 v29, 16, v29
	v_lshrrev_b32_e32 v32, 16, v38
	v_lshrrev_b32_e32 v31, 16, v40
	v_lshlrev_b64 v[48:49], 12, v[48:49]
	v_mov_b32_e32 v38, v33
	v_mov_b32_e32 v46, v45
	v_and_or_b32 v31, v7, s29, v31
	v_and_or_b32 v30, v30, s29, v32
	v_and_or_b32 v29, v34, s29, v29
	v_and_or_b32 v28, v36, s29, v28
	v_lshl_add_u64 v[48:49], v[16:17], 0, v[48:49]
	v_mov_b32_e32 v36, v35
	v_pk_mul_f32 v[8:9], v[8:9], v[38:39]
	v_mov_b32_e32 v42, v41
	v_pk_mul_f32 v[12:13], v[12:13], v[46:47]
	global_store_dwordx4 v[48:49], v[28:31], off sc1
	v_pk_mul_f32 v[10:11], v[10:11], v[36:37]
	v_pk_mul_f32 v[14:15], v[14:15], v[42:43]
	v_bfe_u32 v7, v13, 16, 1
	v_bfe_u32 v29, v9, 16, 1
	v_add3_u32 v9, v9, v29, s23
	v_add3_u32 v7, v13, v7, s23
	v_bfe_u32 v13, v10, 16, 1
	v_bfe_u32 v29, v14, 16, 1
	v_bfe_u32 v28, v12, 16, 1
	v_bfe_u32 v30, v8, 16, 1
	v_add3_u32 v14, v14, v29, s23
	v_add3_u32 v10, v10, v13, s23
	v_add3_u32 v8, v8, v30, s23
	v_add3_u32 v12, v12, v28, s23
	v_bfe_u32 v28, v11, 16, 1
	v_bfe_u32 v30, v15, 16, 1
	v_lshrrev_b32_e32 v13, 16, v10
	v_lshrrev_b32_e32 v10, 16, v14
	v_add3_u32 v15, v15, v30, s23
	v_add3_u32 v11, v11, v28, s23
	v_and_or_b32 v10, v12, s29, v10
	v_and_or_b32 v8, v8, s29, v13
	v_or_b32_e32 v12, s6, v19
	v_mov_b32_e32 v13, v5
	v_lshrrev_b32_e32 v28, 16, v11
	v_lshrrev_b32_e32 v11, 16, v15
	v_lshlrev_b64 v[12:13], 12, v[12:13]
	v_and_or_b32 v11, v7, s29, v11
	v_and_or_b32 v9, v9, s29, v28
	v_lshl_add_u64 v[12:13], v[16:17], 0, v[12:13]
	global_store_dwordx4 v[12:13], v[8:11], off sc1
	s_waitcnt lgkmcnt(0)

; __device__ __forceinline__ unsigned cvt_pk_bf16(float lo, float hi) { f32x2v_ v = {lo, hi}; bf16x2v_ b = __builtin_convertvector(v, bf16x2v_); return __builtin_bit_cast(unsigned, b); }
;     __device__ __forceinline__ void operator()(const f32x4 (&acc)[2][2][4][2], const Unit& u, int wr, int wc, int fr, int fq) const {
;         const int row0 = u.pm * BM + wr * 64 + fr, col0 = u.pn * BM + wc * 32 + 8 * fq;
; #pragma unroll
;         for (int ai = 0; ai < 2; ++ai)
; #pragma unroll
;             for (int m = 0; m < 4; ++m) { const size_t r = (size_t)(row0 + ai * HALF + m * 16); float s = 0.f;
; #pragma unroll
;                 for (int bj = 0; bj < 2; ++bj) { const size_t off = r * 2048 + col0 + bj * HALF;
;                     const f32x4 v0 = *(const f32x4*)(X + off) + acc[ai][bj][m][0], v1 = *(const f32x4*)(X + off + 4) + acc[ai][bj][m][1];
;                     u32x4 w; w.x = cvt_pk_bf16(v0[0], v0[1]); w.y = cvt_pk_bf16(v0[2], v0[3]); w.z = cvt_pk_bf16(v1[0], v1[1]); w.w = cvt_pk_bf16(v1[2], v1[3]);
;                     *(u32x4*)(X1 + off) = w;
;                     s += ((v0[0] * v0[0] + v0[1] * v0[1]) + (v0[2] * v0[2] + v0[3] * v0[3])) + ((v1[0] * v1[0] + v1[1] * v1[1]) + (v1[2] * v1[2] + v1[3] * v1[3])); }
;                 s += __shfl_xor(s, 16); s += __shfl_xor(s, 32);
;                 if (fq == 0) SSQ[r * 32 + u.pn * 4 + wc] = s;
;                 if (m & 1) asm volatile("" ::: "memory"); }
;     }
.LBB0_574:
	v_lshl_add_u32 v148, s48, 8, v1
	v_lshl_or_b32 v146, s10, 8, v151
	v_ashrrev_i32_e32 v149, 31, v148
	v_ashrrev_i32_e32 v147, 31, v146
	v_lshlrev_b64 v[154:155], 11, v[148:149]
	v_lshl_add_u64 v[162:163], v[154:155], 0, v[146:147]
	v_lshl_add_u64 v[164:165], v[162:163], 2, s[14:15]
	global_load_dwordx4 v[154:157], v[164:165], off
	global_load_dwordx4 v[158:161], v[164:165], off offset:16
	v_lshlrev_b64 v[162:163], 1, v[162:163]
	v_lshl_add_u64 v[166:167], s[18:19], 0, v[162:163]
	s_lshl_b32 s10, s10, 2
	v_or_b32_e32 v162, 0x100, v162
	s_ashr_i32 s11, s10, 31
	s_waitcnt vmcnt(0)
	v_pk_add_f32 v[128:129], v[128:129], v[156:157]
	v_pk_add_f32 v[168:169], v[126:127], v[154:155]
	v_pk_add_f32 v[160:161], v[124:125], v[160:161]
	v_pk_add_f32 v[158:159], v[122:123], v[158:159]
	v_cvt_pk_bf16_f32 v122, v168, v169
	v_cvt_pk_bf16_f32 v123, v128, v129
	v_cvt_pk_bf16_f32 v124, v158, v159
	v_cvt_pk_bf16_f32 v125, v160, v161
	global_store_dwordx4 v[166:167], v[122:125], off sc1
	global_load_dwordx4 v[124:127], v[164:165], off offset:512
	s_nop 0
	global_load_dwordx4 v[154:157], v[164:165], off offset:528
	v_and_b32_e32 v123, 64, v153
	v_xor_b32_e32 v122, 16, v153
	v_add_u32_e32 v123, 64, v123
	v_xor_b32_e32 v164, 32, v153
	v_cmp_lt_i32_e32 vcc, v122, v123
	v_mul_f32_e32 v129, v129, v129
	v_mul_f32_e32 v159, v159, v159
	v_cndmask_b32_e32 v122, v153, v122, vcc
	v_cmp_lt_i32_e32 vcc, v164, v123
	v_lshlrev_b32_e32 v123, 2, v122
	v_mul_f32_e32 v161, v161, v161
	v_cndmask_b32_e32 v164, v153, v164, vcc
	v_lshlrev_b32_e32 v122, 2, v164
	v_mul_f32_e32 v164, v169, v169
	v_fmac_f32_e32 v164, v168, v168
	v_fmac_f32_e32 v129, v128, v128
	v_fmac_f32_e32 v159, v158, v158
	v_fmac_f32_e32 v161, v160, v160
	v_add_f32_e32 v128, v164, v129
	v_add_f32_e32 v129, v159, v161
	v_add_f32_e32 v128, v128, v129
	s_waitcnt vmcnt(1)
	v_pk_add_f32 v[120:121], v[120:121], v[126:127]
	v_pk_add_f32 v[118:119], v[118:119], v[124:125]
	s_waitcnt vmcnt(0)
	v_pk_add_f32 v[124:125], v[116:117], v[156:157]
	v_pk_add_f32 v[114:115], v[114:115], v[154:155]
	v_mul_f32_e32 v116, v119, v119
	v_mul_f32_e32 v117, v121, v121
	v_mul_f32_e32 v126, v115, v115
	v_mul_f32_e32 v127, v125, v125
	v_fmac_f32_e32 v116, v118, v118
	v_fmac_f32_e32 v117, v120, v120
	v_fmac_f32_e32 v126, v114, v114
	v_fmac_f32_e32 v127, v124, v124
	v_add_f32_e32 v116, v116, v117
	v_add_f32_e32 v117, v126, v127
	v_add_f32_e32 v116, v116, v117
	v_add_f32_e32 v126, v128, v116
	ds_bpermute_b32 v127, v123, v126
	v_cvt_pk_bf16_f32 v116, v118, v119
	v_cvt_pk_bf16_f32 v118, v114, v115
	v_cvt_pk_bf16_f32 v117, v120, v121
	v_cvt_pk_bf16_f32 v119, v124, v125
	s_waitcnt lgkmcnt(0)
	v_add_f32_e32 v114, v126, v127
	ds_bpermute_b32 v115, v122, v114
	v_lshl_add_u64 v[120:121], s[18:19], 0, v[162:163]
	global_store_dwordx4 v[120:121], v[116:119], off sc1
	s_and_saveexec_b64 s[48:49], s[6:7]
	s_cbranch_execz .LBB0_576
	v_lshlrev_b64 v[116:117], 7, v[148:149]
	v_lshl_add_u64 v[116:117], s[24:25], 0, v[116:117]
	v_lshl_add_u64 v[116:117], s[10:11], 2, v[116:117]
	s_lshl_b32 s36, s61, 2
	s_mov_b32 s37, s8
	v_lshl_add_u64 v[116:117], v[116:117], 0, s[36:37]
	s_waitcnt lgkmcnt(0)
	v_add_f32_e32 v114, v114, v115
	global_store_dword v[116:117], v114, off
.LBB0_576:
	s_or_b64 exec, exec, s[48:49]
	v_or_b32_e32 v114, 16, v148
	s_waitcnt lgkmcnt(0)
	v_ashrrev_i32_e32 v115, 31, v114
	v_lshlrev_b64 v[116:117], 11, v[114:115]
	v_lshl_add_u64 v[120:121], v[116:117], 0, v[146:147]
	v_lshl_add_u64 v[128:129], v[120:121], 2, s[14:15]
	global_load_dwordx4 v[116:119], v[128:129], off
	global_load_dwordx4 v[124:127], v[128:129], off offset:16
	v_lshlrev_b64 v[120:121], 1, v[120:121]
	v_lshl_add_u64 v[154:155], s[18:19], 0, v[120:121]
	v_or_b32_e32 v120, 0x100, v120
	s_waitcnt vmcnt(1)
	v_pk_add_f32 v[118:119], v[112:113], v[118:119]
	v_pk_add_f32 v[116:117], v[110:111], v[116:117]
	s_waitcnt vmcnt(0)
	v_pk_add_f32 v[126:127], v[108:109], v[126:127]
	v_pk_add_f32 v[124:125], v[106:107], v[124:125]
	v_cvt_pk_bf16_f32 v106, v116, v117
	v_cvt_pk_bf16_f32 v107, v118, v119
	v_cvt_pk_bf16_f32 v108, v124, v125
	v_cvt_pk_bf16_f32 v109, v126, v127
	global_store_dwordx4 v[154:155], v[106:109], off sc1
	global_load_dwordx4 v[106:109], v[128:129], off offset:512
	s_nop 0
	global_load_dwordx4 v[110:113], v[128:129], off offset:528
	v_mul_f32_e32 v117, v117, v117
	v_mul_f32_e32 v119, v119, v119
	v_mul_f32_e32 v125, v125, v125
	v_mul_f32_e32 v127, v127, v127
	v_fmac_f32_e32 v117, v116, v116
	v_fmac_f32_e32 v119, v118, v118
	v_fmac_f32_e32 v125, v124, v124
	v_fmac_f32_e32 v127, v126, v126
	v_add_f32_e32 v116, v117, v119
	v_add_f32_e32 v117, v125, v127
	v_add_f32_e32 v116, v116, v117
	s_waitcnt vmcnt(1)
	v_pk_add_f32 v[104:105], v[104:105], v[108:109]
	v_pk_add_f32 v[102:103], v[102:103], v[106:107]
	s_waitcnt vmcnt(0)
	v_pk_add_f32 v[106:107], v[100:101], v[112:113]
	v_pk_add_f32 v[98:99], v[98:99], v[110:111]
	v_mul_f32_e32 v100, v103, v103
	v_mul_f32_e32 v101, v105, v105
	v_mul_f32_e32 v108, v99, v99
	v_mul_f32_e32 v109, v107, v107
	v_fmac_f32_e32 v100, v102, v102
	v_fmac_f32_e32 v101, v104, v104
	v_fmac_f32_e32 v108, v98, v98
	v_fmac_f32_e32 v109, v106, v106
	v_add_f32_e32 v100, v100, v101
	v_add_f32_e32 v101, v108, v109
	v_add_f32_e32 v100, v100, v101
	v_add_f32_e32 v108, v116, v100
	ds_bpermute_b32 v109, v123, v108
	v_cvt_pk_bf16_f32 v100, v102, v103
	v_cvt_pk_bf16_f32 v102, v98, v99
	v_cvt_pk_bf16_f32 v101, v104, v105
	v_cvt_pk_bf16_f32 v103, v106, v107
	s_waitcnt lgkmcnt(0)
	v_add_f32_e32 v98, v108, v109
	ds_bpermute_b32 v99, v122, v98
	v_lshl_add_u64 v[104:105], s[18:19], 0, v[120:121]
	global_store_dwordx4 v[104:105], v[100:103], off sc1
	s_and_saveexec_b64 s[48:49], s[6:7]
	s_cbranch_execz .LBB0_578
	v_lshlrev_b64 v[100:101], 7, v[114:115]
	v_lshl_add_u64 v[100:101], s[24:25], 0, v[100:101]
	v_lshl_add_u64 v[100:101], s[10:11], 2, v[100:101]
	s_lshl_b32 s36, s61, 2
	s_mov_b32 s37, s8
	v_lshl_add_u64 v[100:101], v[100:101], 0, s[36:37]
	s_waitcnt lgkmcnt(0)
	v_add_f32_e32 v98, v98, v99
	global_store_dword v[100:101], v98, off
; __device__ __forceinline__ unsigned cvt_pk_bf16(float lo, float hi) { f32x2v_ v = {lo, hi}; bf16x2v_ b = __builtin_convertvector(v, bf16x2v_); return __builtin_bit_cast(unsigned, b); }
;     __device__ __forceinline__ void operator()(const f32x4 (&acc)[2][2][4][2], const Unit& u, int wr, int wc, int fr, int fq) const {
;         const int row0 = u.pm * BM + wr * 64 + fr, col0 = u.pn * BM + wc * 32 + 8 * fq;
; #pragma unroll
;         for (int ai = 0; ai < 2; ++ai)
; #pragma unroll
;             for (int m = 0; m < 4; ++m) { const size_t r = (size_t)(row0 + ai * HALF + m * 16); float s = 0.f;
; #pragma unroll
;                 for (int bj = 0; bj < 2; ++bj) { const size_t off = r * 2048 + col0 + bj * HALF;
;                     const f32x4 v0 = *(const f32x4*)(X + off) + acc[ai][bj][m][0], v1 = *(const f32x4*)(X + off + 4) + acc[ai][bj][m][1];
;                     u32x4 w; w.x = cvt_pk_bf16(v0[0], v0[1]); w.y = cvt_pk_bf16(v0[2], v0[3]); w.z = cvt_pk_bf16(v1[0], v1[1]); w.w = cvt_pk_bf16(v1[2], v1[3]);
;                     *(u32x4*)(X1 + off) = w;
;                     s += ((v0[0] * v0[0] + v0[1] * v0[1]) + (v0[2] * v0[2] + v0[3] * v0[3])) + ((v1[0] * v1[0] + v1[1] * v1[1]) + (v1[2] * v1[2] + v1[3] * v1[3])); }
;                 s += __shfl_xor(s, 16); s += __shfl_xor(s, 32);
;                 if (fq == 0) SSQ[r * 32 + u.pn * 4 + wc] = s;
;                 if (m & 1) asm volatile("" ::: "memory"); }
;     }
.LBB0_578:
	s_or_b64 exec, exec, s[48:49]
	v_or_b32_e32 v98, 32, v148
	s_waitcnt lgkmcnt(0)
	v_ashrrev_i32_e32 v99, 31, v98
	v_lshlrev_b64 v[100:101], 11, v[98:99]
	v_lshl_add_u64 v[108:109], v[100:101], 0, v[146:147]
	v_lshl_add_u64 v[110:111], v[108:109], 2, s[14:15]
	global_load_dwordx4 v[100:103], v[110:111], off
	global_load_dwordx4 v[104:107], v[110:111], off offset:16
	v_lshlrev_b64 v[108:109], 1, v[108:109]
	v_lshl_add_u64 v[112:113], s[18:19], 0, v[108:109]
	v_or_b32_e32 v108, 0x100, v108
	s_waitcnt vmcnt(1)
	v_pk_add_f32 v[102:103], v[96:97], v[102:103]
	v_pk_add_f32 v[100:101], v[94:95], v[100:101]
	s_waitcnt vmcnt(0)
	v_pk_add_f32 v[106:107], v[92:93], v[106:107]
	v_pk_add_f32 v[104:105], v[90:91], v[104:105]
	v_cvt_pk_bf16_f32 v90, v100, v101
	v_cvt_pk_bf16_f32 v91, v102, v103
	v_cvt_pk_bf16_f32 v92, v104, v105
	v_cvt_pk_bf16_f32 v93, v106, v107
	global_store_dwordx4 v[112:113], v[90:93], off sc1
	global_load_dwordx4 v[90:93], v[110:111], off offset:512
	s_nop 0
	global_load_dwordx4 v[94:97], v[110:111], off offset:528
	v_mul_f32_e32 v101, v101, v101
	v_mul_f32_e32 v103, v103, v103
	v_mul_f32_e32 v105, v105, v105
	v_mul_f32_e32 v107, v107, v107
	v_fmac_f32_e32 v101, v100, v100
	v_fmac_f32_e32 v103, v102, v102
	v_fmac_f32_e32 v105, v104, v104
	v_fmac_f32_e32 v107, v106, v106
	v_add_f32_e32 v100, v101, v103
	v_add_f32_e32 v101, v105, v107
	v_add_f32_e32 v100, v100, v101
	s_waitcnt vmcnt(1)
	v_pk_add_f32 v[88:89], v[88:89], v[92:93]
	v_pk_add_f32 v[86:87], v[86:87], v[90:91]
	s_waitcnt vmcnt(0)
	v_pk_add_f32 v[90:91], v[84:85], v[96:97]
	v_pk_add_f32 v[82:83], v[82:83], v[94:95]
	v_mul_f32_e32 v84, v87, v87
	v_mul_f32_e32 v85, v89, v89
	v_mul_f32_e32 v92, v83, v83
	v_mul_f32_e32 v93, v91, v91
	v_fmac_f32_e32 v84, v86, v86
	v_fmac_f32_e32 v85, v88, v88
	v_fmac_f32_e32 v92, v82, v82
	v_fmac_f32_e32 v93, v90, v90
	v_add_f32_e32 v84, v84, v85
	v_add_f32_e32 v85, v92, v93
	v_add_f32_e32 v84, v84, v85
	v_add_f32_e32 v92, v100, v84
	ds_bpermute_b32 v93, v123, v92
	v_cvt_pk_bf16_f32 v84, v86, v87
	v_cvt_pk_bf16_f32 v86, v82, v83
	v_cvt_pk_bf16_f32 v85, v88, v89
	v_cvt_pk_bf16_f32 v87, v90, v91
	s_waitcnt lgkmcnt(0)
	v_add_f32_e32 v82, v92, v93
	ds_bpermute_b32 v83, v122, v82
	v_lshl_add_u64 v[88:89], s[18:19], 0, v[108:109]
	global_store_dwordx4 v[88:89], v[84:87], off sc1
	s_and_saveexec_b64 s[48:49], s[6:7]
	s_cbranch_execz .LBB0_580
	v_lshlrev_b64 v[84:85], 7, v[98:99]
	v_lshl_add_u64 v[84:85], s[24:25], 0, v[84:85]
	v_lshl_add_u64 v[84:85], s[10:11], 2, v[84:85]
	s_lshl_b32 s36, s61, 2
	s_mov_b32 s37, s8
	v_lshl_add_u64 v[84:85], v[84:85], 0, s[36:37]
	s_waitcnt lgkmcnt(0)
	v_add_f32_e32 v82, v82, v83
	global_store_dword v[84:85], v82, off
.LBB0_580:
	s_or_b64 exec, exec, s[48:49]
	v_or_b32_e32 v82, 48, v148
	s_waitcnt lgkmcnt(0)
	v_ashrrev_i32_e32 v83, 31, v82
	v_lshlrev_b64 v[84:85], 11, v[82:83]
	v_lshl_add_u64 v[92:93], v[84:85], 0, v[146:147]
	v_lshl_add_u64 v[94:95], v[92:93], 2, s[14:15]
	global_load_dwordx4 v[84:87], v[94:95], off
	global_load_dwordx4 v[88:91], v[94:95], off offset:16
	v_lshlrev_b64 v[92:93], 1, v[92:93]
	v_lshl_add_u64 v[96:97], s[18:19], 0, v[92:93]
	v_or_b32_e32 v92, 0x100, v92
	s_waitcnt vmcnt(1)
	v_pk_add_f32 v[86:87], v[80:81], v[86:87]
	v_pk_add_f32 v[84:85], v[78:79], v[84:85]
	s_waitcnt vmcnt(0)
	v_pk_add_f32 v[90:91], v[76:77], v[90:91]
	v_pk_add_f32 v[88:89], v[74:75], v[88:89]
	v_cvt_pk_bf16_f32 v74, v84, v85
	v_cvt_pk_bf16_f32 v75, v86, v87
	v_cvt_pk_bf16_f32 v76, v88, v89
	v_cvt_pk_bf16_f32 v77, v90, v91
	global_store_dwordx4 v[96:97], v[74:77], off sc1
	global_load_dwordx4 v[74:77], v[94:95], off offset:512
	s_nop 0
	global_load_dwordx4 v[78:81], v[94:95], off offset:528
	v_mul_f32_e32 v85, v85, v85
	v_mul_f32_e32 v87, v87, v87
	v_mul_f32_e32 v89, v89, v89
	v_mul_f32_e32 v91, v91, v91
	v_fmac_f32_e32 v85, v84, v84
	v_fmac_f32_e32 v87, v86, v86
	v_fmac_f32_e32 v89, v88, v88
	v_fmac_f32_e32 v91, v90, v90
	v_add_f32_e32 v84, v85, v87
	v_add_f32_e32 v85, v89, v91
	v_add_f32_e32 v84, v84, v85
	s_waitcnt vmcnt(1)
	v_pk_add_f32 v[72:73], v[72:73], v[76:77]
	v_pk_add_f32 v[70:71], v[70:71], v[74:75]
	s_waitcnt vmcnt(0)
	v_pk_add_f32 v[74:75], v[68:69], v[80:81]
	v_pk_add_f32 v[66:67], v[66:67], v[78:79]
	v_mul_f32_e32 v68, v71, v71
	v_mul_f32_e32 v69, v73, v73
	v_mul_f32_e32 v76, v67, v67
	v_mul_f32_e32 v77, v75, v75
	v_fmac_f32_e32 v68, v70, v70
	v_fmac_f32_e32 v69, v72, v72
	v_fmac_f32_e32 v76, v66, v66
	v_fmac_f32_e32 v77, v74, v74
	v_add_f32_e32 v68, v68, v69
	v_add_f32_e32 v69, v76, v77
	v_add_f32_e32 v68, v68, v69
	v_add_f32_e32 v76, v84, v68
	ds_bpermute_b32 v77, v123, v76
	v_cvt_pk_bf16_f32 v68, v70, v71
	v_cvt_pk_bf16_f32 v70, v66, v67
	v_cvt_pk_bf16_f32 v69, v72, v73
	v_cvt_pk_bf16_f32 v71, v74, v75
	s_waitcnt lgkmcnt(0)
	v_add_f32_e32 v66, v76, v77
	ds_bpermute_b32 v67, v122, v66
	v_lshl_add_u64 v[72:73], s[18:19], 0, v[92:93]
	global_store_dwordx4 v[72:73], v[68:71], off sc1
	s_and_saveexec_b64 s[48:49], s[6:7]
	s_cbranch_execz .LBB0_582
	v_lshlrev_b64 v[68:69], 7, v[82:83]
	v_lshl_add_u64 v[68:69], s[24:25], 0, v[68:69]
	v_lshl_add_u64 v[68:69], s[10:11], 2, v[68:69]
	s_lshl_b32 s36, s61, 2
	s_mov_b32 s37, s8
	v_lshl_add_u64 v[68:69], v[68:69], 0, s[36:37]
	s_waitcnt lgkmcnt(0)
	v_add_f32_e32 v66, v66, v67
	global_store_dword v[68:69], v66, off
; __device__ __forceinline__ unsigned cvt_pk_bf16(float lo, float hi) { f32x2v_ v = {lo, hi}; bf16x2v_ b = __builtin_convertvector(v, bf16x2v_); return __builtin_bit_cast(unsigned, b); }
;     __device__ __forceinline__ void operator()(const f32x4 (&acc)[2][2][4][2], const Unit& u, int wr, int wc, int fr, int fq) const {
;         const int row0 = u.pm * BM + wr * 64 + fr, col0 = u.pn * BM + wc * 32 + 8 * fq;
; #pragma unroll
;         for (int ai = 0; ai < 2; ++ai)
; #pragma unroll
;             for (int m = 0; m < 4; ++m) { const size_t r = (size_t)(row0 + ai * HALF + m * 16); float s = 0.f;
; #pragma unroll
;                 for (int bj = 0; bj < 2; ++bj) { const size_t off = r * 2048 + col0 + bj * HALF;
;                     const f32x4 v0 = *(const f32x4*)(X + off) + acc[ai][bj][m][0], v1 = *(const f32x4*)(X + off + 4) + acc[ai][bj][m][1];
;                     u32x4 w; w.x = cvt_pk_bf16(v0[0], v0[1]); w.y = cvt_pk_bf16(v0[2], v0[3]); w.z = cvt_pk_bf16(v1[0], v1[1]); w.w = cvt_pk_bf16(v1[2], v1[3]);
;                     *(u32x4*)(X1 + off) = w;
;                     s += ((v0[0] * v0[0] + v0[1] * v0[1]) + (v0[2] * v0[2] + v0[3] * v0[3])) + ((v1[0] * v1[0] + v1[1] * v1[1]) + (v1[2] * v1[2] + v1[3] * v1[3])); }
;                 s += __shfl_xor(s, 16); s += __shfl_xor(s, 32);
;                 if (fq == 0) SSQ[r * 32 + u.pn * 4 + wc] = s;
;                 if (m & 1) asm volatile("" ::: "memory"); }
;     }
.LBB0_582:
	s_or_b64 exec, exec, s[48:49]
	v_add_u32_e32 v66, 0x80, v148
	s_waitcnt lgkmcnt(0)
	v_ashrrev_i32_e32 v67, 31, v66
	v_lshlrev_b64 v[68:69], 11, v[66:67]
	v_lshl_add_u64 v[76:77], v[68:69], 0, v[146:147]
	v_lshl_add_u64 v[78:79], v[76:77], 2, s[14:15]
	global_load_dwordx4 v[68:71], v[78:79], off
	global_load_dwordx4 v[72:75], v[78:79], off offset:16
	v_lshlrev_b64 v[76:77], 1, v[76:77]
	v_lshl_add_u64 v[80:81], s[18:19], 0, v[76:77]
	v_or_b32_e32 v76, 0x100, v76
	s_waitcnt vmcnt(1)
	v_pk_add_f32 v[70:71], v[64:65], v[70:71]
	v_pk_add_f32 v[68:69], v[62:63], v[68:69]
	s_waitcnt vmcnt(0)
	v_pk_add_f32 v[74:75], v[60:61], v[74:75]
	v_pk_add_f32 v[72:73], v[58:59], v[72:73]
	v_cvt_pk_bf16_f32 v58, v68, v69
	v_cvt_pk_bf16_f32 v59, v70, v71
	v_cvt_pk_bf16_f32 v60, v72, v73
	v_cvt_pk_bf16_f32 v61, v74, v75
	global_store_dwordx4 v[80:81], v[58:61], off sc1
	global_load_dwordx4 v[58:61], v[78:79], off offset:512
	s_nop 0
	global_load_dwordx4 v[62:65], v[78:79], off offset:528
	v_mul_f32_e32 v69, v69, v69
	v_mul_f32_e32 v71, v71, v71
	v_mul_f32_e32 v73, v73, v73
	v_mul_f32_e32 v75, v75, v75
	v_fmac_f32_e32 v69, v68, v68
	v_fmac_f32_e32 v71, v70, v70
	v_fmac_f32_e32 v73, v72, v72
	v_fmac_f32_e32 v75, v74, v74
	v_add_f32_e32 v68, v69, v71
	v_add_f32_e32 v69, v73, v75
	v_add_f32_e32 v68, v68, v69
	s_waitcnt vmcnt(1)
	v_pk_add_f32 v[56:57], v[56:57], v[60:61]
	v_pk_add_f32 v[54:55], v[54:55], v[58:59]
	s_waitcnt vmcnt(0)
	v_pk_add_f32 v[58:59], v[52:53], v[64:65]
	v_pk_add_f32 v[50:51], v[50:51], v[62:63]
	v_mul_f32_e32 v52, v55, v55
	v_mul_f32_e32 v53, v57, v57
	v_mul_f32_e32 v60, v51, v51
	v_mul_f32_e32 v61, v59, v59
	v_fmac_f32_e32 v52, v54, v54
	v_fmac_f32_e32 v53, v56, v56
	v_fmac_f32_e32 v60, v50, v50
	v_fmac_f32_e32 v61, v58, v58
	v_add_f32_e32 v52, v52, v53
	v_add_f32_e32 v53, v60, v61
	v_add_f32_e32 v52, v52, v53
	v_add_f32_e32 v60, v68, v52
	ds_bpermute_b32 v61, v123, v60
	v_cvt_pk_bf16_f32 v52, v54, v55
	v_cvt_pk_bf16_f32 v54, v50, v51
	v_cvt_pk_bf16_f32 v53, v56, v57
	v_cvt_pk_bf16_f32 v55, v58, v59
	s_waitcnt lgkmcnt(0)
	v_add_f32_e32 v50, v60, v61
	ds_bpermute_b32 v51, v122, v50
	v_lshl_add_u64 v[56:57], s[18:19], 0, v[76:77]
	global_store_dwordx4 v[56:57], v[52:55], off sc1
	s_and_saveexec_b64 s[48:49], s[6:7]
	s_cbranch_execz .LBB0_584
	v_lshlrev_b64 v[52:53], 7, v[66:67]
	v_lshl_add_u64 v[52:53], s[24:25], 0, v[52:53]
	v_lshl_add_u64 v[52:53], s[10:11], 2, v[52:53]
	s_lshl_b32 s36, s61, 2
	s_mov_b32 s37, s8
	v_lshl_add_u64 v[52:53], v[52:53], 0, s[36:37]
	s_waitcnt lgkmcnt(0)
	v_add_f32_e32 v50, v50, v51
	global_store_dword v[52:53], v50, off
.LBB0_584:
	s_or_b64 exec, exec, s[48:49]
	v_add_u32_e32 v50, 0x90, v148
	s_waitcnt lgkmcnt(0)
	v_ashrrev_i32_e32 v51, 31, v50
	v_lshlrev_b64 v[52:53], 11, v[50:51]
	v_lshl_add_u64 v[60:61], v[52:53], 0, v[146:147]
	v_lshl_add_u64 v[62:63], v[60:61], 2, s[14:15]
	global_load_dwordx4 v[52:55], v[62:63], off
	global_load_dwordx4 v[56:59], v[62:63], off offset:16
	v_lshlrev_b64 v[60:61], 1, v[60:61]
	v_lshl_add_u64 v[64:65], s[18:19], 0, v[60:61]
	v_or_b32_e32 v60, 0x100, v60
	s_waitcnt vmcnt(1)
	v_pk_add_f32 v[54:55], v[48:49], v[54:55]
	v_pk_add_f32 v[52:53], v[46:47], v[52:53]
	s_waitcnt vmcnt(0)
	v_pk_add_f32 v[58:59], v[44:45], v[58:59]
	v_pk_add_f32 v[56:57], v[42:43], v[56:57]
	v_cvt_pk_bf16_f32 v42, v52, v53
	v_cvt_pk_bf16_f32 v43, v54, v55
	v_cvt_pk_bf16_f32 v44, v56, v57
	v_cvt_pk_bf16_f32 v45, v58, v59
	global_store_dwordx4 v[64:65], v[42:45], off sc1
	global_load_dwordx4 v[42:45], v[62:63], off offset:512
	s_nop 0
	global_load_dwordx4 v[46:49], v[62:63], off offset:528
	v_mul_f32_e32 v53, v53, v53
	v_mul_f32_e32 v55, v55, v55
	v_mul_f32_e32 v57, v57, v57
	v_mul_f32_e32 v59, v59, v59
	v_fmac_f32_e32 v53, v52, v52
	v_fmac_f32_e32 v55, v54, v54
	v_fmac_f32_e32 v57, v56, v56
	v_fmac_f32_e32 v59, v58, v58
	v_add_f32_e32 v52, v53, v55
	v_add_f32_e32 v53, v57, v59
	v_add_f32_e32 v52, v52, v53
	s_waitcnt vmcnt(1)
	v_pk_add_f32 v[40:41], v[40:41], v[44:45]
	v_pk_add_f32 v[38:39], v[38:39], v[42:43]
	s_waitcnt vmcnt(0)
	v_pk_add_f32 v[42:43], v[36:37], v[48:49]
	v_pk_add_f32 v[34:35], v[34:35], v[46:47]
	v_mul_f32_e32 v36, v39, v39
	v_mul_f32_e32 v37, v41, v41
	v_mul_f32_e32 v44, v35, v35
	v_mul_f32_e32 v45, v43, v43
	v_fmac_f32_e32 v36, v38, v38
	v_fmac_f32_e32 v37, v40, v40
	v_fmac_f32_e32 v44, v34, v34
	v_fmac_f32_e32 v45, v42, v42
	v_add_f32_e32 v36, v36, v37
	v_add_f32_e32 v37, v44, v45
	v_add_f32_e32 v36, v36, v37
	v_add_f32_e32 v44, v52, v36
	ds_bpermute_b32 v45, v123, v44
	v_cvt_pk_bf16_f32 v36, v38, v39
	v_cvt_pk_bf16_f32 v38, v34, v35
	v_cvt_pk_bf16_f32 v37, v40, v41
	v_cvt_pk_bf16_f32 v39, v42, v43
	s_waitcnt lgkmcnt(0)
	v_add_f32_e32 v34, v44, v45
	ds_bpermute_b32 v35, v122, v34
	v_lshl_add_u64 v[40:41], s[18:19], 0, v[60:61]
	global_store_dwordx4 v[40:41], v[36:39], off sc1
	s_and_saveexec_b64 s[48:49], s[6:7]
	s_cbranch_execz .LBB0_586
	v_lshlrev_b64 v[36:37], 7, v[50:51]
	v_lshl_add_u64 v[36:37], s[24:25], 0, v[36:37]
	v_lshl_add_u64 v[36:37], s[10:11], 2, v[36:37]
	s_lshl_b32 s36, s61, 2
	s_mov_b32 s37, s8
	v_lshl_add_u64 v[36:37], v[36:37], 0, s[36:37]
	s_waitcnt lgkmcnt(0)
	v_add_f32_e32 v34, v34, v35
	global_store_dword v[36:37], v34, off
; __device__ __forceinline__ unsigned cvt_pk_bf16(float lo, float hi) { f32x2v_ v = {lo, hi}; bf16x2v_ b = __builtin_convertvector(v, bf16x2v_); return __builtin_bit_cast(unsigned, b); }
;     __device__ __forceinline__ void operator()(const f32x4 (&acc)[2][2][4][2], const Unit& u, int wr, int wc, int fr, int fq) const {
;         const int row0 = u.pm * BM + wr * 64 + fr, col0 = u.pn * BM + wc * 32 + 8 * fq;
; #pragma unroll
;         for (int ai = 0; ai < 2; ++ai)
; #pragma unroll
;             for (int m = 0; m < 4; ++m) { const size_t r = (size_t)(row0 + ai * HALF + m * 16); float s = 0.f;
; #pragma unroll
;                 for (int bj = 0; bj < 2; ++bj) { const size_t off = r * 2048 + col0 + bj * HALF;
;                     const f32x4 v0 = *(const f32x4*)(X + off) + acc[ai][bj][m][0], v1 = *(const f32x4*)(X + off + 4) + acc[ai][bj][m][1];
;                     u32x4 w; w.x = cvt_pk_bf16(v0[0], v0[1]); w.y = cvt_pk_bf16(v0[2], v0[3]); w.z = cvt_pk_bf16(v1[0], v1[1]); w.w = cvt_pk_bf16(v1[2], v1[3]);
;                     *(u32x4*)(X1 + off) = w;
;                     s += ((v0[0] * v0[0] + v0[1] * v0[1]) + (v0[2] * v0[2] + v0[3] * v0[3])) + ((v1[0] * v1[0] + v1[1] * v1[1]) + (v1[2] * v1[2] + v1[3] * v1[3])); }
;                 s += __shfl_xor(s, 16); s += __shfl_xor(s, 32);
;                 if (fq == 0) SSQ[r * 32 + u.pn * 4 + wc] = s;
;                 if (m & 1) asm volatile("" ::: "memory"); }
;     }
.LBB0_586:
	s_or_b64 exec, exec, s[48:49]
	v_add_u32_e32 v34, 0xa0, v148
	s_waitcnt lgkmcnt(0)
	v_ashrrev_i32_e32 v35, 31, v34
	v_lshlrev_b64 v[36:37], 11, v[34:35]
	v_lshl_add_u64 v[44:45], v[36:37], 0, v[146:147]
	v_lshl_add_u64 v[46:47], v[44:45], 2, s[14:15]
	global_load_dwordx4 v[36:39], v[46:47], off
	global_load_dwordx4 v[40:43], v[46:47], off offset:16
	v_lshlrev_b64 v[44:45], 1, v[44:45]
	v_lshl_add_u64 v[48:49], s[18:19], 0, v[44:45]
	v_or_b32_e32 v44, 0x100, v44
	s_waitcnt vmcnt(1)
	v_pk_add_f32 v[38:39], v[32:33], v[38:39]
	v_pk_add_f32 v[36:37], v[30:31], v[36:37]
	s_waitcnt vmcnt(0)
	v_pk_add_f32 v[42:43], v[28:29], v[42:43]
	v_pk_add_f32 v[40:41], v[26:27], v[40:41]
	v_cvt_pk_bf16_f32 v26, v36, v37
	v_cvt_pk_bf16_f32 v27, v38, v39
	v_cvt_pk_bf16_f32 v28, v40, v41
	v_cvt_pk_bf16_f32 v29, v42, v43
	global_store_dwordx4 v[48:49], v[26:29], off sc1
	global_load_dwordx4 v[26:29], v[46:47], off offset:512
	s_nop 0
	global_load_dwordx4 v[30:33], v[46:47], off offset:528
	v_mul_f32_e32 v37, v37, v37
	v_mul_f32_e32 v39, v39, v39
	v_mul_f32_e32 v41, v41, v41
	v_mul_f32_e32 v43, v43, v43
	v_fmac_f32_e32 v37, v36, v36
	v_fmac_f32_e32 v39, v38, v38
	v_fmac_f32_e32 v41, v40, v40
	v_fmac_f32_e32 v43, v42, v42
	v_add_f32_e32 v36, v37, v39
	v_add_f32_e32 v37, v41, v43
	v_add_f32_e32 v36, v36, v37
	s_waitcnt vmcnt(1)
	v_pk_add_f32 v[24:25], v[24:25], v[28:29]
	v_pk_add_f32 v[22:23], v[22:23], v[26:27]
	s_waitcnt vmcnt(0)
	v_pk_add_f32 v[26:27], v[20:21], v[32:33]
	v_pk_add_f32 v[18:19], v[18:19], v[30:31]
	v_mul_f32_e32 v20, v23, v23
	v_mul_f32_e32 v21, v25, v25
	v_mul_f32_e32 v28, v19, v19
	v_mul_f32_e32 v29, v27, v27
	v_fmac_f32_e32 v20, v22, v22
	v_fmac_f32_e32 v21, v24, v24
	v_fmac_f32_e32 v28, v18, v18
	v_fmac_f32_e32 v29, v26, v26
	v_add_f32_e32 v20, v20, v21
	v_add_f32_e32 v21, v28, v29
	v_add_f32_e32 v20, v20, v21
	v_add_f32_e32 v28, v36, v20
	ds_bpermute_b32 v29, v123, v28
	v_cvt_pk_bf16_f32 v20, v22, v23
	v_cvt_pk_bf16_f32 v22, v18, v19
	v_cvt_pk_bf16_f32 v21, v24, v25
	v_cvt_pk_bf16_f32 v23, v26, v27
	s_waitcnt lgkmcnt(0)
	v_add_f32_e32 v18, v28, v29
	ds_bpermute_b32 v19, v122, v18
	v_lshl_add_u64 v[24:25], s[18:19], 0, v[44:45]
	global_store_dwordx4 v[24:25], v[20:23], off sc1
	s_and_saveexec_b64 s[48:49], s[6:7]
	s_cbranch_execz .LBB0_588
	v_lshlrev_b64 v[20:21], 7, v[34:35]
	v_lshl_add_u64 v[20:21], s[24:25], 0, v[20:21]
	v_lshl_add_u64 v[20:21], s[10:11], 2, v[20:21]
	s_lshl_b32 s36, s61, 2
	s_mov_b32 s37, s8
	v_lshl_add_u64 v[20:21], v[20:21], 0, s[36:37]
	s_waitcnt lgkmcnt(0)
	v_add_f32_e32 v18, v18, v19
	global_store_dword v[20:21], v18, off
.LBB0_588:
	s_or_b64 exec, exec, s[48:49]
	v_add_u32_e32 v18, 0xb0, v148
	s_waitcnt lgkmcnt(0)
	v_ashrrev_i32_e32 v19, 31, v18
	v_lshlrev_b64 v[20:21], 11, v[18:19]
	v_lshl_add_u64 v[28:29], v[20:21], 0, v[146:147]
	v_lshl_add_u64 v[30:31], v[28:29], 2, s[14:15]
	global_load_dwordx4 v[20:23], v[30:31], off
	global_load_dwordx4 v[24:27], v[30:31], off offset:16
	v_lshlrev_b64 v[28:29], 1, v[28:29]
	v_lshl_add_u64 v[32:33], s[18:19], 0, v[28:29]
	v_or_b32_e32 v28, 0x100, v28
	s_waitcnt vmcnt(1)
	v_pk_add_f32 v[22:23], v[16:17], v[22:23]
	v_pk_add_f32 v[20:21], v[14:15], v[20:21]
	s_waitcnt vmcnt(0)
	v_pk_add_f32 v[26:27], v[12:13], v[26:27]
	v_pk_add_f32 v[24:25], v[10:11], v[24:25]
	v_cvt_pk_bf16_f32 v10, v20, v21
	v_cvt_pk_bf16_f32 v11, v22, v23
	v_cvt_pk_bf16_f32 v12, v24, v25
	v_cvt_pk_bf16_f32 v13, v26, v27
	global_store_dwordx4 v[32:33], v[10:13], off sc1
	global_load_dwordx4 v[10:13], v[30:31], off offset:512
	s_nop 0
	global_load_dwordx4 v[14:17], v[30:31], off offset:528
	v_mul_f32_e32 v21, v21, v21
	v_mul_f32_e32 v23, v23, v23
	v_mul_f32_e32 v25, v25, v25
	v_mul_f32_e32 v27, v27, v27
	v_fmac_f32_e32 v21, v20, v20
	v_fmac_f32_e32 v23, v22, v22
	v_fmac_f32_e32 v25, v24, v24
	v_fmac_f32_e32 v27, v26, v26
	v_add_f32_e32 v20, v21, v23
	v_add_f32_e32 v21, v25, v27
	v_add_f32_e32 v20, v20, v21
	s_waitcnt vmcnt(1)
	v_pk_add_f32 v[8:9], v[8:9], v[12:13]
	v_pk_add_f32 v[6:7], v[6:7], v[10:11]
	s_waitcnt vmcnt(0)
	v_pk_add_f32 v[10:11], v[4:5], v[16:17]
	v_pk_add_f32 v[2:3], v[2:3], v[14:15]
	v_mul_f32_e32 v4, v7, v7
	v_mul_f32_e32 v5, v9, v9
	v_mul_f32_e32 v12, v3, v3
	v_mul_f32_e32 v13, v11, v11
	v_fmac_f32_e32 v4, v6, v6
	v_fmac_f32_e32 v5, v8, v8
	v_fmac_f32_e32 v12, v2, v2
	v_fmac_f32_e32 v13, v10, v10
	v_add_f32_e32 v4, v4, v5
	v_add_f32_e32 v5, v12, v13
	v_add_f32_e32 v4, v4, v5
	v_add_f32_e32 v12, v20, v4
	ds_bpermute_b32 v13, v123, v12
	v_cvt_pk_bf16_f32 v4, v6, v7
	v_cvt_pk_bf16_f32 v6, v2, v3
	v_cvt_pk_bf16_f32 v5, v8, v9
	v_cvt_pk_bf16_f32 v7, v10, v11
	s_waitcnt lgkmcnt(0)
	v_add_f32_e32 v2, v12, v13
	ds_bpermute_b32 v3, v122, v2
	v_lshl_add_u64 v[8:9], s[18:19], 0, v[28:29]
	global_store_dwordx4 v[8:9], v[4:7], off sc1
	s_and_saveexec_b64 s[48:49], s[6:7]
	s_cbranch_execz .LBB0_590
	v_lshlrev_b64 v[4:5], 7, v[18:19]
	v_lshl_add_u64 v[4:5], s[24:25], 0, v[4:5]
	v_lshl_add_u64 v[4:5], s[10:11], 2, v[4:5]
	s_lshl_b32 s10, s61, 2
	s_mov_b32 s11, s8
	v_lshl_add_u64 v[4:5], v[4:5], 0, s[10:11]
	s_waitcnt lgkmcnt(0)
	v_add_f32_e32 v2, v2, v3
	global_store_dword v[4:5], v2, off

; #define GAS __attribute__((address_space(1)))
; #define LAS __attribute__((address_space(3)))
; #define LDS_WAIT() asm volatile("s_waitcnt lgkmcnt(0)" ::: "memory")
; __device__ __forceinline__ unsigned pk2(float lo, float hi) { return f2bf(lo) | (f2bf(hi) << 16); }
; __device__ __forceinline__ void p0_transpose_item(const float* W, int N, int k0, int n0, bf16* WT, int K, int dst_row0, LAS float* scr, int lane, const float* kscale = nullptr, int permhalf = -1) {
;     typedef float f32x4t __attribute__((ext_vector_type(4)));
;     const int c = lane & 7;
;     float ks[8];
; #pragma unroll
;     for (int i = 0; i < 8; ++i) ks[i] = kscale ? kscale[k0 + 8 * c + i] : 1.0f;
; #pragma unroll
;     for (int i = 0; i < 8; ++i) { const int kk = 8 * i + (lane >> 3), nn = (lane & 7) * 4;
;         *(LAS f32x4t*)(scr + kk * 36 + nn) = *(const GAS f32x4t*)(W + (size_t)(k0 + kk) * N + n0 + nn); }
;     LDS_WAIT(); asm volatile("" ::: "memory");
; #pragma unroll
;     for (int j = 0; j < 4; ++j) { const int n = (lane >> 3) + 8 * j; const LAS float* s = scr + (8 * c) * 36 + n;
;         v4u o; o.x = pk2(s[0 * 36] * ks[0], s[1 * 36] * ks[1]); o.y = pk2(s[2 * 36] * ks[2], s[3 * 36] * ks[3]); o.z = pk2(s[4 * 36] * ks[4], s[5 * 36] * ks[5]); o.w = pk2(s[6 * 36] * ks[6], s[7 * 36] * ks[7]);
;         const int drow = permhalf < 0 ? n : (32 * (n >> 4) + 8 * ((n >> 2) & 3) + 4 * permhalf + (n & 3));
;         *(GAS v4u*)(WT + (size_t)(dst_row0 + drow) * K + k0 + 8 * c) = o; }
;     LDS_WAIT(); asm volatile("" ::: "memory");
; }
; __device__ __forceinline__ void conv_item(KArgs a, int r, LAS float* scr, int lane) {
;     ...
;     if (r < CONV_IE) { const int e = r / 512, q = r % 512, kb = q / 16, nb = q % 16, n0 = 32 * nb;
;         p0_transpose_item(a->in[18] + (size_t)e * 2048 * 512, 512, 64 * kb, n0, (bf16*)(ws + WS_W13), 2048, e * 1024 + (n0 >> 7) * 256 + (n0 & 127), scr, lane, a->in[15]); return; } r -= CONV_IE;
.LBB0_670:
	s_load_dwordx2 s[18:19], s[8:9], 0x90
	s_lshl_b32 s5, s36, 4
	s_ashr_i32 s4, s17, 9
	s_sub_i32 s5, s10, s5
	s_sext_i32_i16 s10, s5
	s_ashr_i32 s5, s4, 31
	s_lshl_b32 s24, s10, 5
	s_lshl_b64 s[36:37], s[4:5], 22
	s_waitcnt lgkmcnt(0)
	s_add_u32 s5, s18, s36
	s_addc_u32 s17, s19, s37
	s_lshl_b32 s10, s10, 6
	s_lshl_b32 s4, s4, 10
	s_and_b32 s10, s10, 0xffffff00
	s_add_i32 s10, s10, s4
	s_and_b32 s4, s24, 0x60
	s_ashr_i32 s25, s24, 31
	s_or_b32 s4, s10, s4
	s_lshl_b64 s[18:19], s[24:25], 2
	s_add_u32 s18, s5, s18
	v_or_b32_e32 v30, s16, v1
	s_addc_u32 s19, s17, s19
	v_ashrrev_i32_e32 v31, 31, v30
	v_lshl_add_u64 v[16:17], s[18:19], 0, v[4:5]
	v_lshlrev_b64 v[30:31], 11, v[30:31]
	v_lshl_add_u64 v[38:39], v[16:17], 0, v[30:31]
	v_or_b32_e32 v30, s16, v3
	v_ashrrev_i32_e32 v31, 31, v30
	v_lshlrev_b64 v[30:31], 11, v[30:31]
	v_lshl_add_u64 v[40:41], v[16:17], 0, v[30:31]
	global_load_dwordx4 v[30:33], v[38:39], off
	global_load_dwordx4 v[34:37], v[40:41], off
	v_or_b32_e32 v38, s16, v18
	v_ashrrev_i32_e32 v39, 31, v38
	v_lshlrev_b64 v[38:39], 11, v[38:39]
	v_lshl_add_u64 v[46:47], v[16:17], 0, v[38:39]
	v_or_b32_e32 v38, s16, v19
	v_ashrrev_i32_e32 v39, 31, v38
	v_lshlrev_b64 v[38:39], 11, v[38:39]
	v_lshl_add_u64 v[48:49], v[16:17], 0, v[38:39]
	global_load_dwordx4 v[38:41], v[46:47], off
	global_load_dwordx4 v[42:45], v[48:49], off
	v_or_b32_e32 v46, s16, v20
	v_ashrrev_i32_e32 v47, 31, v46
	v_lshlrev_b64 v[46:47], 11, v[46:47]
	v_lshl_add_u64 v[54:55], v[16:17], 0, v[46:47]
	v_or_b32_e32 v46, s16, v21
	v_ashrrev_i32_e32 v47, 31, v46
	v_lshlrev_b64 v[46:47], 11, v[46:47]
	v_lshl_add_u64 v[56:57], v[16:17], 0, v[46:47]
	global_load_dwordx4 v[46:49], v[54:55], off
	global_load_dwordx4 v[50:53], v[56:57], off
	v_or_b32_e32 v54, s16, v22
	v_ashrrev_i32_e32 v55, 31, v54
	v_lshlrev_b64 v[54:55], 11, v[54:55]
	v_lshl_add_u64 v[62:63], v[16:17], 0, v[54:55]
	v_or_b32_e32 v54, s16, v23
	v_ashrrev_i32_e32 v55, 31, v54
	v_lshlrev_b64 v[54:55], 11, v[54:55]
	v_lshl_add_u64 v[16:17], v[16:17], 0, v[54:55]
	global_load_dwordx4 v[54:57], v[62:63], off
	global_load_dwordx4 v[58:61], v[16:17], off
	s_ashr_i32 s17, s16, 31
	s_lshl_b64 s[16:17], s[16:17], 1
	s_add_u32 s14, s14, s16
	v_mov_b32_e32 v7, v5
	s_addc_u32 s15, s15, s17
	v_lshl_add_u64 v[16:17], s[14:15], 0, v[6:7]
	v_lshl_add_u64 v[16:17], v[16:17], 0, s[12:13]
	s_waitcnt vmcnt(7)
	ds_write_b128 v25, v[30:33]
	s_waitcnt vmcnt(6)
	ds_write_b128 v25, v[34:37] offset:1152
	s_waitcnt vmcnt(5)
	ds_write_b128 v25, v[38:41] offset:2304
	s_waitcnt vmcnt(4)
	ds_write_b128 v25, v[42:45] offset:3456
	s_waitcnt vmcnt(3)
	ds_write_b128 v25, v[46:49] offset:4608
	s_waitcnt vmcnt(2)
	ds_write_b128 v25, v[50:53] offset:5760
	s_waitcnt vmcnt(1)
	ds_write_b128 v25, v[54:57] offset:6912
	s_waitcnt vmcnt(0)
	ds_write_b128 v25, v[58:61] offset:8064
	s_waitcnt lgkmcnt(0)
	ds_read2_b32 v[34:35], v24 offset0:36 offset1:44
	ds_read2_b32 v[36:37], v24 offset0:72 offset1:80
	ds_read2_b32 v[38:39], v24 offset0:108 offset1:116
	ds_read2_b32 v[40:41], v24 offset1:8
	ds_read2_b32 v[42:43], v24 offset0:144 offset1:152
	ds_read2_b32 v[44:45], v24 offset0:180 offset1:188
	ds_read2_b32 v[46:47], v24 offset0:216 offset1:224
	ds_read2_b32 v[48:49], v26 offset0:124 offset1:132
	s_waitcnt lgkmcnt(7)
	v_mov_b32_e32 v32, v34
	s_waitcnt lgkmcnt(5)
	v_mov_b32_e32 v33, v38
	s_waitcnt lgkmcnt(3)
	v_mov_b32_e32 v50, v42
	s_waitcnt lgkmcnt(1)
	v_mov_b32_e32 v51, v46
	v_mov_b32_e32 v30, v40
	v_mov_b32_e32 v31, v36
	v_pk_mul_f32 v[32:33], v[8:9], v[32:33]
	v_pk_mul_f32 v[50:51], v[14:15], v[50:51]
	v_mov_b32_e32 v52, v44
	s_waitcnt lgkmcnt(0)
; #define GAS __attribute__((address_space(1)))
; #define LAS __attribute__((address_space(3)))
; #define LDS_WAIT() asm volatile("s_waitcnt lgkmcnt(0)" ::: "memory")
; __device__ __forceinline__ unsigned pk2(float lo, float hi) { return f2bf(lo) | (f2bf(hi) << 16); }
; __device__ __forceinline__ void p0_transpose_item(const float* W, int N, int k0, int n0, bf16* WT, int K, int dst_row0, LAS float* scr, int lane, const float* kscale = nullptr, int permhalf = -1) {
;     typedef float f32x4t __attribute__((ext_vector_type(4)));
;     const int c = lane & 7;
;     float ks[8];
; #pragma unroll
;     for (int i = 0; i < 8; ++i) ks[i] = kscale ? kscale[k0 + 8 * c + i] : 1.0f;
; #pragma unroll
;     for (int i = 0; i < 8; ++i) { const int kk = 8 * i + (lane >> 3), nn = (lane & 7) * 4;
;         *(LAS f32x4t*)(scr + kk * 36 + nn) = *(const GAS f32x4t*)(W + (size_t)(k0 + kk) * N + n0 + nn); }
;     LDS_WAIT(); asm volatile("" ::: "memory");
; #pragma unroll
;     for (int j = 0; j < 4; ++j) { const int n = (lane >> 3) + 8 * j; const LAS float* s = scr + (8 * c) * 36 + n;
;         v4u o; o.x = pk2(s[0 * 36] * ks[0], s[1 * 36] * ks[1]); o.y = pk2(s[2 * 36] * ks[2], s[3 * 36] * ks[3]); o.z = pk2(s[4 * 36] * ks[4], s[5 * 36] * ks[5]); o.w = pk2(s[6 * 36] * ks[6], s[7 * 36] * ks[7]);
;         const int drow = permhalf < 0 ? n : (32 * (n >> 4) + 8 * ((n >> 2) & 3) + 4 * permhalf + (n & 3));
;         *(GAS v4u*)(WT + (size_t)(dst_row0 + drow) * K + k0 + 8 * c) = o; }
;     LDS_WAIT(); asm volatile("" ::: "memory");
; }
	v_mov_b32_e32 v53, v48
	v_pk_mul_f32 v[30:31], v[10:11], v[30:31]
	v_bfe_u32 v34, v33, 16, 1
	v_bfe_u32 v36, v32, 16, 1
	v_bfe_u32 v38, v50, 16, 1
	v_pk_mul_f32 v[52:53], v[12:13], v[52:53]
	v_add3_u32 v36, v32, v36, s27
	v_add3_u32 v34, v33, v34, s27
	v_bfe_u32 v32, v30, 16, 1
	v_bfe_u32 v33, v31, 16, 1
	v_bfe_u32 v40, v51, 16, 1
	v_add3_u32 v38, v50, v38, s27
	v_or_b32_e32 v50, s4, v1
	v_bfe_u32 v7, v53, 16, 1
	v_bfe_u32 v29, v52, 16, 1
	v_add3_u32 v40, v51, v40, s27
	v_add3_u32 v31, v31, v33, s27
	v_add3_u32 v30, v30, v32, s27
	v_ashrrev_i32_e32 v51, 31, v50
	v_add3_u32 v29, v52, v29, s27
	v_add3_u32 v7, v53, v7, s27
	v_lshrrev_b32_e32 v30, 16, v30
	v_lshrrev_b32_e32 v31, 16, v31
	v_lshrrev_b32_e32 v32, 16, v38
	v_lshrrev_b32_e32 v33, 16, v40
	v_lshlrev_b64 v[50:51], 12, v[50:51]
	v_and_or_b32 v33, v7, s29, v33
	v_and_or_b32 v32, v29, s29, v32
	v_and_or_b32 v31, v34, s29, v31
	v_and_or_b32 v30, v36, s29, v30
	v_lshl_add_u64 v[50:51], v[16:17], 0, v[50:51]
	v_mov_b32_e32 v36, v41
	v_mov_b32_e32 v48, v45
	global_store_dwordx4 v[50:51], v[30:33], off sc1
	v_mov_b32_e32 v38, v35
	v_mov_b32_e32 v46, v43
	v_pk_mul_f32 v[30:31], v[10:11], v[36:37]
	v_pk_mul_f32 v[36:37], v[12:13], v[48:49]
	v_pk_mul_f32 v[32:33], v[8:9], v[38:39]
	v_pk_mul_f32 v[34:35], v[14:15], v[46:47]
	v_bfe_u32 v29, v36, 16, 1
	v_bfe_u32 v7, v37, 16, 1
	v_bfe_u32 v39, v32, 16, 1
	v_add3_u32 v29, v36, v29, s27
	v_bfe_u32 v36, v34, 16, 1
	v_bfe_u32 v38, v33, 16, 1
	v_add3_u32 v39, v32, v39, s27
	v_add3_u32 v7, v37, v7, s27
	v_bfe_u32 v32, v30, 16, 1
	v_bfe_u32 v37, v35, 16, 1
	v_add3_u32 v34, v34, v36, s27
	v_add3_u32 v38, v33, v38, s27
	v_bfe_u32 v33, v31, 16, 1
	v_add3_u32 v35, v35, v37, s27
	v_add3_u32 v30, v30, v32, s27
	v_lshrrev_b32_e32 v32, 16, v34
	v_or_b32_e32 v34, s4, v3
	v_add3_u32 v31, v31, v33, s27
	v_lshrrev_b32_e32 v33, 16, v35
	v_ashrrev_i32_e32 v35, 31, v34
	v_lshrrev_b32_e32 v30, 16, v30
	v_lshrrev_b32_e32 v31, 16, v31
	v_lshlrev_b64 v[34:35], 12, v[34:35]
	v_and_or_b32 v33, v7, s29, v33
	v_and_or_b32 v32, v29, s29, v32
	v_and_or_b32 v31, v38, s29, v31
	v_and_or_b32 v30, v39, s29, v30
	v_lshl_add_u64 v[34:35], v[16:17], 0, v[34:35]
	ds_read2_b32 v[36:37], v24 offset0:16 offset1:24
	ds_read2_b32 v[38:39], v24 offset0:88 offset1:96
	global_store_dwordx4 v[34:35], v[30:33], off sc1
	ds_read2_b32 v[34:35], v24 offset0:52 offset1:60
	ds_read2_b32 v[40:41], v24 offset0:124 offset1:132
	ds_read2_b32 v[42:43], v24 offset0:160 offset1:168
	ds_read2_b32 v[44:45], v24 offset0:232 offset1:240
	ds_read2_b32 v[46:47], v24 offset0:196 offset1:204
	ds_read2_b32 v[48:49], v27 offset0:12 offset1:20
	s_waitcnt lgkmcnt(7)
	v_mov_b32_e32 v30, v36
	s_waitcnt lgkmcnt(5)
	v_mov_b32_e32 v32, v34
	s_waitcnt lgkmcnt(4)
	v_mov_b32_e32 v33, v40
	s_waitcnt lgkmcnt(3)
	v_mov_b32_e32 v50, v42
	s_waitcnt lgkmcnt(2)
	v_mov_b32_e32 v51, v44
	v_mov_b32_e32 v31, v38
	v_pk_mul_f32 v[32:33], v[8:9], v[32:33]
	v_pk_mul_f32 v[50:51], v[14:15], v[50:51]
	v_pk_mul_f32 v[30:31], v[10:11], v[30:31]
	s_waitcnt lgkmcnt(1)
	v_mov_b32_e32 v52, v46
	s_waitcnt lgkmcnt(0)
	v_mov_b32_e32 v53, v48
	v_bfe_u32 v34, v33, 16, 1
	v_bfe_u32 v36, v32, 16, 1
	v_bfe_u32 v38, v50, 16, 1
	v_pk_mul_f32 v[52:53], v[12:13], v[52:53]
	v_add3_u32 v36, v32, v36, s27
	v_add3_u32 v34, v33, v34, s27
	v_bfe_u32 v32, v30, 16, 1
	v_bfe_u32 v33, v31, 16, 1
	v_bfe_u32 v40, v51, 16, 1
	v_add3_u32 v38, v50, v38, s27
	v_or_b32_e32 v50, s4, v18
	v_bfe_u32 v7, v53, 16, 1
	v_bfe_u32 v29, v52, 16, 1
	v_add3_u32 v40, v51, v40, s27
	v_add3_u32 v31, v31, v33, s27
	v_add3_u32 v30, v30, v32, s27
	v_ashrrev_i32_e32 v51, 31, v50
	v_add3_u32 v29, v52, v29, s27
	v_add3_u32 v7, v53, v7, s27
	v_lshrrev_b32_e32 v30, 16, v30
	v_lshrrev_b32_e32 v31, 16, v31
	v_lshrrev_b32_e32 v32, 16, v38
	v_lshrrev_b32_e32 v33, 16, v40
	v_lshlrev_b64 v[50:51], 12, v[50:51]
	v_mov_b32_e32 v40, v35
	v_mov_b32_e32 v48, v47
	v_and_or_b32 v33, v7, s29, v33
	v_and_or_b32 v32, v29, s29, v32
	v_and_or_b32 v31, v34, s29, v31
	v_and_or_b32 v30, v36, s29, v30
	v_lshl_add_u64 v[50:51], v[16:17], 0, v[50:51]
	v_mov_b32_e32 v38, v37
	v_pk_mul_f32 v[8:9], v[8:9], v[40:41]
	v_mov_b32_e32 v44, v43
	v_pk_mul_f32 v[12:13], v[12:13], v[48:49]
	global_store_dwordx4 v[50:51], v[30:33], off sc1
	v_pk_mul_f32 v[10:11], v[10:11], v[38:39]
	v_pk_mul_f32 v[14:15], v[14:15], v[44:45]
	v_bfe_u32 v7, v13, 16, 1
	v_bfe_u32 v30, v9, 16, 1
	v_add3_u32 v9, v9, v30, s27
	v_add3_u32 v7, v13, v7, s27
	v_bfe_u32 v13, v10, 16, 1
	v_bfe_u32 v30, v14, 16, 1
	v_bfe_u32 v29, v12, 16, 1
	v_add3_u32 v14, v14, v30, s27
	v_add3_u32 v10, v10, v13, s27
	v_bfe_u32 v31, v8, 16, 1
	v_add3_u32 v12, v12, v29, s27
	v_lshrrev_b32_e32 v13, 16, v10
	v_lshrrev_b32_e32 v10, 16, v14
	v_add3_u32 v8, v8, v31, s27
	v_bfe_u32 v29, v11, 16, 1
	v_bfe_u32 v31, v15, 16, 1
	v_and_or_b32 v10, v12, s29, v10
	v_or_b32_e32 v12, s4, v19
	v_add3_u32 v15, v15, v31, s27
	v_add3_u32 v11, v11, v29, s27
	v_and_or_b32 v8, v8, s29, v13
	v_ashrrev_i32_e32 v13, 31, v12
	v_lshrrev_b32_e32 v29, 16, v11
	v_lshrrev_b32_e32 v11, 16, v15
	v_lshlrev_b64 v[12:13], 12, v[12:13]
	v_and_or_b32 v11, v7, s29, v11
	v_and_or_b32 v9, v9, s29, v29
	v_lshl_add_u64 v[12:13], v[16:17], 0, v[12:13]
	global_store_dwordx4 v[12:13], v[8:11], off sc1
	s_waitcnt lgkmcnt(0)

; #define GAS __attribute__((address_space(1)))
; #define LAS __attribute__((address_space(3)))
; #define LDS_WAIT() asm volatile("s_waitcnt lgkmcnt(0)" ::: "memory")
; __device__ __forceinline__ unsigned pk2(float lo, float hi) { return f2bf(lo) | (f2bf(hi) << 16); }
; __device__ __forceinline__ void p0_transpose_item(const float* W, int N, int k0, int n0, bf16* WT, int K, int dst_row0, LAS float* scr, int lane, const float* kscale = nullptr, int permhalf = -1) {
;     typedef float f32x4t __attribute__((ext_vector_type(4)));
;     const int c = lane & 7;
;     float ks[8];
; #pragma unroll
;     for (int i = 0; i < 8; ++i) ks[i] = kscale ? kscale[k0 + 8 * c + i] : 1.0f;
; #pragma unroll
;     for (int i = 0; i < 8; ++i) { const int kk = 8 * i + (lane >> 3), nn = (lane & 7) * 4;
;         *(LAS f32x4t*)(scr + kk * 36 + nn) = *(const GAS f32x4t*)(W + (size_t)(k0 + kk) * N + n0 + nn); }
;     LDS_WAIT(); asm volatile("" ::: "memory");
; #pragma unroll
;     for (int j = 0; j < 4; ++j) { const int n = (lane >> 3) + 8 * j; const LAS float* s = scr + (8 * c) * 36 + n;
;         v4u o; o.x = pk2(s[0 * 36] * ks[0], s[1 * 36] * ks[1]); o.y = pk2(s[2 * 36] * ks[2], s[3 * 36] * ks[3]); o.z = pk2(s[4 * 36] * ks[4], s[5 * 36] * ks[5]); o.w = pk2(s[6 * 36] * ks[6], s[7 * 36] * ks[7]);
;         const int drow = permhalf < 0 ? n : (32 * (n >> 4) + 8 * ((n >> 2) & 3) + 4 * permhalf + (n & 3));
;         *(GAS v4u*)(WT + (size_t)(dst_row0 + drow) * K + k0 + 8 * c) = o; }
;     LDS_WAIT(); asm volatile("" ::: "memory");
; }
; __device__ __forceinline__ void conv_item(KArgs a, int r, LAS float* scr, int lane) {
;     ...
;     if (r < CONV_IE) { const int e = r / 512, q = r % 512, kb = q / 16, nb = q % 16, n0 = 32 * nb;
;         p0_transpose_item(a->in[19] + (size_t)e * 2048 * 512, 512, 64 * kb, n0, (bf16*)(ws + WS_W13), 2048, e * 1024 + (n0 >> 7) * 256 + 128 + (n0 & 127), scr, lane, a->in[15]); return; } r -= CONV_IE;
.LBB0_700:
	s_load_dwordx2 s[4:5], s[8:9], 0x98
	s_add_i32 s10, s31, 0xffffc000
	s_lshr_b32 s10, s10, 9
	s_lshl_b32 s18, s31, 5
	s_lshl_b64 s[16:17], s[10:11], 22
	s_waitcnt lgkmcnt(0)
	s_add_u32 s16, s4, s16
	s_addc_u32 s5, s5, s17
	s_lshl_b32 s4, s10, 10
	s_lshl_b32 s10, s31, 6
	s_and_b32 s10, s10, 0x300
	s_or_b32 s4, s4, s10
	s_and_b32 s10, s18, 0x60
	s_or_b32 s4, s4, s10
	s_lshl_b32 s10, s31, 7
	s_bitset1_b32 s4, 7
	s_and_b32 s10, s10, 0x780
	s_add_u32 s16, s16, s10
	s_addc_u32 s17, s5, 0
	v_or_b32_e32 v7, s24, v1
	v_lshl_add_u64 v[16:17], s[16:17], 0, v[4:5]
	v_lshlrev_b32_e32 v30, 11, v7
	v_mov_b32_e32 v31, v5
	v_or_b32_e32 v7, s24, v3
	v_lshl_add_u64 v[38:39], v[16:17], 0, v[30:31]
	v_lshlrev_b32_e32 v30, 11, v7
	v_or_b32_e32 v7, s24, v18
	v_lshl_add_u64 v[40:41], v[16:17], 0, v[30:31]
	global_load_dwordx4 v[30:33], v[38:39], off
	global_load_dwordx4 v[34:37], v[40:41], off
	v_lshlrev_b32_e32 v38, 11, v7
	v_mov_b32_e32 v39, v5
	v_or_b32_e32 v7, s24, v19
	v_lshl_add_u64 v[46:47], v[16:17], 0, v[38:39]
	v_lshlrev_b32_e32 v38, 11, v7
	v_or_b32_e32 v7, s24, v20
	v_lshl_add_u64 v[48:49], v[16:17], 0, v[38:39]
	global_load_dwordx4 v[38:41], v[46:47], off
	global_load_dwordx4 v[42:45], v[48:49], off
	v_lshlrev_b32_e32 v46, 11, v7
	v_mov_b32_e32 v47, v5
	v_or_b32_e32 v7, s24, v21
	v_lshl_add_u64 v[54:55], v[16:17], 0, v[46:47]
	v_lshlrev_b32_e32 v46, 11, v7
	v_or_b32_e32 v7, s24, v22
	v_lshl_add_u64 v[56:57], v[16:17], 0, v[46:47]
	global_load_dwordx4 v[46:49], v[54:55], off
	global_load_dwordx4 v[50:53], v[56:57], off
	v_lshlrev_b32_e32 v54, 11, v7
	v_mov_b32_e32 v55, v5
	v_or_b32_e32 v7, s24, v23
	v_lshl_add_u64 v[62:63], v[16:17], 0, v[54:55]
	v_lshlrev_b32_e32 v54, 11, v7
	v_lshl_add_u64 v[16:17], v[16:17], 0, v[54:55]
	global_load_dwordx4 v[54:57], v[62:63], off
	global_load_dwordx4 v[58:61], v[16:17], off
	s_lshl_b32 s5, s24, 1
	s_add_u32 s16, s14, s5
	v_mov_b32_e32 v7, v5
	s_addc_u32 s17, s15, 0
	v_lshl_add_u64 v[16:17], s[16:17], 0, v[6:7]
	v_lshl_add_u64 v[16:17], v[16:17], 0, s[12:13]
	s_waitcnt vmcnt(7)
	ds_write_b128 v25, v[30:33]
	s_waitcnt vmcnt(6)
	ds_write_b128 v25, v[34:37] offset:1152
	s_waitcnt vmcnt(5)
	ds_write_b128 v25, v[38:41] offset:2304
	s_waitcnt vmcnt(4)
	ds_write_b128 v25, v[42:45] offset:3456
	s_waitcnt vmcnt(3)
	ds_write_b128 v25, v[46:49] offset:4608
	s_waitcnt vmcnt(2)
	ds_write_b128 v25, v[50:53] offset:5760
	s_waitcnt vmcnt(1)
	ds_write_b128 v25, v[54:57] offset:6912
	s_waitcnt vmcnt(0)
	ds_write_b128 v25, v[58:61] offset:8064
	s_waitcnt lgkmcnt(0)
	ds_read2_b32 v[34:35], v24 offset0:36 offset1:44
	ds_read2_b32 v[36:37], v24 offset0:72 offset1:80
	ds_read2_b32 v[38:39], v24 offset0:108 offset1:116
	ds_read2_b32 v[40:41], v24 offset1:8
	ds_read2_b32 v[42:43], v24 offset0:144 offset1:152
	ds_read2_b32 v[44:45], v24 offset0:180 offset1:188
	ds_read2_b32 v[46:47], v24 offset0:216 offset1:224
	ds_read2_b32 v[48:49], v26 offset0:124 offset1:132
	s_waitcnt lgkmcnt(4)
	v_mov_b32_e32 v30, v40
	v_mov_b32_e32 v31, v36
	v_mov_b32_e32 v32, v34
	v_mov_b32_e32 v33, v38
	s_waitcnt lgkmcnt(3)
	v_mov_b32_e32 v50, v42
	s_waitcnt lgkmcnt(1)
	v_mov_b32_e32 v51, v46
	v_mov_b32_e32 v52, v44
	s_waitcnt lgkmcnt(0)
; #define GAS __attribute__((address_space(1)))
; #define LAS __attribute__((address_space(3)))
; #define LDS_WAIT() asm volatile("s_waitcnt lgkmcnt(0)" ::: "memory")
; __device__ __forceinline__ unsigned pk2(float lo, float hi) { return f2bf(lo) | (f2bf(hi) << 16); }
; __device__ __forceinline__ void p0_transpose_item(const float* W, int N, int k0, int n0, bf16* WT, int K, int dst_row0, LAS float* scr, int lane, const float* kscale = nullptr, int permhalf = -1) {
;     typedef float f32x4t __attribute__((ext_vector_type(4)));
;     const int c = lane & 7;
;     float ks[8];
; #pragma unroll
;     for (int i = 0; i < 8; ++i) ks[i] = kscale ? kscale[k0 + 8 * c + i] : 1.0f;
; #pragma unroll
;     for (int i = 0; i < 8; ++i) { const int kk = 8 * i + (lane >> 3), nn = (lane & 7) * 4;
;         *(LAS f32x4t*)(scr + kk * 36 + nn) = *(const GAS f32x4t*)(W + (size_t)(k0 + kk) * N + n0 + nn); }
;     LDS_WAIT(); asm volatile("" ::: "memory");
; #pragma unroll
;     for (int j = 0; j < 4; ++j) { const int n = (lane >> 3) + 8 * j; const LAS float* s = scr + (8 * c) * 36 + n;
;         v4u o; o.x = pk2(s[0 * 36] * ks[0], s[1 * 36] * ks[1]); o.y = pk2(s[2 * 36] * ks[2], s[3 * 36] * ks[3]); o.z = pk2(s[4 * 36] * ks[4], s[5 * 36] * ks[5]); o.w = pk2(s[6 * 36] * ks[6], s[7 * 36] * ks[7]);
;         const int drow = permhalf < 0 ? n : (32 * (n >> 4) + 8 * ((n >> 2) & 3) + 4 * permhalf + (n & 3));
;         *(GAS v4u*)(WT + (size_t)(dst_row0 + drow) * K + k0 + 8 * c) = o; }
;     LDS_WAIT(); asm volatile("" ::: "memory");
; }
	v_mov_b32_e32 v53, v48
	v_pk_mul_f32 v[30:31], v[10:11], v[30:31]
	v_pk_mul_f32 v[32:33], v[8:9], v[32:33]
	v_pk_mul_f32 v[50:51], v[14:15], v[50:51]
	v_pk_mul_f32 v[52:53], v[12:13], v[52:53]
	v_bfe_u32 v34, v33, 16, 1
	v_bfe_u32 v36, v32, 16, 1
	v_bfe_u32 v38, v30, 16, 1
	v_bfe_u32 v40, v31, 16, 1
	v_bfe_u32 v42, v50, 16, 1
	v_bfe_u32 v44, v51, 16, 1
	v_bfe_u32 v7, v53, 16, 1
	v_bfe_u32 v29, v52, 16, 1
	v_add3_u32 v36, v32, v36, s27
	v_add3_u32 v34, v33, v34, s27
	v_add3_u32 v32, v51, v44, s27
	v_add3_u32 v33, v50, v42, s27
	v_add3_u32 v31, v31, v40, s27
	v_add3_u32 v30, v30, v38, s27
	v_or_b32_e32 v50, s4, v1
	v_mov_b32_e32 v51, v5
	v_add3_u32 v29, v52, v29, s27
	v_add3_u32 v7, v53, v7, s27
	v_lshrrev_b32_e32 v30, 16, v30
	v_lshrrev_b32_e32 v31, 16, v31
	v_lshrrev_b32_e32 v38, 16, v33
	v_lshrrev_b32_e32 v32, 16, v32
	v_lshlrev_b64 v[50:51], 12, v[50:51]
	v_and_or_b32 v33, v7, s29, v32
	v_and_or_b32 v32, v29, s29, v38
	v_and_or_b32 v31, v34, s29, v31
	v_and_or_b32 v30, v36, s29, v30
	v_lshl_add_u64 v[50:51], v[16:17], 0, v[50:51]
	v_mov_b32_e32 v36, v41
	v_mov_b32_e32 v48, v45
	global_store_dwordx4 v[50:51], v[30:33], off sc1
	v_mov_b32_e32 v38, v35
	v_mov_b32_e32 v46, v43
	v_pk_mul_f32 v[30:31], v[10:11], v[36:37]
	v_pk_mul_f32 v[36:37], v[12:13], v[48:49]
	v_pk_mul_f32 v[32:33], v[8:9], v[38:39]
	v_pk_mul_f32 v[34:35], v[14:15], v[46:47]
	v_bfe_u32 v7, v37, 16, 1
	v_bfe_u32 v29, v36, 16, 1
	v_bfe_u32 v38, v33, 16, 1
	v_bfe_u32 v39, v32, 16, 1
	v_add3_u32 v29, v36, v29, s27
	v_add3_u32 v7, v37, v7, s27
	v_bfe_u32 v36, v34, 16, 1
	v_bfe_u32 v37, v35, 16, 1
	v_add3_u32 v39, v32, v39, s27
	v_add3_u32 v38, v33, v38, s27
	v_bfe_u32 v32, v30, 16, 1
	v_bfe_u32 v33, v31, 16, 1
	v_add3_u32 v35, v35, v37, s27
	v_add3_u32 v34, v34, v36, s27
	v_add3_u32 v31, v31, v33, s27
	v_add3_u32 v30, v30, v32, s27
	v_lshrrev_b32_e32 v32, 16, v34
	v_lshrrev_b32_e32 v33, 16, v35
	v_or_b32_e32 v34, s4, v3
	v_mov_b32_e32 v35, v5
	v_lshrrev_b32_e32 v30, 16, v30
	v_lshrrev_b32_e32 v31, 16, v31
	v_lshlrev_b64 v[34:35], 12, v[34:35]
	v_and_or_b32 v33, v7, s29, v33
	v_and_or_b32 v32, v29, s29, v32
	v_and_or_b32 v31, v38, s29, v31
	v_and_or_b32 v30, v39, s29, v30
	v_lshl_add_u64 v[34:35], v[16:17], 0, v[34:35]
	ds_read2_b32 v[36:37], v24 offset0:16 offset1:24
	ds_read2_b32 v[38:39], v24 offset0:88 offset1:96
	global_store_dwordx4 v[34:35], v[30:33], off sc1
	ds_read2_b32 v[34:35], v24 offset0:52 offset1:60
	ds_read2_b32 v[40:41], v24 offset0:124 offset1:132
	ds_read2_b32 v[42:43], v24 offset0:160 offset1:168
	ds_read2_b32 v[44:45], v24 offset0:232 offset1:240
	ds_read2_b32 v[46:47], v24 offset0:196 offset1:204
	ds_read2_b32 v[48:49], v27 offset0:12 offset1:20
	s_waitcnt lgkmcnt(7)
	v_mov_b32_e32 v30, v36
	s_waitcnt lgkmcnt(5)
	v_mov_b32_e32 v32, v34
	s_waitcnt lgkmcnt(4)
	v_mov_b32_e32 v33, v40
	v_mov_b32_e32 v31, v38
	v_pk_mul_f32 v[32:33], v[8:9], v[32:33]
	s_waitcnt lgkmcnt(3)
	v_mov_b32_e32 v50, v42
	s_waitcnt lgkmcnt(2)
	v_mov_b32_e32 v51, v44
	v_pk_mul_f32 v[30:31], v[10:11], v[30:31]
	v_pk_mul_f32 v[50:51], v[14:15], v[50:51]
	s_waitcnt lgkmcnt(1)
	v_mov_b32_e32 v52, v46
	s_waitcnt lgkmcnt(0)
	v_mov_b32_e32 v53, v48
	v_bfe_u32 v34, v33, 16, 1
	v_bfe_u32 v36, v32, 16, 1
	v_pk_mul_f32 v[52:53], v[12:13], v[52:53]
	v_add3_u32 v36, v32, v36, s27
	v_add3_u32 v34, v33, v34, s27
	v_bfe_u32 v32, v30, 16, 1
	v_bfe_u32 v33, v31, 16, 1
	v_bfe_u32 v38, v50, 16, 1
	v_bfe_u32 v40, v51, 16, 1
	v_bfe_u32 v7, v53, 16, 1
	v_bfe_u32 v29, v52, 16, 1
	v_add3_u32 v40, v51, v40, s27
	v_add3_u32 v38, v50, v38, s27
	v_add3_u32 v31, v31, v33, s27
	v_add3_u32 v30, v30, v32, s27
	v_or_b32_e32 v50, s4, v18
	v_mov_b32_e32 v51, v5
	v_add3_u32 v29, v52, v29, s27
	v_add3_u32 v7, v53, v7, s27
	v_lshrrev_b32_e32 v30, 16, v30
	v_lshrrev_b32_e32 v31, 16, v31
	v_lshrrev_b32_e32 v32, 16, v38
	v_lshrrev_b32_e32 v33, 16, v40
	v_lshlrev_b64 v[50:51], 12, v[50:51]
	v_mov_b32_e32 v40, v35
	v_mov_b32_e32 v48, v47
	v_and_or_b32 v33, v7, s29, v33
	v_and_or_b32 v32, v29, s29, v32
	v_and_or_b32 v31, v34, s29, v31
	v_and_or_b32 v30, v36, s29, v30
	v_lshl_add_u64 v[50:51], v[16:17], 0, v[50:51]
	v_mov_b32_e32 v38, v37
	v_pk_mul_f32 v[8:9], v[8:9], v[40:41]
	v_mov_b32_e32 v44, v43
	v_pk_mul_f32 v[12:13], v[12:13], v[48:49]
	global_store_dwordx4 v[50:51], v[30:33], off sc1
	v_pk_mul_f32 v[10:11], v[10:11], v[38:39]
	v_pk_mul_f32 v[14:15], v[14:15], v[44:45]
	v_bfe_u32 v7, v13, 16, 1
	v_bfe_u32 v30, v9, 16, 1
	v_add3_u32 v9, v9, v30, s27
	v_add3_u32 v7, v13, v7, s27
	v_bfe_u32 v13, v10, 16, 1
	v_bfe_u32 v30, v14, 16, 1
	v_bfe_u32 v29, v12, 16, 1
	v_bfe_u32 v31, v8, 16, 1
	v_add3_u32 v14, v14, v30, s27
	v_add3_u32 v10, v10, v13, s27
	v_add3_u32 v8, v8, v31, s27
	v_add3_u32 v12, v12, v29, s27
	v_bfe_u32 v29, v11, 16, 1
	v_bfe_u32 v31, v15, 16, 1
	v_lshrrev_b32_e32 v13, 16, v10
	v_lshrrev_b32_e32 v10, 16, v14
	v_add3_u32 v15, v15, v31, s27
	v_add3_u32 v11, v11, v29, s27
	v_and_or_b32 v10, v12, s29, v10
	v_and_or_b32 v8, v8, s29, v13
	v_or_b32_e32 v12, s4, v19
	v_mov_b32_e32 v13, v5
	v_lshrrev_b32_e32 v29, 16, v11
	v_lshrrev_b32_e32 v11, 16, v15
	v_lshlrev_b64 v[12:13], 12, v[12:13]
	v_and_or_b32 v11, v7, s29, v11
	v_and_or_b32 v9, v9, s29, v29
	v_lshl_add_u64 v[12:13], v[16:17], 0, v[12:13]
	global_store_dwordx4 v[12:13], v[8:11], off sc1
	s_waitcnt lgkmcnt(0)
	s_mov_b64 s[4:5], 0

; __device__ __forceinline__ float sigmoid_f(float x) { return __builtin_amdgcn_rcpf(1.0f + __builtin_amdgcn_exp2f(-1.4426950408889634f * x)); }
;     __device__ __forceinline__ void operator()(const f32x4 (&acc)[2][2][4][2], const Unit& u, int wr, int wc, int fr, int fq) const {
;         const int row0 = u.pm * BM + wr * 64 + fr, col0 = u.pn * HALF + wc * 32 + 8 * fq;
;         const int slot0 = (u.pm - tab[32 + u.ex]) * BM + wr * 64 + fr, cnt = tab[u.ex];
;         float rs[2][4], wt[2][4];
; #pragma unroll
;         for (int ai = 0; ai < 2; ++ai)
; #pragma unroll
;             for (int m = 0; m < 4; ++m) { const int slot = slot0 + ai * HALF + m * 16; const bool ok = slot < cnt; const size_t ix = (size_t)u.ex * 32768 + (ok ? slot : 0);
;                 const float lr_ = LR[ix], lw_ = LW[ix];
;                 rs[ai][m] = ok ? lr_ : 0.f; wt[ai][m] = ok ? lw_ : 0.f; }
; #pragma unroll
;         for (int ai = 0; ai < 2; ++ai)
; #pragma unroll
;             for (int m = 0; m < 4; ++m) { f32x4 v0, v1; const float r_ = rs[ai][m], rw = r_ * wt[ai][m];
; #pragma unroll
;                 for (int e = 0; e < 4; ++e) { const float g0 = acc[ai][0][m][0][e] * r_, g1 = acc[ai][0][m][1][e] * r_;
;                     v0[e] = g0 * sigmoid_f(g0) * (acc[ai][1][m][0][e] * rw); v1[e] = g1 * sigmoid_f(g1) * (acc[ai][1][m][1][e] * rw); }
.LBB0_795:
	s_lshl_b32 s6, s14, 2
	s_add_i32 s6, s6, 0
	s_add_i32 s6, s6, 0x23800
	v_mov_b32_e32 v134, s6
	ds_read2_b32 v[138:139], v134 offset1:32
	s_ashr_i32 s15, s14, 31
	s_lshl_b64 s[68:69], s[14:15], 15
	s_waitcnt lgkmcnt(0)
	v_sub_u32_e32 v134, s25, v139
	v_lshl_add_u32 v134, v134, 8, v137
	v_or_b32_e32 v136, 16, v134
	v_cmp_lt_i32_e64 s[6:7], v136, v138
	v_cmp_lt_i32_e32 vcc, v134, v138
	v_add_u32_e32 v139, 0x80, v134
	v_cndmask_b32_e64 v144, 0, v136, s[6:7]
	v_or_b32_e32 v136, 32, v134
	v_cmp_lt_i32_e64 s[8:9], v136, v138
	v_cndmask_b32_e32 v140, 0, v134, vcc
	v_ashrrev_i32_e32 v141, 31, v140
	v_cndmask_b32_e64 v164, 0, v136, s[8:9]
	v_or_b32_e32 v136, 48, v134
	v_cmp_lt_i32_e64 s[10:11], v136, v138
	v_lshl_add_u64 v[140:141], s[68:69], 0, v[140:141]
	v_ashrrev_i32_e32 v145, 31, v144
	v_cndmask_b32_e64 v168, 0, v136, s[10:11]
	v_ashrrev_i32_e32 v169, 31, v168
	v_ashrrev_i32_e32 v165, 31, v164
	v_lshl_add_u64 v[168:169], s[68:69], 0, v[168:169]
	v_lshlrev_b64 v[140:141], 2, v[140:141]
	v_lshl_add_u64 v[144:145], s[68:69], 0, v[144:145]
	v_lshl_add_u64 v[164:165], s[68:69], 0, v[164:165]
	v_lshlrev_b64 v[168:169], 2, v[168:169]
	v_lshl_add_u64 v[142:143], s[48:49], 0, v[140:141]
	v_lshl_add_u64 v[140:141], s[50:51], 0, v[140:141]
	v_lshlrev_b64 v[144:145], 2, v[144:145]
	v_lshlrev_b64 v[164:165], 2, v[164:165]
	v_lshl_add_u64 v[170:171], s[48:49], 0, v[168:169]
	v_cmp_lt_i32_e64 s[12:13], v139, v138
	v_lshl_add_u64 v[162:163], s[48:49], 0, v[144:145]
	v_lshl_add_u64 v[144:145], s[50:51], 0, v[144:145]
	v_lshl_add_u64 v[166:167], s[48:49], 0, v[164:165]
	v_lshl_add_u64 v[164:165], s[50:51], 0, v[164:165]
	v_lshl_add_u64 v[168:169], s[50:51], 0, v[168:169]
	global_load_dword v136, v[142:143], off
	global_load_dword v146, v[140:141], off
	global_load_dword v161, v[162:163], off
	global_load_dword v172, v[144:145], off
	global_load_dword v173, v[166:167], off
	global_load_dword v174, v[164:165], off
	s_nop 0
	global_load_dword v170, v[170:171], off
	s_nop 0
	global_load_dword v171, v[168:169], off
	v_cndmask_b32_e64 v140, 0, v139, s[12:13]
	v_add_u32_e32 v139, 0x90, v134
	v_cmp_lt_i32_e64 s[14:15], v139, v138
	v_ashrrev_i32_e32 v141, 31, v140
	v_lshl_add_u64 v[140:141], s[68:69], 0, v[140:141]
	v_cndmask_b32_e64 v144, 0, v139, s[14:15]
	v_add_u32_e32 v139, 0xa0, v134
	v_add_u32_e32 v134, 0xb0, v134
	v_cmp_lt_i32_e64 s[16:17], v139, v138
	v_cmp_lt_i32_e64 s[18:19], v134, v138
	v_ashrrev_i32_e32 v145, 31, v144
	v_cndmask_b32_e64 v164, 0, v139, s[16:17]
	v_cndmask_b32_e64 v138, 0, v134, s[18:19]
	v_ashrrev_i32_e32 v165, 31, v164
	v_ashrrev_i32_e32 v139, 31, v138
	v_lshl_add_u64 v[144:145], s[68:69], 0, v[144:145]
	v_lshl_add_u64 v[164:165], s[68:69], 0, v[164:165]
	v_lshl_add_u64 v[138:139], s[68:69], 0, v[138:139]
	v_lshlrev_b64 v[140:141], 2, v[140:141]
	v_lshlrev_b64 v[144:145], 2, v[144:145]
	v_lshlrev_b64 v[164:165], 2, v[164:165]
	v_lshlrev_b64 v[138:139], 2, v[138:139]
	v_lshl_add_u64 v[142:143], s[48:49], 0, v[140:141]
	v_lshl_add_u64 v[140:141], s[50:51], 0, v[140:141]
	v_lshl_add_u64 v[162:163], s[48:49], 0, v[144:145]
	v_lshl_add_u64 v[166:167], s[48:49], 0, v[164:165]
	v_lshl_add_u64 v[164:165], s[50:51], 0, v[164:165]
	v_lshl_add_u64 v[168:169], s[48:49], 0, v[138:139]
	v_lshl_add_u64 v[138:139], s[50:51], 0, v[138:139]
	v_lshl_add_u64 v[144:145], s[50:51], 0, v[144:145]
	global_load_dword v134, v[142:143], off
	s_nop 0
	global_load_dword v141, v[140:141], off
	s_nop 0
	global_load_dword v142, v[162:163], off
	global_load_dword v143, v[144:145], off
	s_nop 0
	global_load_dword v163, v[166:167], off
	s_nop 0
	global_load_dword v165, v[164:165], off
	s_nop 0
	global_load_dword v166, v[168:169], off
	s_nop 0
	global_load_dword v139, v[138:139], off
	s_waitcnt vmcnt(0)
	v_cndmask_b32_e32 v162, 0, v136, vcc
	v_cndmask_b32_e32 v168, 0, v146, vcc
	v_mul_f32_e32 v168, v162, v168
	v_cndmask_b32_e64 v164, 0, v161, s[6:7]
	v_cndmask_b32_e64 v161, 0, v172, s[6:7]
	v_cndmask_b32_e64 v169, 0, v174, s[8:9]
	v_cndmask_b32_e64 v144, 0, v170, s[10:11]
	v_cndmask_b32_e64 v174, 0, v171, s[10:11]
	v_pk_mul_f32 v[122:123], v[122:123], v[168:169] op_sel_hi:[1,0]
	v_cndmask_b32_e64 v146, 0, v173, s[8:9]
	v_pk_mul_f32 v[114:115], v[114:115], v[168:169] op_sel_hi:[1,0]
	v_pk_mul_f32 v[124:125], v[124:125], v[168:169] op_sel_hi:[1,0]
	v_pk_mul_f32 v[116:117], v[116:117], v[168:169] op_sel_hi:[1,0]
	v_pk_mul_f32 v[94:95], v[94:95], v[146:147] op_sel_hi:[1,0]
	v_pk_mul_f32 v[86:87], v[86:87], v[146:147] op_sel_hi:[1,0]
	v_pk_mul_f32 v[88:89], v[88:89], v[146:147] op_sel_hi:[1,0]
	v_cndmask_b32_e64 v140, 0, v134, s[12:13]
	v_cndmask_b32_e64 v175, 0, v141, s[12:13]
	v_cndmask_b32_e64 v138, 0, v142, s[14:15]
	v_cndmask_b32_e64 v145, 0, v143, s[14:15]
	v_pk_mul_f32 v[126:127], v[126:127], v[162:163] op_sel_hi:[1,0]
	v_cndmask_b32_e64 v136, 0, v163, s[16:17]
	v_mul_f32_e32 v143, 0xbfb8aa3b, v126
	v_mul_f32_e32 v163, 0xbfb8aa3b, v127
	v_exp_f32_e32 v143, v143
	v_exp_f32_e32 v163, v163
	v_cndmask_b32_e64 v141, 0, v165, s[16:17]
	v_lshl_add_u32 v142, s25, 8, v137
	v_add_f32_e32 v143, 1.0, v143
	v_pk_mul_f32 v[118:119], v[118:119], v[162:163] op_sel_hi:[1,0]
	v_rcp_f32_e32 v170, v143
	v_add_f32_e32 v143, 1.0, v163
	v_mul_f32_e32 v163, 0xbfb8aa3b, v118
	v_exp_f32_e32 v163, v163
	v_mul_f32_e32 v165, 0xbfb8aa3b, v119
	v_rcp_f32_e32 v171, v143
	v_exp_f32_e32 v165, v165
	v_add_f32_e32 v143, 1.0, v163
	v_rcp_f32_e32 v172, v143
	v_pk_mul_f32 v[126:127], v[126:127], v[170:171]
	v_add_f32_e32 v143, 1.0, v165
	v_pk_mul_f32 v[122:123], v[122:123], v[126:127]
	v_pk_mul_f32 v[126:127], v[128:129], v[162:163] op_sel_hi:[1,0]
	v_rcp_f32_e32 v173, v143
	v_mul_f32_e32 v128, 0xbfb8aa3b, v126
; __device__ __forceinline__ unsigned cvt_pk_bf16(float lo, float hi) { f32x2v_ v = {lo, hi}; bf16x2v_ b = __builtin_convertvector(v, bf16x2v_); return __builtin_bit_cast(unsigned, b); }
; __device__ __forceinline__ float sigmoid_f(float x) { return __builtin_amdgcn_rcpf(1.0f + __builtin_amdgcn_exp2f(-1.4426950408889634f * x)); }
;     __device__ __forceinline__ void operator()(const f32x4 (&acc)[2][2][4][2], const Unit& u, int wr, int wc, int fr, int fq) const {
;     ...
;             for (int m = 0; m < 4; ++m) { f32x4 v0, v1; const float r_ = rs[ai][m], rw = r_ * wt[ai][m];
; #pragma unroll
;                 for (int e = 0; e < 4; ++e) { const float g0 = acc[ai][0][m][0][e] * r_, g1 = acc[ai][0][m][1][e] * r_;
;                     v0[e] = g0 * sigmoid_f(g0) * (acc[ai][1][m][0][e] * rw); v1[e] = g1 * sigmoid_f(g1) * (acc[ai][1][m][1][e] * rw); }
;                 u32x4 w; w.x = cvt_pk_bf16(v0[0], v0[1]); w.y = cvt_pk_bf16(v0[2], v0[3]); w.z = cvt_pk_bf16(v1[0], v1[1]); w.w = cvt_pk_bf16(v1[2], v1[3]);
;                 *(u32x4*)(U + (size_t)(row0 + ai * HALF + m * 16) * 512 + col0) = w; }
	v_mul_f32_e32 v129, 0xbfb8aa3b, v127
	v_exp_f32_e32 v128, v128
	v_exp_f32_e32 v129, v129
	v_pk_mul_f32 v[118:119], v[118:119], v[172:173]
	v_pk_mul_f32 v[120:121], v[120:121], v[162:163] op_sel_hi:[1,0]
	v_pk_mul_f32 v[114:115], v[114:115], v[118:119]
	v_add_f32_e32 v118, 1.0, v128
	v_add_f32_e32 v119, 1.0, v129
	v_mul_f32_e32 v128, 0xbfb8aa3b, v120
	v_mul_f32_e32 v129, 0xbfb8aa3b, v121
	v_exp_f32_e32 v128, v128
	v_exp_f32_e32 v129, v129
	v_rcp_f32_e32 v118, v118
	v_rcp_f32_e32 v119, v119
	v_add_f32_e32 v128, 1.0, v128
	v_add_f32_e32 v129, 1.0, v129
	v_rcp_f32_e32 v128, v128
	v_rcp_f32_e32 v129, v129
	v_pk_mul_f32 v[118:119], v[126:127], v[118:119]
	v_cndmask_b32_e64 v134, 0, v166, s[18:19]
	v_lshl_or_b32 v166, s26, 7, v154
	v_pk_mul_f32 v[124:125], v[124:125], v[118:119]
	v_pk_mul_f32 v[118:119], v[120:121], v[128:129]
	v_ashrrev_i32_e32 v143, 31, v142
	v_ashrrev_i32_e32 v167, 31, v166
	v_pk_mul_f32 v[116:117], v[116:117], v[118:119]
	v_cvt_pk_bf16_f32 v120, v114, v115
	v_lshlrev_b64 v[114:115], 10, v[142:143]
	v_cvt_pk_bf16_f32 v121, v116, v117
	v_lshl_add_u64 v[114:115], s[46:47], 0, v[114:115]
	v_lshlrev_b64 v[116:117], 1, v[166:167]
	v_cvt_pk_bf16_f32 v118, v122, v123
	v_cvt_pk_bf16_f32 v119, v124, v125
	v_lshl_add_u64 v[114:115], v[114:115], 0, v[116:117]
	v_pk_mul_f32 v[110:111], v[110:111], v[164:165] op_sel_hi:[1,0]
	global_store_dwordx4 v[114:115], v[118:121], off sc1
	v_pk_mul_f32 v[102:103], v[102:103], v[164:165] op_sel_hi:[1,0]
	v_pk_mul_f32 v[104:105], v[104:105], v[164:165] op_sel_hi:[1,0]
	v_mul_f32_e32 v118, 0xbfb8aa3b, v110
	v_exp_f32_e32 v119, v118
	v_mul_f32_e32 v118, 0xbfb8aa3b, v111
	v_exp_f32_e32 v121, v118
	v_mul_f32_e32 v118, v164, v161
	v_add_f32_e32 v119, 1.0, v119
	v_rcp_f32_e32 v120, v119
	v_add_f32_e32 v119, 1.0, v121
	v_mul_f32_e32 v121, 0xbfb8aa3b, v102
	v_exp_f32_e32 v122, v121
	v_mul_f32_e32 v121, 0xbfb8aa3b, v103
	v_exp_f32_e32 v123, v121
	v_rcp_f32_e32 v121, v119
	v_add_f32_e32 v119, 1.0, v122
	v_rcp_f32_e32 v122, v119
	v_add_f32_e32 v119, 1.0, v123
	v_pk_mul_f32 v[110:111], v[110:111], v[120:121]
	v_pk_mul_f32 v[106:107], v[106:107], v[118:119] op_sel_hi:[1,0]
	v_rcp_f32_e32 v123, v119
	v_pk_mul_f32 v[106:107], v[106:107], v[110:111]
	v_pk_mul_f32 v[110:111], v[112:113], v[164:165] op_sel_hi:[1,0]
	v_pk_mul_f32 v[98:99], v[98:99], v[118:119] op_sel_hi:[1,0]
	v_mul_f32_e32 v112, 0xbfb8aa3b, v110
	v_mul_f32_e32 v113, 0xbfb8aa3b, v111
	v_exp_f32_e32 v112, v112
	v_exp_f32_e32 v113, v113
	v_pk_mul_f32 v[102:103], v[102:103], v[122:123]
	v_pk_mul_f32 v[108:109], v[108:109], v[118:119] op_sel_hi:[1,0]
	v_pk_mul_f32 v[102:103], v[98:99], v[102:103]
	v_add_f32_e32 v98, 1.0, v112
	v_add_f32_e32 v99, 1.0, v113
	v_mul_f32_e32 v112, 0xbfb8aa3b, v104
	v_mul_f32_e32 v113, 0xbfb8aa3b, v105
	v_exp_f32_e32 v112, v112
	v_exp_f32_e32 v113, v113
	v_rcp_f32_e32 v98, v98
	v_rcp_f32_e32 v99, v99
	v_add_f32_e32 v112, 1.0, v112
	v_add_f32_e32 v113, 1.0, v113
	v_rcp_f32_e32 v112, v112
	v_rcp_f32_e32 v113, v113
	v_pk_mul_f32 v[98:99], v[110:111], v[98:99]
	v_pk_mul_f32 v[100:101], v[100:101], v[118:119] op_sel_hi:[1,0]
	v_pk_mul_f32 v[108:109], v[108:109], v[98:99]
	v_pk_mul_f32 v[98:99], v[104:105], v[112:113]
	v_pk_mul_f32 v[78:79], v[78:79], v[144:145] op_sel_hi:[1,0]
	v_pk_mul_f32 v[104:105], v[100:101], v[98:99]
	v_cvt_pk_bf16_f32 v100, v102, v103
	v_or_b32_e32 v102, 16, v142
	v_ashrrev_i32_e32 v103, 31, v102
	v_lshlrev_b64 v[102:103], 10, v[102:103]
	v_lshl_add_u64 v[102:103], s[46:47], 0, v[102:103]
	v_cvt_pk_bf16_f32 v98, v106, v107
	v_cvt_pk_bf16_f32 v99, v108, v109
	v_cvt_pk_bf16_f32 v101, v104, v105
	v_lshl_add_u64 v[102:103], v[102:103], 0, v[116:117]
	global_store_dwordx4 v[102:103], v[98:101], off sc1
	v_pk_mul_f32 v[70:71], v[70:71], v[144:145] op_sel_hi:[1,0]
	v_pk_mul_f32 v[72:73], v[72:73], v[144:145] op_sel_hi:[1,0]
	v_mul_f32_e32 v98, 0xbfb8aa3b, v94
	v_exp_f32_e32 v99, v98
	v_mul_f32_e32 v98, 0xbfb8aa3b, v95
	v_exp_f32_e32 v101, v98
	v_mul_f32_e32 v98, v146, v169
	v_add_f32_e32 v99, 1.0, v99
	v_rcp_f32_e32 v100, v99
	v_add_f32_e32 v99, 1.0, v101
	v_mul_f32_e32 v101, 0xbfb8aa3b, v86
	v_exp_f32_e32 v102, v101
	v_mul_f32_e32 v101, 0xbfb8aa3b, v87
	v_exp_f32_e32 v103, v101
	v_rcp_f32_e32 v101, v99
	v_add_f32_e32 v99, 1.0, v102
	v_rcp_f32_e32 v102, v99
	v_add_f32_e32 v99, 1.0, v103
	v_pk_mul_f32 v[94:95], v[94:95], v[100:101]
	v_pk_mul_f32 v[90:91], v[90:91], v[98:99] op_sel_hi:[1,0]
	v_rcp_f32_e32 v103, v99
	v_pk_mul_f32 v[90:91], v[90:91], v[94:95]
	v_pk_mul_f32 v[94:95], v[96:97], v[146:147] op_sel_hi:[1,0]
	v_pk_mul_f32 v[82:83], v[82:83], v[98:99] op_sel_hi:[1,0]
	v_mul_f32_e32 v96, 0xbfb8aa3b, v94
	v_mul_f32_e32 v97, 0xbfb8aa3b, v95
	v_exp_f32_e32 v96, v96
	v_exp_f32_e32 v97, v97
	v_pk_mul_f32 v[86:87], v[86:87], v[102:103]
	v_pk_mul_f32 v[92:93], v[92:93], v[98:99] op_sel_hi:[1,0]
	v_pk_mul_f32 v[86:87], v[82:83], v[86:87]
	v_add_f32_e32 v82, 1.0, v96
	v_add_f32_e32 v83, 1.0, v97
	v_mul_f32_e32 v96, 0xbfb8aa3b, v88
	v_mul_f32_e32 v97, 0xbfb8aa3b, v89
	v_exp_f32_e32 v96, v96
	v_exp_f32_e32 v97, v97
	v_rcp_f32_e32 v82, v82
	v_rcp_f32_e32 v83, v83
	v_add_f32_e32 v96, 1.0, v96
	v_add_f32_e32 v97, 1.0, v97
	v_rcp_f32_e32 v96, v96
	v_rcp_f32_e32 v97, v97
	v_pk_mul_f32 v[82:83], v[94:95], v[82:83]
	v_pk_mul_f32 v[84:85], v[84:85], v[98:99] op_sel_hi:[1,0]
	v_pk_mul_f32 v[92:93], v[92:93], v[82:83]
	v_pk_mul_f32 v[82:83], v[88:89], v[96:97]
	v_pk_mul_f32 v[62:63], v[62:63], v[140:141] op_sel_hi:[1,0]
	v_pk_mul_f32 v[88:89], v[84:85], v[82:83]
	v_cvt_pk_bf16_f32 v84, v86, v87
	v_or_b32_e32 v86, 32, v142
	v_ashrrev_i32_e32 v87, 31, v86
	v_lshlrev_b64 v[86:87], 10, v[86:87]
	v_lshl_add_u64 v[86:87], s[46:47], 0, v[86:87]
; __device__ __forceinline__ unsigned cvt_pk_bf16(float lo, float hi) { f32x2v_ v = {lo, hi}; bf16x2v_ b = __builtin_convertvector(v, bf16x2v_); return __builtin_bit_cast(unsigned, b); }
; __device__ __forceinline__ float sigmoid_f(float x) { return __builtin_amdgcn_rcpf(1.0f + __builtin_amdgcn_exp2f(-1.4426950408889634f * x)); }
;     __device__ __forceinline__ void operator()(const f32x4 (&acc)[2][2][4][2], const Unit& u, int wr, int wc, int fr, int fq) const {
;     ...
;             for (int m = 0; m < 4; ++m) { f32x4 v0, v1; const float r_ = rs[ai][m], rw = r_ * wt[ai][m];
; #pragma unroll
;                 for (int e = 0; e < 4; ++e) { const float g0 = acc[ai][0][m][0][e] * r_, g1 = acc[ai][0][m][1][e] * r_;
;                     v0[e] = g0 * sigmoid_f(g0) * (acc[ai][1][m][0][e] * rw); v1[e] = g1 * sigmoid_f(g1) * (acc[ai][1][m][1][e] * rw); }
;                 u32x4 w; w.x = cvt_pk_bf16(v0[0], v0[1]); w.y = cvt_pk_bf16(v0[2], v0[3]); w.z = cvt_pk_bf16(v1[0], v1[1]); w.w = cvt_pk_bf16(v1[2], v1[3]);
;                 *(u32x4*)(U + (size_t)(row0 + ai * HALF + m * 16) * 512 + col0) = w; }
	v_cvt_pk_bf16_f32 v82, v90, v91
	v_cvt_pk_bf16_f32 v83, v92, v93
	v_cvt_pk_bf16_f32 v85, v88, v89
	v_lshl_add_u64 v[86:87], v[86:87], 0, v[116:117]
	global_store_dwordx4 v[86:87], v[82:85], off sc1
	v_pk_mul_f32 v[54:55], v[54:55], v[140:141] op_sel_hi:[1,0]
	v_pk_mul_f32 v[56:57], v[56:57], v[140:141] op_sel_hi:[1,0]
	v_mul_f32_e32 v82, 0xbfb8aa3b, v78
	v_exp_f32_e32 v83, v82
	v_mul_f32_e32 v82, 0xbfb8aa3b, v79
	v_exp_f32_e32 v85, v82
	v_mul_f32_e32 v82, v144, v174
	v_add_f32_e32 v83, 1.0, v83
	v_rcp_f32_e32 v84, v83
	v_add_f32_e32 v83, 1.0, v85
	v_mul_f32_e32 v85, 0xbfb8aa3b, v70
	v_exp_f32_e32 v86, v85
	v_mul_f32_e32 v85, 0xbfb8aa3b, v71
	v_exp_f32_e32 v87, v85
	v_rcp_f32_e32 v85, v83
	v_add_f32_e32 v83, 1.0, v86
	v_rcp_f32_e32 v86, v83
	v_add_f32_e32 v83, 1.0, v87
	v_pk_mul_f32 v[78:79], v[78:79], v[84:85]
	v_pk_mul_f32 v[74:75], v[74:75], v[82:83] op_sel_hi:[1,0]
	v_rcp_f32_e32 v87, v83
	v_pk_mul_f32 v[74:75], v[74:75], v[78:79]
	v_pk_mul_f32 v[78:79], v[80:81], v[144:145] op_sel_hi:[1,0]
	v_pk_mul_f32 v[66:67], v[66:67], v[82:83] op_sel_hi:[1,0]
	v_mul_f32_e32 v80, 0xbfb8aa3b, v78
	v_mul_f32_e32 v81, 0xbfb8aa3b, v79
	v_exp_f32_e32 v80, v80
	v_exp_f32_e32 v81, v81
	v_pk_mul_f32 v[70:71], v[70:71], v[86:87]
	v_pk_mul_f32 v[76:77], v[76:77], v[82:83] op_sel_hi:[1,0]
	v_pk_mul_f32 v[70:71], v[66:67], v[70:71]
	v_add_f32_e32 v66, 1.0, v80
	v_add_f32_e32 v67, 1.0, v81
	v_mul_f32_e32 v80, 0xbfb8aa3b, v72
	v_mul_f32_e32 v81, 0xbfb8aa3b, v73
	v_exp_f32_e32 v80, v80
	v_exp_f32_e32 v81, v81
	v_rcp_f32_e32 v66, v66
	v_rcp_f32_e32 v67, v67
	v_add_f32_e32 v80, 1.0, v80
	v_add_f32_e32 v81, 1.0, v81
	v_rcp_f32_e32 v80, v80
	v_rcp_f32_e32 v81, v81
	v_pk_mul_f32 v[66:67], v[78:79], v[66:67]
	v_pk_mul_f32 v[68:69], v[68:69], v[82:83] op_sel_hi:[1,0]
	v_pk_mul_f32 v[76:77], v[76:77], v[66:67]
	v_pk_mul_f32 v[66:67], v[72:73], v[80:81]
	v_cndmask_b32_e64 v139, 0, v139, s[18:19]
	v_pk_mul_f32 v[72:73], v[68:69], v[66:67]
	v_cvt_pk_bf16_f32 v68, v70, v71
	v_or_b32_e32 v70, 48, v142
	v_ashrrev_i32_e32 v71, 31, v70
	v_lshlrev_b64 v[70:71], 10, v[70:71]
	v_lshl_add_u64 v[70:71], s[46:47], 0, v[70:71]
	v_cvt_pk_bf16_f32 v66, v74, v75
	v_cvt_pk_bf16_f32 v67, v76, v77
	v_cvt_pk_bf16_f32 v69, v72, v73
	v_lshl_add_u64 v[70:71], v[70:71], 0, v[116:117]
	global_store_dwordx4 v[70:71], v[66:69], off sc1
	v_pk_mul_f32 v[46:47], v[46:47], v[138:139] op_sel_hi:[1,0]
	v_pk_mul_f32 v[38:39], v[38:39], v[138:139] op_sel_hi:[1,0]
	v_mul_f32_e32 v66, 0xbfb8aa3b, v62
	v_exp_f32_e32 v67, v66
	v_mul_f32_e32 v66, 0xbfb8aa3b, v63
	v_exp_f32_e32 v69, v66
	v_mul_f32_e32 v66, v140, v175
	v_add_f32_e32 v67, 1.0, v67
	v_rcp_f32_e32 v68, v67
	v_add_f32_e32 v67, 1.0, v69
	v_mul_f32_e32 v69, 0xbfb8aa3b, v54
	v_exp_f32_e32 v70, v69
	v_mul_f32_e32 v69, 0xbfb8aa3b, v55
	v_exp_f32_e32 v71, v69
	v_rcp_f32_e32 v69, v67
	v_add_f32_e32 v67, 1.0, v70
	v_rcp_f32_e32 v70, v67
	v_add_f32_e32 v67, 1.0, v71
	v_pk_mul_f32 v[62:63], v[62:63], v[68:69]
	v_pk_mul_f32 v[58:59], v[58:59], v[66:67] op_sel_hi:[1,0]
	v_rcp_f32_e32 v71, v67
	v_pk_mul_f32 v[58:59], v[58:59], v[62:63]
	v_pk_mul_f32 v[62:63], v[64:65], v[140:141] op_sel_hi:[1,0]
	v_pk_mul_f32 v[50:51], v[50:51], v[66:67] op_sel_hi:[1,0]
	v_mul_f32_e32 v64, 0xbfb8aa3b, v62
	v_mul_f32_e32 v65, 0xbfb8aa3b, v63
	v_exp_f32_e32 v64, v64
	v_exp_f32_e32 v65, v65
	v_pk_mul_f32 v[54:55], v[54:55], v[70:71]
	v_pk_mul_f32 v[60:61], v[60:61], v[66:67] op_sel_hi:[1,0]
	v_pk_mul_f32 v[54:55], v[50:51], v[54:55]
	v_add_f32_e32 v50, 1.0, v64
	v_add_f32_e32 v51, 1.0, v65
	v_mul_f32_e32 v64, 0xbfb8aa3b, v56
	v_mul_f32_e32 v65, 0xbfb8aa3b, v57
	v_exp_f32_e32 v64, v64
	v_exp_f32_e32 v65, v65
	v_rcp_f32_e32 v50, v50
	v_rcp_f32_e32 v51, v51
	v_add_f32_e32 v64, 1.0, v64
	v_add_f32_e32 v65, 1.0, v65
	v_rcp_f32_e32 v64, v64
	v_rcp_f32_e32 v65, v65
	v_pk_mul_f32 v[50:51], v[62:63], v[50:51]
	v_pk_mul_f32 v[52:53], v[52:53], v[66:67] op_sel_hi:[1,0]
	v_pk_mul_f32 v[60:61], v[60:61], v[50:51]
	v_pk_mul_f32 v[50:51], v[56:57], v[64:65]
	v_pk_mul_f32 v[40:41], v[40:41], v[138:139] op_sel_hi:[1,0]
	v_pk_mul_f32 v[56:57], v[52:53], v[50:51]
	v_cvt_pk_bf16_f32 v52, v54, v55
	v_add_co_u32_e32 v54, vcc, s86, v114
	v_cvt_pk_bf16_f32 v50, v58, v59
	v_cvt_pk_bf16_f32 v51, v60, v61
	v_cvt_pk_bf16_f32 v53, v56, v57
	v_addc_co_u32_e32 v55, vcc, 0, v115, vcc
	global_store_dwordx4 v[54:55], v[50:53], off sc1
	v_pk_mul_f32 v[30:31], v[30:31], v[136:137] op_sel_hi:[1,0]
	v_pk_mul_f32 v[22:23], v[22:23], v[136:137] op_sel_hi:[1,0]
	v_mul_f32_e32 v50, 0xbfb8aa3b, v46
	v_exp_f32_e32 v51, v50
	v_mul_f32_e32 v50, 0xbfb8aa3b, v47
	v_exp_f32_e32 v53, v50
	v_mul_f32_e32 v50, v138, v145
	v_add_f32_e32 v51, 1.0, v51
	v_rcp_f32_e32 v52, v51
	v_add_f32_e32 v51, 1.0, v53
	v_mul_f32_e32 v53, 0xbfb8aa3b, v38
	v_exp_f32_e32 v54, v53
	v_mul_f32_e32 v53, 0xbfb8aa3b, v39
	v_exp_f32_e32 v55, v53
	v_rcp_f32_e32 v53, v51
	v_add_f32_e32 v51, 1.0, v54
	v_rcp_f32_e32 v54, v51
	v_add_f32_e32 v51, 1.0, v55
	v_pk_mul_f32 v[46:47], v[46:47], v[52:53]
	v_pk_mul_f32 v[42:43], v[42:43], v[50:51] op_sel_hi:[1,0]
	v_rcp_f32_e32 v55, v51
	v_pk_mul_f32 v[42:43], v[42:43], v[46:47]
	v_pk_mul_f32 v[46:47], v[48:49], v[138:139] op_sel_hi:[1,0]
	v_pk_mul_f32 v[34:35], v[34:35], v[50:51] op_sel_hi:[1,0]
	v_mul_f32_e32 v48, 0xbfb8aa3b, v46
	v_mul_f32_e32 v49, 0xbfb8aa3b, v47
	v_exp_f32_e32 v48, v48
	v_exp_f32_e32 v49, v49
	v_pk_mul_f32 v[38:39], v[38:39], v[54:55]
	v_pk_mul_f32 v[44:45], v[44:45], v[50:51] op_sel_hi:[1,0]
	v_pk_mul_f32 v[38:39], v[34:35], v[38:39]
	v_add_f32_e32 v34, 1.0, v48
	v_add_f32_e32 v35, 1.0, v49
	v_mul_f32_e32 v48, 0xbfb8aa3b, v40
	v_mul_f32_e32 v49, 0xbfb8aa3b, v41
	v_exp_f32_e32 v48, v48
; __device__ __forceinline__ unsigned cvt_pk_bf16(float lo, float hi) { f32x2v_ v = {lo, hi}; bf16x2v_ b = __builtin_convertvector(v, bf16x2v_); return __builtin_bit_cast(unsigned, b); }
; __device__ __forceinline__ float sigmoid_f(float x) { return __builtin_amdgcn_rcpf(1.0f + __builtin_amdgcn_exp2f(-1.4426950408889634f * x)); }
; #define PG8_BAR __builtin_amdgcn_s_barrier()
;     __device__ __forceinline__ void operator()(const f32x4 (&acc)[2][2][4][2], const Unit& u, int wr, int wc, int fr, int fq) const {
;     ...
;             for (int m = 0; m < 4; ++m) { f32x4 v0, v1; const float r_ = rs[ai][m], rw = r_ * wt[ai][m];
; #pragma unroll
;                 for (int e = 0; e < 4; ++e) { const float g0 = acc[ai][0][m][0][e] * r_, g1 = acc[ai][0][m][1][e] * r_;
;                     v0[e] = g0 * sigmoid_f(g0) * (acc[ai][1][m][0][e] * rw); v1[e] = g1 * sigmoid_f(g1) * (acc[ai][1][m][1][e] * rw); }
;                 u32x4 w; w.x = cvt_pk_bf16(v0[0], v0[1]); w.y = cvt_pk_bf16(v0[2], v0[3]); w.z = cvt_pk_bf16(v1[0], v1[1]); w.w = cvt_pk_bf16(v1[2], v1[3]);
;                 *(u32x4*)(U + (size_t)(row0 + ai * HALF + m * 16) * 512 + col0) = w; }
; template <class Epi, class Sched, bool ALIGN_EPI = false, bool SP2 = false>
; __device__ __forceinline__ void gemm_phase(PG8_LAS unsigned char* lds, const Gemm g, const Sched& S, const Epi& E) {
;     ...
;         if (!has_next) break;
; #pragma unroll
;         for (int a = 0; a < 2; ++a)
; #pragma unroll
;             for (int b = 0; b < 2; ++b)
; #pragma unroll
;                 for (int m = 0; m < 4; ++m)
; #pragma unroll
;                     for (int n = 0; n < 2; ++n) { acc[a][b][m][n] = (f32x4){0.f, 0.f, 0.f, 0.f}; asm volatile("" : "+v"(acc[a][b][m][n])); }
;         cur = nxt; cA = nA; cB = nB; ++ui;
;         if constexpr (Sched::GATHER) {
; #pragma unroll
;             for (int h = 0; h < 2; ++h)
; #pragma unroll
;                 for (int i = 0; i < 2; ++i) voffAc[h][i] = voffAn[h][i]; }
;         if constexpr (ALIGN_EPI) { if (wr == 1) PG8_BAR; }
	v_exp_f32_e32 v49, v49
	v_rcp_f32_e32 v34, v34
	v_rcp_f32_e32 v35, v35
	v_add_f32_e32 v48, 1.0, v48
	v_add_f32_e32 v49, 1.0, v49
	v_rcp_f32_e32 v48, v48
	v_rcp_f32_e32 v49, v49
	v_pk_mul_f32 v[34:35], v[46:47], v[34:35]
	v_pk_mul_f32 v[36:37], v[36:37], v[50:51] op_sel_hi:[1,0]
	v_pk_mul_f32 v[44:45], v[44:45], v[34:35]
	v_pk_mul_f32 v[34:35], v[40:41], v[48:49]
	v_pk_mul_f32 v[24:25], v[24:25], v[136:137] op_sel_hi:[1,0]
	v_pk_mul_f32 v[40:41], v[36:37], v[34:35]
	v_cvt_pk_bf16_f32 v36, v38, v39
	v_add_co_u32_e32 v38, vcc, s87, v114
	v_cvt_pk_bf16_f32 v34, v42, v43
	v_cvt_pk_bf16_f32 v35, v44, v45
	v_cvt_pk_bf16_f32 v37, v40, v41
	v_addc_co_u32_e32 v39, vcc, 0, v115, vcc
	global_store_dwordx4 v[38:39], v[34:37], off sc1
	v_pk_mul_f32 v[14:15], v[14:15], v[134:135] op_sel_hi:[1,0]
	v_pk_mul_f32 v[6:7], v[6:7], v[134:135] op_sel_hi:[1,0]
	v_mul_f32_e32 v34, 0xbfb8aa3b, v30
	v_exp_f32_e32 v35, v34
	v_mul_f32_e32 v34, 0xbfb8aa3b, v31
	v_exp_f32_e32 v37, v34
	v_mul_f32_e32 v34, v136, v141
	v_add_f32_e32 v35, 1.0, v35
	v_rcp_f32_e32 v36, v35
	v_add_f32_e32 v35, 1.0, v37
	v_mul_f32_e32 v37, 0xbfb8aa3b, v22
	v_exp_f32_e32 v38, v37
	v_mul_f32_e32 v37, 0xbfb8aa3b, v23
	v_exp_f32_e32 v39, v37
	v_rcp_f32_e32 v37, v35
	v_add_f32_e32 v35, 1.0, v38
	v_rcp_f32_e32 v38, v35
	v_add_f32_e32 v35, 1.0, v39
	v_pk_mul_f32 v[30:31], v[30:31], v[36:37]
	v_pk_mul_f32 v[26:27], v[26:27], v[34:35] op_sel_hi:[1,0]
	v_rcp_f32_e32 v39, v35
	v_pk_mul_f32 v[26:27], v[26:27], v[30:31]
	v_pk_mul_f32 v[30:31], v[32:33], v[136:137] op_sel_hi:[1,0]
	v_pk_mul_f32 v[18:19], v[18:19], v[34:35] op_sel_hi:[1,0]
	v_mul_f32_e32 v32, 0xbfb8aa3b, v30
	v_mul_f32_e32 v33, 0xbfb8aa3b, v31
	v_exp_f32_e32 v32, v32
	v_exp_f32_e32 v33, v33
	v_pk_mul_f32 v[22:23], v[22:23], v[38:39]
	v_pk_mul_f32 v[28:29], v[28:29], v[34:35] op_sel_hi:[1,0]
	v_pk_mul_f32 v[22:23], v[18:19], v[22:23]
	v_add_f32_e32 v18, 1.0, v32
	v_add_f32_e32 v19, 1.0, v33
	v_mul_f32_e32 v32, 0xbfb8aa3b, v24
	v_mul_f32_e32 v33, 0xbfb8aa3b, v25
	v_exp_f32_e32 v32, v32
	v_exp_f32_e32 v33, v33
	v_rcp_f32_e32 v18, v18
	v_rcp_f32_e32 v19, v19
	v_add_f32_e32 v32, 1.0, v32
	v_add_f32_e32 v33, 1.0, v33
	v_rcp_f32_e32 v32, v32
	v_rcp_f32_e32 v33, v33
	v_pk_mul_f32 v[18:19], v[30:31], v[18:19]
	v_pk_mul_f32 v[20:21], v[20:21], v[34:35] op_sel_hi:[1,0]
	v_pk_mul_f32 v[28:29], v[28:29], v[18:19]
	v_pk_mul_f32 v[18:19], v[24:25], v[32:33]
	v_pk_mul_f32 v[8:9], v[8:9], v[134:135] op_sel_hi:[1,0]
	v_pk_mul_f32 v[24:25], v[20:21], v[18:19]
	v_cvt_pk_bf16_f32 v20, v22, v23
	v_add_co_u32_e32 v22, vcc, s88, v114
	v_cvt_pk_bf16_f32 v18, v26, v27
	v_cvt_pk_bf16_f32 v19, v28, v29
	v_cvt_pk_bf16_f32 v21, v24, v25
	v_addc_co_u32_e32 v23, vcc, 0, v115, vcc
	global_store_dwordx4 v[22:23], v[18:21], off sc1
	s_nop 1
	v_mul_f32_e32 v18, 0xbfb8aa3b, v14
	v_exp_f32_e32 v19, v18
	v_mul_f32_e32 v18, 0xbfb8aa3b, v15
	v_exp_f32_e32 v21, v18
	v_mul_f32_e32 v18, v134, v139
	v_add_f32_e32 v19, 1.0, v19
	v_rcp_f32_e32 v20, v19
	v_add_f32_e32 v19, 1.0, v21
	v_mul_f32_e32 v21, 0xbfb8aa3b, v6
	v_exp_f32_e32 v22, v21
	v_mul_f32_e32 v21, 0xbfb8aa3b, v7
	v_exp_f32_e32 v23, v21
	v_rcp_f32_e32 v21, v19
	v_add_f32_e32 v19, 1.0, v22
	v_rcp_f32_e32 v22, v19
	v_add_f32_e32 v19, 1.0, v23
	v_pk_mul_f32 v[14:15], v[14:15], v[20:21]
	v_pk_mul_f32 v[10:11], v[10:11], v[18:19] op_sel_hi:[1,0]
	v_rcp_f32_e32 v23, v19
	v_pk_mul_f32 v[10:11], v[10:11], v[14:15]
	v_pk_mul_f32 v[14:15], v[16:17], v[134:135] op_sel_hi:[1,0]
	v_pk_mul_f32 v[2:3], v[2:3], v[18:19] op_sel_hi:[1,0]
	v_mul_f32_e32 v16, 0xbfb8aa3b, v14
	v_mul_f32_e32 v17, 0xbfb8aa3b, v15
	v_exp_f32_e32 v16, v16
	v_exp_f32_e32 v17, v17
	v_pk_mul_f32 v[6:7], v[6:7], v[22:23]
	v_pk_mul_f32 v[12:13], v[12:13], v[18:19] op_sel_hi:[1,0]
	v_pk_mul_f32 v[6:7], v[2:3], v[6:7]
	v_add_f32_e32 v2, 1.0, v16
	v_add_f32_e32 v3, 1.0, v17
	v_mul_f32_e32 v16, 0xbfb8aa3b, v8
	v_mul_f32_e32 v17, 0xbfb8aa3b, v9
	v_exp_f32_e32 v16, v16
	v_exp_f32_e32 v17, v17
	v_rcp_f32_e32 v2, v2
	v_rcp_f32_e32 v3, v3
	v_add_f32_e32 v16, 1.0, v16
	v_add_f32_e32 v17, 1.0, v17
	v_rcp_f32_e32 v16, v16
	v_rcp_f32_e32 v17, v17
	v_pk_mul_f32 v[2:3], v[14:15], v[2:3]
	v_pk_mul_f32 v[4:5], v[4:5], v[18:19] op_sel_hi:[1,0]
	v_pk_mul_f32 v[12:13], v[12:13], v[2:3]
	v_pk_mul_f32 v[2:3], v[8:9], v[16:17]
	s_nop 0
	v_pk_mul_f32 v[8:9], v[4:5], v[2:3]
	v_cvt_pk_bf16_f32 v4, v6, v7
	v_add_co_u32_e32 v6, vcc, 0x2c000, v114
	v_cvt_pk_bf16_f32 v2, v10, v11
	s_nop 0
	v_addc_co_u32_e32 v7, vcc, 0, v115, vcc
	v_cvt_pk_bf16_f32 v3, v12, v13
	v_cvt_pk_bf16_f32 v5, v8, v9
	s_and_b64 vcc, exec, s[4:5]
	s_mov_b64 s[4:5], -1
	global_store_dwordx4 v[6:7], v[2:5], off sc1
	s_cbranch_vccnz .LBB0_784
	s_mov_b32 s25, s24
	s_mov_b32 s26, s24
	s_mov_b32 s27, s24
	v_mov_b64_e32 v[2:3], s[24:25]
	v_mov_b64_e32 v[128:129], s[26:27]
	v_mov_b64_e32 v[120:121], s[26:27]
	v_mov_b64_e32 v[112:113], s[26:27]
	v_mov_b64_e32 v[104:105], s[26:27]
	v_mov_b64_e32 v[96:97], s[26:27]
	v_mov_b64_e32 v[88:89], s[26:27]
	v_mov_b64_e32 v[80:81], s[26:27]
	v_mov_b64_e32 v[72:73], s[26:27]
	v_mov_b64_e32 v[124:125], s[26:27]
	v_mov_b64_e32 v[116:117], s[26:27]
	v_mov_b64_e32 v[108:109], s[26:27]
	v_mov_b64_e32 v[100:101], s[26:27]
	v_mov_b64_e32 v[92:93], s[26:27]
	v_mov_b64_e32 v[84:85], s[26:27]
	v_mov_b64_e32 v[76:77], s[26:27]
	v_mov_b64_e32 v[68:69], s[26:27]
	v_mov_b64_e32 v[64:65], s[26:27]
	v_mov_b64_e32 v[56:57], s[26:27]
	v_mov_b64_e32 v[48:49], s[26:27]
	v_mov_b64_e32 v[40:41], s[26:27]
	v_mov_b64_e32 v[32:33], s[26:27]
	v_mov_b64_e32 v[22:23], s[24:25]
	v_mov_b64_e32 v[14:15], s[24:25]
	v_mov_b64_e32 v[6:7], s[24:25]
	v_mov_b64_e32 v[60:61], s[26:27]
	v_mov_b64_e32 v[52:53], s[26:27]
	v_mov_b64_e32 v[44:45], s[26:27]
	v_mov_b64_e32 v[36:37], s[26:27]
	v_mov_b64_e32 v[28:29], s[26:27]
	v_mov_b64_e32 v[18:19], s[24:25]
	v_mov_b64_e32 v[10:11], s[24:25]
	v_mov_b64_e32 v[4:5], s[26:27]
	v_mov_b64_e32 v[126:127], s[24:25]
	v_mov_b64_e32 v[118:119], s[24:25]
	v_mov_b64_e32 v[110:111], s[24:25]
	v_mov_b64_e32 v[102:103], s[24:25]
	v_mov_b64_e32 v[94:95], s[24:25]
	v_mov_b64_e32 v[86:87], s[24:25]
	v_mov_b64_e32 v[78:79], s[24:25]
	v_mov_b64_e32 v[70:71], s[24:25]
	v_mov_b64_e32 v[122:123], s[24:25]
	v_mov_b64_e32 v[114:115], s[24:25]
	v_mov_b64_e32 v[106:107], s[24:25]
	v_mov_b64_e32 v[98:99], s[24:25]
	v_mov_b64_e32 v[90:91], s[24:25]
	v_mov_b64_e32 v[82:83], s[24:25]
	v_mov_b64_e32 v[74:75], s[24:25]
	v_mov_b64_e32 v[66:67], s[24:25]
	v_mov_b64_e32 v[62:63], s[24:25]
	v_mov_b64_e32 v[54:55], s[24:25]
	v_mov_b64_e32 v[46:47], s[24:25]
	v_mov_b64_e32 v[38:39], s[24:25]
	v_mov_b64_e32 v[30:31], s[24:25]
	v_mov_b64_e32 v[24:25], s[26:27]
	v_mov_b64_e32 v[16:17], s[26:27]
	v_mov_b64_e32 v[8:9], s[26:27]
	v_mov_b64_e32 v[58:59], s[24:25]
	v_mov_b64_e32 v[50:51], s[24:25]
	v_mov_b64_e32 v[42:43], s[24:25]
	v_mov_b64_e32 v[34:35], s[24:25]
	v_mov_b64_e32 v[26:27], s[24:25]
	v_mov_b64_e32 v[20:21], s[26:27]
	v_mov_b64_e32 v[12:13], s[26:27]
	s_andn2_b64 vcc, exec, s[44:45]
	s_cbranch_vccnz .LBB0_783
	s_barrier
	s_branch .LBB0_783

; #define GAS __attribute__((address_space(1)))
; #define LAS __attribute__((address_space(3)))
; #define LDS_WAIT() asm volatile("s_waitcnt lgkmcnt(0)" ::: "memory")
; __device__ __forceinline__ unsigned pk2(float lo, float hi) { return f2bf(lo) | (f2bf(hi) << 16); }
; __device__ __forceinline__ void p0_transpose_item(const float* W, int N, int k0, int n0, bf16* WT, int K, int dst_row0, LAS float* scr, int lane, const float* kscale = nullptr, int permhalf = -1) {
;     typedef float f32x4t __attribute__((ext_vector_type(4)));
;     const int c = lane & 7;
;     float ks[8];
; #pragma unroll
;     for (int i = 0; i < 8; ++i) ks[i] = kscale ? kscale[k0 + 8 * c + i] : 1.0f;
; #pragma unroll
;     for (int i = 0; i < 8; ++i) { const int kk = 8 * i + (lane >> 3), nn = (lane & 7) * 4;
;         *(LAS f32x4t*)(scr + kk * 36 + nn) = *(const GAS f32x4t*)(W + (size_t)(k0 + kk) * N + n0 + nn); }
;     LDS_WAIT(); asm volatile("" ::: "memory");
; #pragma unroll
;     for (int j = 0; j < 4; ++j) { const int n = (lane >> 3) + 8 * j; const LAS float* s = scr + (8 * c) * 36 + n;
;         v4u o; o.x = pk2(s[0 * 36] * ks[0], s[1 * 36] * ks[1]); o.y = pk2(s[2 * 36] * ks[2], s[3 * 36] * ks[3]); o.z = pk2(s[4 * 36] * ks[4], s[5 * 36] * ks[5]); o.w = pk2(s[6 * 36] * ks[6], s[7 * 36] * ks[7]);
;         const int drow = permhalf < 0 ? n : (32 * (n >> 4) + 8 * ((n >> 2) & 3) + 4 * permhalf + (n & 3));
;         *(GAS v4u*)(WT + (size_t)(dst_row0 + drow) * K + k0 + 8 * c) = o; }
; __device__ __forceinline__ void conv_item(KArgs a, int r, LAS float* scr, int lane) {
;     ...
;     if (r < CONV_IE) { const int e = r / 512, q = r % 512, kb = q / 16, nb = q % 16, n0 = 32 * nb;
;         p0_transpose_item(a->in[18] + (size_t)e * 2048 * 512, 512, 64 * kb, n0, (bf16*)(ws + WS_W13), 2048, e * 1024 + (n0 >> 7) * 256 + (n0 & 127), scr, lane, a->in[15]); return; } r -= CONV_IE;
.LBB0_801:
	s_load_dwordx2 s[24:25], s[8:9], 0x90
	s_lshl_b32 s5, s36, 4
	s_ashr_i32 s4, s19, 9
	s_sub_i32 s5, s10, s5
	s_sext_i32_i16 s10, s5
	s_ashr_i32 s5, s4, 31
	s_lshl_b32 s26, s10, 5
	s_lshl_b64 s[36:37], s[4:5], 22
	s_waitcnt lgkmcnt(0)
	s_add_u32 s5, s24, s36
	s_addc_u32 s19, s25, s37
	s_lshl_b32 s10, s10, 6
	s_lshl_b32 s4, s4, 10
	s_and_b32 s10, s10, 0xffffff00
	s_add_i32 s10, s10, s4
	s_and_b32 s4, s26, 0x60
	s_ashr_i32 s27, s26, 31
	s_or_b32 s4, s10, s4
	s_lshl_b64 s[24:25], s[26:27], 2
	s_add_u32 s24, s5, s24
	v_or_b32_e32 v30, s18, v1
	s_addc_u32 s25, s19, s25
	v_ashrrev_i32_e32 v31, 31, v30
	v_lshl_add_u64 v[16:17], s[24:25], 0, v[4:5]
	v_lshlrev_b64 v[30:31], 11, v[30:31]
	v_lshl_add_u64 v[38:39], v[16:17], 0, v[30:31]
	v_or_b32_e32 v30, s18, v3
	v_ashrrev_i32_e32 v31, 31, v30
	v_lshlrev_b64 v[30:31], 11, v[30:31]
	v_lshl_add_u64 v[40:41], v[16:17], 0, v[30:31]
	global_load_dwordx4 v[30:33], v[38:39], off
	global_load_dwordx4 v[34:37], v[40:41], off
	v_or_b32_e32 v38, s18, v18
	v_ashrrev_i32_e32 v39, 31, v38
	v_lshlrev_b64 v[38:39], 11, v[38:39]
	v_lshl_add_u64 v[46:47], v[16:17], 0, v[38:39]
	v_or_b32_e32 v38, s18, v19
	v_ashrrev_i32_e32 v39, 31, v38
	v_lshlrev_b64 v[38:39], 11, v[38:39]
	v_lshl_add_u64 v[48:49], v[16:17], 0, v[38:39]
	global_load_dwordx4 v[38:41], v[46:47], off
	global_load_dwordx4 v[42:45], v[48:49], off
	v_or_b32_e32 v46, s18, v20
	v_ashrrev_i32_e32 v47, 31, v46
	v_lshlrev_b64 v[46:47], 11, v[46:47]
	v_lshl_add_u64 v[54:55], v[16:17], 0, v[46:47]
	v_or_b32_e32 v46, s18, v21
	v_ashrrev_i32_e32 v47, 31, v46
	v_lshlrev_b64 v[46:47], 11, v[46:47]
	v_lshl_add_u64 v[56:57], v[16:17], 0, v[46:47]
	global_load_dwordx4 v[46:49], v[54:55], off
	global_load_dwordx4 v[50:53], v[56:57], off
	v_or_b32_e32 v54, s18, v22
	v_ashrrev_i32_e32 v55, 31, v54
	v_lshlrev_b64 v[54:55], 11, v[54:55]
	v_lshl_add_u64 v[62:63], v[16:17], 0, v[54:55]
	v_or_b32_e32 v54, s18, v23
	v_ashrrev_i32_e32 v55, 31, v54
	v_lshlrev_b64 v[54:55], 11, v[54:55]
	v_lshl_add_u64 v[16:17], v[16:17], 0, v[54:55]
	global_load_dwordx4 v[54:57], v[62:63], off
	global_load_dwordx4 v[58:61], v[16:17], off
	s_ashr_i32 s19, s18, 31
	s_lshl_b64 s[18:19], s[18:19], 1
	s_add_u32 s16, s16, s18
	v_mov_b32_e32 v7, v5
	s_addc_u32 s17, s17, s19
	v_lshl_add_u64 v[16:17], s[16:17], 0, v[6:7]
	v_lshl_add_u64 v[16:17], v[16:17], 0, s[14:15]
	s_waitcnt vmcnt(7)
	ds_write_b128 v25, v[30:33]
	s_waitcnt vmcnt(6)
	ds_write_b128 v25, v[34:37] offset:1152
	s_waitcnt vmcnt(5)
	ds_write_b128 v25, v[38:41] offset:2304
	s_waitcnt vmcnt(4)
	ds_write_b128 v25, v[42:45] offset:3456
	s_waitcnt vmcnt(3)
	ds_write_b128 v25, v[46:49] offset:4608
	s_waitcnt vmcnt(2)
	ds_write_b128 v25, v[50:53] offset:5760
	s_waitcnt vmcnt(1)
	ds_write_b128 v25, v[54:57] offset:6912
	s_waitcnt vmcnt(0)
	ds_write_b128 v25, v[58:61] offset:8064
	s_waitcnt lgkmcnt(0)
	ds_read2_b32 v[34:35], v24 offset0:36 offset1:44
	ds_read2_b32 v[36:37], v24 offset0:72 offset1:80
	ds_read2_b32 v[38:39], v24 offset0:108 offset1:116
	ds_read2_b32 v[40:41], v24 offset1:8
	ds_read2_b32 v[42:43], v24 offset0:144 offset1:152
	ds_read2_b32 v[44:45], v24 offset0:180 offset1:188
	ds_read2_b32 v[46:47], v24 offset0:216 offset1:224
	ds_read2_b32 v[48:49], v26 offset0:124 offset1:132
	s_waitcnt lgkmcnt(7)
	v_mov_b32_e32 v32, v34
	s_waitcnt lgkmcnt(5)
	v_mov_b32_e32 v33, v38
	s_waitcnt lgkmcnt(3)
	v_mov_b32_e32 v50, v42
	s_waitcnt lgkmcnt(1)
	v_mov_b32_e32 v51, v46
	v_mov_b32_e32 v30, v40
	v_mov_b32_e32 v31, v36
	v_pk_mul_f32 v[32:33], v[8:9], v[32:33]
	v_pk_mul_f32 v[50:51], v[14:15], v[50:51]
	v_mov_b32_e32 v52, v44
	s_waitcnt lgkmcnt(0)
; #define GAS __attribute__((address_space(1)))
; #define LAS __attribute__((address_space(3)))
; __device__ __forceinline__ unsigned pk2(float lo, float hi) { return f2bf(lo) | (f2bf(hi) << 16); }
; __device__ __forceinline__ void p0_transpose_item(const float* W, int N, int k0, int n0, bf16* WT, int K, int dst_row0, LAS float* scr, int lane, const float* kscale = nullptr, int permhalf = -1) {
;     ...
;     for (int j = 0; j < 4; ++j) { const int n = (lane >> 3) + 8 * j; const LAS float* s = scr + (8 * c) * 36 + n;
;         v4u o; o.x = pk2(s[0 * 36] * ks[0], s[1 * 36] * ks[1]); o.y = pk2(s[2 * 36] * ks[2], s[3 * 36] * ks[3]); o.z = pk2(s[4 * 36] * ks[4], s[5 * 36] * ks[5]); o.w = pk2(s[6 * 36] * ks[6], s[7 * 36] * ks[7]);
;         const int drow = permhalf < 0 ? n : (32 * (n >> 4) + 8 * ((n >> 2) & 3) + 4 * permhalf + (n & 3));
;         *(GAS v4u*)(WT + (size_t)(dst_row0 + drow) * K + k0 + 8 * c) = o; }
	v_mov_b32_e32 v53, v48
	v_pk_mul_f32 v[30:31], v[10:11], v[30:31]
	v_bfe_u32 v34, v33, 16, 1
	v_bfe_u32 v36, v32, 16, 1
	v_bfe_u32 v38, v50, 16, 1
	v_pk_mul_f32 v[52:53], v[12:13], v[52:53]
	v_add3_u32 v36, v32, v36, s31
	v_add3_u32 v34, v33, v34, s31
	v_bfe_u32 v32, v30, 16, 1
	v_bfe_u32 v33, v31, 16, 1
	v_bfe_u32 v40, v51, 16, 1
	v_add3_u32 v38, v50, v38, s31
	v_or_b32_e32 v50, s4, v1
	v_bfe_u32 v7, v53, 16, 1
	v_bfe_u32 v29, v52, 16, 1
	v_add3_u32 v40, v51, v40, s31
	v_add3_u32 v31, v31, v33, s31
	v_add3_u32 v30, v30, v32, s31
	v_ashrrev_i32_e32 v51, 31, v50
	v_add3_u32 v29, v52, v29, s31
	v_add3_u32 v7, v53, v7, s31
	v_lshrrev_b32_e32 v30, 16, v30
	v_lshrrev_b32_e32 v31, 16, v31
	v_lshrrev_b32_e32 v32, 16, v38
	v_lshrrev_b32_e32 v33, 16, v40
	v_lshlrev_b64 v[50:51], 12, v[50:51]
	v_and_or_b32 v33, v7, s40, v33
	v_and_or_b32 v32, v29, s40, v32
	v_and_or_b32 v31, v34, s40, v31
	v_and_or_b32 v30, v36, s40, v30
	v_lshl_add_u64 v[50:51], v[16:17], 0, v[50:51]
	v_mov_b32_e32 v36, v41
	v_mov_b32_e32 v48, v45
	global_store_dwordx4 v[50:51], v[30:33], off sc1
	v_mov_b32_e32 v38, v35
	v_mov_b32_e32 v46, v43
	v_pk_mul_f32 v[30:31], v[10:11], v[36:37]
	v_pk_mul_f32 v[36:37], v[12:13], v[48:49]
	v_pk_mul_f32 v[32:33], v[8:9], v[38:39]
	v_pk_mul_f32 v[34:35], v[14:15], v[46:47]
	v_bfe_u32 v29, v36, 16, 1
	v_bfe_u32 v7, v37, 16, 1
	v_bfe_u32 v39, v32, 16, 1
	v_add3_u32 v29, v36, v29, s31
	v_bfe_u32 v36, v34, 16, 1
	v_bfe_u32 v38, v33, 16, 1
	v_add3_u32 v39, v32, v39, s31
	v_add3_u32 v7, v37, v7, s31
	v_bfe_u32 v32, v30, 16, 1
	v_bfe_u32 v37, v35, 16, 1
	v_add3_u32 v34, v34, v36, s31
	v_add3_u32 v38, v33, v38, s31
	v_bfe_u32 v33, v31, 16, 1
	v_add3_u32 v35, v35, v37, s31
	v_add3_u32 v30, v30, v32, s31
	v_lshrrev_b32_e32 v32, 16, v34
	v_or_b32_e32 v34, s4, v3
	v_add3_u32 v31, v31, v33, s31
	v_lshrrev_b32_e32 v33, 16, v35
	v_ashrrev_i32_e32 v35, 31, v34
	v_lshrrev_b32_e32 v30, 16, v30
	v_lshrrev_b32_e32 v31, 16, v31
	v_lshlrev_b64 v[34:35], 12, v[34:35]
	v_and_or_b32 v33, v7, s40, v33
	v_and_or_b32 v32, v29, s40, v32
	v_and_or_b32 v31, v38, s40, v31
	v_and_or_b32 v30, v39, s40, v30
	v_lshl_add_u64 v[34:35], v[16:17], 0, v[34:35]
	ds_read2_b32 v[36:37], v24 offset0:16 offset1:24
	ds_read2_b32 v[38:39], v24 offset0:88 offset1:96
	global_store_dwordx4 v[34:35], v[30:33], off sc1
	ds_read2_b32 v[34:35], v24 offset0:52 offset1:60
	ds_read2_b32 v[40:41], v24 offset0:124 offset1:132
	ds_read2_b32 v[42:43], v24 offset0:160 offset1:168
	ds_read2_b32 v[44:45], v24 offset0:232 offset1:240
	ds_read2_b32 v[46:47], v24 offset0:196 offset1:204
	ds_read2_b32 v[48:49], v27 offset0:12 offset1:20
	s_waitcnt lgkmcnt(7)
	v_mov_b32_e32 v30, v36
	s_waitcnt lgkmcnt(5)
	v_mov_b32_e32 v32, v34
	s_waitcnt lgkmcnt(4)
	v_mov_b32_e32 v33, v40
	s_waitcnt lgkmcnt(3)
	v_mov_b32_e32 v50, v42
	s_waitcnt lgkmcnt(2)
	v_mov_b32_e32 v51, v44
	v_mov_b32_e32 v31, v38
	v_pk_mul_f32 v[32:33], v[8:9], v[32:33]
	v_pk_mul_f32 v[50:51], v[14:15], v[50:51]
	v_pk_mul_f32 v[30:31], v[10:11], v[30:31]
	s_waitcnt lgkmcnt(1)
	v_mov_b32_e32 v52, v46
	s_waitcnt lgkmcnt(0)
	v_mov_b32_e32 v53, v48
	v_bfe_u32 v34, v33, 16, 1
	v_bfe_u32 v36, v32, 16, 1
	v_bfe_u32 v38, v50, 16, 1
	v_pk_mul_f32 v[52:53], v[12:13], v[52:53]
	v_add3_u32 v36, v32, v36, s31
	v_add3_u32 v34, v33, v34, s31
	v_bfe_u32 v32, v30, 16, 1
	v_bfe_u32 v33, v31, 16, 1
	v_bfe_u32 v40, v51, 16, 1
	v_add3_u32 v38, v50, v38, s31
	v_or_b32_e32 v50, s4, v18
	v_bfe_u32 v7, v53, 16, 1
	v_bfe_u32 v29, v52, 16, 1
	v_add3_u32 v40, v51, v40, s31
	v_add3_u32 v31, v31, v33, s31
	v_add3_u32 v30, v30, v32, s31
	v_ashrrev_i32_e32 v51, 31, v50
	v_add3_u32 v29, v52, v29, s31
	v_add3_u32 v7, v53, v7, s31
	v_lshrrev_b32_e32 v30, 16, v30
	v_lshrrev_b32_e32 v31, 16, v31
	v_lshrrev_b32_e32 v32, 16, v38
	v_lshrrev_b32_e32 v33, 16, v40
	v_lshlrev_b64 v[50:51], 12, v[50:51]
	v_mov_b32_e32 v40, v35
	v_mov_b32_e32 v48, v47
	v_and_or_b32 v33, v7, s40, v33
	v_and_or_b32 v32, v29, s40, v32
	v_and_or_b32 v31, v34, s40, v31
	v_and_or_b32 v30, v36, s40, v30
	v_lshl_add_u64 v[50:51], v[16:17], 0, v[50:51]
	v_mov_b32_e32 v38, v37
	v_pk_mul_f32 v[8:9], v[8:9], v[40:41]
	v_mov_b32_e32 v44, v43
	v_pk_mul_f32 v[12:13], v[12:13], v[48:49]
	global_store_dwordx4 v[50:51], v[30:33], off sc1
	v_pk_mul_f32 v[10:11], v[10:11], v[38:39]
	v_pk_mul_f32 v[14:15], v[14:15], v[44:45]
	v_bfe_u32 v7, v13, 16, 1
	v_bfe_u32 v30, v9, 16, 1
	v_add3_u32 v9, v9, v30, s31
	v_add3_u32 v7, v13, v7, s31
	v_bfe_u32 v13, v10, 16, 1
	v_bfe_u32 v30, v14, 16, 1
	v_bfe_u32 v29, v12, 16, 1
	v_add3_u32 v14, v14, v30, s31
	v_add3_u32 v10, v10, v13, s31
	v_bfe_u32 v31, v8, 16, 1
	v_add3_u32 v12, v12, v29, s31
	v_lshrrev_b32_e32 v13, 16, v10
	v_lshrrev_b32_e32 v10, 16, v14
	v_add3_u32 v8, v8, v31, s31
	v_bfe_u32 v29, v11, 16, 1
	v_bfe_u32 v31, v15, 16, 1
	v_and_or_b32 v10, v12, s40, v10
	v_or_b32_e32 v12, s4, v19
	v_add3_u32 v15, v15, v31, s31
	v_add3_u32 v11, v11, v29, s31
	v_and_or_b32 v8, v8, s40, v13
	v_ashrrev_i32_e32 v13, 31, v12
	v_lshrrev_b32_e32 v29, 16, v11
	v_lshrrev_b32_e32 v11, 16, v15
	v_lshlrev_b64 v[12:13], 12, v[12:13]
	v_and_or_b32 v11, v7, s40, v11
	v_and_or_b32 v9, v9, s40, v29
	v_lshl_add_u64 v[12:13], v[16:17], 0, v[12:13]
	global_store_dwordx4 v[12:13], v[8:11], off sc1
	s_waitcnt lgkmcnt(0)

; #define GAS __attribute__((address_space(1)))
; #define LAS __attribute__((address_space(3)))
; #define LDS_WAIT() asm volatile("s_waitcnt lgkmcnt(0)" ::: "memory")
; __device__ __forceinline__ unsigned pk2(float lo, float hi) { return f2bf(lo) | (f2bf(hi) << 16); }
; __device__ __forceinline__ void p0_transpose_item(const float* W, int N, int k0, int n0, bf16* WT, int K, int dst_row0, LAS float* scr, int lane, const float* kscale = nullptr, int permhalf = -1) {
;     typedef float f32x4t __attribute__((ext_vector_type(4)));
;     const int c = lane & 7;
;     float ks[8];
; #pragma unroll
;     for (int i = 0; i < 8; ++i) ks[i] = kscale ? kscale[k0 + 8 * c + i] : 1.0f;
; #pragma unroll
;     for (int i = 0; i < 8; ++i) { const int kk = 8 * i + (lane >> 3), nn = (lane & 7) * 4;
;         *(LAS f32x4t*)(scr + kk * 36 + nn) = *(const GAS f32x4t*)(W + (size_t)(k0 + kk) * N + n0 + nn); }
;     LDS_WAIT(); asm volatile("" ::: "memory");
; #pragma unroll
;     for (int j = 0; j < 4; ++j) { const int n = (lane >> 3) + 8 * j; const LAS float* s = scr + (8 * c) * 36 + n;
;         v4u o; o.x = pk2(s[0 * 36] * ks[0], s[1 * 36] * ks[1]); o.y = pk2(s[2 * 36] * ks[2], s[3 * 36] * ks[3]); o.z = pk2(s[4 * 36] * ks[4], s[5 * 36] * ks[5]); o.w = pk2(s[6 * 36] * ks[6], s[7 * 36] * ks[7]);
; __device__ __forceinline__ void conv_item(KArgs a, int r, LAS float* scr, int lane) {
;     unsigned char* ws = a->ws;
;     if (r < CONV_IE) { const int e = r / 512, q = r % 512, kb = q / 16, nb = q % 16, n0 = 32 * nb;
;         p0_transpose_item(a->in[18] + (size_t)e * 2048 * 512, 512, 64 * kb, n0, (bf16*)(ws + WS_W13), 2048, e * 1024 + (n0 >> 7) * 256 + (n0 & 127), scr, lane, a->in[15]); return; } r -= CONV_IE;
;     if (r < CONV_IE) { const int e = r / 512, q = r % 512, kb = q / 16, nb = q % 16, n0 = 32 * nb;
;         p0_transpose_item(a->in[19] + (size_t)e * 2048 * 512, 512, 64 * kb, n0, (bf16*)(ws + WS_W13), 2048, e * 1024 + (n0 >> 7) * 256 + 128 + (n0 & 127), scr, lane, a->in[15]); return; } r -= CONV_IE;
;     { const int e = r / 512, q = r % 512, kb = q / 64, nb = q % 64;
;       p0_transpose_item(a->in[20] + (size_t)e * 512 * 2048, 2048, 64 * kb, 32 * nb, (bf16*)(ws + WS_W2), 512, e * 2048 + 32 * nb, scr, lane); }
.LBB0_812:
	s_and_b64 vcc, exec, s[18:19]
	s_cbranch_vccz .LBB0_803
	s_cmp_lt_i32 s41, 0xc000
	s_cbranch_scc0 .LBB0_803
	s_load_dwordx2 s[16:17], s[8:9], 0xb8
	s_cmpk_gt_i32 s41, 0x3fff
	s_cbranch_scc0 .LBB0_836
	s_cmpk_gt_u32 s41, 0x7fff
	s_cbranch_scc0 .LBB0_817
	s_load_dwordx2 s[4:5], s[8:9], 0xa0
	s_add_i32 s24, s41, 0xffff8000
	s_and_b32 s10, s24, 0xfffffe00
	s_and_b32 s25, s41, 0x1c0
	s_lshl_b64 s[18:19], s[10:11], 13
	s_waitcnt lgkmcnt(0)
	s_add_u32 s10, s4, s18
	s_addc_u32 s5, s5, s19
	s_lshl_b32 s4, s41, 5
	s_and_b32 s18, s4, 0x7e0
	s_lshl_b32 s4, s24, 2
	s_and_b32 s4, s4, 0x7ffff800
	s_or_b32 s4, s4, s18
	s_lshl_b32 s18, s18, 2
	s_add_u32 s18, s10, s18
	s_addc_u32 s19, s5, 0
	v_or_b32_e32 v7, s25, v1
	v_lshl_add_u64 v[16:17], s[18:19], 0, v[4:5]
	v_lshlrev_b32_e32 v8, 13, v7
	v_mov_b32_e32 v9, v5
	v_or_b32_e32 v7, s25, v3
	v_lshl_add_u64 v[30:31], v[16:17], 0, v[8:9]
	v_lshlrev_b32_e32 v8, 13, v7
	v_or_b32_e32 v7, s25, v18
	v_lshl_add_u64 v[32:33], v[16:17], 0, v[8:9]
	global_load_dwordx4 v[8:11], v[30:31], off
	global_load_dwordx4 v[12:15], v[32:33], off
	v_lshlrev_b32_e32 v30, 13, v7
	v_mov_b32_e32 v31, v5
	v_or_b32_e32 v7, s25, v19
	v_lshl_add_u64 v[38:39], v[16:17], 0, v[30:31]
	v_lshlrev_b32_e32 v30, 13, v7
	v_or_b32_e32 v7, s25, v20
	v_lshl_add_u64 v[40:41], v[16:17], 0, v[30:31]
	global_load_dwordx4 v[30:33], v[38:39], off
	global_load_dwordx4 v[34:37], v[40:41], off
	v_lshlrev_b32_e32 v38, 13, v7
	v_mov_b32_e32 v39, v5
	v_or_b32_e32 v7, s25, v21
	v_lshl_add_u64 v[46:47], v[16:17], 0, v[38:39]
	v_lshlrev_b32_e32 v38, 13, v7
	v_or_b32_e32 v7, s25, v22
	v_lshl_add_u64 v[48:49], v[16:17], 0, v[38:39]
	global_load_dwordx4 v[38:41], v[46:47], off
	global_load_dwordx4 v[42:45], v[48:49], off
	v_lshlrev_b32_e32 v46, 13, v7
	v_mov_b32_e32 v47, v5
	v_or_b32_e32 v7, s25, v23
	v_lshl_add_u64 v[54:55], v[16:17], 0, v[46:47]
	v_lshlrev_b32_e32 v46, 13, v7
	v_lshl_add_u64 v[16:17], v[16:17], 0, v[46:47]
	global_load_dwordx4 v[46:49], v[54:55], off
	global_load_dwordx4 v[50:53], v[16:17], off
	s_lshl_b32 s5, s25, 1
	s_add_u32 s18, s16, s5
	v_mov_b32_e32 v7, v5
	s_addc_u32 s19, s17, 0
	v_lshl_add_u64 v[54:55], s[18:19], 0, v[6:7]
	v_or_b32_e32 v16, s4, v1
	v_lshl_add_u64 v[54:55], v[54:55], 0, s[12:13]
	s_waitcnt vmcnt(7)
	ds_write_b128 v25, v[8:11]
	s_waitcnt vmcnt(6)
	ds_write_b128 v25, v[12:15] offset:1152
	s_waitcnt vmcnt(5)
	ds_write_b128 v25, v[30:33] offset:2304
	s_waitcnt vmcnt(4)
	ds_write_b128 v25, v[34:37] offset:3456
	s_waitcnt vmcnt(3)
	ds_write_b128 v25, v[38:41] offset:4608
	s_waitcnt vmcnt(2)
	ds_write_b128 v25, v[42:45] offset:5760
	s_waitcnt vmcnt(1)
	ds_write_b128 v25, v[46:49] offset:6912
	s_waitcnt vmcnt(0)
	ds_write_b128 v25, v[50:53] offset:8064
	s_waitcnt lgkmcnt(0)
	ds_read2_b32 v[12:13], v24 offset0:36 offset1:44
	ds_read2_b32 v[14:15], v24 offset1:8
	ds_read2_b32 v[30:31], v24 offset0:72 offset1:80
	ds_read2_b32 v[32:33], v24 offset0:108 offset1:116
	ds_read2_b32 v[34:35], v24 offset0:144 offset1:152
	ds_read2_b32 v[36:37], v24 offset0:180 offset1:188
	ds_read2_b32 v[38:39], v24 offset0:216 offset1:224
	ds_read2_b32 v[40:41], v26 offset0:124 offset1:132
	s_waitcnt lgkmcnt(6)
	v_bfe_u32 v7, v14, 16, 1
	s_waitcnt lgkmcnt(5)
	v_bfe_u32 v9, v30, 16, 1
	s_waitcnt lgkmcnt(3)
	v_bfe_u32 v11, v34, 16, 1
	s_waitcnt lgkmcnt(1)
	v_bfe_u32 v29, v38, 16, 1
	v_bfe_u32 v8, v12, 16, 1
	v_bfe_u32 v10, v32, 16, 1
	v_bfe_u32 v17, v36, 16, 1
	s_waitcnt lgkmcnt(0)
; #define GAS __attribute__((address_space(1)))
; #define LAS __attribute__((address_space(3)))
; __device__ __forceinline__ unsigned pk2(float lo, float hi) { return f2bf(lo) | (f2bf(hi) << 16); }
; __device__ __forceinline__ void p0_transpose_item(const float* W, int N, int k0, int n0, bf16* WT, int K, int dst_row0, LAS float* scr, int lane, const float* kscale = nullptr, int permhalf = -1) {
;     ...
;     for (int j = 0; j < 4; ++j) { const int n = (lane >> 3) + 8 * j; const LAS float* s = scr + (8 * c) * 36 + n;
;         v4u o; o.x = pk2(s[0 * 36] * ks[0], s[1 * 36] * ks[1]); o.y = pk2(s[2 * 36] * ks[2], s[3 * 36] * ks[3]); o.z = pk2(s[4 * 36] * ks[4], s[5 * 36] * ks[5]); o.w = pk2(s[6 * 36] * ks[6], s[7 * 36] * ks[7]);
;         const int drow = permhalf < 0 ? n : (32 * (n >> 4) + 8 * ((n >> 2) & 3) + 4 * permhalf + (n & 3));
;         *(GAS v4u*)(WT + (size_t)(dst_row0 + drow) * K + k0 + 8 * c) = o; }
	v_bfe_u32 v42, v40, 16, 1
	v_add3_u32 v7, v14, v7, s31
	v_add3_u32 v9, v30, v9, s31
	v_add3_u32 v11, v34, v11, s31
	v_add3_u32 v14, v38, v29, s31
	v_add3_u32 v8, v12, v8, s31
	v_add3_u32 v10, v32, v10, s31
	v_add3_u32 v12, v36, v17, s31
	v_add3_u32 v17, v40, v42, s31
	v_lshrrev_b32_e32 v9, 16, v9
	v_lshrrev_b32_e32 v11, 16, v11
	v_lshrrev_b32_e32 v14, 16, v14
	v_and_or_b32 v9, v10, s40, v9
	v_and_or_b32 v10, v12, s40, v11
	v_and_or_b32 v11, v17, s40, v14
	v_mov_b32_e32 v17, v5
	v_lshrrev_b32_e32 v7, 16, v7
	v_lshlrev_b64 v[16:17], 10, v[16:17]
	v_and_or_b32 v8, v8, s40, v7
	v_lshl_add_u64 v[16:17], v[54:55], 0, v[16:17]
	v_bfe_u32 v7, v15, 16, 1
	global_store_dwordx4 v[16:17], v[8:11], off sc1
	v_add3_u32 v7, v15, v7, s31
	v_lshrrev_b32_e32 v7, 16, v7
	v_bfe_u32 v8, v13, 16, 1
	v_add3_u32 v8, v13, v8, s31
	v_and_or_b32 v8, v8, s40, v7
	v_bfe_u32 v7, v31, 16, 1
	v_add3_u32 v7, v31, v7, s31
	v_bfe_u32 v9, v33, 16, 1
	v_lshrrev_b32_e32 v7, 16, v7
	v_add3_u32 v9, v33, v9, s31
	v_and_or_b32 v9, v9, s40, v7
	v_bfe_u32 v7, v35, 16, 1
	v_add3_u32 v7, v35, v7, s31
	v_bfe_u32 v10, v37, 16, 1
	v_lshrrev_b32_e32 v7, 16, v7
	v_add3_u32 v10, v37, v10, s31
	v_and_or_b32 v10, v10, s40, v7
	v_bfe_u32 v7, v39, 16, 1
	v_add3_u32 v7, v39, v7, s31
	v_bfe_u32 v11, v41, 16, 1
	v_or_b32_e32 v12, s4, v3
	v_mov_b32_e32 v13, v5
	v_lshrrev_b32_e32 v7, 16, v7
	v_add3_u32 v11, v41, v11, s31
	v_lshlrev_b64 v[12:13], 10, v[12:13]
	v_and_or_b32 v11, v11, s40, v7
	ds_read2_b32 v[14:15], v24 offset0:16 offset1:24
	v_lshl_add_u64 v[12:13], v[54:55], 0, v[12:13]
	global_store_dwordx4 v[12:13], v[8:11], off sc1
	ds_read2_b32 v[12:13], v24 offset0:52 offset1:60
	ds_read2_b32 v[16:17], v24 offset0:88 offset1:96
	ds_read2_b32 v[30:31], v24 offset0:124 offset1:132
	s_waitcnt lgkmcnt(3)
	v_bfe_u32 v7, v14, 16, 1
	v_add3_u32 v7, v14, v7, s31
	s_waitcnt lgkmcnt(2)
	v_bfe_u32 v8, v12, 16, 1
	ds_read2_b32 v[32:33], v24 offset0:160 offset1:168
	v_lshrrev_b32_e32 v7, 16, v7
	v_add3_u32 v8, v12, v8, s31
	ds_read2_b32 v[34:35], v24 offset0:196 offset1:204
	v_and_or_b32 v8, v8, s40, v7
	s_waitcnt lgkmcnt(3)
	v_bfe_u32 v7, v16, 16, 1
	v_add3_u32 v7, v16, v7, s31
	s_waitcnt lgkmcnt(2)
	v_bfe_u32 v9, v30, 16, 1
	ds_read2_b32 v[36:37], v24 offset0:232 offset1:240
	v_lshrrev_b32_e32 v7, 16, v7
	v_add3_u32 v9, v30, v9, s31
	ds_read2_b32 v[38:39], v27 offset0:12 offset1:20
	v_and_or_b32 v9, v9, s40, v7
	s_waitcnt lgkmcnt(3)
	v_bfe_u32 v7, v32, 16, 1
	v_add3_u32 v7, v32, v7, s31
	s_waitcnt lgkmcnt(2)
	v_bfe_u32 v10, v34, 16, 1
	v_lshrrev_b32_e32 v7, 16, v7
	v_add3_u32 v10, v34, v10, s31
	v_and_or_b32 v10, v10, s40, v7
	s_waitcnt lgkmcnt(1)
	v_bfe_u32 v7, v36, 16, 1
	v_add3_u32 v7, v36, v7, s31
	s_waitcnt lgkmcnt(0)
	v_bfe_u32 v11, v38, 16, 1
	v_or_b32_e32 v40, s4, v18
	v_mov_b32_e32 v41, v5
	v_lshrrev_b32_e32 v7, 16, v7
	v_add3_u32 v11, v38, v11, s31
	v_lshlrev_b64 v[40:41], 10, v[40:41]
	v_and_or_b32 v11, v11, s40, v7
	v_lshl_add_u64 v[40:41], v[54:55], 0, v[40:41]
	v_bfe_u32 v7, v15, 16, 1
	global_store_dwordx4 v[40:41], v[8:11], off sc1
	v_add3_u32 v7, v15, v7, s31
	v_lshrrev_b32_e32 v7, 16, v7
	v_bfe_u32 v8, v13, 16, 1
	v_add3_u32 v8, v13, v8, s31
	v_and_or_b32 v8, v8, s40, v7
	v_bfe_u32 v7, v17, 16, 1
	v_add3_u32 v7, v17, v7, s31
	v_bfe_u32 v9, v31, 16, 1
	v_lshrrev_b32_e32 v7, 16, v7
	v_add3_u32 v9, v31, v9, s31
	v_and_or_b32 v9, v9, s40, v7
	v_bfe_u32 v7, v33, 16, 1
	v_add3_u32 v7, v33, v7, s31
	v_bfe_u32 v10, v35, 16, 1
	v_lshrrev_b32_e32 v7, 16, v7
	v_add3_u32 v10, v35, v10, s31
	v_and_or_b32 v10, v10, s40, v7
	v_bfe_u32 v7, v37, 16, 1
	v_add3_u32 v7, v37, v7, s31
	v_bfe_u32 v11, v39, 16, 1
	v_or_b32_e32 v12, s4, v19
	v_mov_b32_e32 v13, v5
	v_lshrrev_b32_e32 v7, 16, v7
	v_add3_u32 v11, v39, v11, s31
	v_lshlrev_b64 v[12:13], 10, v[12:13]
	v_and_or_b32 v11, v11, s40, v7
	v_lshl_add_u64 v[12:13], v[54:55], 0, v[12:13]
	global_store_dwordx4 v[12:13], v[8:11], off sc1
	s_waitcnt lgkmcnt(0)
	s_mov_b64 s[4:5], 0

; #define GAS __attribute__((address_space(1)))
; #define LAS __attribute__((address_space(3)))
; #define LDS_WAIT() asm volatile("s_waitcnt lgkmcnt(0)" ::: "memory")
; __device__ __forceinline__ unsigned pk2(float lo, float hi) { return f2bf(lo) | (f2bf(hi) << 16); }
; __device__ __forceinline__ void p0_transpose_item(const float* W, int N, int k0, int n0, bf16* WT, int K, int dst_row0, LAS float* scr, int lane, const float* kscale = nullptr, int permhalf = -1) {
;     typedef float f32x4t __attribute__((ext_vector_type(4)));
;     const int c = lane & 7;
;     float ks[8];
; #pragma unroll
;     for (int i = 0; i < 8; ++i) ks[i] = kscale ? kscale[k0 + 8 * c + i] : 1.0f;
; #pragma unroll
;     for (int i = 0; i < 8; ++i) { const int kk = 8 * i + (lane >> 3), nn = (lane & 7) * 4;
;         *(LAS f32x4t*)(scr + kk * 36 + nn) = *(const GAS f32x4t*)(W + (size_t)(k0 + kk) * N + n0 + nn); }
;     LDS_WAIT(); asm volatile("" ::: "memory");
; #pragma unroll
;     for (int j = 0; j < 4; ++j) { const int n = (lane >> 3) + 8 * j; const LAS float* s = scr + (8 * c) * 36 + n;
;         v4u o; o.x = pk2(s[0 * 36] * ks[0], s[1 * 36] * ks[1]); o.y = pk2(s[2 * 36] * ks[2], s[3 * 36] * ks[3]); o.z = pk2(s[4 * 36] * ks[4], s[5 * 36] * ks[5]); o.w = pk2(s[6 * 36] * ks[6], s[7 * 36] * ks[7]);
; __device__ __forceinline__ void conv_item(KArgs a, int r, LAS float* scr, int lane) {
;     ...
;     if (r < CONV_IE) { const int e = r / 512, q = r % 512, kb = q / 16, nb = q % 16, n0 = 32 * nb;
;         p0_transpose_item(a->in[19] + (size_t)e * 2048 * 512, 512, 64 * kb, n0, (bf16*)(ws + WS_W13), 2048, e * 1024 + (n0 >> 7) * 256 + 128 + (n0 & 127), scr, lane, a->in[15]); return; } r -= CONV_IE;
.LBB0_834:
	s_load_dwordx2 s[4:5], s[8:9], 0x98
	s_add_i32 s10, s41, 0xffffc000
	s_lshr_b32 s10, s10, 9
	s_lshl_b32 s24, s41, 5
	s_lshl_b64 s[18:19], s[10:11], 22
	s_waitcnt lgkmcnt(0)
	s_add_u32 s18, s4, s18
	s_addc_u32 s5, s5, s19
	s_lshl_b32 s4, s10, 10
	s_lshl_b32 s10, s41, 6
	s_and_b32 s10, s10, 0x300
	s_or_b32 s4, s4, s10
	s_and_b32 s10, s24, 0x60
	s_or_b32 s4, s4, s10
	s_lshl_b32 s10, s41, 7
	s_bitset1_b32 s4, 7
	s_and_b32 s10, s10, 0x780
	s_add_u32 s18, s18, s10
	s_addc_u32 s19, s5, 0
	v_or_b32_e32 v7, s26, v1
	v_lshl_add_u64 v[16:17], s[18:19], 0, v[4:5]
	v_lshlrev_b32_e32 v30, 11, v7
	v_mov_b32_e32 v31, v5
	v_or_b32_e32 v7, s26, v3
	v_lshl_add_u64 v[38:39], v[16:17], 0, v[30:31]
	v_lshlrev_b32_e32 v30, 11, v7
	v_or_b32_e32 v7, s26, v18
	v_lshl_add_u64 v[40:41], v[16:17], 0, v[30:31]
	global_load_dwordx4 v[30:33], v[38:39], off
	global_load_dwordx4 v[34:37], v[40:41], off
	v_lshlrev_b32_e32 v38, 11, v7
	v_mov_b32_e32 v39, v5
	v_or_b32_e32 v7, s26, v19
	v_lshl_add_u64 v[46:47], v[16:17], 0, v[38:39]
	v_lshlrev_b32_e32 v38, 11, v7
	v_or_b32_e32 v7, s26, v20
	v_lshl_add_u64 v[48:49], v[16:17], 0, v[38:39]
	global_load_dwordx4 v[38:41], v[46:47], off
	global_load_dwordx4 v[42:45], v[48:49], off
	v_lshlrev_b32_e32 v46, 11, v7
	v_mov_b32_e32 v47, v5
	v_or_b32_e32 v7, s26, v21
	v_lshl_add_u64 v[54:55], v[16:17], 0, v[46:47]
	v_lshlrev_b32_e32 v46, 11, v7
	v_or_b32_e32 v7, s26, v22
	v_lshl_add_u64 v[56:57], v[16:17], 0, v[46:47]
	global_load_dwordx4 v[46:49], v[54:55], off
	global_load_dwordx4 v[50:53], v[56:57], off
	v_lshlrev_b32_e32 v54, 11, v7
	v_mov_b32_e32 v55, v5
	v_or_b32_e32 v7, s26, v23
	v_lshl_add_u64 v[62:63], v[16:17], 0, v[54:55]
	v_lshlrev_b32_e32 v54, 11, v7
	v_lshl_add_u64 v[16:17], v[16:17], 0, v[54:55]
	global_load_dwordx4 v[54:57], v[62:63], off
	global_load_dwordx4 v[58:61], v[16:17], off
	s_lshl_b32 s5, s26, 1
	s_add_u32 s18, s16, s5
	v_mov_b32_e32 v7, v5
	s_addc_u32 s19, s17, 0
	v_lshl_add_u64 v[16:17], s[18:19], 0, v[6:7]
	v_lshl_add_u64 v[16:17], v[16:17], 0, s[14:15]
	s_waitcnt vmcnt(7)
	ds_write_b128 v25, v[30:33]
	s_waitcnt vmcnt(6)
	ds_write_b128 v25, v[34:37] offset:1152
	s_waitcnt vmcnt(5)
	ds_write_b128 v25, v[38:41] offset:2304
	s_waitcnt vmcnt(4)
	ds_write_b128 v25, v[42:45] offset:3456
	s_waitcnt vmcnt(3)
	ds_write_b128 v25, v[46:49] offset:4608
	s_waitcnt vmcnt(2)
	ds_write_b128 v25, v[50:53] offset:5760
	s_waitcnt vmcnt(1)
	ds_write_b128 v25, v[54:57] offset:6912
	s_waitcnt vmcnt(0)
	ds_write_b128 v25, v[58:61] offset:8064
	s_waitcnt lgkmcnt(0)
	ds_read2_b32 v[34:35], v24 offset0:36 offset1:44
	ds_read2_b32 v[36:37], v24 offset0:72 offset1:80
	ds_read2_b32 v[38:39], v24 offset0:108 offset1:116
	ds_read2_b32 v[40:41], v24 offset1:8
	ds_read2_b32 v[42:43], v24 offset0:144 offset1:152
	ds_read2_b32 v[44:45], v24 offset0:180 offset1:188
	ds_read2_b32 v[46:47], v24 offset0:216 offset1:224
	ds_read2_b32 v[48:49], v26 offset0:124 offset1:132
	s_waitcnt lgkmcnt(4)
	v_mov_b32_e32 v30, v40
	v_mov_b32_e32 v31, v36
	v_mov_b32_e32 v32, v34
	v_mov_b32_e32 v33, v38
	s_waitcnt lgkmcnt(3)
	v_mov_b32_e32 v50, v42
	s_waitcnt lgkmcnt(1)
	v_mov_b32_e32 v51, v46
	v_mov_b32_e32 v52, v44
	s_waitcnt lgkmcnt(0)
; #define GAS __attribute__((address_space(1)))
; #define LAS __attribute__((address_space(3)))
; __device__ __forceinline__ unsigned pk2(float lo, float hi) { return f2bf(lo) | (f2bf(hi) << 16); }
; __device__ __forceinline__ void p0_transpose_item(const float* W, int N, int k0, int n0, bf16* WT, int K, int dst_row0, LAS float* scr, int lane, const float* kscale = nullptr, int permhalf = -1) {
;     ...
;     for (int j = 0; j < 4; ++j) { const int n = (lane >> 3) + 8 * j; const LAS float* s = scr + (8 * c) * 36 + n;
;         v4u o; o.x = pk2(s[0 * 36] * ks[0], s[1 * 36] * ks[1]); o.y = pk2(s[2 * 36] * ks[2], s[3 * 36] * ks[3]); o.z = pk2(s[4 * 36] * ks[4], s[5 * 36] * ks[5]); o.w = pk2(s[6 * 36] * ks[6], s[7 * 36] * ks[7]);
;         const int drow = permhalf < 0 ? n : (32 * (n >> 4) + 8 * ((n >> 2) & 3) + 4 * permhalf + (n & 3));
;         *(GAS v4u*)(WT + (size_t)(dst_row0 + drow) * K + k0 + 8 * c) = o; }
	v_mov_b32_e32 v53, v48
	v_pk_mul_f32 v[30:31], v[10:11], v[30:31]
	v_pk_mul_f32 v[32:33], v[8:9], v[32:33]
	v_pk_mul_f32 v[50:51], v[14:15], v[50:51]
	v_pk_mul_f32 v[52:53], v[12:13], v[52:53]
	v_bfe_u32 v34, v33, 16, 1
	v_bfe_u32 v36, v32, 16, 1
	v_bfe_u32 v38, v30, 16, 1
	v_bfe_u32 v40, v31, 16, 1
	v_bfe_u32 v42, v50, 16, 1
	v_bfe_u32 v44, v51, 16, 1
	v_bfe_u32 v7, v53, 16, 1
	v_bfe_u32 v29, v52, 16, 1
	v_add3_u32 v36, v32, v36, s31
	v_add3_u32 v34, v33, v34, s31
	v_add3_u32 v32, v51, v44, s31
	v_add3_u32 v33, v50, v42, s31
	v_add3_u32 v31, v31, v40, s31
	v_add3_u32 v30, v30, v38, s31
	v_or_b32_e32 v50, s4, v1
	v_mov_b32_e32 v51, v5
	v_add3_u32 v29, v52, v29, s31
	v_add3_u32 v7, v53, v7, s31
	v_lshrrev_b32_e32 v30, 16, v30
	v_lshrrev_b32_e32 v31, 16, v31
	v_lshrrev_b32_e32 v38, 16, v33
	v_lshrrev_b32_e32 v32, 16, v32
	v_lshlrev_b64 v[50:51], 12, v[50:51]
	v_and_or_b32 v33, v7, s40, v32
	v_and_or_b32 v32, v29, s40, v38
	v_and_or_b32 v31, v34, s40, v31
	v_and_or_b32 v30, v36, s40, v30
	v_lshl_add_u64 v[50:51], v[16:17], 0, v[50:51]
	v_mov_b32_e32 v36, v41
	v_mov_b32_e32 v48, v45
	global_store_dwordx4 v[50:51], v[30:33], off sc1
	v_mov_b32_e32 v38, v35
	v_mov_b32_e32 v46, v43
	v_pk_mul_f32 v[30:31], v[10:11], v[36:37]
	v_pk_mul_f32 v[36:37], v[12:13], v[48:49]
	v_pk_mul_f32 v[32:33], v[8:9], v[38:39]
	v_pk_mul_f32 v[34:35], v[14:15], v[46:47]
	v_bfe_u32 v7, v37, 16, 1
	v_bfe_u32 v29, v36, 16, 1
	v_bfe_u32 v38, v33, 16, 1
	v_bfe_u32 v39, v32, 16, 1
	v_add3_u32 v29, v36, v29, s31
	v_add3_u32 v7, v37, v7, s31
	v_bfe_u32 v36, v34, 16, 1
	v_bfe_u32 v37, v35, 16, 1
	v_add3_u32 v39, v32, v39, s31
	v_add3_u32 v38, v33, v38, s31
	v_bfe_u32 v32, v30, 16, 1
	v_bfe_u32 v33, v31, 16, 1
	v_add3_u32 v35, v35, v37, s31
	v_add3_u32 v34, v34, v36, s31
	v_add3_u32 v31, v31, v33, s31
	v_add3_u32 v30, v30, v32, s31
	v_lshrrev_b32_e32 v32, 16, v34
	v_lshrrev_b32_e32 v33, 16, v35
	v_or_b32_e32 v34, s4, v3
	v_mov_b32_e32 v35, v5
	v_lshrrev_b32_e32 v30, 16, v30
	v_lshrrev_b32_e32 v31, 16, v31
	v_lshlrev_b64 v[34:35], 12, v[34:35]
	v_and_or_b32 v33, v7, s40, v33
	v_and_or_b32 v32, v29, s40, v32
	v_and_or_b32 v31, v38, s40, v31
	v_and_or_b32 v30, v39, s40, v30
	v_lshl_add_u64 v[34:35], v[16:17], 0, v[34:35]
	ds_read2_b32 v[36:37], v24 offset0:16 offset1:24
	ds_read2_b32 v[38:39], v24 offset0:88 offset1:96
	global_store_dwordx4 v[34:35], v[30:33], off sc1
	ds_read2_b32 v[34:35], v24 offset0:52 offset1:60
	ds_read2_b32 v[40:41], v24 offset0:124 offset1:132
	ds_read2_b32 v[42:43], v24 offset0:160 offset1:168
	ds_read2_b32 v[44:45], v24 offset0:232 offset1:240
	ds_read2_b32 v[46:47], v24 offset0:196 offset1:204
	ds_read2_b32 v[48:49], v27 offset0:12 offset1:20
	s_waitcnt lgkmcnt(7)
	v_mov_b32_e32 v30, v36
	s_waitcnt lgkmcnt(5)
	v_mov_b32_e32 v32, v34
	s_waitcnt lgkmcnt(4)
	v_mov_b32_e32 v33, v40
	v_mov_b32_e32 v31, v38
	v_pk_mul_f32 v[32:33], v[8:9], v[32:33]
	s_waitcnt lgkmcnt(3)
	v_mov_b32_e32 v50, v42
	s_waitcnt lgkmcnt(2)
	v_mov_b32_e32 v51, v44
	v_pk_mul_f32 v[30:31], v[10:11], v[30:31]
	v_pk_mul_f32 v[50:51], v[14:15], v[50:51]
	s_waitcnt lgkmcnt(1)
	v_mov_b32_e32 v52, v46
	s_waitcnt lgkmcnt(0)
	v_mov_b32_e32 v53, v48
	v_bfe_u32 v34, v33, 16, 1
	v_bfe_u32 v36, v32, 16, 1
	v_pk_mul_f32 v[52:53], v[12:13], v[52:53]
	v_add3_u32 v36, v32, v36, s31
	v_add3_u32 v34, v33, v34, s31
	v_bfe_u32 v32, v30, 16, 1
	v_bfe_u32 v33, v31, 16, 1
	v_bfe_u32 v38, v50, 16, 1
	v_bfe_u32 v40, v51, 16, 1
	v_bfe_u32 v7, v53, 16, 1
	v_bfe_u32 v29, v52, 16, 1
	v_add3_u32 v40, v51, v40, s31
	v_add3_u32 v38, v50, v38, s31
	v_add3_u32 v31, v31, v33, s31
	v_add3_u32 v30, v30, v32, s31
	v_or_b32_e32 v50, s4, v18
	v_mov_b32_e32 v51, v5
	v_add3_u32 v29, v52, v29, s31
	v_add3_u32 v7, v53, v7, s31
	v_lshrrev_b32_e32 v30, 16, v30
	v_lshrrev_b32_e32 v31, 16, v31
	v_lshrrev_b32_e32 v32, 16, v38
	v_lshrrev_b32_e32 v33, 16, v40
	v_lshlrev_b64 v[50:51], 12, v[50:51]
	v_mov_b32_e32 v40, v35
	v_mov_b32_e32 v48, v47
	v_and_or_b32 v33, v7, s40, v33
	v_and_or_b32 v32, v29, s40, v32
	v_and_or_b32 v31, v34, s40, v31
	v_and_or_b32 v30, v36, s40, v30
	v_lshl_add_u64 v[50:51], v[16:17], 0, v[50:51]
	v_mov_b32_e32 v38, v37
	v_pk_mul_f32 v[8:9], v[8:9], v[40:41]
	v_mov_b32_e32 v44, v43
	v_pk_mul_f32 v[12:13], v[12:13], v[48:49]
	global_store_dwordx4 v[50:51], v[30:33], off sc1
	v_pk_mul_f32 v[10:11], v[10:11], v[38:39]
	v_pk_mul_f32 v[14:15], v[14:15], v[44:45]
	v_bfe_u32 v7, v13, 16, 1
	v_bfe_u32 v30, v9, 16, 1
	v_add3_u32 v9, v9, v30, s31
	v_add3_u32 v7, v13, v7, s31
	v_bfe_u32 v13, v10, 16, 1
	v_bfe_u32 v30, v14, 16, 1
	v_bfe_u32 v29, v12, 16, 1
	v_bfe_u32 v31, v8, 16, 1
	v_add3_u32 v14, v14, v30, s31
	v_add3_u32 v10, v10, v13, s31
	v_add3_u32 v8, v8, v31, s31
	v_add3_u32 v12, v12, v29, s31
	v_bfe_u32 v29, v11, 16, 1
	v_bfe_u32 v31, v15, 16, 1
	v_lshrrev_b32_e32 v13, 16, v10
	v_lshrrev_b32_e32 v10, 16, v14
	v_add3_u32 v15, v15, v31, s31
	v_add3_u32 v11, v11, v29, s31
	v_and_or_b32 v10, v12, s40, v10
	v_and_or_b32 v8, v8, s40, v13
	v_or_b32_e32 v12, s4, v19
	v_mov_b32_e32 v13, v5
	v_lshrrev_b32_e32 v29, 16, v11
	v_lshrrev_b32_e32 v11, 16, v15
	v_lshlrev_b64 v[12:13], 12, v[12:13]
	v_and_or_b32 v11, v7, s40, v11
	v_and_or_b32 v9, v9, s40, v29
	v_lshl_add_u64 v[12:13], v[16:17], 0, v[12:13]
	global_store_dwordx4 v[12:13], v[8:11], off sc1
	s_waitcnt lgkmcnt(0)

; #define GAS __attribute__((address_space(1)))
; __device__ __forceinline__ float bflo(unsigned w) { return __uint_as_float(w << 16); }
; __device__ __forceinline__ float bfhi(unsigned w) { return __uint_as_float(w & 0xffff0000u); }
; __device__ __forceinline__ void p6_final(const Frame& F, KArgs a) {
;     ...
;     for (int t0 = F.gw; t0 < T; t0 += 2 * F.NGW) {
;         const int t1 = (t0 + F.NGW < T) ? t0 + F.NGW : t0;
;         const int ea0 = TOKES[2 * t0], ea1 = TOKES[2 * t0 + 1], eb0 = TOKES[2 * t1], eb1 = TOKES[2 * t1 + 1];
;         GAS f32x4* xa = (GAS f32x4*)(a->out + (size_t)t0 * DM) + F.lane; GAS f32x4* xb = (GAS f32x4*)(a->out + (size_t)t1 * DM) + F.lane;
;         const GAS v2u* x1a = (const GAS v2u*)((const bf16*)(ws + WS_X1B) + (size_t)t0 * DM) + F.lane; const GAS v2u* x1b = (const GAS v2u*)((const bf16*)(ws + WS_X1B) + (size_t)t1 * DM) + F.lane;
;         f32x4 va[8], vb[8];
; #pragma unroll
;         for (int j = 0; j < 8; ++j) { const v2u wa = x1a[64 * j], wb = x1b[64 * j]; va[j] = (f32x4){bflo(wa.x), bfhi(wa.x), bflo(wa.y), bfhi(wa.y)}; vb[j] = (f32x4){bflo(wb.x), bfhi(wb.x), bflo(wb.y), bfhi(wb.y)}; }
;         const GAS unsigned* ya0 = (const GAS unsigned*)(YC + (size_t)(tab[32 + (ea0 >> 16)] * 256 + (ea0 & 0xffff)) * DM) + F.lane; const GAS unsigned* ya1 = (const GAS unsigned*)(YC + (size_t)(tab[32 + (ea1 >> 16)] * 256 + (ea1 & 0xffff)) * DM) + F.lane;
;         const GAS unsigned* yb0 = (const GAS unsigned*)(YC + (size_t)(tab[32 + (eb0 >> 16)] * 256 + (eb0 & 0xffff)) * DM) + F.lane; const GAS unsigned* yb1 = (const GAS unsigned*)(YC + (size_t)(tab[32 + (eb1 >> 16)] * 256 + (eb1 & 0xffff)) * DM) + F.lane;
;         unsigned pa[8], qa[8], pb[8], qb[8];
; #pragma unroll
;         for (int j = 0; j < 8; ++j) { pa[j] = ya0[64 * j]; qa[j] = ya1[64 * j]; pb[j] = yb0[64 * j]; qb[j] = yb1[64 * j]; }
.LBB0_997:
	s_add_i32 s0, s28, s22
	s_cmp_lt_i32 s0, 0x8000
	s_cselect_b32 s12, s0, s22
	s_ashr_i32 s7, s6, 31
	s_lshl_b64 s[0:1], s[6:7], 2
	s_add_u32 s0, s11, s0
	s_addc_u32 s1, s16, s1
	global_load_dwordx2 v[0:1], v5, s[0:1]
	s_lshl_b32 s0, s12, 1
	s_ashr_i32 s1, s0, 31
	s_lshl_b64 s[0:1], s[0:1], 2
	s_add_u32 s0, s11, s0
	s_addc_u32 s1, s16, s1
	global_load_dwordx2 v[2:3], v5, s[0:1]
	global_load_dwordx2 v[26:27], v[24:25], off offset:512
	global_load_dwordx2 v[38:39], v[24:25], off offset:1024
	global_load_dwordx2 v[40:41], v[24:25], off offset:1536
	s_ashr_i32 s13, s12, 31
	s_lshl_b64 s[0:1], s[12:13], 12
	v_lshl_add_u64 v[44:45], v[16:17], 0, s[0:1]
	global_load_dwordx2 v[46:47], v[44:45], off
	global_load_dwordx2 v[48:49], v[44:45], off offset:512
	global_load_dwordx2 v[50:51], v[44:45], off offset:1024
	s_lshl_b64 s[14:15], s[12:13], 13
	s_cmp_lg_u32 s22, s12
	s_waitcnt vmcnt(7)
	v_lshlrev_b32_sdwa v4, v114, sext(v0) dst_sel:DWORD dst_unused:UNUSED_PAD src0_sel:DWORD src1_sel:WORD_1
	v_lshlrev_b32_sdwa v28, v114, sext(v1) dst_sel:DWORD dst_unused:UNUSED_PAD src0_sel:DWORD src1_sel:WORD_1
	v_add_u32_e32 v4, s3, v4
	v_add_u32_e32 v28, s3, v28
	ds_read_b32 v4, v4 offset:128
	ds_read_b32 v28, v28 offset:128
	s_waitcnt vmcnt(6)
	v_lshlrev_b32_sdwa v29, v114, sext(v2) dst_sel:DWORD dst_unused:UNUSED_PAD src0_sel:DWORD src1_sel:WORD_1
	v_lshlrev_b32_sdwa v30, v114, sext(v3) dst_sel:DWORD dst_unused:UNUSED_PAD src0_sel:DWORD src1_sel:WORD_1
	v_add_u32_e32 v29, s3, v29
	v_add_u32_e32 v30, s3, v30
	s_waitcnt lgkmcnt(1)
	v_lshlrev_b32_e32 v4, 8, v4
	s_waitcnt lgkmcnt(0)
	v_lshlrev_b32_e32 v28, 8, v28
	ds_read_b32 v31, v29 offset:128
	ds_read_b32 v30, v30 offset:128
	v_add_u32_sdwa v0, v4, v0 dst_sel:DWORD dst_unused:UNUSED_PAD src0_sel:DWORD src1_sel:WORD_0
	v_add_u32_sdwa v28, v28, v1 dst_sel:DWORD dst_unused:UNUSED_PAD src0_sel:DWORD src1_sel:WORD_0
	v_ashrrev_i32_e32 v1, 31, v0
	v_ashrrev_i32_e32 v29, 31, v28
	v_lshlrev_b64 v[0:1], 11, v[0:1]
	v_lshlrev_b64 v[28:29], 11, v[28:29]
	v_lshl_add_u64 v[52:53], v[20:21], 0, v[0:1]
	v_lshl_add_u64 v[54:55], v[20:21], 0, v[28:29]
	s_waitcnt lgkmcnt(1)
	v_lshlrev_b32_e32 v0, 8, v31
	global_load_dword v4, v[52:53], off
	global_load_dword v64, v[54:55], off
	global_load_dword v65, v[52:53], off offset:256
	s_waitcnt lgkmcnt(0)
	v_lshlrev_b32_e32 v1, 8, v30
	v_add_u32_sdwa v0, v0, v2 dst_sel:DWORD dst_unused:UNUSED_PAD src0_sel:DWORD src1_sel:WORD_0
	global_load_dword v68, v[54:55], off offset:256
	global_load_dword v69, v[52:53], off offset:512
	global_load_dword v82, v[52:53], off offset:768
	global_load_dword v78, v[54:55], off offset:512
	global_load_dword v86, v[54:55], off offset:768
	v_add_u32_sdwa v2, v1, v3 dst_sel:DWORD dst_unused:UNUSED_PAD src0_sel:DWORD src1_sel:WORD_0
	v_ashrrev_i32_e32 v1, 31, v0
	v_lshlrev_b64 v[0:1], 11, v[0:1]
	v_lshl_add_u64 v[56:57], v[20:21], 0, v[0:1]
	global_load_dword v100, v[56:57], off
	v_ashrrev_i32_e32 v3, 31, v2
	v_lshlrev_b64 v[2:3], 11, v[2:3]
	v_lshl_add_u64 v[58:59], v[20:21], 0, v[2:3]
	global_load_dword v104, v[58:59], off
	global_load_dword v115, v[56:57], off offset:256
	global_load_dword v122, v[58:59], off offset:256
	global_load_dword v124, v[56:57], off offset:512
	global_load_dwordx2 v[70:71], v[24:25], off
	global_load_dword v128, v[58:59], off offset:512
	global_load_dword v132, v[56:57], off offset:768
	global_load_dwordx2 v[34:35], v[24:25], off offset:2048
	global_load_dwordx2 v[28:29], v[24:25], off offset:2560
	global_load_dwordx2 v[2:3], v[24:25], off offset:3072
	global_load_dwordx2 v[0:1], v[24:25], off offset:3584
	global_load_dword v136, v[58:59], off offset:768
	global_load_dwordx2 v[62:63], v[44:45], off offset:1536
	global_load_dwordx2 v[36:37], v[44:45], off offset:2048
	global_load_dwordx2 v[30:31], v[44:45], off offset:2560
	global_load_dwordx2 v[32:33], v[44:45], off offset:3072
	global_load_dwordx2 v[42:43], v[44:45], off offset:3584
	global_load_dword v138, v[52:53], off offset:1024
	global_load_dword v139, v[52:53], off offset:1280
	global_load_dword v140, v[52:53], off offset:1536
	global_load_dword v154, v[52:53], off offset:1792
	global_load_dword v141, v[54:55], off offset:1024
	global_load_dword v142, v[54:55], off offset:1280
	global_load_dword v143, v[54:55], off offset:1536
	global_load_dword v155, v[54:55], off offset:1792
	global_load_dword v144, v[56:57], off offset:1024
	global_load_dword v145, v[56:57], off offset:1280
	global_load_dword v146, v[56:57], off offset:1536
	global_load_dword v150, v[56:57], off offset:1792
	global_load_dword v147, v[58:59], off offset:1024
	global_load_dword v148, v[58:59], off offset:1280
	global_load_dword v149, v[58:59], off offset:1536
	global_load_dword v151, v[58:59], off offset:1792
	s_waitcnt vmcnt(42)
	v_lshlrev_b32_e32 v76, 16, v50
	v_and_b32_e32 v77, 0xffff0000, v50
	v_lshlrev_b32_e32 v96, 16, v51
	v_and_b32_e32 v97, 0xffff0000, v51
	v_lshlrev_b32_e32 v60, 16, v38
	v_and_b32_e32 v61, 0xffff0000, v38
	v_lshlrev_b32_e32 v38, 16, v39
	v_and_b32_e32 v39, 0xffff0000, v39
	v_lshlrev_b32_e32 v44, 16, v26
	v_and_b32_e32 v45, 0xffff0000, v26
	v_lshlrev_b32_e32 v26, 16, v27
	v_and_b32_e32 v27, 0xffff0000, v27
	v_lshlrev_b32_e32 v66, 16, v40
	v_and_b32_e32 v67, 0xffff0000, v40
	v_lshlrev_b32_e32 v40, 16, v41
	v_and_b32_e32 v41, 0xffff0000, v41
	v_lshlrev_b32_e32 v74, 16, v48
	v_and_b32_e32 v75, 0xffff0000, v48
	v_lshlrev_b32_e32 v48, 16, v49
	v_and_b32_e32 v49, 0xffff0000, v49
	v_lshlrev_b32_e32 v72, 16, v46
	v_and_b32_e32 v73, 0xffff0000, v46
	v_lshlrev_b32_e32 v46, 16, v47
	v_and_b32_e32 v47, 0xffff0000, v47
	s_waitcnt vmcnt(32)
	v_cvt_pk_f32_fp8_e32 v[102:103], v104
	s_waitcnt vmcnt(31)
; __device__ __forceinline__ void p6_final(const Frame& F, KArgs a) {
;     ...
;         float sa = 0.f, sb = 0.f;
; #pragma unroll
;         for (int j = 0; j < 8; ++j) {
;             const f32x2p pal = __builtin_amdgcn_cvt_pk_f32_fp8((int)pa[j], false), pah = __builtin_amdgcn_cvt_pk_f32_fp8((int)pa[j], true), qal = __builtin_amdgcn_cvt_pk_f32_fp8((int)qa[j], false), qah = __builtin_amdgcn_cvt_pk_f32_fp8((int)qa[j], true);
;             const f32x2p pbl = __builtin_amdgcn_cvt_pk_f32_fp8((int)pb[j], false), pbh = __builtin_amdgcn_cvt_pk_f32_fp8((int)pb[j], true), qbl = __builtin_amdgcn_cvt_pk_f32_fp8((int)qb[j], false), qbh = __builtin_amdgcn_cvt_pk_f32_fp8((int)qb[j], true);
;             va[j].x += (pal[0] + qal[0]) * 0.0625f; va[j].y += (pal[1] + qal[1]) * 0.0625f; va[j].z += (pah[0] + qah[0]) * 0.0625f; va[j].w += (pah[1] + qah[1]) * 0.0625f;
;             vb[j].x += (pbl[0] + qbl[0]) * 0.0625f; vb[j].y += (pbl[1] + qbl[1]) * 0.0625f; vb[j].z += (pbh[0] + qbh[0]) * 0.0625f; vb[j].w += (pbh[1] + qbh[1]) * 0.0625f;
;             sa += (va[j].x * va[j].x + va[j].y * va[j].y) + (va[j].z * va[j].z + va[j].w * va[j].w); sb += (vb[j].x * vb[j].x + vb[j].y * vb[j].y) + (vb[j].z * vb[j].z + vb[j].w * vb[j].w); }
	v_cvt_pk_f32_fp8_sdwa v[118:119], v115 src0_sel:WORD_1
	s_waitcnt vmcnt(30)
	v_cvt_pk_f32_fp8_e32 v[120:121], v122
	v_cvt_pk_f32_fp8_e32 v[94:95], v64
	v_cvt_pk_f32_fp8_sdwa v[90:91], v64 src0_sel:WORD_1
	v_cvt_pk_f32_fp8_e32 v[50:51], v65
	v_cvt_pk_f32_fp8_sdwa v[52:53], v65 src0_sel:WORD_1
	v_cvt_pk_f32_fp8_e32 v[54:55], v68
	v_cvt_pk_f32_fp8_sdwa v[56:57], v68 src0_sel:WORD_1
	v_cvt_pk_f32_fp8_e32 v[58:59], v69
	v_cvt_pk_f32_fp8_sdwa v[64:65], v69 src0_sel:WORD_1
	v_cvt_pk_f32_fp8_e32 v[68:69], v78
	v_cvt_pk_f32_fp8_sdwa v[78:79], v78 src0_sel:WORD_1
	v_cvt_pk_f32_fp8_e32 v[80:81], v82
	v_cvt_pk_f32_fp8_sdwa v[82:83], v82 src0_sel:WORD_1
	v_cvt_pk_f32_fp8_e32 v[84:85], v86
	v_cvt_pk_f32_fp8_sdwa v[86:87], v86 src0_sel:WORD_1
	v_cvt_pk_f32_fp8_sdwa v[122:123], v122 src0_sel:WORD_1
	v_pk_add_f32 v[50:51], v[50:51], v[54:55]
	v_pk_add_f32 v[52:53], v[52:53], v[56:57]
	s_waitcnt vmcnt(29)
	v_cvt_pk_f32_fp8_e32 v[56:57], v124
	v_cvt_pk_f32_fp8_sdwa v[124:125], v124 src0_sel:WORD_1
	s_waitcnt vmcnt(27)
	v_cvt_pk_f32_fp8_e32 v[126:127], v128
	v_cvt_pk_f32_fp8_sdwa v[128:129], v128 src0_sel:WORD_1
	v_pk_add_f32 v[54:55], v[58:59], v[68:69]
	v_pk_add_f32 v[58:59], v[64:65], v[78:79]
	v_cvt_pk_f32_fp8_e32 v[98:99], v100
	v_cvt_pk_f32_fp8_sdwa v[100:101], v100 src0_sel:WORD_1
	v_cvt_pk_f32_fp8_sdwa v[104:105], v104 src0_sel:WORD_1
	s_waitcnt vmcnt(26)
	v_cvt_pk_f32_fp8_e32 v[130:131], v132
	s_waitcnt vmcnt(21)
	v_cvt_pk_f32_fp8_e32 v[134:135], v136
	v_pk_fma_f32 v[64:65], v[54:55], s[10:11], v[60:61] op_sel_hi:[1,0,1]
	v_pk_fma_f32 v[54:55], v[58:59], s[10:11], v[38:39] op_sel_hi:[1,0,1]
	v_cvt_pk_f32_fp8_e32 v[116:117], v115
	v_cvt_pk_f32_fp8_sdwa v[132:133], v132 src0_sel:WORD_1
	v_cvt_pk_f32_fp8_sdwa v[136:137], v136 src0_sel:WORD_1
	v_pk_add_f32 v[78:79], v[80:81], v[84:85]
	v_pk_add_f32 v[80:81], v[82:83], v[86:87]
	v_pk_mov_b32 v[38:39], v[64:65], v[54:55] op_sel:[1,0]
	v_pk_fma_f32 v[68:69], v[52:53], s[10:11], v[26:27] op_sel_hi:[1,0,1]
	v_pk_fma_f32 v[26:27], v[80:81], s[10:11], v[40:41] op_sel_hi:[1,0,1]
	v_mov_b32_e32 v40, v64
	v_mov_b32_e32 v41, v55
	v_pk_mul_f32 v[38:39], v[38:39], v[38:39]
	v_pk_fma_f32 v[82:83], v[50:51], s[10:11], v[44:45] op_sel_hi:[1,0,1]
	v_pk_fma_f32 v[50:51], v[78:79], s[10:11], v[66:67] op_sel_hi:[1,0,1]
	v_pk_add_f32 v[60:61], v[118:119], v[122:123]
	v_pk_add_f32 v[66:67], v[124:125], v[128:129]
	v_pk_fma_f32 v[38:39], v[40:41], v[40:41], v[38:39]
	v_pk_add_f32 v[52:53], v[100:101], v[104:105]
	v_pk_fma_f32 v[80:81], v[60:61], s[10:11], v[48:49] op_sel_hi:[1,0,1]
	v_pk_fma_f32 v[60:61], v[66:67], s[10:11], v[96:97] op_sel_hi:[1,0,1]
	v_pk_add_f32 v[96:97], v[38:39], v[38:39] op_sel:[0,1] op_sel_hi:[1,0]
	s_waitcnt vmcnt(20)
	v_lshlrev_b32_e32 v38, 16, v62
	v_and_b32_e32 v39, 0xffff0000, v62
	v_pk_add_f32 v[40:41], v[130:131], v[134:135]
	v_pk_add_f32 v[44:45], v[98:99], v[102:103]
	v_pk_add_f32 v[58:59], v[116:117], v[120:121]
	v_pk_add_f32 v[56:57], v[56:57], v[126:127]
	v_pk_fma_f32 v[86:87], v[52:53], s[10:11], v[46:47] op_sel_hi:[1,0,1]
	v_pk_fma_f32 v[52:53], v[40:41], s[10:11], v[38:39] op_sel_hi:[1,0,1]
	v_lshlrev_b32_e32 v38, 16, v63
	v_and_b32_e32 v39, 0xffff0000, v63
	v_pk_add_f32 v[40:41], v[132:133], v[136:137]
	v_pk_fma_f32 v[84:85], v[44:45], s[10:11], v[72:73] op_sel_hi:[1,0,1]
	v_pk_fma_f32 v[78:79], v[58:59], s[10:11], v[74:75] op_sel_hi:[1,0,1]
	v_pk_fma_f32 v[58:59], v[56:57], s[10:11], v[76:77] op_sel_hi:[1,0,1]
	v_pk_fma_f32 v[56:57], v[40:41], s[10:11], v[38:39] op_sel_hi:[1,0,1]
	s_waitcnt vmcnt(15)
	v_cvt_pk_f32_fp8_e32 v[38:39], v138
	s_waitcnt vmcnt(11)
	v_cvt_pk_f32_fp8_e32 v[44:45], v141
	v_cvt_pk_f32_fp8_sdwa v[40:41], v138 src0_sel:WORD_1
	v_cvt_pk_f32_fp8_sdwa v[48:49], v141 src0_sel:WORD_1
	s_waitcnt vmcnt(7)
	v_cvt_pk_f32_fp8_e32 v[62:63], v144
	s_waitcnt vmcnt(3)
	v_cvt_pk_f32_fp8_e32 v[104:105], v147
	v_cvt_pk_f32_fp8_sdwa v[102:103], v144 src0_sel:WORD_1
	v_cvt_pk_f32_fp8_sdwa v[124:125], v147 src0_sel:WORD_1
	v_lshlrev_b32_e32 v46, 16, v34
	v_and_b32_e32 v47, 0xffff0000, v34
	v_pk_add_f32 v[38:39], v[38:39], v[44:45]
	v_lshlrev_b32_e32 v34, 16, v35
	v_pk_fma_f32 v[46:47], v[38:39], s[10:11], v[46:47] op_sel_hi:[1,0,1]
	v_and_b32_e32 v35, 0xffff0000, v35
	v_pk_add_f32 v[38:39], v[40:41], v[48:49]
	v_pk_add_f32 v[40:41], v[62:63], v[104:105]
	v_pk_fma_f32 v[38:39], v[38:39], s[10:11], v[34:35] op_sel_hi:[1,0,1]
	v_lshlrev_b32_e32 v34, 16, v36
	v_and_b32_e32 v35, 0xffff0000, v36
	v_pk_fma_f32 v[34:35], v[40:41], s[10:11], v[34:35] op_sel_hi:[1,0,1]
	v_lshlrev_b32_e32 v36, 16, v37
	v_and_b32_e32 v37, 0xffff0000, v37
	v_pk_add_f32 v[40:41], v[102:103], v[124:125]
	v_cvt_pk_f32_fp8_e32 v[48:49], v142
	v_pk_fma_f32 v[40:41], v[40:41], s[10:11], v[36:37] op_sel_hi:[1,0,1]
	v_cvt_pk_f32_fp8_e32 v[36:37], v139
	v_cvt_pk_f32_fp8_sdwa v[44:45], v139 src0_sel:WORD_1
	v_cvt_pk_f32_fp8_sdwa v[128:129], v142 src0_sel:WORD_1
	v_cvt_pk_f32_fp8_e32 v[130:131], v145
	s_waitcnt vmcnt(2)
; __device__ __forceinline__ void p6_final(const Frame& F, KArgs a) {
;     ...
;         float sa = 0.f, sb = 0.f;
; #pragma unroll
;         for (int j = 0; j < 8; ++j) {
;             const f32x2p pal = __builtin_amdgcn_cvt_pk_f32_fp8((int)pa[j], false), pah = __builtin_amdgcn_cvt_pk_f32_fp8((int)pa[j], true), qal = __builtin_amdgcn_cvt_pk_f32_fp8((int)qa[j], false), qah = __builtin_amdgcn_cvt_pk_f32_fp8((int)qa[j], true);
;             const f32x2p pbl = __builtin_amdgcn_cvt_pk_f32_fp8((int)pb[j], false), pbh = __builtin_amdgcn_cvt_pk_f32_fp8((int)pb[j], true), qbl = __builtin_amdgcn_cvt_pk_f32_fp8((int)qb[j], false), qbh = __builtin_amdgcn_cvt_pk_f32_fp8((int)qb[j], true);
;             va[j].x += (pal[0] + qal[0]) * 0.0625f; va[j].y += (pal[1] + qal[1]) * 0.0625f; va[j].z += (pah[0] + qah[0]) * 0.0625f; va[j].w += (pah[1] + qah[1]) * 0.0625f;
;             vb[j].x += (pbl[0] + qbl[0]) * 0.0625f; vb[j].y += (pbl[1] + qbl[1]) * 0.0625f; vb[j].z += (pbh[0] + qbh[0]) * 0.0625f; vb[j].w += (pbh[1] + qbh[1]) * 0.0625f;
;             sa += (va[j].x * va[j].x + va[j].y * va[j].y) + (va[j].z * va[j].z + va[j].w * va[j].w); sb += (vb[j].x * vb[j].x + vb[j].y * vb[j].y) + (vb[j].z * vb[j].z + vb[j].w * vb[j].w); }
;         const float ra = 1.0f / sqrtf(wave_sum(sa) * (1.0f / DM) + EPS), rb = 1.0f / sqrtf(wave_sum(sb) * (1.0f / DM) + EPS);
	v_cvt_pk_f32_fp8_e32 v[134:135], v148
	v_cvt_pk_f32_fp8_sdwa v[132:133], v145 src0_sel:WORD_1
	v_cvt_pk_f32_fp8_sdwa v[136:137], v148 src0_sel:WORD_1
	v_lshlrev_b32_e32 v62, 16, v28
	v_and_b32_e32 v63, 0xffff0000, v28
	v_pk_add_f32 v[36:37], v[36:37], v[48:49]
	v_lshlrev_b32_e32 v28, 16, v29
	v_pk_fma_f32 v[62:63], v[36:37], s[10:11], v[62:63] op_sel_hi:[1,0,1]
	v_and_b32_e32 v29, 0xffff0000, v29
	v_pk_add_f32 v[36:37], v[44:45], v[128:129]
	v_pk_add_f32 v[44:45], v[130:131], v[134:135]
	v_pk_fma_f32 v[28:29], v[36:37], s[10:11], v[28:29] op_sel_hi:[1,0,1]
	v_lshlrev_b32_e32 v36, 16, v30
	v_and_b32_e32 v37, 0xffff0000, v30
	v_pk_fma_f32 v[44:45], v[44:45], s[10:11], v[36:37] op_sel_hi:[1,0,1]
	v_lshlrev_b32_e32 v30, 16, v31
	v_and_b32_e32 v31, 0xffff0000, v31
	v_pk_add_f32 v[36:37], v[132:133], v[136:137]
	v_cvt_pk_f32_fp8_e32 v[92:93], v4
	v_pk_fma_f32 v[48:49], v[36:37], s[10:11], v[30:31] op_sel_hi:[1,0,1]
	v_pk_mov_b32 v[30:31], v[62:63], v[28:29] op_sel:[1,0]
	v_cvt_pk_f32_fp8_sdwa v[88:89], v4 src0_sel:WORD_1
	v_mul_f32_e32 v4, v51, v51
	v_pk_mul_f32 v[30:31], v[30:31], v[30:31]
	v_mov_b32_e32 v36, v62
	v_mov_b32_e32 v37, v29
	v_pk_mul_f32 v[74:75], v[78:79], v[78:79]
	v_pk_mul_f32 v[76:77], v[80:81], v[80:81]
	v_pk_fma_f32 v[98:99], v[50:51], v[50:51], v[4:5] op_sel_hi:[1,1,0]
	v_mul_f32_e32 v4, v27, v27
	v_pk_fma_f32 v[30:31], v[36:37], v[36:37], v[30:31]
	v_pk_mul_f32 v[66:67], v[84:85], v[84:85]
	v_pk_mul_f32 v[72:73], v[86:87], v[86:87]
	v_pk_fma_f32 v[100:101], v[26:27], v[26:27], v[4:5] op_sel_hi:[1,1,0]
	v_pk_add_f32 v[128:129], v[30:31], v[30:31] op_sel:[0,1] op_sel_hi:[1,0]
	v_cvt_pk_f32_fp8_e32 v[30:31], v140
	v_cvt_pk_f32_fp8_sdwa v[134:135], v140 src0_sel:WORD_1
	v_cvt_pk_f32_fp8_e32 v[36:37], v143
	v_cvt_pk_f32_fp8_sdwa v[136:137], v143 src0_sel:WORD_1
	v_cvt_pk_f32_fp8_e32 v[138:139], v146
	v_cvt_pk_f32_fp8_sdwa v[140:141], v146 src0_sel:WORD_1
	s_waitcnt vmcnt(1)
	v_cvt_pk_f32_fp8_e32 v[142:143], v149
	v_lshlrev_b32_e32 v146, 16, v2
	v_and_b32_e32 v147, 0xffff0000, v2
	v_add_f32_e32 v2, v76, v77
	v_add_f32_e32 v4, v74, v75
	v_cvt_pk_f32_fp8_sdwa v[144:145], v149 src0_sel:WORD_1
	v_add_f32_e32 v2, v4, v2
	v_add_f32_e32 v4, v72, v73
	v_add_f32_e32 v66, v66, v67
	v_pk_mul_f32 v[116:117], v[58:59], v[58:59]
	v_pk_mul_f32 v[118:119], v[60:61], v[60:61]
	v_add_f32_e32 v4, v66, v4
	v_add_f32_e32 v2, v4, v2
	v_add_f32_e32 v4, v118, v119
	v_add_f32_e32 v66, v116, v117
	v_pk_mul_f32 v[120:121], v[52:53], v[52:53]
	v_pk_mul_f32 v[122:123], v[56:57], v[56:57]
	v_pk_add_f32 v[148:149], v[30:31], v[36:37]
	v_lshlrev_b32_e32 v30, 16, v32
	v_and_b32_e32 v31, 0xffff0000, v32
	v_pk_add_f32 v[36:37], v[138:139], v[142:143]
	v_add_f32_e32 v4, v66, v4
	v_pk_fma_f32 v[30:31], v[36:37], s[10:11], v[30:31] op_sel_hi:[1,0,1]
	v_lshlrev_b32_e32 v32, 16, v33
	v_and_b32_e32 v33, 0xffff0000, v33
	v_pk_add_f32 v[36:37], v[140:141], v[144:145]
	v_add_f32_e32 v2, v2, v4
	v_add_f32_e32 v4, v122, v123
	v_add_f32_e32 v66, v120, v121
	v_pk_mul_f32 v[124:125], v[34:35], v[34:35]
	v_pk_mul_f32 v[126:127], v[40:41], v[40:41]
	v_pk_fma_f32 v[32:33], v[36:37], s[10:11], v[32:33] op_sel_hi:[1,0,1]
	v_cvt_pk_f32_fp8_e32 v[36:37], v150
	v_cvt_pk_f32_fp8_sdwa v[142:143], v150 src0_sel:WORD_1
	s_waitcnt vmcnt(0)
	v_cvt_pk_f32_fp8_e32 v[144:145], v151
	v_cvt_pk_f32_fp8_sdwa v[150:151], v151 src0_sel:WORD_1
	v_add_f32_e32 v4, v66, v4
	v_add_f32_e32 v2, v2, v4
	v_add_f32_e32 v4, v126, v127
	v_add_f32_e32 v66, v124, v125
	v_pk_mul_f32 v[130:131], v[44:45], v[44:45]
	v_pk_mul_f32 v[132:133], v[48:49], v[48:49]
	v_add_f32_e32 v4, v66, v4
	v_add_f32_e32 v2, v2, v4
	v_add_f32_e32 v4, v132, v133
	v_add_f32_e32 v66, v130, v131
	v_pk_mul_f32 v[138:139], v[30:31], v[30:31]
	v_pk_mul_f32 v[140:141], v[32:33], v[32:33]
	v_lshlrev_b32_e32 v152, 16, v42
	v_and_b32_e32 v153, 0xffff0000, v42
	v_pk_add_f32 v[36:37], v[36:37], v[144:145]
	v_lshlrev_b32_e32 v42, 16, v43
	v_and_b32_e32 v43, 0xffff0000, v43
	v_pk_add_f32 v[142:143], v[142:143], v[150:151]
	v_add_f32_e32 v4, v66, v4
	v_pk_fma_f32 v[36:37], v[36:37], s[10:11], v[152:153] op_sel_hi:[1,0,1]
	v_pk_fma_f32 v[42:43], v[142:143], s[10:11], v[42:43] op_sel_hi:[1,0,1]
	v_add_f32_e32 v2, v2, v4
	v_add_f32_e32 v4, v140, v141
	v_add_f32_e32 v66, v138, v139
	v_pk_mul_f32 v[142:143], v[36:37], v[36:37]
	v_pk_mul_f32 v[144:145], v[42:43], v[42:43]
	v_add_f32_e32 v4, v66, v4
	v_add_f32_e32 v2, v2, v4
	v_add_f32_e32 v4, v144, v145
	v_add_f32_e32 v66, v142, v143
	v_add_f32_e32 v4, v66, v4
	v_add_f32_e32 v4, v2, v4
	ds_bpermute_b32 v72, v106, v4
	v_pk_fma_f32 v[74:75], v[148:149], s[10:11], v[146:147] op_sel_hi:[1,0,1]
	v_lshlrev_b32_e32 v2, 16, v3
	v_and_b32_e32 v3, 0xffff0000, v3
	v_pk_add_f32 v[66:67], v[134:135], v[136:137]
	s_waitcnt lgkmcnt(0)
	v_add_f32_e32 v4, v4, v72
	ds_bpermute_b32 v76, v107, v4
	v_pk_fma_f32 v[72:73], v[66:67], s[10:11], v[2:3] op_sel_hi:[1,0,1]
	v_mul_f32_e32 v2, v75, v75
	v_pk_fma_f32 v[116:117], v[74:75], v[74:75], v[2:3] op_sel_hi:[1,1,0]
	v_mul_f32_e32 v2, v73, v73
	s_waitcnt lgkmcnt(0)
	v_add_f32_e32 v4, v4, v76
	ds_bpermute_b32 v97, v108, v4
	v_pk_fma_f32 v[118:119], v[72:73], v[72:73], v[2:3] op_sel_hi:[1,1,0]
	v_cvt_pk_f32_fp8_e32 v[2:3], v154
	v_cvt_pk_f32_fp8_e32 v[76:77], v155
	v_cvt_pk_f32_fp8_sdwa v[66:67], v154 src0_sel:WORD_1
	s_waitcnt lgkmcnt(0)
	v_add_f32_e32 v4, v4, v97
	ds_bpermute_b32 v97, v109, v4
	v_cvt_pk_f32_fp8_sdwa v[120:121], v155 src0_sel:WORD_1
	v_lshlrev_b32_e32 v122, 16, v0
	v_and_b32_e32 v123, 0xffff0000, v0
	v_pk_add_f32 v[2:3], v[2:3], v[76:77]
	s_waitcnt lgkmcnt(0)
; __device__ __forceinline__ float wave_sum(float v) {
; #pragma unroll
;     for (int o = 1; o < 64; o <<= 1) v += __shfl_xor(v, o);
;     return v;
; __device__ __forceinline__ void p6_final(const Frame& F, KArgs a) {
;     ...
;             va[j].x += (pal[0] + qal[0]) * 0.0625f; va[j].y += (pal[1] + qal[1]) * 0.0625f; va[j].z += (pah[0] + qah[0]) * 0.0625f; va[j].w += (pah[1] + qah[1]) * 0.0625f;
;             vb[j].x += (pbl[0] + qbl[0]) * 0.0625f; vb[j].y += (pbl[1] + qbl[1]) * 0.0625f; vb[j].z += (pbh[0] + qbh[0]) * 0.0625f; vb[j].w += (pbh[1] + qbh[1]) * 0.0625f;
;             sa += (va[j].x * va[j].x + va[j].y * va[j].y) + (va[j].z * va[j].z + va[j].w * va[j].w); sb += (vb[j].x * vb[j].x + vb[j].y * vb[j].y) + (vb[j].z * vb[j].z + vb[j].w * vb[j].w); }
;         const float ra = 1.0f / sqrtf(wave_sum(sa) * (1.0f / DM) + EPS), rb = 1.0f / sqrtf(wave_sum(sb) * (1.0f / DM) + EPS);
; #pragma unroll
;         for (int j = 0; j < 8; ++j) { const f32x4 g = g4[64 * j]; xa[64 * j] = (f32x4){va[j].x * ra * g.x, va[j].y * ra * g.y, va[j].z * ra * g.z, va[j].w * ra * g.w};
;             if (t1 != t0) xb[64 * j] = (f32x4){vb[j].x * rb * g.x, vb[j].y * rb * g.y, vb[j].z * rb * g.z, vb[j].w * rb * g.w}; }
	v_add_f32_e32 v4, v4, v97
	ds_bpermute_b32 v97, v110, v4
	v_pk_fma_f32 v[76:77], v[2:3], s[10:11], v[122:123] op_sel_hi:[1,0,1]
	v_lshlrev_b32_e32 v0, 16, v1
	v_and_b32_e32 v1, 0xffff0000, v1
	v_pk_add_f32 v[2:3], v[66:67], v[120:121]
	s_waitcnt lgkmcnt(0)
	v_add_f32_e32 v4, v4, v97
	ds_bpermute_b32 v97, v111, v4
	v_lshlrev_b32_e32 v124, 16, v70
	v_and_b32_e32 v125, 0xffff0000, v70
	v_pk_add_f32 v[92:93], v[92:93], v[94:95]
	v_pk_fma_f32 v[66:67], v[2:3], s[10:11], v[0:1] op_sel_hi:[1,0,1]
	s_waitcnt lgkmcnt(0)
	v_add_f32_e32 v0, v4, v97
	v_pk_fma_f32 v[92:93], v[92:93], s[10:11], v[124:125] op_sel_hi:[1,0,1]
	v_lshlrev_b32_e32 v70, 16, v71
	v_and_b32_e32 v71, 0xffff0000, v71
	v_pk_add_f32 v[88:89], v[88:89], v[90:91]
	v_fmamk_f32 v0, v0, 0x3a000000, v112
	v_pk_fma_f32 v[90:91], v[88:89], s[10:11], v[70:71] op_sel_hi:[1,0,1]
	v_mov_b32_e32 v88, v93
	v_mov_b32_e32 v89, v83
	v_mul_f32_e32 v1, 0x4f800000, v0
	v_cmp_gt_f32_e32 vcc, s18, v0
	v_mov_b32_e32 v70, v92
	v_mov_b32_e32 v71, v82
	v_pk_mul_f32 v[88:89], v[88:89], v[88:89]
	v_cndmask_b32_e32 v4, v0, v1, vcc
	global_load_dwordx4 v[0:3], v[6:7], off
	v_pk_fma_f32 v[70:71], v[70:71], v[70:71], v[88:89]
	v_mov_b32_e32 v88, v90
	v_mov_b32_e32 v89, v68
	v_pk_mul_f32 v[88:89], v[88:89], v[88:89]
	v_mov_b32_e32 v94, v91
	v_mov_b32_e32 v95, v69
	v_pk_fma_f32 v[88:89], v[94:95], v[94:95], v[88:89]
	v_pk_mul_f32 v[102:103], v[46:47], v[46:47]
	v_pk_add_f32 v[70:71], v[70:71], v[88:89]
	v_pk_mul_f32 v[104:105], v[38:39], v[38:39]
	v_pk_add_f32 v[70:71], v[70:71], v[70:71] op_sel:[0,1] op_sel_hi:[1,0]
	v_mov_b32_e32 v99, v105
	v_mov_b32_e32 v101, v104
	v_mov_b32_e32 v71, v102
	v_mov_b32_e32 v97, v103
	v_pk_add_f32 v[88:89], v[98:99], v[100:101]
	v_pk_add_f32 v[70:71], v[70:71], v[96:97]
	v_pk_mul_f32 v[120:121], v[76:77], v[76:77]
	v_pk_add_f32 v[70:71], v[70:71], v[88:89]
	v_pk_mul_f32 v[122:123], v[66:67], v[66:67]
	v_pk_add_f32 v[70:71], v[70:71], v[70:71] op_sel:[0,1] op_sel_hi:[1,0]
	v_mov_b32_e32 v117, v123
	v_mov_b32_e32 v119, v122
	v_mov_b32_e32 v71, v120
	v_mov_b32_e32 v129, v121
	v_pk_add_f32 v[88:89], v[116:117], v[118:119]
	v_pk_add_f32 v[70:71], v[70:71], v[128:129]
	v_sqrt_f32_e32 v115, v4
	v_pk_add_f32 v[70:71], v[70:71], v[88:89]
	v_add_u32_e32 v88, -1, v115
	v_add_f32_e32 v70, v70, v71
	ds_bpermute_b32 v71, v106, v70
	v_fma_f32 v89, -v88, v115, v4
	v_cmp_ge_f32_e64 s[0:1], 0, v89
	v_add_u32_e32 v89, 1, v115
	v_fma_f32 v94, -v89, v115, v4
	s_waitcnt lgkmcnt(0)
	v_add_f32_e32 v70, v70, v71
	ds_bpermute_b32 v71, v107, v70
	v_cndmask_b32_e64 v88, v115, v88, s[0:1]
	v_cmp_lt_f32_e64 s[0:1], 0, v94
	s_waitcnt lgkmcnt(0)
	v_add_f32_e32 v70, v70, v71
	ds_bpermute_b32 v71, v108, v70
	v_cndmask_b32_e64 v88, v88, v89, s[0:1]
	v_mul_f32_e32 v89, 0x37800000, v88
	v_cndmask_b32_e32 v88, v88, v89, vcc
	v_cmp_class_f32_e32 vcc, v4, v113
	s_nop 1
	v_cndmask_b32_e32 v4, v88, v4, vcc
	s_waitcnt lgkmcnt(0)
	v_add_f32_e32 v88, v70, v71
	ds_bpermute_b32 v89, v109, v88
	v_div_scale_f32 v94, s[0:1], v4, v4, 1.0
	v_rcp_f32_e32 v95, v94
	v_lshl_add_u64 v[70:71], v[18:19], 0, s[14:15]
	s_waitcnt lgkmcnt(0)
	v_add_f32_e32 v88, v88, v89
	ds_bpermute_b32 v89, v110, v88
	v_fma_f32 v96, -v94, v95, 1.0
	v_fmac_f32_e32 v95, v96, v95
	v_div_scale_f32 v96, vcc, 1.0, v4, 1.0
	s_waitcnt lgkmcnt(0)
	v_add_f32_e32 v88, v88, v89
	ds_bpermute_b32 v89, v111, v88
	v_mul_f32_e32 v97, v96, v95
	v_fma_f32 v98, -v94, v97, v96
	v_fmac_f32_e32 v97, v98, v95
	v_fma_f32 v94, -v94, v97, v96
	s_waitcnt lgkmcnt(0)
	v_add_f32_e32 v88, v88, v89
	v_fmamk_f32 v88, v88, 0x3a000000, v112
	v_mul_f32_e32 v89, 0x4f800000, v88
	v_cmp_gt_f32_e64 s[0:1], s18, v88
	v_div_fmas_f32 v94, v94, v95, v97
	v_div_fixup_f32 v4, v94, v4, 1.0
	v_cndmask_b32_e64 v88, v88, v89, s[0:1]
	v_sqrt_f32_e32 v89, v88
	s_cselect_b64 s[14:15], -1, 0
	s_cmp_eq_u32 s22, s12
	v_add_u32_e32 v94, -1, v89
	v_fma_f32 v95, -v94, v89, v88
	v_cmp_ge_f32_e32 vcc, 0, v95
	v_add_u32_e32 v95, 1, v89
	s_nop 0
	v_cndmask_b32_e32 v94, v89, v94, vcc
	v_fma_f32 v89, -v95, v89, v88
	v_cmp_lt_f32_e32 vcc, 0, v89
	s_nop 1
	v_cndmask_b32_e32 v89, v94, v95, vcc
	v_mul_f32_e32 v94, 0x37800000, v89
	v_cndmask_b32_e64 v89, v89, v94, s[0:1]
	v_cmp_class_f32_e32 vcc, v88, v113
	s_nop 1
	v_cndmask_b32_e32 v88, v89, v88, vcc
	v_div_scale_f32 v89, s[0:1], v88, v88, 1.0
	v_rcp_f32_e32 v94, v89
	s_mov_b64 s[0:1], -1
	v_fma_f32 v95, -v89, v94, 1.0
	v_fmac_f32_e32 v94, v95, v94
	v_div_scale_f32 v95, vcc, 1.0, v88, 1.0
	v_mul_f32_e32 v96, v95, v94
	v_fma_f32 v97, -v89, v96, v95
	v_fmac_f32_e32 v96, v97, v94
	v_fma_f32 v89, -v89, v96, v95
	v_div_fmas_f32 v89, v89, v94, v96
	v_div_fixup_f32 v88, v89, v88, 1.0
	v_mov_b32_e32 v89, v88
	v_pk_mul_f32 v[94:95], v[92:93], v[88:89] op_sel_hi:[1,0]
	v_pk_mul_f32 v[90:91], v[90:91], v[88:89] op_sel_hi:[1,0]
	v_pk_mul_f32 v[82:83], v[82:83], v[88:89]
	s_waitcnt vmcnt(0)
	v_pk_mul_f32 v[92:93], v[2:3], v[90:91]
	v_pk_mul_f32 v[90:91], v[0:1], v[94:95]
	v_add_co_u32_e32 v94, vcc, 0xfffff000, v22
	s_nop 1
	v_addc_co_u32_e32 v95, vcc, -1, v23, vcc
	global_store_dwordx4 v[94:95], v[90:93], off offset:-3072 sc1
	s_cbranch_scc1 .LBB0_999
	v_pk_mul_f32 v[84:85], v[84:85], v[4:5] op_sel_hi:[1,0]
	v_pk_mul_f32 v[86:87], v[86:87], v[4:5] op_sel_hi:[1,0]
	v_pk_mul_f32 v[0:1], v[0:1], v[84:85]
	v_pk_mul_f32 v[2:3], v[2:3], v[86:87]
	global_store_dwordx4 v[70:71], v[0:3], off sc1
	global_load_dwordx4 v[0:3], v[6:7], off offset:1024
	v_mov_b32_e32 v84, v88
	v_mov_b32_e32 v85, v88
	v_add_co_u32_e32 v86, vcc, 0xfffff000, v22
	v_pk_mul_f32 v[90:91], v[78:79], v[4:5] op_sel_hi:[1,0]
	v_pk_mul_f32 v[78:79], v[68:69], v[84:85]
	v_pk_mul_f32 v[92:93], v[80:81], v[4:5] op_sel_hi:[1,0]
	v_addc_co_u32_e32 v87, vcc, -1, v23, vcc
	s_mov_b64 s[0:1], 0
	s_waitcnt vmcnt(0)
	v_pk_mul_f32 v[80:81], v[78:79], v[2:3]
	v_pk_mul_f32 v[78:79], v[82:83], v[0:1]
	v_pk_mul_f32 v[2:3], v[92:93], v[2:3]
	v_pk_mul_f32 v[0:1], v[90:91], v[0:1]
	global_store_dwordx4 v[86:87], v[78:81], off offset:-2048 sc1
	global_store_dwordx4 v[70:71], v[0:3], off offset:1024 sc1
; __device__ __forceinline__ void p6_final(const Frame& F, KArgs a) {
;     ...
; #pragma unroll
;         for (int j = 0; j < 8; ++j) { const f32x4 g = g4[64 * j]; xa[64 * j] = (f32x4){va[j].x * ra * g.x, va[j].y * ra * g.y, va[j].z * ra * g.z, va[j].w * ra * g.w};
;             if (t1 != t0) xb[64 * j] = (f32x4){vb[j].x * rb * g.x, vb[j].y * rb * g.y, vb[j].z * rb * g.z, vb[j].w * rb * g.w}; }
.LBB0_999:
	s_andn2_b64 vcc, exec, s[0:1]
	s_cbranch_vccnz .LBB0_1001
	global_load_dwordx4 v[0:3], v[6:7], off offset:1024
	v_mov_b32_e32 v78, v88
	v_mov_b32_e32 v79, v88
	v_add_co_u32_e32 v80, vcc, 0xfffff000, v22
	v_pk_mul_f32 v[68:69], v[68:69], v[78:79]
	s_nop 0
	v_addc_co_u32_e32 v81, vcc, -1, v23, vcc
	s_waitcnt vmcnt(0)
	v_pk_mul_f32 v[2:3], v[68:69], v[2:3]
	v_pk_mul_f32 v[0:1], v[82:83], v[0:1]
	global_store_dwordx4 v[80:81], v[0:3], off offset:-2048 sc1
.LBB0_1001:
	global_load_dwordx4 v[0:3], v[6:7], off offset:2048
	v_pk_mul_f32 v[68:69], v[64:65], v[88:89]
	v_mov_b32_e32 v64, v88
	v_mov_b32_e32 v65, v88
	v_add_co_u32_e32 v82, vcc, 0xfffff000, v22
	v_cndmask_b32_e64 v78, 0, 1, s[14:15]
	v_pk_mul_f32 v[54:55], v[54:55], v[64:65]
	v_addc_co_u32_e32 v83, vcc, -1, v23, vcc
	s_mov_b64 s[12:13], -1
	v_cmp_ne_u32_e64 s[0:1], 1, v78
	s_andn2_b64 vcc, exec, s[14:15]
	v_pk_mul_f32 v[50:51], v[50:51], v[88:89]
	s_waitcnt vmcnt(0)
	v_pk_mul_f32 v[80:81], v[54:55], v[2:3]
	v_pk_mul_f32 v[78:79], v[68:69], v[0:1]
	global_store_dwordx4 v[82:83], v[78:81], off offset:-1024 sc1
	s_cbranch_vccnz .LBB0_1003
	v_pk_mul_f32 v[54:55], v[58:59], v[4:5] op_sel_hi:[1,0]
	v_pk_mul_f32 v[58:59], v[60:61], v[4:5] op_sel_hi:[1,0]
	v_pk_mul_f32 v[0:1], v[54:55], v[0:1]
	v_pk_mul_f32 v[2:3], v[58:59], v[2:3]
	global_store_dwordx4 v[70:71], v[0:3], off offset:2048 sc1
	global_load_dwordx4 v[0:3], v[6:7], off offset:3072
	v_pk_mul_f32 v[54:55], v[26:27], v[64:65]
	v_pk_mul_f32 v[58:59], v[52:53], v[4:5] op_sel_hi:[1,0]
	v_pk_mul_f32 v[56:57], v[56:57], v[4:5] op_sel_hi:[1,0]
	s_mov_b64 s[12:13], 0
	s_waitcnt vmcnt(0)
	v_pk_mul_f32 v[54:55], v[54:55], v[2:3]
	v_pk_mul_f32 v[52:53], v[50:51], v[0:1]
	v_pk_mul_f32 v[2:3], v[56:57], v[2:3]
	v_pk_mul_f32 v[0:1], v[58:59], v[0:1]
	global_store_dwordx4 v[22:23], v[52:55], off offset:-4096 sc1
	global_store_dwordx4 v[70:71], v[0:3], off offset:3072 sc1
.LBB0_1003:
	s_andn2_b64 vcc, exec, s[12:13]
	s_cbranch_vccnz .LBB0_1005
	global_load_dwordx4 v[0:3], v[6:7], off offset:3072
	v_mov_b32_e32 v52, v88
	v_mov_b32_e32 v53, v88
	v_pk_mul_f32 v[26:27], v[26:27], v[52:53]
	s_waitcnt vmcnt(0)
	v_pk_mul_f32 v[0:1], v[50:51], v[0:1]
	v_pk_mul_f32 v[2:3], v[26:27], v[2:3]
	global_store_dwordx4 v[22:23], v[0:3], off offset:-4096 sc1
.LBB0_1005:
	global_load_dwordx4 v[0:3], v[8:9], off
	v_pk_mul_f32 v[26:27], v[46:47], v[88:89]
	v_mov_b32_e32 v46, v88
	v_mov_b32_e32 v47, v88
	v_pk_mul_f32 v[38:39], v[38:39], v[46:47]
	s_mov_b64 s[12:13], -1
	s_and_b64 vcc, exec, s[0:1]
	s_waitcnt vmcnt(0)
	v_pk_mul_f32 v[52:53], v[38:39], v[2:3]
	v_pk_mul_f32 v[50:51], v[26:27], v[0:1]
	v_pk_mul_f32 v[26:27], v[62:63], v[88:89]
	global_store_dwordx4 v[22:23], v[50:53], off offset:-3072 sc1
	s_cbranch_vccnz .LBB0_1007
	v_pk_mul_f32 v[34:35], v[34:35], v[4:5] op_sel_hi:[1,0]
	v_pk_mul_f32 v[38:39], v[40:41], v[4:5] op_sel_hi:[1,0]
	v_pk_mul_f32 v[0:1], v[34:35], v[0:1]
	v_add_co_u32_e32 v34, vcc, 0x1000, v70
	v_pk_mul_f32 v[2:3], v[38:39], v[2:3]
	s_nop 0
	v_addc_co_u32_e32 v35, vcc, 0, v71, vcc
	global_store_dwordx4 v[34:35], v[0:3], off sc1
	global_load_dwordx4 v[0:3], v[10:11], off
	v_pk_mul_f32 v[38:39], v[28:29], v[46:47]
	v_pk_mul_f32 v[44:45], v[44:45], v[4:5] op_sel_hi:[1,0]
	v_pk_mul_f32 v[46:47], v[48:49], v[4:5] op_sel_hi:[1,0]
	s_mov_b64 s[12:13], 0
	s_waitcnt vmcnt(0)
	v_pk_mul_f32 v[40:41], v[38:39], v[2:3]
	v_pk_mul_f32 v[38:39], v[26:27], v[0:1]
	v_pk_mul_f32 v[2:3], v[46:47], v[2:3]
	v_pk_mul_f32 v[0:1], v[44:45], v[0:1]
	global_store_dwordx4 v[22:23], v[38:41], off offset:-2048 sc1
	global_store_dwordx4 v[34:35], v[0:3], off offset:1024 sc1
.LBB0_1007:
	s_andn2_b64 vcc, exec, s[12:13]
	s_cbranch_vccnz .LBB0_1009
	global_load_dwordx4 v[0:3], v[10:11], off
	v_mov_b32_e32 v34, v88
	v_mov_b32_e32 v35, v88
	v_pk_mul_f32 v[28:29], v[28:29], v[34:35]
	s_waitcnt vmcnt(0)
	v_pk_mul_f32 v[0:1], v[26:27], v[0:1]
	v_pk_mul_f32 v[2:3], v[28:29], v[2:3]
	global_store_dwordx4 v[22:23], v[0:3], off offset:-2048 sc1
.LBB0_1009:
	global_load_dwordx4 v[0:3], v[12:13], off
	v_mov_b32_e32 v28, v88
	v_mov_b32_e32 v29, v88
	v_pk_mul_f32 v[26:27], v[74:75], v[88:89]
	v_pk_mul_f32 v[34:35], v[72:73], v[28:29]
	s_mov_b64 s[12:13], -1
	s_and_b64 vcc, exec, s[0:1]
	s_waitcnt vmcnt(0)
	v_pk_mul_f32 v[40:41], v[34:35], v[2:3]
	v_pk_mul_f32 v[38:39], v[26:27], v[0:1]
	v_pk_mul_f32 v[26:27], v[76:77], v[88:89]
	global_store_dwordx4 v[22:23], v[38:41], off offset:-1024 sc1
	s_cbranch_vccnz .LBB0_1011
	v_pk_mul_f32 v[32:33], v[32:33], v[4:5] op_sel_hi:[1,0]
	v_pk_mul_f32 v[30:31], v[30:31], v[4:5] op_sel_hi:[1,0]
	v_pk_mul_f32 v[2:3], v[32:33], v[2:3]
	v_add_co_u32_e32 v32, vcc, 0x1000, v70
	v_pk_mul_f32 v[0:1], v[30:31], v[0:1]
	s_nop 0
	v_addc_co_u32_e32 v33, vcc, 0, v71, vcc
	global_store_dwordx4 v[32:33], v[0:3], off offset:2048 sc1
	global_load_dwordx4 v[0:3], v[14:15], off
	v_pk_mul_f32 v[28:29], v[66:67], v[28:29]
	v_pk_mul_f32 v[34:35], v[36:37], v[4:5] op_sel_hi:[1,0]
	v_pk_mul_f32 v[36:37], v[42:43], v[4:5] op_sel_hi:[1,0]
	s_mov_b64 s[12:13], 0
	s_waitcnt vmcnt(0)
	v_pk_mul_f32 v[30:31], v[28:29], v[2:3]
	v_pk_mul_f32 v[28:29], v[26:27], v[0:1]
	v_pk_mul_f32 v[2:3], v[36:37], v[2:3]
	v_pk_mul_f32 v[0:1], v[34:35], v[0:1]
	global_store_dwordx4 v[22:23], v[28:31], off sc1
	global_store_dwordx4 v[32:33], v[0:3], off offset:3072 sc1
.LBB0_1011:
	s_andn2_b64 vcc, exec, s[12:13]
	s_cbranch_vccnz .LBB0_996
	global_load_dwordx4 v[0:3], v[14:15], off
	v_mov_b32_e32 v89, v88
	v_pk_mul_f32 v[28:29], v[66:67], v[88:89]
	s_waitcnt vmcnt(0)
	v_pk_mul_f32 v[0:1], v[26:27], v[0:1]
	v_pk_mul_f32 v[2:3], v[28:29], v[2:3]
	global_store_dwordx4 v[22:23], v[0:3], off sc1
	s_branch .LBB0_996
